# whole layer-1 w_down transposition in the layer-1 in-projection idle slot, loads four region steps ahead
# speedup vs baseline: 1.0022x; 1.0022x over previous
;     const int pr = item >> 1, kb = 2 * (pr / nblk) + (item & 1), nb = pr % nblk, k0 = 64 * kb, n0 = 32 * nb;
;     const int nr = n0 + (lane & 31); const int sc = MAP == 1 ? src_col_in(nr) : nr;
;     float v[32];
; #pragma unroll
;     for (int i = 0; i < 32; ++i) v[i] = sc >= 0 ? W[(size_t)(k0 + 2 * i + (lane >> 5)) * Nsrc + sc] : 0.f;
; #pragma unroll
;     for (int i = 0; i < 32; ++i) { const int k = k0 + 2 * i + (lane >> 5); float x = v[i] * wscale; if (KS) x *= (k < ksplit ? ksA[k] : ksB[k - ksplit]); scr[(2 * i + (lane >> 5)) * 33 + (lane & 31)] = x; }
; __global__ void __launch_bounds__(NWAVES * 64, 2) hybrid_fwd(Args args) {
;     ...
;             p0_transpose_item_f8<false>(args.in[16] + (size_t)l * FF * DM, FF, DM, DM / 32, (unsigned char*)(ws + WS_WDN + l * SZ_WDN), 128.f, args.in[16], args.in[16], 0, scr, r, lane);
.LBB0_575:
	s_waitcnt vmcnt(0)
	s_barrier
	s_cmpk_lt_u32 s77, 0xa0
	s_cbranch_scc1 .Llite_skip
	s_sub_i32 s16, s77, 160
	v_and_b32_e32 v17, 63, v0
	v_lshrrev_b32_e32 v18, 6, v0
	v_lshrrev_b32_e32 v14, 5, v17
	v_lshl_add_u32 v15, v18, 4, v14
	v_and_b32_e32 v16, 31, v17
	v_xor_b32_e32 v16, v16, v18
	v_lshlrev_b32_e32 v16, 4, v16
	v_lshl_add_u32 v4, v15, 9, v16
	v_add_u32_e32 v5, 0x10000, v4
	v_and_b32_e32 v16, 31, v17
	v_lshlrev_b32_e32 v16, 4, v16
	s_mov_b32 s21, 0x4000
	v_mad_u32_u24 v10, v15, s21, v16
	v_and_b32_e32 v14, 7, v17
	v_lshrrev_b32_e32 v15, 5, v17
	v_lshl_add_u32 v15, v18, 2, v15
	v_xor_b32_e32 v15, v15, v14
	v_lshlrev_b32_e32 v15, 4, v15
	v_lshl_add_u32 v15, v14, 13, v15
	v_bfe_u32 v16, v17, 3, 2
	v_lshl_add_u32 v6, v16, 2, v15
	v_add_u32_e32 v7, 0x10000, v6
	v_and_b32_e32 v14, 7, v17
	v_lshrrev_b32_e32 v15, 5, v17
	v_lshl_add_u32 v15, v18, 2, v15
	v_add_u32_e32 v15, 2, v15
	v_xor_b32_e32 v15, v15, v14
	v_lshlrev_b32_e32 v15, 4, v15
	v_lshl_add_u32 v15, v14, 13, v15
	v_bfe_u32 v16, v17, 3, 2
	v_lshl_add_u32 v8, v16, 2, v15
	v_add_u32_e32 v9, 0x10000, v8
	v_lshrrev_b32_e32 v14, 3, v17
	v_lshl_add_u32 v14, v18, 4, v14
	v_and_b32_e32 v15, 7, v17
	v_lshlrev_b32_e32 v15, 4, v15
	v_lshl_add_u32 v11, v14, 14, v15
	v_lshrrev_b32_e32 v14, 3, v17
	v_lshl_add_u32 v14, v18, 4, v14
	v_add_u32_e32 v14, 8, v14
	v_and_b32_e32 v15, 7, v17
	v_lshlrev_b32_e32 v15, 4, v15
	v_lshl_add_u32 v12, v14, 14, v15
	v_mov_b32_e32 v13, 0x43e00000
	s_mov_b32 s20, 0xc3e00000
	v_readlane_b32 s2, v253, 35
	v_readlane_b32 s3, v253, 36
	v_readlane_b32 s4, v253, 41
	v_readlane_b32 s5, v253, 42
	s_add_u32 s2, s2, 0x10000000
	s_addc_u32 s3, s3, 0
	s_add_u32 s4, s4, 0x27600000
	s_addc_u32 s5, s5, 0
	s_add_i32 s17, s16, 0
	s_min_u32 s17, s17, 0xfff
	s_lshr_b32 s18, s17, 5
	s_add_i32 s18, s18, 0
	s_and_b32 s19, s17, 31
	s_lshl_b32 s18, s18, 21
	s_lshl_b32 s19, s19, 9
	s_add_u32 s18, s18, s19
	s_add_u32 s12, s2, s18
	s_addc_u32 s13, s3, 0
	global_load_dwordx4 v[36:39], v10, s[12:13]
	s_add_u32 s12, s12, 0x8000
	s_addc_u32 s13, s13, 0
	global_load_dwordx4 v[40:43], v10, s[12:13]
	s_add_u32 s12, s12, 0x8000
	s_addc_u32 s13, s13, 0
	global_load_dwordx4 v[44:47], v10, s[12:13]
	s_add_u32 s12, s12, 0x8000
	s_addc_u32 s13, s13, 0
	global_load_dwordx4 v[48:51], v10, s[12:13]
	s_add_u32 s12, s12, 0x8000
	s_addc_u32 s13, s13, 0
	global_load_dwordx4 v[52:55], v10, s[12:13]
	s_add_u32 s12, s12, 0x8000
	s_addc_u32 s13, s13, 0
	global_load_dwordx4 v[56:59], v10, s[12:13]
	s_add_u32 s12, s12, 0x8000
	s_addc_u32 s13, s13, 0
	global_load_dwordx4 v[60:63], v10, s[12:13]
	s_add_u32 s12, s12, 0x8000
	s_addc_u32 s13, s13, 0
	global_load_dwordx4 v[64:67], v10, s[12:13]
	s_add_i32 s17, s16, 96
	s_min_u32 s17, s17, 0xfff
	s_lshr_b32 s18, s17, 5
	s_add_i32 s18, s18, 0
	s_and_b32 s19, s17, 31
	s_lshl_b32 s18, s18, 21
	s_lshl_b32 s19, s19, 9
	s_add_u32 s18, s18, s19
	s_add_u32 s12, s2, s18
	s_addc_u32 s13, s3, 0
	global_load_dwordx4 v[68:71], v10, s[12:13]
	s_add_u32 s12, s12, 0x8000
	s_addc_u32 s13, s13, 0
	global_load_dwordx4 v[72:75], v10, s[12:13]
	s_add_u32 s12, s12, 0x8000
	s_addc_u32 s13, s13, 0
	global_load_dwordx4 v[76:79], v10, s[12:13]
	s_add_u32 s12, s12, 0x8000
	s_addc_u32 s13, s13, 0
	global_load_dwordx4 v[80:83], v10, s[12:13]
	s_add_u32 s12, s12, 0x8000
	s_addc_u32 s13, s13, 0
	global_load_dwordx4 v[84:87], v10, s[12:13]
	s_add_u32 s12, s12, 0x8000
	s_addc_u32 s13, s13, 0
	global_load_dwordx4 v[88:91], v10, s[12:13]
	s_add_u32 s12, s12, 0x8000
	s_addc_u32 s13, s13, 0
	global_load_dwordx4 v[92:95], v10, s[12:13]
	s_add_u32 s12, s12, 0x8000
	s_addc_u32 s13, s13, 0
	global_load_dwordx4 v[96:99], v10, s[12:13]
	s_add_i32 s17, s16, 192
	s_min_u32 s17, s17, 0xfff
	s_lshr_b32 s18, s17, 5
	s_add_i32 s18, s18, 0
	s_and_b32 s19, s17, 31
	s_lshl_b32 s18, s18, 21
	s_lshl_b32 s19, s19, 9
	s_add_u32 s18, s18, s19
	s_add_u32 s12, s2, s18
	s_addc_u32 s13, s3, 0
	global_load_dwordx4 v[100:103], v10, s[12:13]
	s_add_u32 s12, s12, 0x8000
	s_addc_u32 s13, s13, 0
	global_load_dwordx4 v[104:107], v10, s[12:13]
	s_add_u32 s12, s12, 0x8000
	s_addc_u32 s13, s13, 0
	global_load_dwordx4 v[108:111], v10, s[12:13]
	s_add_u32 s12, s12, 0x8000
	s_addc_u32 s13, s13, 0
	global_load_dwordx4 v[112:115], v10, s[12:13]
	s_add_u32 s12, s12, 0x8000
	s_addc_u32 s13, s13, 0
	global_load_dwordx4 v[116:119], v10, s[12:13]
	s_add_u32 s12, s12, 0x8000
	s_addc_u32 s13, s13, 0
	global_load_dwordx4 v[120:123], v10, s[12:13]
	s_add_u32 s12, s12, 0x8000
	s_addc_u32 s13, s13, 0
	global_load_dwordx4 v[124:127], v10, s[12:13]
	s_add_u32 s12, s12, 0x8000
	s_addc_u32 s13, s13, 0
	global_load_dwordx4 v[128:131], v10, s[12:13]
	s_add_i32 s17, s16, 288
	s_min_u32 s17, s17, 0xfff
	s_lshr_b32 s18, s17, 5
	s_add_i32 s18, s18, 0
	s_and_b32 s19, s17, 31
	s_lshl_b32 s18, s18, 21
	s_lshl_b32 s19, s19, 9
	s_add_u32 s18, s18, s19
	s_add_u32 s12, s2, s18
	s_addc_u32 s13, s3, 0
	global_load_dwordx4 v[132:135], v10, s[12:13]
	s_add_u32 s12, s12, 0x8000
	s_addc_u32 s13, s13, 0
	global_load_dwordx4 v[136:139], v10, s[12:13]
	s_add_u32 s12, s12, 0x8000
	s_addc_u32 s13, s13, 0
	global_load_dwordx4 v[140:143], v10, s[12:13]
	s_add_u32 s12, s12, 0x8000
	s_addc_u32 s13, s13, 0
	global_load_dwordx4 v[144:147], v10, s[12:13]
	s_add_u32 s12, s12, 0x8000
	s_addc_u32 s13, s13, 0
	global_load_dwordx4 v[148:151], v10, s[12:13]
	s_add_u32 s12, s12, 0x8000
	s_addc_u32 s13, s13, 0
	global_load_dwordx4 v[152:155], v10, s[12:13]
	s_add_u32 s12, s12, 0x8000
	s_addc_u32 s13, s13, 0
	global_load_dwordx4 v[156:159], v10, s[12:13]
	s_add_u32 s12, s12, 0x8000
	s_addc_u32 s13, s13, 0
	global_load_dwordx4 v[160:163], v10, s[12:13]
	s_waitcnt vmcnt(24)
; #define GAS __attribute__((address_space(1)))
; #define LAS __attribute__((address_space(3)))
; #define LDS_WAIT() asm volatile("s_waitcnt lgkmcnt(0)" ::: "memory")
; __device__ __forceinline__ unsigned pk4_fp8(float a, float b, float c, float d) {
;     a = fminf(fmaxf(a, -448.f), 448.f); b = fminf(fmaxf(b, -448.f), 448.f); c = fminf(fmaxf(c, -448.f), 448.f); d = fminf(fmaxf(d, -448.f), 448.f);
;     int w = __builtin_amdgcn_cvt_pk_fp8_f32(a, b, 0, false); w = __builtin_amdgcn_cvt_pk_fp8_f32(c, d, w, true); return (unsigned)w; }
;     ...
;     for (int i = 0; i < 32; ++i) v[i] = sc >= 0 ? W[(size_t)(k0 + 2 * i + (lane >> 5)) * Nsrc + sc] : 0.f;
; #pragma unroll
;     for (int i = 0; i < 32; ++i) { const int k = k0 + 2 * i + (lane >> 5); float x = v[i] * wscale; if (KS) x *= (k < ksplit ? ksA[k] : ksB[k - ksplit]); scr[(2 * i + (lane >> 5)) * 33 + (lane & 31)] = x; }
;     LDS_WAIT(); asm volatile("" ::: "memory");
;     const int c = lane & 7;
; #pragma unroll
;     for (int j = 0; j < 4; ++j) { const int n = (lane >> 3) + 8 * j; const LAS float* s = scr + (8 * c) * 33 + n;
;         const unsigned long long o = (unsigned long long)pg8::pk4_fp8(s[0 * 33], s[1 * 33], s[2 * 33], s[3 * 33]) | ((unsigned long long)pg8::pk4_fp8(s[4 * 33], s[5 * 33], s[6 * 33], s[7 * 33]) << 32);
;         *(GAS unsigned long long*)(WT + (size_t)(n0 + n) * K + k0 + 8 * c) = o; }
	v_mul_f32_e32 v36, 0x43000000, v36
	v_mul_f32_e32 v37, 0x43000000, v37
	v_mul_f32_e32 v38, 0x43000000, v38
	v_mul_f32_e32 v39, 0x43000000, v39
	ds_write_b128 v4, v[36:39]
	v_mul_f32_e32 v40, 0x43000000, v40
	v_mul_f32_e32 v41, 0x43000000, v41
	v_mul_f32_e32 v42, 0x43000000, v42
	v_mul_f32_e32 v43, 0x43000000, v43
	ds_write_b128 v4, v[40:43] offset:1024
	v_mul_f32_e32 v44, 0x43000000, v44
	v_mul_f32_e32 v45, 0x43000000, v45
	v_mul_f32_e32 v46, 0x43000000, v46
	v_mul_f32_e32 v47, 0x43000000, v47
	ds_write_b128 v4, v[44:47] offset:2048
	v_mul_f32_e32 v48, 0x43000000, v48
	v_mul_f32_e32 v49, 0x43000000, v49
	v_mul_f32_e32 v50, 0x43000000, v50
	v_mul_f32_e32 v51, 0x43000000, v51
	ds_write_b128 v4, v[48:51] offset:3072
	v_mul_f32_e32 v52, 0x43000000, v52
	v_mul_f32_e32 v53, 0x43000000, v53
	v_mul_f32_e32 v54, 0x43000000, v54
	v_mul_f32_e32 v55, 0x43000000, v55
	ds_write_b128 v4, v[52:55] offset:4096
	v_mul_f32_e32 v56, 0x43000000, v56
	v_mul_f32_e32 v57, 0x43000000, v57
	v_mul_f32_e32 v58, 0x43000000, v58
	v_mul_f32_e32 v59, 0x43000000, v59
	ds_write_b128 v4, v[56:59] offset:5120
	v_mul_f32_e32 v60, 0x43000000, v60
	v_mul_f32_e32 v61, 0x43000000, v61
	v_mul_f32_e32 v62, 0x43000000, v62
	v_mul_f32_e32 v63, 0x43000000, v63
	ds_write_b128 v4, v[60:63] offset:6144
	v_mul_f32_e32 v64, 0x43000000, v64
	v_mul_f32_e32 v65, 0x43000000, v65
	v_mul_f32_e32 v66, 0x43000000, v66
	v_mul_f32_e32 v67, 0x43000000, v67
	ds_write_b128 v4, v[64:67] offset:7168
	s_waitcnt lgkmcnt(0)
	s_barrier
	s_add_i32 s17, s16, 384
	s_min_u32 s17, s17, 0xfff
	s_lshr_b32 s18, s17, 5
	s_add_i32 s18, s18, 0
	s_and_b32 s19, s17, 31
	s_lshl_b32 s18, s18, 21
	s_lshl_b32 s19, s19, 9
	s_add_u32 s18, s18, s19
	s_add_u32 s12, s2, s18
	s_addc_u32 s13, s3, 0
	global_load_dwordx4 v[36:39], v10, s[12:13]
	s_add_u32 s12, s12, 0x8000
	s_addc_u32 s13, s13, 0
	global_load_dwordx4 v[40:43], v10, s[12:13]
	s_add_u32 s12, s12, 0x8000
	s_addc_u32 s13, s13, 0
	global_load_dwordx4 v[44:47], v10, s[12:13]
	s_add_u32 s12, s12, 0x8000
	s_addc_u32 s13, s13, 0
	global_load_dwordx4 v[48:51], v10, s[12:13]
	s_add_u32 s12, s12, 0x8000
	s_addc_u32 s13, s13, 0
	global_load_dwordx4 v[52:55], v10, s[12:13]
	s_add_u32 s12, s12, 0x8000
	s_addc_u32 s13, s13, 0
	global_load_dwordx4 v[56:59], v10, s[12:13]
	s_add_u32 s12, s12, 0x8000
	s_addc_u32 s13, s13, 0
	global_load_dwordx4 v[60:63], v10, s[12:13]
	s_add_u32 s12, s12, 0x8000
	s_addc_u32 s13, s13, 0
	global_load_dwordx4 v[64:67], v10, s[12:13]
	s_add_i32 s17, s16, 0
	s_min_u32 s17, s17, 0xfff
	s_lshr_b32 s18, s17, 5
	s_add_i32 s18, s18, 0
	s_and_b32 s19, s17, 31
	s_lshl_b32 s19, s19, 21
	s_lshl_b32 s18, s18, 7
	s_add_u32 s18, s18, s19
	s_add_u32 s14, s4, s18
	s_addc_u32 s15, s5, 0
	ds_read_b32 v170, v6
	ds_read_b32 v171, v6 offset:512
	ds_read_b32 v172, v6 offset:1024
	ds_read_b32 v173, v6 offset:1536
	ds_read_b32 v174, v6 offset:2048
	ds_read_b32 v175, v6 offset:2560
	ds_read_b32 v176, v6 offset:3072
	ds_read_b32 v177, v6 offset:3584
	ds_read_b32 v196, v6 offset:4096
	ds_read_b32 v197, v6 offset:4608
	ds_read_b32 v198, v6 offset:5120
	ds_read_b32 v199, v6 offset:5632
	ds_read_b32 v200, v6 offset:6144
	ds_read_b32 v201, v6 offset:6656
	ds_read_b32 v202, v6 offset:7168
	ds_read_b32 v203, v6 offset:7680
	s_waitcnt lgkmcnt(0)
	v_max_f32_e32 v170, v170, v170
	v_max_f32_e32 v171, v171, v171
	v_max_f32_e32 v172, v172, v172
	v_max_f32_e32 v173, v173, v173
	v_max_f32_e32 v174, v174, v174
	v_max_f32_e32 v175, v175, v175
	v_max_f32_e32 v176, v176, v176
	v_max_f32_e32 v177, v177, v177
	v_max_f32_e32 v196, v196, v196
	v_max_f32_e32 v197, v197, v197
	v_max_f32_e32 v198, v198, v198
	v_max_f32_e32 v199, v199, v199
	v_max_f32_e32 v200, v200, v200
	v_max_f32_e32 v201, v201, v201
	v_max_f32_e32 v202, v202, v202
	v_max_f32_e32 v203, v203, v203
	v_med3_f32 v170, v170, s20, v13
	v_med3_f32 v171, v171, s20, v13
	v_med3_f32 v172, v172, s20, v13
	v_med3_f32 v173, v173, s20, v13
	v_med3_f32 v174, v174, s20, v13
	v_med3_f32 v175, v175, s20, v13
	v_med3_f32 v176, v176, s20, v13
	v_med3_f32 v177, v177, s20, v13
	v_med3_f32 v196, v196, s20, v13
	v_med3_f32 v197, v197, s20, v13
	v_med3_f32 v198, v198, s20, v13
	v_med3_f32 v199, v199, s20, v13
	v_med3_f32 v200, v200, s20, v13
	v_med3_f32 v201, v201, s20, v13
	v_med3_f32 v202, v202, s20, v13
	v_med3_f32 v203, v203, s20, v13
	v_mov_b32_e32 v208, 0
	v_mov_b32_e32 v209, 0
	v_mov_b32_e32 v210, 0
	v_mov_b32_e32 v211, 0
	v_cvt_pk_fp8_f32 v208, v170, v171
	v_cvt_pk_fp8_f32 v209, v174, v175
	v_cvt_pk_fp8_f32 v210, v196, v197
	v_cvt_pk_fp8_f32 v211, v200, v201
	v_cvt_pk_fp8_f32 v208, v172, v173 op_sel:[0,0,1]
	v_cvt_pk_fp8_f32 v209, v176, v177 op_sel:[0,0,1]
	v_cvt_pk_fp8_f32 v210, v198, v199 op_sel:[0,0,1]
	v_cvt_pk_fp8_f32 v211, v202, v203 op_sel:[0,0,1]
	s_nop 0
	global_store_dwordx4 v11, v[208:211], s[14:15]
	ds_read_b32 v170, v8
	ds_read_b32 v171, v8 offset:512
	ds_read_b32 v172, v8 offset:1024
	ds_read_b32 v173, v8 offset:1536
	ds_read_b32 v174, v8 offset:2048
	ds_read_b32 v175, v8 offset:2560
	ds_read_b32 v176, v8 offset:3072
	ds_read_b32 v177, v8 offset:3584
	ds_read_b32 v196, v8 offset:4096
	ds_read_b32 v197, v8 offset:4608
	ds_read_b32 v198, v8 offset:5120
	ds_read_b32 v199, v8 offset:5632
	ds_read_b32 v200, v8 offset:6144
	ds_read_b32 v201, v8 offset:6656
	ds_read_b32 v202, v8 offset:7168
	ds_read_b32 v203, v8 offset:7680
	s_waitcnt lgkmcnt(0)
; #define GAS __attribute__((address_space(1)))
; #define LAS __attribute__((address_space(3)))
; #define LDS_WAIT() asm volatile("s_waitcnt lgkmcnt(0)" ::: "memory")
; __device__ __forceinline__ unsigned pk4_fp8(float a, float b, float c, float d) {
;     a = fminf(fmaxf(a, -448.f), 448.f); b = fminf(fmaxf(b, -448.f), 448.f); c = fminf(fmaxf(c, -448.f), 448.f); d = fminf(fmaxf(d, -448.f), 448.f);
;     int w = __builtin_amdgcn_cvt_pk_fp8_f32(a, b, 0, false); w = __builtin_amdgcn_cvt_pk_fp8_f32(c, d, w, true); return (unsigned)w; }
;     const int pr = item >> 1, kb = 2 * (pr / nblk) + (item & 1), nb = pr % nblk, k0 = 64 * kb, n0 = 32 * nb;
;     const int nr = n0 + (lane & 31); const int sc = MAP == 1 ? src_col_in(nr) : nr;
;     float v[32];
; #pragma unroll
;     for (int i = 0; i < 32; ++i) v[i] = sc >= 0 ? W[(size_t)(k0 + 2 * i + (lane >> 5)) * Nsrc + sc] : 0.f;
; #pragma unroll
;     for (int i = 0; i < 32; ++i) { const int k = k0 + 2 * i + (lane >> 5); float x = v[i] * wscale; if (KS) x *= (k < ksplit ? ksA[k] : ksB[k - ksplit]); scr[(2 * i + (lane >> 5)) * 33 + (lane & 31)] = x; }
;     LDS_WAIT(); asm volatile("" ::: "memory");
;     const int c = lane & 7;
; #pragma unroll
;     for (int j = 0; j < 4; ++j) { const int n = (lane >> 3) + 8 * j; const LAS float* s = scr + (8 * c) * 33 + n;
;         const unsigned long long o = (unsigned long long)pg8::pk4_fp8(s[0 * 33], s[1 * 33], s[2 * 33], s[3 * 33]) | ((unsigned long long)pg8::pk4_fp8(s[4 * 33], s[5 * 33], s[6 * 33], s[7 * 33]) << 32);
;         *(GAS unsigned long long*)(WT + (size_t)(n0 + n) * K + k0 + 8 * c) = o; }
;     LDS_WAIT(); asm volatile("" ::: "memory");
	v_max_f32_e32 v170, v170, v170
	v_max_f32_e32 v171, v171, v171
	v_max_f32_e32 v172, v172, v172
	v_max_f32_e32 v173, v173, v173
	v_max_f32_e32 v174, v174, v174
	v_max_f32_e32 v175, v175, v175
	v_max_f32_e32 v176, v176, v176
	v_max_f32_e32 v177, v177, v177
	v_max_f32_e32 v196, v196, v196
	v_max_f32_e32 v197, v197, v197
	v_max_f32_e32 v198, v198, v198
	v_max_f32_e32 v199, v199, v199
	v_max_f32_e32 v200, v200, v200
	v_max_f32_e32 v201, v201, v201
	v_max_f32_e32 v202, v202, v202
	v_max_f32_e32 v203, v203, v203
	v_med3_f32 v170, v170, s20, v13
	v_med3_f32 v171, v171, s20, v13
	v_med3_f32 v172, v172, s20, v13
	v_med3_f32 v173, v173, s20, v13
	v_med3_f32 v174, v174, s20, v13
	v_med3_f32 v175, v175, s20, v13
	v_med3_f32 v176, v176, s20, v13
	v_med3_f32 v177, v177, s20, v13
	v_med3_f32 v196, v196, s20, v13
	v_med3_f32 v197, v197, s20, v13
	v_med3_f32 v198, v198, s20, v13
	v_med3_f32 v199, v199, s20, v13
	v_med3_f32 v200, v200, s20, v13
	v_med3_f32 v201, v201, s20, v13
	v_med3_f32 v202, v202, s20, v13
	v_med3_f32 v203, v203, s20, v13
	v_mov_b32_e32 v208, 0
	v_mov_b32_e32 v209, 0
	v_mov_b32_e32 v210, 0
	v_mov_b32_e32 v211, 0
	v_cvt_pk_fp8_f32 v208, v170, v171
	v_cvt_pk_fp8_f32 v209, v174, v175
	v_cvt_pk_fp8_f32 v210, v196, v197
	v_cvt_pk_fp8_f32 v211, v200, v201
	v_cvt_pk_fp8_f32 v208, v172, v173 op_sel:[0,0,1]
	v_cvt_pk_fp8_f32 v209, v176, v177 op_sel:[0,0,1]
	v_cvt_pk_fp8_f32 v210, v198, v199 op_sel:[0,0,1]
	v_cvt_pk_fp8_f32 v211, v202, v203 op_sel:[0,0,1]
	s_nop 0
	global_store_dwordx4 v12, v[208:211], s[14:15]
	s_waitcnt vmcnt(26)
	v_mul_f32_e32 v68, 0x43000000, v68
	v_mul_f32_e32 v69, 0x43000000, v69
	v_mul_f32_e32 v70, 0x43000000, v70
	v_mul_f32_e32 v71, 0x43000000, v71
	ds_write_b128 v5, v[68:71]
	v_mul_f32_e32 v72, 0x43000000, v72
	v_mul_f32_e32 v73, 0x43000000, v73
	v_mul_f32_e32 v74, 0x43000000, v74
	v_mul_f32_e32 v75, 0x43000000, v75
	ds_write_b128 v5, v[72:75] offset:1024
	v_mul_f32_e32 v76, 0x43000000, v76
	v_mul_f32_e32 v77, 0x43000000, v77
	v_mul_f32_e32 v78, 0x43000000, v78
	v_mul_f32_e32 v79, 0x43000000, v79
	ds_write_b128 v5, v[76:79] offset:2048
	v_mul_f32_e32 v80, 0x43000000, v80
	v_mul_f32_e32 v81, 0x43000000, v81
	v_mul_f32_e32 v82, 0x43000000, v82
	v_mul_f32_e32 v83, 0x43000000, v83
	ds_write_b128 v5, v[80:83] offset:3072
	v_mul_f32_e32 v84, 0x43000000, v84
	v_mul_f32_e32 v85, 0x43000000, v85
	v_mul_f32_e32 v86, 0x43000000, v86
	v_mul_f32_e32 v87, 0x43000000, v87
	ds_write_b128 v5, v[84:87] offset:4096
	v_mul_f32_e32 v88, 0x43000000, v88
	v_mul_f32_e32 v89, 0x43000000, v89
	v_mul_f32_e32 v90, 0x43000000, v90
	v_mul_f32_e32 v91, 0x43000000, v91
	ds_write_b128 v5, v[88:91] offset:5120
	v_mul_f32_e32 v92, 0x43000000, v92
	v_mul_f32_e32 v93, 0x43000000, v93
	v_mul_f32_e32 v94, 0x43000000, v94
	v_mul_f32_e32 v95, 0x43000000, v95
	ds_write_b128 v5, v[92:95] offset:6144
	v_mul_f32_e32 v96, 0x43000000, v96
	v_mul_f32_e32 v97, 0x43000000, v97
	v_mul_f32_e32 v98, 0x43000000, v98
	v_mul_f32_e32 v99, 0x43000000, v99
	ds_write_b128 v5, v[96:99] offset:7168
	s_waitcnt lgkmcnt(0)
	s_barrier
	s_add_i32 s17, s16, 480
	s_min_u32 s17, s17, 0xfff
	s_lshr_b32 s18, s17, 5
	s_add_i32 s18, s18, 0
	s_and_b32 s19, s17, 31
	s_lshl_b32 s18, s18, 21
	s_lshl_b32 s19, s19, 9
	s_add_u32 s18, s18, s19
	s_add_u32 s12, s2, s18
	s_addc_u32 s13, s3, 0
	global_load_dwordx4 v[68:71], v10, s[12:13]
	s_add_u32 s12, s12, 0x8000
	s_addc_u32 s13, s13, 0
	global_load_dwordx4 v[72:75], v10, s[12:13]
	s_add_u32 s12, s12, 0x8000
	s_addc_u32 s13, s13, 0
	global_load_dwordx4 v[76:79], v10, s[12:13]
	s_add_u32 s12, s12, 0x8000
	s_addc_u32 s13, s13, 0
	global_load_dwordx4 v[80:83], v10, s[12:13]
	s_add_u32 s12, s12, 0x8000
	s_addc_u32 s13, s13, 0
	global_load_dwordx4 v[84:87], v10, s[12:13]
	s_add_u32 s12, s12, 0x8000
	s_addc_u32 s13, s13, 0
	global_load_dwordx4 v[88:91], v10, s[12:13]
	s_add_u32 s12, s12, 0x8000
	s_addc_u32 s13, s13, 0
	global_load_dwordx4 v[92:95], v10, s[12:13]
	s_add_u32 s12, s12, 0x8000
	s_addc_u32 s13, s13, 0
	global_load_dwordx4 v[96:99], v10, s[12:13]
	s_add_i32 s17, s16, 96
	s_min_u32 s17, s17, 0xfff
	s_lshr_b32 s18, s17, 5
	s_add_i32 s18, s18, 0
	s_and_b32 s19, s17, 31
	s_lshl_b32 s19, s19, 21
	s_lshl_b32 s18, s18, 7
	s_add_u32 s18, s18, s19
	s_add_u32 s14, s4, s18
	s_addc_u32 s15, s5, 0
	ds_read_b32 v170, v7
	ds_read_b32 v171, v7 offset:512
	ds_read_b32 v172, v7 offset:1024
	ds_read_b32 v173, v7 offset:1536
	ds_read_b32 v174, v7 offset:2048
	ds_read_b32 v175, v7 offset:2560
	ds_read_b32 v176, v7 offset:3072
	ds_read_b32 v177, v7 offset:3584
	ds_read_b32 v196, v7 offset:4096
	ds_read_b32 v197, v7 offset:4608
	ds_read_b32 v198, v7 offset:5120
	ds_read_b32 v199, v7 offset:5632
	ds_read_b32 v200, v7 offset:6144
	ds_read_b32 v201, v7 offset:6656
	ds_read_b32 v202, v7 offset:7168
	ds_read_b32 v203, v7 offset:7680
	s_waitcnt lgkmcnt(0)
; #define GAS __attribute__((address_space(1)))
; #define LAS __attribute__((address_space(3)))
; #define LDS_WAIT() asm volatile("s_waitcnt lgkmcnt(0)" ::: "memory")
; __device__ __forceinline__ unsigned pk4_fp8(float a, float b, float c, float d) {
;     a = fminf(fmaxf(a, -448.f), 448.f); b = fminf(fmaxf(b, -448.f), 448.f); c = fminf(fmaxf(c, -448.f), 448.f); d = fminf(fmaxf(d, -448.f), 448.f);
;     int w = __builtin_amdgcn_cvt_pk_fp8_f32(a, b, 0, false); w = __builtin_amdgcn_cvt_pk_fp8_f32(c, d, w, true); return (unsigned)w; }
;     const int pr = item >> 1, kb = 2 * (pr / nblk) + (item & 1), nb = pr % nblk, k0 = 64 * kb, n0 = 32 * nb;
;     const int nr = n0 + (lane & 31); const int sc = MAP == 1 ? src_col_in(nr) : nr;
;     float v[32];
; #pragma unroll
;     for (int i = 0; i < 32; ++i) v[i] = sc >= 0 ? W[(size_t)(k0 + 2 * i + (lane >> 5)) * Nsrc + sc] : 0.f;
; #pragma unroll
;     for (int i = 0; i < 32; ++i) { const int k = k0 + 2 * i + (lane >> 5); float x = v[i] * wscale; if (KS) x *= (k < ksplit ? ksA[k] : ksB[k - ksplit]); scr[(2 * i + (lane >> 5)) * 33 + (lane & 31)] = x; }
;     LDS_WAIT(); asm volatile("" ::: "memory");
;     const int c = lane & 7;
; #pragma unroll
;     for (int j = 0; j < 4; ++j) { const int n = (lane >> 3) + 8 * j; const LAS float* s = scr + (8 * c) * 33 + n;
;         const unsigned long long o = (unsigned long long)pg8::pk4_fp8(s[0 * 33], s[1 * 33], s[2 * 33], s[3 * 33]) | ((unsigned long long)pg8::pk4_fp8(s[4 * 33], s[5 * 33], s[6 * 33], s[7 * 33]) << 32);
;         *(GAS unsigned long long*)(WT + (size_t)(n0 + n) * K + k0 + 8 * c) = o; }
;     LDS_WAIT(); asm volatile("" ::: "memory");
	v_max_f32_e32 v170, v170, v170
	v_max_f32_e32 v171, v171, v171
	v_max_f32_e32 v172, v172, v172
	v_max_f32_e32 v173, v173, v173
	v_max_f32_e32 v174, v174, v174
	v_max_f32_e32 v175, v175, v175
	v_max_f32_e32 v176, v176, v176
	v_max_f32_e32 v177, v177, v177
	v_max_f32_e32 v196, v196, v196
	v_max_f32_e32 v197, v197, v197
	v_max_f32_e32 v198, v198, v198
	v_max_f32_e32 v199, v199, v199
	v_max_f32_e32 v200, v200, v200
	v_max_f32_e32 v201, v201, v201
	v_max_f32_e32 v202, v202, v202
	v_max_f32_e32 v203, v203, v203
	v_med3_f32 v170, v170, s20, v13
	v_med3_f32 v171, v171, s20, v13
	v_med3_f32 v172, v172, s20, v13
	v_med3_f32 v173, v173, s20, v13
	v_med3_f32 v174, v174, s20, v13
	v_med3_f32 v175, v175, s20, v13
	v_med3_f32 v176, v176, s20, v13
	v_med3_f32 v177, v177, s20, v13
	v_med3_f32 v196, v196, s20, v13
	v_med3_f32 v197, v197, s20, v13
	v_med3_f32 v198, v198, s20, v13
	v_med3_f32 v199, v199, s20, v13
	v_med3_f32 v200, v200, s20, v13
	v_med3_f32 v201, v201, s20, v13
	v_med3_f32 v202, v202, s20, v13
	v_med3_f32 v203, v203, s20, v13
	v_mov_b32_e32 v208, 0
	v_mov_b32_e32 v209, 0
	v_mov_b32_e32 v210, 0
	v_mov_b32_e32 v211, 0
	v_cvt_pk_fp8_f32 v208, v170, v171
	v_cvt_pk_fp8_f32 v209, v174, v175
	v_cvt_pk_fp8_f32 v210, v196, v197
	v_cvt_pk_fp8_f32 v211, v200, v201
	v_cvt_pk_fp8_f32 v208, v172, v173 op_sel:[0,0,1]
	v_cvt_pk_fp8_f32 v209, v176, v177 op_sel:[0,0,1]
	v_cvt_pk_fp8_f32 v210, v198, v199 op_sel:[0,0,1]
	v_cvt_pk_fp8_f32 v211, v202, v203 op_sel:[0,0,1]
	s_nop 0
	global_store_dwordx4 v11, v[208:211], s[14:15]
	ds_read_b32 v170, v9
	ds_read_b32 v171, v9 offset:512
	ds_read_b32 v172, v9 offset:1024
	ds_read_b32 v173, v9 offset:1536
	ds_read_b32 v174, v9 offset:2048
	ds_read_b32 v175, v9 offset:2560
	ds_read_b32 v176, v9 offset:3072
	ds_read_b32 v177, v9 offset:3584
	ds_read_b32 v196, v9 offset:4096
	ds_read_b32 v197, v9 offset:4608
	ds_read_b32 v198, v9 offset:5120
	ds_read_b32 v199, v9 offset:5632
	ds_read_b32 v200, v9 offset:6144
	ds_read_b32 v201, v9 offset:6656
	ds_read_b32 v202, v9 offset:7168
	ds_read_b32 v203, v9 offset:7680
	s_waitcnt lgkmcnt(0)
	v_max_f32_e32 v170, v170, v170
	v_max_f32_e32 v171, v171, v171
	v_max_f32_e32 v172, v172, v172
	v_max_f32_e32 v173, v173, v173
	v_max_f32_e32 v174, v174, v174
	v_max_f32_e32 v175, v175, v175
	v_max_f32_e32 v176, v176, v176
	v_max_f32_e32 v177, v177, v177
	v_max_f32_e32 v196, v196, v196
	v_max_f32_e32 v197, v197, v197
	v_max_f32_e32 v198, v198, v198
	v_max_f32_e32 v199, v199, v199
	v_max_f32_e32 v200, v200, v200
	v_max_f32_e32 v201, v201, v201
	v_max_f32_e32 v202, v202, v202
	v_max_f32_e32 v203, v203, v203
	v_med3_f32 v170, v170, s20, v13
	v_med3_f32 v171, v171, s20, v13
	v_med3_f32 v172, v172, s20, v13
	v_med3_f32 v173, v173, s20, v13
	v_med3_f32 v174, v174, s20, v13
	v_med3_f32 v175, v175, s20, v13
	v_med3_f32 v176, v176, s20, v13
	v_med3_f32 v177, v177, s20, v13
	v_med3_f32 v196, v196, s20, v13
	v_med3_f32 v197, v197, s20, v13
	v_med3_f32 v198, v198, s20, v13
	v_med3_f32 v199, v199, s20, v13
	v_med3_f32 v200, v200, s20, v13
	v_med3_f32 v201, v201, s20, v13
	v_med3_f32 v202, v202, s20, v13
	v_med3_f32 v203, v203, s20, v13
	v_mov_b32_e32 v208, 0
	v_mov_b32_e32 v209, 0
	v_mov_b32_e32 v210, 0
	v_mov_b32_e32 v211, 0
	v_cvt_pk_fp8_f32 v208, v170, v171
	v_cvt_pk_fp8_f32 v209, v174, v175
	v_cvt_pk_fp8_f32 v210, v196, v197
	v_cvt_pk_fp8_f32 v211, v200, v201
	v_cvt_pk_fp8_f32 v208, v172, v173 op_sel:[0,0,1]
	v_cvt_pk_fp8_f32 v209, v176, v177 op_sel:[0,0,1]
	v_cvt_pk_fp8_f32 v210, v198, v199 op_sel:[0,0,1]
	v_cvt_pk_fp8_f32 v211, v202, v203 op_sel:[0,0,1]
	s_nop 0
	global_store_dwordx4 v12, v[208:211], s[14:15]
	s_waitcnt vmcnt(28)
	v_mul_f32_e32 v100, 0x43000000, v100
	v_mul_f32_e32 v101, 0x43000000, v101
	v_mul_f32_e32 v102, 0x43000000, v102
	v_mul_f32_e32 v103, 0x43000000, v103
	ds_write_b128 v4, v[100:103]
	v_mul_f32_e32 v104, 0x43000000, v104
	v_mul_f32_e32 v105, 0x43000000, v105
	v_mul_f32_e32 v106, 0x43000000, v106
	v_mul_f32_e32 v107, 0x43000000, v107
	ds_write_b128 v4, v[104:107] offset:1024
	v_mul_f32_e32 v108, 0x43000000, v108
	v_mul_f32_e32 v109, 0x43000000, v109
	v_mul_f32_e32 v110, 0x43000000, v110
	v_mul_f32_e32 v111, 0x43000000, v111
	ds_write_b128 v4, v[108:111] offset:2048
	v_mul_f32_e32 v112, 0x43000000, v112
	v_mul_f32_e32 v113, 0x43000000, v113
	v_mul_f32_e32 v114, 0x43000000, v114
	v_mul_f32_e32 v115, 0x43000000, v115
	ds_write_b128 v4, v[112:115] offset:3072
	v_mul_f32_e32 v116, 0x43000000, v116
	v_mul_f32_e32 v117, 0x43000000, v117
	v_mul_f32_e32 v118, 0x43000000, v118
	v_mul_f32_e32 v119, 0x43000000, v119
	ds_write_b128 v4, v[116:119] offset:4096
	v_mul_f32_e32 v120, 0x43000000, v120
	v_mul_f32_e32 v121, 0x43000000, v121
	v_mul_f32_e32 v122, 0x43000000, v122
	v_mul_f32_e32 v123, 0x43000000, v123
	ds_write_b128 v4, v[120:123] offset:5120
	v_mul_f32_e32 v124, 0x43000000, v124
	v_mul_f32_e32 v125, 0x43000000, v125
	v_mul_f32_e32 v126, 0x43000000, v126
	v_mul_f32_e32 v127, 0x43000000, v127
	ds_write_b128 v4, v[124:127] offset:6144
	v_mul_f32_e32 v128, 0x43000000, v128
	v_mul_f32_e32 v129, 0x43000000, v129
	v_mul_f32_e32 v130, 0x43000000, v130
	v_mul_f32_e32 v131, 0x43000000, v131
	ds_write_b128 v4, v[128:131] offset:7168
	s_waitcnt lgkmcnt(0)
	s_barrier
; #define GAS __attribute__((address_space(1)))
; #define LAS __attribute__((address_space(3)))
; #define LDS_WAIT() asm volatile("s_waitcnt lgkmcnt(0)" ::: "memory")
; __device__ __forceinline__ unsigned pk4_fp8(float a, float b, float c, float d) {
;     a = fminf(fmaxf(a, -448.f), 448.f); b = fminf(fmaxf(b, -448.f), 448.f); c = fminf(fmaxf(c, -448.f), 448.f); d = fminf(fmaxf(d, -448.f), 448.f);
;     int w = __builtin_amdgcn_cvt_pk_fp8_f32(a, b, 0, false); w = __builtin_amdgcn_cvt_pk_fp8_f32(c, d, w, true); return (unsigned)w; }
;     const int pr = item >> 1, kb = 2 * (pr / nblk) + (item & 1), nb = pr % nblk, k0 = 64 * kb, n0 = 32 * nb;
;     const int nr = n0 + (lane & 31); const int sc = MAP == 1 ? src_col_in(nr) : nr;
;     float v[32];
; #pragma unroll
;     for (int i = 0; i < 32; ++i) v[i] = sc >= 0 ? W[(size_t)(k0 + 2 * i + (lane >> 5)) * Nsrc + sc] : 0.f;
; #pragma unroll
;     for (int i = 0; i < 32; ++i) { const int k = k0 + 2 * i + (lane >> 5); float x = v[i] * wscale; if (KS) x *= (k < ksplit ? ksA[k] : ksB[k - ksplit]); scr[(2 * i + (lane >> 5)) * 33 + (lane & 31)] = x; }
;     LDS_WAIT(); asm volatile("" ::: "memory");
;     const int c = lane & 7;
; #pragma unroll
;     for (int j = 0; j < 4; ++j) { const int n = (lane >> 3) + 8 * j; const LAS float* s = scr + (8 * c) * 33 + n;
;         const unsigned long long o = (unsigned long long)pg8::pk4_fp8(s[0 * 33], s[1 * 33], s[2 * 33], s[3 * 33]) | ((unsigned long long)pg8::pk4_fp8(s[4 * 33], s[5 * 33], s[6 * 33], s[7 * 33]) << 32);
;         *(GAS unsigned long long*)(WT + (size_t)(n0 + n) * K + k0 + 8 * c) = o; }
;     LDS_WAIT(); asm volatile("" ::: "memory");
	s_add_i32 s17, s16, 576
	s_min_u32 s17, s17, 0xfff
	s_lshr_b32 s18, s17, 5
	s_add_i32 s18, s18, 0
	s_and_b32 s19, s17, 31
	s_lshl_b32 s18, s18, 21
	s_lshl_b32 s19, s19, 9
	s_add_u32 s18, s18, s19
	s_add_u32 s12, s2, s18
	s_addc_u32 s13, s3, 0
	global_load_dwordx4 v[100:103], v10, s[12:13]
	s_add_u32 s12, s12, 0x8000
	s_addc_u32 s13, s13, 0
	global_load_dwordx4 v[104:107], v10, s[12:13]
	s_add_u32 s12, s12, 0x8000
	s_addc_u32 s13, s13, 0
	global_load_dwordx4 v[108:111], v10, s[12:13]
	s_add_u32 s12, s12, 0x8000
	s_addc_u32 s13, s13, 0
	global_load_dwordx4 v[112:115], v10, s[12:13]
	s_add_u32 s12, s12, 0x8000
	s_addc_u32 s13, s13, 0
	global_load_dwordx4 v[116:119], v10, s[12:13]
	s_add_u32 s12, s12, 0x8000
	s_addc_u32 s13, s13, 0
	global_load_dwordx4 v[120:123], v10, s[12:13]
	s_add_u32 s12, s12, 0x8000
	s_addc_u32 s13, s13, 0
	global_load_dwordx4 v[124:127], v10, s[12:13]
	s_add_u32 s12, s12, 0x8000
	s_addc_u32 s13, s13, 0
	global_load_dwordx4 v[128:131], v10, s[12:13]
	s_add_i32 s17, s16, 192
	s_min_u32 s17, s17, 0xfff
	s_lshr_b32 s18, s17, 5
	s_add_i32 s18, s18, 0
	s_and_b32 s19, s17, 31
	s_lshl_b32 s19, s19, 21
	s_lshl_b32 s18, s18, 7
	s_add_u32 s18, s18, s19
	s_add_u32 s14, s4, s18
	s_addc_u32 s15, s5, 0
	ds_read_b32 v170, v6
	ds_read_b32 v171, v6 offset:512
	ds_read_b32 v172, v6 offset:1024
	ds_read_b32 v173, v6 offset:1536
	ds_read_b32 v174, v6 offset:2048
	ds_read_b32 v175, v6 offset:2560
	ds_read_b32 v176, v6 offset:3072
	ds_read_b32 v177, v6 offset:3584
	ds_read_b32 v196, v6 offset:4096
	ds_read_b32 v197, v6 offset:4608
	ds_read_b32 v198, v6 offset:5120
	ds_read_b32 v199, v6 offset:5632
	ds_read_b32 v200, v6 offset:6144
	ds_read_b32 v201, v6 offset:6656
	ds_read_b32 v202, v6 offset:7168
	ds_read_b32 v203, v6 offset:7680
	s_waitcnt lgkmcnt(0)
	v_max_f32_e32 v170, v170, v170
	v_max_f32_e32 v171, v171, v171
	v_max_f32_e32 v172, v172, v172
	v_max_f32_e32 v173, v173, v173
	v_max_f32_e32 v174, v174, v174
	v_max_f32_e32 v175, v175, v175
	v_max_f32_e32 v176, v176, v176
	v_max_f32_e32 v177, v177, v177
	v_max_f32_e32 v196, v196, v196
	v_max_f32_e32 v197, v197, v197
	v_max_f32_e32 v198, v198, v198
	v_max_f32_e32 v199, v199, v199
	v_max_f32_e32 v200, v200, v200
	v_max_f32_e32 v201, v201, v201
	v_max_f32_e32 v202, v202, v202
	v_max_f32_e32 v203, v203, v203
	v_med3_f32 v170, v170, s20, v13
	v_med3_f32 v171, v171, s20, v13
	v_med3_f32 v172, v172, s20, v13
	v_med3_f32 v173, v173, s20, v13
	v_med3_f32 v174, v174, s20, v13
	v_med3_f32 v175, v175, s20, v13
	v_med3_f32 v176, v176, s20, v13
	v_med3_f32 v177, v177, s20, v13
	v_med3_f32 v196, v196, s20, v13
	v_med3_f32 v197, v197, s20, v13
	v_med3_f32 v198, v198, s20, v13
	v_med3_f32 v199, v199, s20, v13
	v_med3_f32 v200, v200, s20, v13
	v_med3_f32 v201, v201, s20, v13
	v_med3_f32 v202, v202, s20, v13
	v_med3_f32 v203, v203, s20, v13
	v_mov_b32_e32 v208, 0
	v_mov_b32_e32 v209, 0
	v_mov_b32_e32 v210, 0
	v_mov_b32_e32 v211, 0
	v_cvt_pk_fp8_f32 v208, v170, v171
	v_cvt_pk_fp8_f32 v209, v174, v175
	v_cvt_pk_fp8_f32 v210, v196, v197
	v_cvt_pk_fp8_f32 v211, v200, v201
	v_cvt_pk_fp8_f32 v208, v172, v173 op_sel:[0,0,1]
	v_cvt_pk_fp8_f32 v209, v176, v177 op_sel:[0,0,1]
	v_cvt_pk_fp8_f32 v210, v198, v199 op_sel:[0,0,1]
	v_cvt_pk_fp8_f32 v211, v202, v203 op_sel:[0,0,1]
	s_nop 0
	global_store_dwordx4 v11, v[208:211], s[14:15]
	ds_read_b32 v170, v8
	ds_read_b32 v171, v8 offset:512
	ds_read_b32 v172, v8 offset:1024
	ds_read_b32 v173, v8 offset:1536
	ds_read_b32 v174, v8 offset:2048
	ds_read_b32 v175, v8 offset:2560
	ds_read_b32 v176, v8 offset:3072
	ds_read_b32 v177, v8 offset:3584
	ds_read_b32 v196, v8 offset:4096
	ds_read_b32 v197, v8 offset:4608
	ds_read_b32 v198, v8 offset:5120
	ds_read_b32 v199, v8 offset:5632
	ds_read_b32 v200, v8 offset:6144
	ds_read_b32 v201, v8 offset:6656
	ds_read_b32 v202, v8 offset:7168
	ds_read_b32 v203, v8 offset:7680
	s_waitcnt lgkmcnt(0)
	v_max_f32_e32 v170, v170, v170
	v_max_f32_e32 v171, v171, v171
	v_max_f32_e32 v172, v172, v172
	v_max_f32_e32 v173, v173, v173
	v_max_f32_e32 v174, v174, v174
	v_max_f32_e32 v175, v175, v175
	v_max_f32_e32 v176, v176, v176
	v_max_f32_e32 v177, v177, v177
	v_max_f32_e32 v196, v196, v196
	v_max_f32_e32 v197, v197, v197
	v_max_f32_e32 v198, v198, v198
	v_max_f32_e32 v199, v199, v199
	v_max_f32_e32 v200, v200, v200
	v_max_f32_e32 v201, v201, v201
	v_max_f32_e32 v202, v202, v202
	v_max_f32_e32 v203, v203, v203
	v_med3_f32 v170, v170, s20, v13
	v_med3_f32 v171, v171, s20, v13
	v_med3_f32 v172, v172, s20, v13
	v_med3_f32 v173, v173, s20, v13
	v_med3_f32 v174, v174, s20, v13
	v_med3_f32 v175, v175, s20, v13
	v_med3_f32 v176, v176, s20, v13
	v_med3_f32 v177, v177, s20, v13
	v_med3_f32 v196, v196, s20, v13
	v_med3_f32 v197, v197, s20, v13
	v_med3_f32 v198, v198, s20, v13
	v_med3_f32 v199, v199, s20, v13
	v_med3_f32 v200, v200, s20, v13
	v_med3_f32 v201, v201, s20, v13
	v_med3_f32 v202, v202, s20, v13
	v_med3_f32 v203, v203, s20, v13
	v_mov_b32_e32 v208, 0
	v_mov_b32_e32 v209, 0
	v_mov_b32_e32 v210, 0
	v_mov_b32_e32 v211, 0
	v_cvt_pk_fp8_f32 v208, v170, v171
	v_cvt_pk_fp8_f32 v209, v174, v175
	v_cvt_pk_fp8_f32 v210, v196, v197
	v_cvt_pk_fp8_f32 v211, v200, v201
	v_cvt_pk_fp8_f32 v208, v172, v173 op_sel:[0,0,1]
	v_cvt_pk_fp8_f32 v209, v176, v177 op_sel:[0,0,1]
	v_cvt_pk_fp8_f32 v210, v198, v199 op_sel:[0,0,1]
	v_cvt_pk_fp8_f32 v211, v202, v203 op_sel:[0,0,1]
	s_nop 0
	global_store_dwordx4 v12, v[208:211], s[14:15]
	s_waitcnt vmcnt(30)
	v_mul_f32_e32 v132, 0x43000000, v132
	v_mul_f32_e32 v133, 0x43000000, v133
	v_mul_f32_e32 v134, 0x43000000, v134
	v_mul_f32_e32 v135, 0x43000000, v135
	ds_write_b128 v5, v[132:135]
	v_mul_f32_e32 v136, 0x43000000, v136
	v_mul_f32_e32 v137, 0x43000000, v137
	v_mul_f32_e32 v138, 0x43000000, v138
	v_mul_f32_e32 v139, 0x43000000, v139
	ds_write_b128 v5, v[136:139] offset:1024
	v_mul_f32_e32 v140, 0x43000000, v140
	v_mul_f32_e32 v141, 0x43000000, v141
	v_mul_f32_e32 v142, 0x43000000, v142
	v_mul_f32_e32 v143, 0x43000000, v143
	ds_write_b128 v5, v[140:143] offset:2048
	v_mul_f32_e32 v144, 0x43000000, v144
	v_mul_f32_e32 v145, 0x43000000, v145
	v_mul_f32_e32 v146, 0x43000000, v146
	v_mul_f32_e32 v147, 0x43000000, v147
	ds_write_b128 v5, v[144:147] offset:3072
	v_mul_f32_e32 v148, 0x43000000, v148
	v_mul_f32_e32 v149, 0x43000000, v149
	v_mul_f32_e32 v150, 0x43000000, v150
	v_mul_f32_e32 v151, 0x43000000, v151
	ds_write_b128 v5, v[148:151] offset:4096
	v_mul_f32_e32 v152, 0x43000000, v152
	v_mul_f32_e32 v153, 0x43000000, v153
	v_mul_f32_e32 v154, 0x43000000, v154
	v_mul_f32_e32 v155, 0x43000000, v155
	ds_write_b128 v5, v[152:155] offset:5120
	v_mul_f32_e32 v156, 0x43000000, v156
	v_mul_f32_e32 v157, 0x43000000, v157
	v_mul_f32_e32 v158, 0x43000000, v158
	v_mul_f32_e32 v159, 0x43000000, v159
	ds_write_b128 v5, v[156:159] offset:6144
	v_mul_f32_e32 v160, 0x43000000, v160
	v_mul_f32_e32 v161, 0x43000000, v161
	v_mul_f32_e32 v162, 0x43000000, v162
	v_mul_f32_e32 v163, 0x43000000, v163
	ds_write_b128 v5, v[160:163] offset:7168
	s_waitcnt lgkmcnt(0)
	s_barrier
; #define GAS __attribute__((address_space(1)))
; #define LAS __attribute__((address_space(3)))
; #define LDS_WAIT() asm volatile("s_waitcnt lgkmcnt(0)" ::: "memory")
; __device__ __forceinline__ unsigned pk4_fp8(float a, float b, float c, float d) {
;     a = fminf(fmaxf(a, -448.f), 448.f); b = fminf(fmaxf(b, -448.f), 448.f); c = fminf(fmaxf(c, -448.f), 448.f); d = fminf(fmaxf(d, -448.f), 448.f);
;     int w = __builtin_amdgcn_cvt_pk_fp8_f32(a, b, 0, false); w = __builtin_amdgcn_cvt_pk_fp8_f32(c, d, w, true); return (unsigned)w; }
;     const int pr = item >> 1, kb = 2 * (pr / nblk) + (item & 1), nb = pr % nblk, k0 = 64 * kb, n0 = 32 * nb;
;     const int nr = n0 + (lane & 31); const int sc = MAP == 1 ? src_col_in(nr) : nr;
;     float v[32];
; #pragma unroll
;     for (int i = 0; i < 32; ++i) v[i] = sc >= 0 ? W[(size_t)(k0 + 2 * i + (lane >> 5)) * Nsrc + sc] : 0.f;
; #pragma unroll
;     for (int i = 0; i < 32; ++i) { const int k = k0 + 2 * i + (lane >> 5); float x = v[i] * wscale; if (KS) x *= (k < ksplit ? ksA[k] : ksB[k - ksplit]); scr[(2 * i + (lane >> 5)) * 33 + (lane & 31)] = x; }
;     LDS_WAIT(); asm volatile("" ::: "memory");
;     const int c = lane & 7;
; #pragma unroll
;     for (int j = 0; j < 4; ++j) { const int n = (lane >> 3) + 8 * j; const LAS float* s = scr + (8 * c) * 33 + n;
;         const unsigned long long o = (unsigned long long)pg8::pk4_fp8(s[0 * 33], s[1 * 33], s[2 * 33], s[3 * 33]) | ((unsigned long long)pg8::pk4_fp8(s[4 * 33], s[5 * 33], s[6 * 33], s[7 * 33]) << 32);
;         *(GAS unsigned long long*)(WT + (size_t)(n0 + n) * K + k0 + 8 * c) = o; }
;     LDS_WAIT(); asm volatile("" ::: "memory");
	s_add_i32 s17, s16, 672
	s_min_u32 s17, s17, 0xfff
	s_lshr_b32 s18, s17, 5
	s_add_i32 s18, s18, 0
	s_and_b32 s19, s17, 31
	s_lshl_b32 s18, s18, 21
	s_lshl_b32 s19, s19, 9
	s_add_u32 s18, s18, s19
	s_add_u32 s12, s2, s18
	s_addc_u32 s13, s3, 0
	global_load_dwordx4 v[132:135], v10, s[12:13]
	s_add_u32 s12, s12, 0x8000
	s_addc_u32 s13, s13, 0
	global_load_dwordx4 v[136:139], v10, s[12:13]
	s_add_u32 s12, s12, 0x8000
	s_addc_u32 s13, s13, 0
	global_load_dwordx4 v[140:143], v10, s[12:13]
	s_add_u32 s12, s12, 0x8000
	s_addc_u32 s13, s13, 0
	global_load_dwordx4 v[144:147], v10, s[12:13]
	s_add_u32 s12, s12, 0x8000
	s_addc_u32 s13, s13, 0
	global_load_dwordx4 v[148:151], v10, s[12:13]
	s_add_u32 s12, s12, 0x8000
	s_addc_u32 s13, s13, 0
	global_load_dwordx4 v[152:155], v10, s[12:13]
	s_add_u32 s12, s12, 0x8000
	s_addc_u32 s13, s13, 0
	global_load_dwordx4 v[156:159], v10, s[12:13]
	s_add_u32 s12, s12, 0x8000
	s_addc_u32 s13, s13, 0
	global_load_dwordx4 v[160:163], v10, s[12:13]
	s_add_i32 s17, s16, 288
	s_min_u32 s17, s17, 0xfff
	s_lshr_b32 s18, s17, 5
	s_add_i32 s18, s18, 0
	s_and_b32 s19, s17, 31
	s_lshl_b32 s19, s19, 21
	s_lshl_b32 s18, s18, 7
	s_add_u32 s18, s18, s19
	s_add_u32 s14, s4, s18
	s_addc_u32 s15, s5, 0
	ds_read_b32 v170, v7
	ds_read_b32 v171, v7 offset:512
	ds_read_b32 v172, v7 offset:1024
	ds_read_b32 v173, v7 offset:1536
	ds_read_b32 v174, v7 offset:2048
	ds_read_b32 v175, v7 offset:2560
	ds_read_b32 v176, v7 offset:3072
	ds_read_b32 v177, v7 offset:3584
	ds_read_b32 v196, v7 offset:4096
	ds_read_b32 v197, v7 offset:4608
	ds_read_b32 v198, v7 offset:5120
	ds_read_b32 v199, v7 offset:5632
	ds_read_b32 v200, v7 offset:6144
	ds_read_b32 v201, v7 offset:6656
	ds_read_b32 v202, v7 offset:7168
	ds_read_b32 v203, v7 offset:7680
	s_waitcnt lgkmcnt(0)
	v_max_f32_e32 v170, v170, v170
	v_max_f32_e32 v171, v171, v171
	v_max_f32_e32 v172, v172, v172
	v_max_f32_e32 v173, v173, v173
	v_max_f32_e32 v174, v174, v174
	v_max_f32_e32 v175, v175, v175
	v_max_f32_e32 v176, v176, v176
	v_max_f32_e32 v177, v177, v177
	v_max_f32_e32 v196, v196, v196
	v_max_f32_e32 v197, v197, v197
	v_max_f32_e32 v198, v198, v198
	v_max_f32_e32 v199, v199, v199
	v_max_f32_e32 v200, v200, v200
	v_max_f32_e32 v201, v201, v201
	v_max_f32_e32 v202, v202, v202
	v_max_f32_e32 v203, v203, v203
	v_med3_f32 v170, v170, s20, v13
	v_med3_f32 v171, v171, s20, v13
	v_med3_f32 v172, v172, s20, v13
	v_med3_f32 v173, v173, s20, v13
	v_med3_f32 v174, v174, s20, v13
	v_med3_f32 v175, v175, s20, v13
	v_med3_f32 v176, v176, s20, v13
	v_med3_f32 v177, v177, s20, v13
	v_med3_f32 v196, v196, s20, v13
	v_med3_f32 v197, v197, s20, v13
	v_med3_f32 v198, v198, s20, v13
	v_med3_f32 v199, v199, s20, v13
	v_med3_f32 v200, v200, s20, v13
	v_med3_f32 v201, v201, s20, v13
	v_med3_f32 v202, v202, s20, v13
	v_med3_f32 v203, v203, s20, v13
	v_mov_b32_e32 v208, 0
	v_mov_b32_e32 v209, 0
	v_mov_b32_e32 v210, 0
	v_mov_b32_e32 v211, 0
	v_cvt_pk_fp8_f32 v208, v170, v171
	v_cvt_pk_fp8_f32 v209, v174, v175
	v_cvt_pk_fp8_f32 v210, v196, v197
	v_cvt_pk_fp8_f32 v211, v200, v201
	v_cvt_pk_fp8_f32 v208, v172, v173 op_sel:[0,0,1]
	v_cvt_pk_fp8_f32 v209, v176, v177 op_sel:[0,0,1]
	v_cvt_pk_fp8_f32 v210, v198, v199 op_sel:[0,0,1]
	v_cvt_pk_fp8_f32 v211, v202, v203 op_sel:[0,0,1]
	s_nop 0
	global_store_dwordx4 v11, v[208:211], s[14:15]
	ds_read_b32 v170, v9
	ds_read_b32 v171, v9 offset:512
	ds_read_b32 v172, v9 offset:1024
	ds_read_b32 v173, v9 offset:1536
	ds_read_b32 v174, v9 offset:2048
	ds_read_b32 v175, v9 offset:2560
	ds_read_b32 v176, v9 offset:3072
	ds_read_b32 v177, v9 offset:3584
	ds_read_b32 v196, v9 offset:4096
	ds_read_b32 v197, v9 offset:4608
	ds_read_b32 v198, v9 offset:5120
	ds_read_b32 v199, v9 offset:5632
	ds_read_b32 v200, v9 offset:6144
	ds_read_b32 v201, v9 offset:6656
	ds_read_b32 v202, v9 offset:7168
	ds_read_b32 v203, v9 offset:7680
	s_waitcnt lgkmcnt(0)
	v_max_f32_e32 v170, v170, v170
	v_max_f32_e32 v171, v171, v171
	v_max_f32_e32 v172, v172, v172
	v_max_f32_e32 v173, v173, v173
	v_max_f32_e32 v174, v174, v174
	v_max_f32_e32 v175, v175, v175
	v_max_f32_e32 v176, v176, v176
	v_max_f32_e32 v177, v177, v177
	v_max_f32_e32 v196, v196, v196
	v_max_f32_e32 v197, v197, v197
	v_max_f32_e32 v198, v198, v198
	v_max_f32_e32 v199, v199, v199
	v_max_f32_e32 v200, v200, v200
	v_max_f32_e32 v201, v201, v201
	v_max_f32_e32 v202, v202, v202
	v_max_f32_e32 v203, v203, v203
	v_med3_f32 v170, v170, s20, v13
	v_med3_f32 v171, v171, s20, v13
	v_med3_f32 v172, v172, s20, v13
	v_med3_f32 v173, v173, s20, v13
	v_med3_f32 v174, v174, s20, v13
	v_med3_f32 v175, v175, s20, v13
	v_med3_f32 v176, v176, s20, v13
	v_med3_f32 v177, v177, s20, v13
	v_med3_f32 v196, v196, s20, v13
	v_med3_f32 v197, v197, s20, v13
	v_med3_f32 v198, v198, s20, v13
	v_med3_f32 v199, v199, s20, v13
	v_med3_f32 v200, v200, s20, v13
	v_med3_f32 v201, v201, s20, v13
	v_med3_f32 v202, v202, s20, v13
	v_med3_f32 v203, v203, s20, v13
	v_mov_b32_e32 v208, 0
	v_mov_b32_e32 v209, 0
	v_mov_b32_e32 v210, 0
	v_mov_b32_e32 v211, 0
	v_cvt_pk_fp8_f32 v208, v170, v171
	v_cvt_pk_fp8_f32 v209, v174, v175
	v_cvt_pk_fp8_f32 v210, v196, v197
	v_cvt_pk_fp8_f32 v211, v200, v201
	v_cvt_pk_fp8_f32 v208, v172, v173 op_sel:[0,0,1]
	v_cvt_pk_fp8_f32 v209, v176, v177 op_sel:[0,0,1]
	v_cvt_pk_fp8_f32 v210, v198, v199 op_sel:[0,0,1]
	v_cvt_pk_fp8_f32 v211, v202, v203 op_sel:[0,0,1]
	s_nop 0
	global_store_dwordx4 v12, v[208:211], s[14:15]
	s_waitcnt vmcnt(32)
	v_mul_f32_e32 v36, 0x43000000, v36
	v_mul_f32_e32 v37, 0x43000000, v37
	v_mul_f32_e32 v38, 0x43000000, v38
	v_mul_f32_e32 v39, 0x43000000, v39
	ds_write_b128 v4, v[36:39]
	v_mul_f32_e32 v40, 0x43000000, v40
	v_mul_f32_e32 v41, 0x43000000, v41
	v_mul_f32_e32 v42, 0x43000000, v42
	v_mul_f32_e32 v43, 0x43000000, v43
	ds_write_b128 v4, v[40:43] offset:1024
	v_mul_f32_e32 v44, 0x43000000, v44
	v_mul_f32_e32 v45, 0x43000000, v45
	v_mul_f32_e32 v46, 0x43000000, v46
	v_mul_f32_e32 v47, 0x43000000, v47
	ds_write_b128 v4, v[44:47] offset:2048
	v_mul_f32_e32 v48, 0x43000000, v48
	v_mul_f32_e32 v49, 0x43000000, v49
	v_mul_f32_e32 v50, 0x43000000, v50
	v_mul_f32_e32 v51, 0x43000000, v51
	ds_write_b128 v4, v[48:51] offset:3072
	v_mul_f32_e32 v52, 0x43000000, v52
	v_mul_f32_e32 v53, 0x43000000, v53
	v_mul_f32_e32 v54, 0x43000000, v54
	v_mul_f32_e32 v55, 0x43000000, v55
	ds_write_b128 v4, v[52:55] offset:4096
	v_mul_f32_e32 v56, 0x43000000, v56
	v_mul_f32_e32 v57, 0x43000000, v57
	v_mul_f32_e32 v58, 0x43000000, v58
	v_mul_f32_e32 v59, 0x43000000, v59
	ds_write_b128 v4, v[56:59] offset:5120
	v_mul_f32_e32 v60, 0x43000000, v60
	v_mul_f32_e32 v61, 0x43000000, v61
	v_mul_f32_e32 v62, 0x43000000, v62
	v_mul_f32_e32 v63, 0x43000000, v63
	ds_write_b128 v4, v[60:63] offset:6144
	v_mul_f32_e32 v64, 0x43000000, v64
	v_mul_f32_e32 v65, 0x43000000, v65
	v_mul_f32_e32 v66, 0x43000000, v66
	v_mul_f32_e32 v67, 0x43000000, v67
	ds_write_b128 v4, v[64:67] offset:7168
	s_waitcnt lgkmcnt(0)
	s_barrier
; #define GAS __attribute__((address_space(1)))
; #define LAS __attribute__((address_space(3)))
; #define LDS_WAIT() asm volatile("s_waitcnt lgkmcnt(0)" ::: "memory")
; __device__ __forceinline__ unsigned pk4_fp8(float a, float b, float c, float d) {
;     a = fminf(fmaxf(a, -448.f), 448.f); b = fminf(fmaxf(b, -448.f), 448.f); c = fminf(fmaxf(c, -448.f), 448.f); d = fminf(fmaxf(d, -448.f), 448.f);
;     int w = __builtin_amdgcn_cvt_pk_fp8_f32(a, b, 0, false); w = __builtin_amdgcn_cvt_pk_fp8_f32(c, d, w, true); return (unsigned)w; }
;     const int pr = item >> 1, kb = 2 * (pr / nblk) + (item & 1), nb = pr % nblk, k0 = 64 * kb, n0 = 32 * nb;
;     const int nr = n0 + (lane & 31); const int sc = MAP == 1 ? src_col_in(nr) : nr;
;     float v[32];
; #pragma unroll
;     for (int i = 0; i < 32; ++i) v[i] = sc >= 0 ? W[(size_t)(k0 + 2 * i + (lane >> 5)) * Nsrc + sc] : 0.f;
; #pragma unroll
;     for (int i = 0; i < 32; ++i) { const int k = k0 + 2 * i + (lane >> 5); float x = v[i] * wscale; if (KS) x *= (k < ksplit ? ksA[k] : ksB[k - ksplit]); scr[(2 * i + (lane >> 5)) * 33 + (lane & 31)] = x; }
;     LDS_WAIT(); asm volatile("" ::: "memory");
;     const int c = lane & 7;
; #pragma unroll
;     for (int j = 0; j < 4; ++j) { const int n = (lane >> 3) + 8 * j; const LAS float* s = scr + (8 * c) * 33 + n;
;         const unsigned long long o = (unsigned long long)pg8::pk4_fp8(s[0 * 33], s[1 * 33], s[2 * 33], s[3 * 33]) | ((unsigned long long)pg8::pk4_fp8(s[4 * 33], s[5 * 33], s[6 * 33], s[7 * 33]) << 32);
;         *(GAS unsigned long long*)(WT + (size_t)(n0 + n) * K + k0 + 8 * c) = o; }
;     LDS_WAIT(); asm volatile("" ::: "memory");
	s_add_i32 s17, s16, 768
	s_min_u32 s17, s17, 0xfff
	s_lshr_b32 s18, s17, 5
	s_add_i32 s18, s18, 0
	s_and_b32 s19, s17, 31
	s_lshl_b32 s18, s18, 21
	s_lshl_b32 s19, s19, 9
	s_add_u32 s18, s18, s19
	s_add_u32 s12, s2, s18
	s_addc_u32 s13, s3, 0
	global_load_dwordx4 v[36:39], v10, s[12:13]
	s_add_u32 s12, s12, 0x8000
	s_addc_u32 s13, s13, 0
	global_load_dwordx4 v[40:43], v10, s[12:13]
	s_add_u32 s12, s12, 0x8000
	s_addc_u32 s13, s13, 0
	global_load_dwordx4 v[44:47], v10, s[12:13]
	s_add_u32 s12, s12, 0x8000
	s_addc_u32 s13, s13, 0
	global_load_dwordx4 v[48:51], v10, s[12:13]
	s_add_u32 s12, s12, 0x8000
	s_addc_u32 s13, s13, 0
	global_load_dwordx4 v[52:55], v10, s[12:13]
	s_add_u32 s12, s12, 0x8000
	s_addc_u32 s13, s13, 0
	global_load_dwordx4 v[56:59], v10, s[12:13]
	s_add_u32 s12, s12, 0x8000
	s_addc_u32 s13, s13, 0
	global_load_dwordx4 v[60:63], v10, s[12:13]
	s_add_u32 s12, s12, 0x8000
	s_addc_u32 s13, s13, 0
	global_load_dwordx4 v[64:67], v10, s[12:13]
	s_add_i32 s17, s16, 384
	s_min_u32 s17, s17, 0xfff
	s_lshr_b32 s18, s17, 5
	s_add_i32 s18, s18, 0
	s_and_b32 s19, s17, 31
	s_lshl_b32 s19, s19, 21
	s_lshl_b32 s18, s18, 7
	s_add_u32 s18, s18, s19
	s_add_u32 s14, s4, s18
	s_addc_u32 s15, s5, 0
	ds_read_b32 v170, v6
	ds_read_b32 v171, v6 offset:512
	ds_read_b32 v172, v6 offset:1024
	ds_read_b32 v173, v6 offset:1536
	ds_read_b32 v174, v6 offset:2048
	ds_read_b32 v175, v6 offset:2560
	ds_read_b32 v176, v6 offset:3072
	ds_read_b32 v177, v6 offset:3584
	ds_read_b32 v196, v6 offset:4096
	ds_read_b32 v197, v6 offset:4608
	ds_read_b32 v198, v6 offset:5120
	ds_read_b32 v199, v6 offset:5632
	ds_read_b32 v200, v6 offset:6144
	ds_read_b32 v201, v6 offset:6656
	ds_read_b32 v202, v6 offset:7168
	ds_read_b32 v203, v6 offset:7680
	s_waitcnt lgkmcnt(0)
	v_max_f32_e32 v170, v170, v170
	v_max_f32_e32 v171, v171, v171
	v_max_f32_e32 v172, v172, v172
	v_max_f32_e32 v173, v173, v173
	v_max_f32_e32 v174, v174, v174
	v_max_f32_e32 v175, v175, v175
	v_max_f32_e32 v176, v176, v176
	v_max_f32_e32 v177, v177, v177
	v_max_f32_e32 v196, v196, v196
	v_max_f32_e32 v197, v197, v197
	v_max_f32_e32 v198, v198, v198
	v_max_f32_e32 v199, v199, v199
	v_max_f32_e32 v200, v200, v200
	v_max_f32_e32 v201, v201, v201
	v_max_f32_e32 v202, v202, v202
	v_max_f32_e32 v203, v203, v203
	v_med3_f32 v170, v170, s20, v13
	v_med3_f32 v171, v171, s20, v13
	v_med3_f32 v172, v172, s20, v13
	v_med3_f32 v173, v173, s20, v13
	v_med3_f32 v174, v174, s20, v13
	v_med3_f32 v175, v175, s20, v13
	v_med3_f32 v176, v176, s20, v13
	v_med3_f32 v177, v177, s20, v13
	v_med3_f32 v196, v196, s20, v13
	v_med3_f32 v197, v197, s20, v13
	v_med3_f32 v198, v198, s20, v13
	v_med3_f32 v199, v199, s20, v13
	v_med3_f32 v200, v200, s20, v13
	v_med3_f32 v201, v201, s20, v13
	v_med3_f32 v202, v202, s20, v13
	v_med3_f32 v203, v203, s20, v13
	v_mov_b32_e32 v208, 0
	v_mov_b32_e32 v209, 0
	v_mov_b32_e32 v210, 0
	v_mov_b32_e32 v211, 0
	v_cvt_pk_fp8_f32 v208, v170, v171
	v_cvt_pk_fp8_f32 v209, v174, v175
	v_cvt_pk_fp8_f32 v210, v196, v197
	v_cvt_pk_fp8_f32 v211, v200, v201
	v_cvt_pk_fp8_f32 v208, v172, v173 op_sel:[0,0,1]
	v_cvt_pk_fp8_f32 v209, v176, v177 op_sel:[0,0,1]
	v_cvt_pk_fp8_f32 v210, v198, v199 op_sel:[0,0,1]
	v_cvt_pk_fp8_f32 v211, v202, v203 op_sel:[0,0,1]
	s_nop 0
	global_store_dwordx4 v11, v[208:211], s[14:15]
	ds_read_b32 v170, v8
	ds_read_b32 v171, v8 offset:512
	ds_read_b32 v172, v8 offset:1024
	ds_read_b32 v173, v8 offset:1536
	ds_read_b32 v174, v8 offset:2048
	ds_read_b32 v175, v8 offset:2560
	ds_read_b32 v176, v8 offset:3072
	ds_read_b32 v177, v8 offset:3584
	ds_read_b32 v196, v8 offset:4096
	ds_read_b32 v197, v8 offset:4608
	ds_read_b32 v198, v8 offset:5120
	ds_read_b32 v199, v8 offset:5632
	ds_read_b32 v200, v8 offset:6144
	ds_read_b32 v201, v8 offset:6656
	ds_read_b32 v202, v8 offset:7168
	ds_read_b32 v203, v8 offset:7680
	s_waitcnt lgkmcnt(0)
	v_max_f32_e32 v170, v170, v170
	v_max_f32_e32 v171, v171, v171
	v_max_f32_e32 v172, v172, v172
	v_max_f32_e32 v173, v173, v173
	v_max_f32_e32 v174, v174, v174
	v_max_f32_e32 v175, v175, v175
	v_max_f32_e32 v176, v176, v176
	v_max_f32_e32 v177, v177, v177
	v_max_f32_e32 v196, v196, v196
	v_max_f32_e32 v197, v197, v197
	v_max_f32_e32 v198, v198, v198
	v_max_f32_e32 v199, v199, v199
	v_max_f32_e32 v200, v200, v200
	v_max_f32_e32 v201, v201, v201
	v_max_f32_e32 v202, v202, v202
	v_max_f32_e32 v203, v203, v203
	v_med3_f32 v170, v170, s20, v13
	v_med3_f32 v171, v171, s20, v13
	v_med3_f32 v172, v172, s20, v13
	v_med3_f32 v173, v173, s20, v13
	v_med3_f32 v174, v174, s20, v13
	v_med3_f32 v175, v175, s20, v13
	v_med3_f32 v176, v176, s20, v13
	v_med3_f32 v177, v177, s20, v13
	v_med3_f32 v196, v196, s20, v13
	v_med3_f32 v197, v197, s20, v13
	v_med3_f32 v198, v198, s20, v13
	v_med3_f32 v199, v199, s20, v13
	v_med3_f32 v200, v200, s20, v13
	v_med3_f32 v201, v201, s20, v13
	v_med3_f32 v202, v202, s20, v13
	v_med3_f32 v203, v203, s20, v13
	v_mov_b32_e32 v208, 0
	v_mov_b32_e32 v209, 0
	v_mov_b32_e32 v210, 0
	v_mov_b32_e32 v211, 0
	v_cvt_pk_fp8_f32 v208, v170, v171
	v_cvt_pk_fp8_f32 v209, v174, v175
	v_cvt_pk_fp8_f32 v210, v196, v197
	v_cvt_pk_fp8_f32 v211, v200, v201
	v_cvt_pk_fp8_f32 v208, v172, v173 op_sel:[0,0,1]
	v_cvt_pk_fp8_f32 v209, v176, v177 op_sel:[0,0,1]
	v_cvt_pk_fp8_f32 v210, v198, v199 op_sel:[0,0,1]
	v_cvt_pk_fp8_f32 v211, v202, v203 op_sel:[0,0,1]
	s_nop 0
	global_store_dwordx4 v12, v[208:211], s[14:15]
	s_waitcnt vmcnt(32)
	v_mul_f32_e32 v68, 0x43000000, v68
	v_mul_f32_e32 v69, 0x43000000, v69
	v_mul_f32_e32 v70, 0x43000000, v70
	v_mul_f32_e32 v71, 0x43000000, v71
	ds_write_b128 v5, v[68:71]
	v_mul_f32_e32 v72, 0x43000000, v72
	v_mul_f32_e32 v73, 0x43000000, v73
	v_mul_f32_e32 v74, 0x43000000, v74
	v_mul_f32_e32 v75, 0x43000000, v75
	ds_write_b128 v5, v[72:75] offset:1024
	v_mul_f32_e32 v76, 0x43000000, v76
	v_mul_f32_e32 v77, 0x43000000, v77
	v_mul_f32_e32 v78, 0x43000000, v78
	v_mul_f32_e32 v79, 0x43000000, v79
	ds_write_b128 v5, v[76:79] offset:2048
	v_mul_f32_e32 v80, 0x43000000, v80
	v_mul_f32_e32 v81, 0x43000000, v81
	v_mul_f32_e32 v82, 0x43000000, v82
	v_mul_f32_e32 v83, 0x43000000, v83
	ds_write_b128 v5, v[80:83] offset:3072
	v_mul_f32_e32 v84, 0x43000000, v84
	v_mul_f32_e32 v85, 0x43000000, v85
	v_mul_f32_e32 v86, 0x43000000, v86
	v_mul_f32_e32 v87, 0x43000000, v87
	ds_write_b128 v5, v[84:87] offset:4096
	v_mul_f32_e32 v88, 0x43000000, v88
	v_mul_f32_e32 v89, 0x43000000, v89
	v_mul_f32_e32 v90, 0x43000000, v90
	v_mul_f32_e32 v91, 0x43000000, v91
	ds_write_b128 v5, v[88:91] offset:5120
	v_mul_f32_e32 v92, 0x43000000, v92
	v_mul_f32_e32 v93, 0x43000000, v93
	v_mul_f32_e32 v94, 0x43000000, v94
	v_mul_f32_e32 v95, 0x43000000, v95
	ds_write_b128 v5, v[92:95] offset:6144
	v_mul_f32_e32 v96, 0x43000000, v96
	v_mul_f32_e32 v97, 0x43000000, v97
	v_mul_f32_e32 v98, 0x43000000, v98
	v_mul_f32_e32 v99, 0x43000000, v99
	ds_write_b128 v5, v[96:99] offset:7168
	s_waitcnt lgkmcnt(0)
	s_barrier
; #define GAS __attribute__((address_space(1)))
; #define LAS __attribute__((address_space(3)))
; #define LDS_WAIT() asm volatile("s_waitcnt lgkmcnt(0)" ::: "memory")
; __device__ __forceinline__ unsigned pk4_fp8(float a, float b, float c, float d) {
;     a = fminf(fmaxf(a, -448.f), 448.f); b = fminf(fmaxf(b, -448.f), 448.f); c = fminf(fmaxf(c, -448.f), 448.f); d = fminf(fmaxf(d, -448.f), 448.f);
;     int w = __builtin_amdgcn_cvt_pk_fp8_f32(a, b, 0, false); w = __builtin_amdgcn_cvt_pk_fp8_f32(c, d, w, true); return (unsigned)w; }
;     const int pr = item >> 1, kb = 2 * (pr / nblk) + (item & 1), nb = pr % nblk, k0 = 64 * kb, n0 = 32 * nb;
;     const int nr = n0 + (lane & 31); const int sc = MAP == 1 ? src_col_in(nr) : nr;
;     float v[32];
; #pragma unroll
;     for (int i = 0; i < 32; ++i) v[i] = sc >= 0 ? W[(size_t)(k0 + 2 * i + (lane >> 5)) * Nsrc + sc] : 0.f;
; #pragma unroll
;     for (int i = 0; i < 32; ++i) { const int k = k0 + 2 * i + (lane >> 5); float x = v[i] * wscale; if (KS) x *= (k < ksplit ? ksA[k] : ksB[k - ksplit]); scr[(2 * i + (lane >> 5)) * 33 + (lane & 31)] = x; }
;     LDS_WAIT(); asm volatile("" ::: "memory");
;     const int c = lane & 7;
; #pragma unroll
;     for (int j = 0; j < 4; ++j) { const int n = (lane >> 3) + 8 * j; const LAS float* s = scr + (8 * c) * 33 + n;
;         const unsigned long long o = (unsigned long long)pg8::pk4_fp8(s[0 * 33], s[1 * 33], s[2 * 33], s[3 * 33]) | ((unsigned long long)pg8::pk4_fp8(s[4 * 33], s[5 * 33], s[6 * 33], s[7 * 33]) << 32);
;         *(GAS unsigned long long*)(WT + (size_t)(n0 + n) * K + k0 + 8 * c) = o; }
;     LDS_WAIT(); asm volatile("" ::: "memory");
	s_add_i32 s17, s16, 864
	s_min_u32 s17, s17, 0xfff
	s_lshr_b32 s18, s17, 5
	s_add_i32 s18, s18, 0
	s_and_b32 s19, s17, 31
	s_lshl_b32 s18, s18, 21
	s_lshl_b32 s19, s19, 9
	s_add_u32 s18, s18, s19
	s_add_u32 s12, s2, s18
	s_addc_u32 s13, s3, 0
	global_load_dwordx4 v[68:71], v10, s[12:13]
	s_add_u32 s12, s12, 0x8000
	s_addc_u32 s13, s13, 0
	global_load_dwordx4 v[72:75], v10, s[12:13]
	s_add_u32 s12, s12, 0x8000
	s_addc_u32 s13, s13, 0
	global_load_dwordx4 v[76:79], v10, s[12:13]
	s_add_u32 s12, s12, 0x8000
	s_addc_u32 s13, s13, 0
	global_load_dwordx4 v[80:83], v10, s[12:13]
	s_add_u32 s12, s12, 0x8000
	s_addc_u32 s13, s13, 0
	global_load_dwordx4 v[84:87], v10, s[12:13]
	s_add_u32 s12, s12, 0x8000
	s_addc_u32 s13, s13, 0
	global_load_dwordx4 v[88:91], v10, s[12:13]
	s_add_u32 s12, s12, 0x8000
	s_addc_u32 s13, s13, 0
	global_load_dwordx4 v[92:95], v10, s[12:13]
	s_add_u32 s12, s12, 0x8000
	s_addc_u32 s13, s13, 0
	global_load_dwordx4 v[96:99], v10, s[12:13]
	s_add_i32 s17, s16, 480
	s_min_u32 s17, s17, 0xfff
	s_lshr_b32 s18, s17, 5
	s_add_i32 s18, s18, 0
	s_and_b32 s19, s17, 31
	s_lshl_b32 s19, s19, 21
	s_lshl_b32 s18, s18, 7
	s_add_u32 s18, s18, s19
	s_add_u32 s14, s4, s18
	s_addc_u32 s15, s5, 0
	ds_read_b32 v170, v7
	ds_read_b32 v171, v7 offset:512
	ds_read_b32 v172, v7 offset:1024
	ds_read_b32 v173, v7 offset:1536
	ds_read_b32 v174, v7 offset:2048
	ds_read_b32 v175, v7 offset:2560
	ds_read_b32 v176, v7 offset:3072
	ds_read_b32 v177, v7 offset:3584
	ds_read_b32 v196, v7 offset:4096
	ds_read_b32 v197, v7 offset:4608
	ds_read_b32 v198, v7 offset:5120
	ds_read_b32 v199, v7 offset:5632
	ds_read_b32 v200, v7 offset:6144
	ds_read_b32 v201, v7 offset:6656
	ds_read_b32 v202, v7 offset:7168
	ds_read_b32 v203, v7 offset:7680
	s_waitcnt lgkmcnt(0)
	v_max_f32_e32 v170, v170, v170
	v_max_f32_e32 v171, v171, v171
	v_max_f32_e32 v172, v172, v172
	v_max_f32_e32 v173, v173, v173
	v_max_f32_e32 v174, v174, v174
	v_max_f32_e32 v175, v175, v175
	v_max_f32_e32 v176, v176, v176
	v_max_f32_e32 v177, v177, v177
	v_max_f32_e32 v196, v196, v196
	v_max_f32_e32 v197, v197, v197
	v_max_f32_e32 v198, v198, v198
	v_max_f32_e32 v199, v199, v199
	v_max_f32_e32 v200, v200, v200
	v_max_f32_e32 v201, v201, v201
	v_max_f32_e32 v202, v202, v202
	v_max_f32_e32 v203, v203, v203
	v_med3_f32 v170, v170, s20, v13
	v_med3_f32 v171, v171, s20, v13
	v_med3_f32 v172, v172, s20, v13
	v_med3_f32 v173, v173, s20, v13
	v_med3_f32 v174, v174, s20, v13
	v_med3_f32 v175, v175, s20, v13
	v_med3_f32 v176, v176, s20, v13
	v_med3_f32 v177, v177, s20, v13
	v_med3_f32 v196, v196, s20, v13
	v_med3_f32 v197, v197, s20, v13
	v_med3_f32 v198, v198, s20, v13
	v_med3_f32 v199, v199, s20, v13
	v_med3_f32 v200, v200, s20, v13
	v_med3_f32 v201, v201, s20, v13
	v_med3_f32 v202, v202, s20, v13
	v_med3_f32 v203, v203, s20, v13
	v_mov_b32_e32 v208, 0
	v_mov_b32_e32 v209, 0
	v_mov_b32_e32 v210, 0
	v_mov_b32_e32 v211, 0
	v_cvt_pk_fp8_f32 v208, v170, v171
	v_cvt_pk_fp8_f32 v209, v174, v175
	v_cvt_pk_fp8_f32 v210, v196, v197
	v_cvt_pk_fp8_f32 v211, v200, v201
	v_cvt_pk_fp8_f32 v208, v172, v173 op_sel:[0,0,1]
	v_cvt_pk_fp8_f32 v209, v176, v177 op_sel:[0,0,1]
	v_cvt_pk_fp8_f32 v210, v198, v199 op_sel:[0,0,1]
	v_cvt_pk_fp8_f32 v211, v202, v203 op_sel:[0,0,1]
	s_nop 0
	global_store_dwordx4 v11, v[208:211], s[14:15]
	ds_read_b32 v170, v9
	ds_read_b32 v171, v9 offset:512
	ds_read_b32 v172, v9 offset:1024
	ds_read_b32 v173, v9 offset:1536
	ds_read_b32 v174, v9 offset:2048
	ds_read_b32 v175, v9 offset:2560
	ds_read_b32 v176, v9 offset:3072
	ds_read_b32 v177, v9 offset:3584
	ds_read_b32 v196, v9 offset:4096
	ds_read_b32 v197, v9 offset:4608
	ds_read_b32 v198, v9 offset:5120
	ds_read_b32 v199, v9 offset:5632
	ds_read_b32 v200, v9 offset:6144
	ds_read_b32 v201, v9 offset:6656
	ds_read_b32 v202, v9 offset:7168
	ds_read_b32 v203, v9 offset:7680
	s_waitcnt lgkmcnt(0)
	v_max_f32_e32 v170, v170, v170
	v_max_f32_e32 v171, v171, v171
	v_max_f32_e32 v172, v172, v172
	v_max_f32_e32 v173, v173, v173
	v_max_f32_e32 v174, v174, v174
	v_max_f32_e32 v175, v175, v175
	v_max_f32_e32 v176, v176, v176
	v_max_f32_e32 v177, v177, v177
	v_max_f32_e32 v196, v196, v196
	v_max_f32_e32 v197, v197, v197
	v_max_f32_e32 v198, v198, v198
	v_max_f32_e32 v199, v199, v199
	v_max_f32_e32 v200, v200, v200
	v_max_f32_e32 v201, v201, v201
	v_max_f32_e32 v202, v202, v202
	v_max_f32_e32 v203, v203, v203
	v_med3_f32 v170, v170, s20, v13
	v_med3_f32 v171, v171, s20, v13
	v_med3_f32 v172, v172, s20, v13
	v_med3_f32 v173, v173, s20, v13
	v_med3_f32 v174, v174, s20, v13
	v_med3_f32 v175, v175, s20, v13
	v_med3_f32 v176, v176, s20, v13
	v_med3_f32 v177, v177, s20, v13
	v_med3_f32 v196, v196, s20, v13
	v_med3_f32 v197, v197, s20, v13
	v_med3_f32 v198, v198, s20, v13
	v_med3_f32 v199, v199, s20, v13
	v_med3_f32 v200, v200, s20, v13
	v_med3_f32 v201, v201, s20, v13
	v_med3_f32 v202, v202, s20, v13
	v_med3_f32 v203, v203, s20, v13
	v_mov_b32_e32 v208, 0
	v_mov_b32_e32 v209, 0
	v_mov_b32_e32 v210, 0
	v_mov_b32_e32 v211, 0
	v_cvt_pk_fp8_f32 v208, v170, v171
	v_cvt_pk_fp8_f32 v209, v174, v175
	v_cvt_pk_fp8_f32 v210, v196, v197
	v_cvt_pk_fp8_f32 v211, v200, v201
	v_cvt_pk_fp8_f32 v208, v172, v173 op_sel:[0,0,1]
	v_cvt_pk_fp8_f32 v209, v176, v177 op_sel:[0,0,1]
	v_cvt_pk_fp8_f32 v210, v198, v199 op_sel:[0,0,1]
	v_cvt_pk_fp8_f32 v211, v202, v203 op_sel:[0,0,1]
	s_nop 0
	global_store_dwordx4 v12, v[208:211], s[14:15]
	s_waitcnt vmcnt(32)
	v_mul_f32_e32 v100, 0x43000000, v100
	v_mul_f32_e32 v101, 0x43000000, v101
	v_mul_f32_e32 v102, 0x43000000, v102
	v_mul_f32_e32 v103, 0x43000000, v103
	ds_write_b128 v4, v[100:103]
	v_mul_f32_e32 v104, 0x43000000, v104
	v_mul_f32_e32 v105, 0x43000000, v105
	v_mul_f32_e32 v106, 0x43000000, v106
	v_mul_f32_e32 v107, 0x43000000, v107
	ds_write_b128 v4, v[104:107] offset:1024
	v_mul_f32_e32 v108, 0x43000000, v108
	v_mul_f32_e32 v109, 0x43000000, v109
	v_mul_f32_e32 v110, 0x43000000, v110
	v_mul_f32_e32 v111, 0x43000000, v111
	ds_write_b128 v4, v[108:111] offset:2048
	v_mul_f32_e32 v112, 0x43000000, v112
	v_mul_f32_e32 v113, 0x43000000, v113
	v_mul_f32_e32 v114, 0x43000000, v114
	v_mul_f32_e32 v115, 0x43000000, v115
	ds_write_b128 v4, v[112:115] offset:3072
	v_mul_f32_e32 v116, 0x43000000, v116
	v_mul_f32_e32 v117, 0x43000000, v117
	v_mul_f32_e32 v118, 0x43000000, v118
	v_mul_f32_e32 v119, 0x43000000, v119
	ds_write_b128 v4, v[116:119] offset:4096
	v_mul_f32_e32 v120, 0x43000000, v120
	v_mul_f32_e32 v121, 0x43000000, v121
	v_mul_f32_e32 v122, 0x43000000, v122
	v_mul_f32_e32 v123, 0x43000000, v123
	ds_write_b128 v4, v[120:123] offset:5120
	v_mul_f32_e32 v124, 0x43000000, v124
	v_mul_f32_e32 v125, 0x43000000, v125
	v_mul_f32_e32 v126, 0x43000000, v126
	v_mul_f32_e32 v127, 0x43000000, v127
	ds_write_b128 v4, v[124:127] offset:6144
	v_mul_f32_e32 v128, 0x43000000, v128
	v_mul_f32_e32 v129, 0x43000000, v129
	v_mul_f32_e32 v130, 0x43000000, v130
	v_mul_f32_e32 v131, 0x43000000, v131
	ds_write_b128 v4, v[128:131] offset:7168
	s_waitcnt lgkmcnt(0)
	s_barrier
; #define GAS __attribute__((address_space(1)))
; #define LAS __attribute__((address_space(3)))
; #define LDS_WAIT() asm volatile("s_waitcnt lgkmcnt(0)" ::: "memory")
; __device__ __forceinline__ unsigned pk4_fp8(float a, float b, float c, float d) {
;     a = fminf(fmaxf(a, -448.f), 448.f); b = fminf(fmaxf(b, -448.f), 448.f); c = fminf(fmaxf(c, -448.f), 448.f); d = fminf(fmaxf(d, -448.f), 448.f);
;     int w = __builtin_amdgcn_cvt_pk_fp8_f32(a, b, 0, false); w = __builtin_amdgcn_cvt_pk_fp8_f32(c, d, w, true); return (unsigned)w; }
;     const int pr = item >> 1, kb = 2 * (pr / nblk) + (item & 1), nb = pr % nblk, k0 = 64 * kb, n0 = 32 * nb;
;     const int nr = n0 + (lane & 31); const int sc = MAP == 1 ? src_col_in(nr) : nr;
;     float v[32];
; #pragma unroll
;     for (int i = 0; i < 32; ++i) v[i] = sc >= 0 ? W[(size_t)(k0 + 2 * i + (lane >> 5)) * Nsrc + sc] : 0.f;
; #pragma unroll
;     for (int i = 0; i < 32; ++i) { const int k = k0 + 2 * i + (lane >> 5); float x = v[i] * wscale; if (KS) x *= (k < ksplit ? ksA[k] : ksB[k - ksplit]); scr[(2 * i + (lane >> 5)) * 33 + (lane & 31)] = x; }
;     LDS_WAIT(); asm volatile("" ::: "memory");
;     const int c = lane & 7;
; #pragma unroll
;     for (int j = 0; j < 4; ++j) { const int n = (lane >> 3) + 8 * j; const LAS float* s = scr + (8 * c) * 33 + n;
;         const unsigned long long o = (unsigned long long)pg8::pk4_fp8(s[0 * 33], s[1 * 33], s[2 * 33], s[3 * 33]) | ((unsigned long long)pg8::pk4_fp8(s[4 * 33], s[5 * 33], s[6 * 33], s[7 * 33]) << 32);
;         *(GAS unsigned long long*)(WT + (size_t)(n0 + n) * K + k0 + 8 * c) = o; }
;     LDS_WAIT(); asm volatile("" ::: "memory");
	s_add_i32 s17, s16, 960
	s_min_u32 s17, s17, 0xfff
	s_lshr_b32 s18, s17, 5
	s_add_i32 s18, s18, 0
	s_and_b32 s19, s17, 31
	s_lshl_b32 s18, s18, 21
	s_lshl_b32 s19, s19, 9
	s_add_u32 s18, s18, s19
	s_add_u32 s12, s2, s18
	s_addc_u32 s13, s3, 0
	global_load_dwordx4 v[100:103], v10, s[12:13]
	s_add_u32 s12, s12, 0x8000
	s_addc_u32 s13, s13, 0
	global_load_dwordx4 v[104:107], v10, s[12:13]
	s_add_u32 s12, s12, 0x8000
	s_addc_u32 s13, s13, 0
	global_load_dwordx4 v[108:111], v10, s[12:13]
	s_add_u32 s12, s12, 0x8000
	s_addc_u32 s13, s13, 0
	global_load_dwordx4 v[112:115], v10, s[12:13]
	s_add_u32 s12, s12, 0x8000
	s_addc_u32 s13, s13, 0
	global_load_dwordx4 v[116:119], v10, s[12:13]
	s_add_u32 s12, s12, 0x8000
	s_addc_u32 s13, s13, 0
	global_load_dwordx4 v[120:123], v10, s[12:13]
	s_add_u32 s12, s12, 0x8000
	s_addc_u32 s13, s13, 0
	global_load_dwordx4 v[124:127], v10, s[12:13]
	s_add_u32 s12, s12, 0x8000
	s_addc_u32 s13, s13, 0
	global_load_dwordx4 v[128:131], v10, s[12:13]
	s_add_i32 s17, s16, 576
	s_min_u32 s17, s17, 0xfff
	s_lshr_b32 s18, s17, 5
	s_add_i32 s18, s18, 0
	s_and_b32 s19, s17, 31
	s_lshl_b32 s19, s19, 21
	s_lshl_b32 s18, s18, 7
	s_add_u32 s18, s18, s19
	s_add_u32 s14, s4, s18
	s_addc_u32 s15, s5, 0
	ds_read_b32 v170, v6
	ds_read_b32 v171, v6 offset:512
	ds_read_b32 v172, v6 offset:1024
	ds_read_b32 v173, v6 offset:1536
	ds_read_b32 v174, v6 offset:2048
	ds_read_b32 v175, v6 offset:2560
	ds_read_b32 v176, v6 offset:3072
	ds_read_b32 v177, v6 offset:3584
	ds_read_b32 v196, v6 offset:4096
	ds_read_b32 v197, v6 offset:4608
	ds_read_b32 v198, v6 offset:5120
	ds_read_b32 v199, v6 offset:5632
	ds_read_b32 v200, v6 offset:6144
	ds_read_b32 v201, v6 offset:6656
	ds_read_b32 v202, v6 offset:7168
	ds_read_b32 v203, v6 offset:7680
	s_waitcnt lgkmcnt(0)
	v_max_f32_e32 v170, v170, v170
	v_max_f32_e32 v171, v171, v171
	v_max_f32_e32 v172, v172, v172
	v_max_f32_e32 v173, v173, v173
	v_max_f32_e32 v174, v174, v174
	v_max_f32_e32 v175, v175, v175
	v_max_f32_e32 v176, v176, v176
	v_max_f32_e32 v177, v177, v177
	v_max_f32_e32 v196, v196, v196
	v_max_f32_e32 v197, v197, v197
	v_max_f32_e32 v198, v198, v198
	v_max_f32_e32 v199, v199, v199
	v_max_f32_e32 v200, v200, v200
	v_max_f32_e32 v201, v201, v201
	v_max_f32_e32 v202, v202, v202
	v_max_f32_e32 v203, v203, v203
	v_med3_f32 v170, v170, s20, v13
	v_med3_f32 v171, v171, s20, v13
	v_med3_f32 v172, v172, s20, v13
	v_med3_f32 v173, v173, s20, v13
	v_med3_f32 v174, v174, s20, v13
	v_med3_f32 v175, v175, s20, v13
	v_med3_f32 v176, v176, s20, v13
	v_med3_f32 v177, v177, s20, v13
	v_med3_f32 v196, v196, s20, v13
	v_med3_f32 v197, v197, s20, v13
	v_med3_f32 v198, v198, s20, v13
	v_med3_f32 v199, v199, s20, v13
	v_med3_f32 v200, v200, s20, v13
	v_med3_f32 v201, v201, s20, v13
	v_med3_f32 v202, v202, s20, v13
	v_med3_f32 v203, v203, s20, v13
	v_mov_b32_e32 v208, 0
	v_mov_b32_e32 v209, 0
	v_mov_b32_e32 v210, 0
	v_mov_b32_e32 v211, 0
	v_cvt_pk_fp8_f32 v208, v170, v171
	v_cvt_pk_fp8_f32 v209, v174, v175
	v_cvt_pk_fp8_f32 v210, v196, v197
	v_cvt_pk_fp8_f32 v211, v200, v201
	v_cvt_pk_fp8_f32 v208, v172, v173 op_sel:[0,0,1]
	v_cvt_pk_fp8_f32 v209, v176, v177 op_sel:[0,0,1]
	v_cvt_pk_fp8_f32 v210, v198, v199 op_sel:[0,0,1]
	v_cvt_pk_fp8_f32 v211, v202, v203 op_sel:[0,0,1]
	s_nop 0
	global_store_dwordx4 v11, v[208:211], s[14:15]
	ds_read_b32 v170, v8
	ds_read_b32 v171, v8 offset:512
	ds_read_b32 v172, v8 offset:1024
	ds_read_b32 v173, v8 offset:1536
	ds_read_b32 v174, v8 offset:2048
	ds_read_b32 v175, v8 offset:2560
	ds_read_b32 v176, v8 offset:3072
	ds_read_b32 v177, v8 offset:3584
	ds_read_b32 v196, v8 offset:4096
	ds_read_b32 v197, v8 offset:4608
	ds_read_b32 v198, v8 offset:5120
	ds_read_b32 v199, v8 offset:5632
	ds_read_b32 v200, v8 offset:6144
	ds_read_b32 v201, v8 offset:6656
	ds_read_b32 v202, v8 offset:7168
	ds_read_b32 v203, v8 offset:7680
	s_waitcnt lgkmcnt(0)
	v_max_f32_e32 v170, v170, v170
	v_max_f32_e32 v171, v171, v171
	v_max_f32_e32 v172, v172, v172
	v_max_f32_e32 v173, v173, v173
	v_max_f32_e32 v174, v174, v174
	v_max_f32_e32 v175, v175, v175
	v_max_f32_e32 v176, v176, v176
	v_max_f32_e32 v177, v177, v177
	v_max_f32_e32 v196, v196, v196
	v_max_f32_e32 v197, v197, v197
	v_max_f32_e32 v198, v198, v198
	v_max_f32_e32 v199, v199, v199
	v_max_f32_e32 v200, v200, v200
	v_max_f32_e32 v201, v201, v201
	v_max_f32_e32 v202, v202, v202
	v_max_f32_e32 v203, v203, v203
	v_med3_f32 v170, v170, s20, v13
	v_med3_f32 v171, v171, s20, v13
	v_med3_f32 v172, v172, s20, v13
	v_med3_f32 v173, v173, s20, v13
	v_med3_f32 v174, v174, s20, v13
	v_med3_f32 v175, v175, s20, v13
	v_med3_f32 v176, v176, s20, v13
	v_med3_f32 v177, v177, s20, v13
	v_med3_f32 v196, v196, s20, v13
	v_med3_f32 v197, v197, s20, v13
	v_med3_f32 v198, v198, s20, v13
	v_med3_f32 v199, v199, s20, v13
	v_med3_f32 v200, v200, s20, v13
	v_med3_f32 v201, v201, s20, v13
	v_med3_f32 v202, v202, s20, v13
	v_med3_f32 v203, v203, s20, v13
	v_mov_b32_e32 v208, 0
	v_mov_b32_e32 v209, 0
	v_mov_b32_e32 v210, 0
	v_mov_b32_e32 v211, 0
	v_cvt_pk_fp8_f32 v208, v170, v171
	v_cvt_pk_fp8_f32 v209, v174, v175
	v_cvt_pk_fp8_f32 v210, v196, v197
	v_cvt_pk_fp8_f32 v211, v200, v201
	v_cvt_pk_fp8_f32 v208, v172, v173 op_sel:[0,0,1]
	v_cvt_pk_fp8_f32 v209, v176, v177 op_sel:[0,0,1]
	v_cvt_pk_fp8_f32 v210, v198, v199 op_sel:[0,0,1]
	v_cvt_pk_fp8_f32 v211, v202, v203 op_sel:[0,0,1]
	s_nop 0
	global_store_dwordx4 v12, v[208:211], s[14:15]
	s_waitcnt vmcnt(32)
	v_mul_f32_e32 v132, 0x43000000, v132
	v_mul_f32_e32 v133, 0x43000000, v133
	v_mul_f32_e32 v134, 0x43000000, v134
	v_mul_f32_e32 v135, 0x43000000, v135
	ds_write_b128 v5, v[132:135]
	v_mul_f32_e32 v136, 0x43000000, v136
	v_mul_f32_e32 v137, 0x43000000, v137
	v_mul_f32_e32 v138, 0x43000000, v138
	v_mul_f32_e32 v139, 0x43000000, v139
	ds_write_b128 v5, v[136:139] offset:1024
	v_mul_f32_e32 v140, 0x43000000, v140
	v_mul_f32_e32 v141, 0x43000000, v141
	v_mul_f32_e32 v142, 0x43000000, v142
	v_mul_f32_e32 v143, 0x43000000, v143
	ds_write_b128 v5, v[140:143] offset:2048
	v_mul_f32_e32 v144, 0x43000000, v144
	v_mul_f32_e32 v145, 0x43000000, v145
	v_mul_f32_e32 v146, 0x43000000, v146
	v_mul_f32_e32 v147, 0x43000000, v147
	ds_write_b128 v5, v[144:147] offset:3072
	v_mul_f32_e32 v148, 0x43000000, v148
	v_mul_f32_e32 v149, 0x43000000, v149
	v_mul_f32_e32 v150, 0x43000000, v150
	v_mul_f32_e32 v151, 0x43000000, v151
	ds_write_b128 v5, v[148:151] offset:4096
	v_mul_f32_e32 v152, 0x43000000, v152
	v_mul_f32_e32 v153, 0x43000000, v153
	v_mul_f32_e32 v154, 0x43000000, v154
	v_mul_f32_e32 v155, 0x43000000, v155
	ds_write_b128 v5, v[152:155] offset:5120
	v_mul_f32_e32 v156, 0x43000000, v156
	v_mul_f32_e32 v157, 0x43000000, v157
	v_mul_f32_e32 v158, 0x43000000, v158
	v_mul_f32_e32 v159, 0x43000000, v159
	ds_write_b128 v5, v[156:159] offset:6144
	v_mul_f32_e32 v160, 0x43000000, v160
	v_mul_f32_e32 v161, 0x43000000, v161
	v_mul_f32_e32 v162, 0x43000000, v162
	v_mul_f32_e32 v163, 0x43000000, v163
	ds_write_b128 v5, v[160:163] offset:7168
	s_waitcnt lgkmcnt(0)
	s_barrier
; #define GAS __attribute__((address_space(1)))
; #define LAS __attribute__((address_space(3)))
; #define LDS_WAIT() asm volatile("s_waitcnt lgkmcnt(0)" ::: "memory")
; __device__ __forceinline__ unsigned pk4_fp8(float a, float b, float c, float d) {
;     a = fminf(fmaxf(a, -448.f), 448.f); b = fminf(fmaxf(b, -448.f), 448.f); c = fminf(fmaxf(c, -448.f), 448.f); d = fminf(fmaxf(d, -448.f), 448.f);
;     int w = __builtin_amdgcn_cvt_pk_fp8_f32(a, b, 0, false); w = __builtin_amdgcn_cvt_pk_fp8_f32(c, d, w, true); return (unsigned)w; }
;     const int pr = item >> 1, kb = 2 * (pr / nblk) + (item & 1), nb = pr % nblk, k0 = 64 * kb, n0 = 32 * nb;
;     const int nr = n0 + (lane & 31); const int sc = MAP == 1 ? src_col_in(nr) : nr;
;     float v[32];
; #pragma unroll
;     for (int i = 0; i < 32; ++i) v[i] = sc >= 0 ? W[(size_t)(k0 + 2 * i + (lane >> 5)) * Nsrc + sc] : 0.f;
; #pragma unroll
;     for (int i = 0; i < 32; ++i) { const int k = k0 + 2 * i + (lane >> 5); float x = v[i] * wscale; if (KS) x *= (k < ksplit ? ksA[k] : ksB[k - ksplit]); scr[(2 * i + (lane >> 5)) * 33 + (lane & 31)] = x; }
;     LDS_WAIT(); asm volatile("" ::: "memory");
;     const int c = lane & 7;
; #pragma unroll
;     for (int j = 0; j < 4; ++j) { const int n = (lane >> 3) + 8 * j; const LAS float* s = scr + (8 * c) * 33 + n;
;         const unsigned long long o = (unsigned long long)pg8::pk4_fp8(s[0 * 33], s[1 * 33], s[2 * 33], s[3 * 33]) | ((unsigned long long)pg8::pk4_fp8(s[4 * 33], s[5 * 33], s[6 * 33], s[7 * 33]) << 32);
;         *(GAS unsigned long long*)(WT + (size_t)(n0 + n) * K + k0 + 8 * c) = o; }
;     LDS_WAIT(); asm volatile("" ::: "memory");
	s_add_i32 s17, s16, 1056
	s_min_u32 s17, s17, 0xfff
	s_lshr_b32 s18, s17, 5
	s_add_i32 s18, s18, 0
	s_and_b32 s19, s17, 31
	s_lshl_b32 s18, s18, 21
	s_lshl_b32 s19, s19, 9
	s_add_u32 s18, s18, s19
	s_add_u32 s12, s2, s18
	s_addc_u32 s13, s3, 0
	global_load_dwordx4 v[132:135], v10, s[12:13]
	s_add_u32 s12, s12, 0x8000
	s_addc_u32 s13, s13, 0
	global_load_dwordx4 v[136:139], v10, s[12:13]
	s_add_u32 s12, s12, 0x8000
	s_addc_u32 s13, s13, 0
	global_load_dwordx4 v[140:143], v10, s[12:13]
	s_add_u32 s12, s12, 0x8000
	s_addc_u32 s13, s13, 0
	global_load_dwordx4 v[144:147], v10, s[12:13]
	s_add_u32 s12, s12, 0x8000
	s_addc_u32 s13, s13, 0
	global_load_dwordx4 v[148:151], v10, s[12:13]
	s_add_u32 s12, s12, 0x8000
	s_addc_u32 s13, s13, 0
	global_load_dwordx4 v[152:155], v10, s[12:13]
	s_add_u32 s12, s12, 0x8000
	s_addc_u32 s13, s13, 0
	global_load_dwordx4 v[156:159], v10, s[12:13]
	s_add_u32 s12, s12, 0x8000
	s_addc_u32 s13, s13, 0
	global_load_dwordx4 v[160:163], v10, s[12:13]
	s_add_i32 s17, s16, 672
	s_min_u32 s17, s17, 0xfff
	s_lshr_b32 s18, s17, 5
	s_add_i32 s18, s18, 0
	s_and_b32 s19, s17, 31
	s_lshl_b32 s19, s19, 21
	s_lshl_b32 s18, s18, 7
	s_add_u32 s18, s18, s19
	s_add_u32 s14, s4, s18
	s_addc_u32 s15, s5, 0
	ds_read_b32 v170, v7
	ds_read_b32 v171, v7 offset:512
	ds_read_b32 v172, v7 offset:1024
	ds_read_b32 v173, v7 offset:1536
	ds_read_b32 v174, v7 offset:2048
	ds_read_b32 v175, v7 offset:2560
	ds_read_b32 v176, v7 offset:3072
	ds_read_b32 v177, v7 offset:3584
	ds_read_b32 v196, v7 offset:4096
	ds_read_b32 v197, v7 offset:4608
	ds_read_b32 v198, v7 offset:5120
	ds_read_b32 v199, v7 offset:5632
	ds_read_b32 v200, v7 offset:6144
	ds_read_b32 v201, v7 offset:6656
	ds_read_b32 v202, v7 offset:7168
	ds_read_b32 v203, v7 offset:7680
	s_waitcnt lgkmcnt(0)
	v_max_f32_e32 v170, v170, v170
	v_max_f32_e32 v171, v171, v171
	v_max_f32_e32 v172, v172, v172
	v_max_f32_e32 v173, v173, v173
	v_max_f32_e32 v174, v174, v174
	v_max_f32_e32 v175, v175, v175
	v_max_f32_e32 v176, v176, v176
	v_max_f32_e32 v177, v177, v177
	v_max_f32_e32 v196, v196, v196
	v_max_f32_e32 v197, v197, v197
	v_max_f32_e32 v198, v198, v198
	v_max_f32_e32 v199, v199, v199
	v_max_f32_e32 v200, v200, v200
	v_max_f32_e32 v201, v201, v201
	v_max_f32_e32 v202, v202, v202
	v_max_f32_e32 v203, v203, v203
	v_med3_f32 v170, v170, s20, v13
	v_med3_f32 v171, v171, s20, v13
	v_med3_f32 v172, v172, s20, v13
	v_med3_f32 v173, v173, s20, v13
	v_med3_f32 v174, v174, s20, v13
	v_med3_f32 v175, v175, s20, v13
	v_med3_f32 v176, v176, s20, v13
	v_med3_f32 v177, v177, s20, v13
	v_med3_f32 v196, v196, s20, v13
	v_med3_f32 v197, v197, s20, v13
	v_med3_f32 v198, v198, s20, v13
	v_med3_f32 v199, v199, s20, v13
	v_med3_f32 v200, v200, s20, v13
	v_med3_f32 v201, v201, s20, v13
	v_med3_f32 v202, v202, s20, v13
	v_med3_f32 v203, v203, s20, v13
	v_mov_b32_e32 v208, 0
	v_mov_b32_e32 v209, 0
	v_mov_b32_e32 v210, 0
	v_mov_b32_e32 v211, 0
	v_cvt_pk_fp8_f32 v208, v170, v171
	v_cvt_pk_fp8_f32 v209, v174, v175
	v_cvt_pk_fp8_f32 v210, v196, v197
	v_cvt_pk_fp8_f32 v211, v200, v201
	v_cvt_pk_fp8_f32 v208, v172, v173 op_sel:[0,0,1]
	v_cvt_pk_fp8_f32 v209, v176, v177 op_sel:[0,0,1]
	v_cvt_pk_fp8_f32 v210, v198, v199 op_sel:[0,0,1]
	v_cvt_pk_fp8_f32 v211, v202, v203 op_sel:[0,0,1]
	s_nop 0
	global_store_dwordx4 v11, v[208:211], s[14:15]
	ds_read_b32 v170, v9
	ds_read_b32 v171, v9 offset:512
	ds_read_b32 v172, v9 offset:1024
	ds_read_b32 v173, v9 offset:1536
	ds_read_b32 v174, v9 offset:2048
	ds_read_b32 v175, v9 offset:2560
	ds_read_b32 v176, v9 offset:3072
	ds_read_b32 v177, v9 offset:3584
	ds_read_b32 v196, v9 offset:4096
	ds_read_b32 v197, v9 offset:4608
	ds_read_b32 v198, v9 offset:5120
	ds_read_b32 v199, v9 offset:5632
	ds_read_b32 v200, v9 offset:6144
	ds_read_b32 v201, v9 offset:6656
	ds_read_b32 v202, v9 offset:7168
	ds_read_b32 v203, v9 offset:7680
	s_waitcnt lgkmcnt(0)
	v_max_f32_e32 v170, v170, v170
	v_max_f32_e32 v171, v171, v171
	v_max_f32_e32 v172, v172, v172
	v_max_f32_e32 v173, v173, v173
	v_max_f32_e32 v174, v174, v174
	v_max_f32_e32 v175, v175, v175
	v_max_f32_e32 v176, v176, v176
	v_max_f32_e32 v177, v177, v177
	v_max_f32_e32 v196, v196, v196
	v_max_f32_e32 v197, v197, v197
	v_max_f32_e32 v198, v198, v198
	v_max_f32_e32 v199, v199, v199
	v_max_f32_e32 v200, v200, v200
	v_max_f32_e32 v201, v201, v201
	v_max_f32_e32 v202, v202, v202
	v_max_f32_e32 v203, v203, v203
	v_med3_f32 v170, v170, s20, v13
	v_med3_f32 v171, v171, s20, v13
	v_med3_f32 v172, v172, s20, v13
	v_med3_f32 v173, v173, s20, v13
	v_med3_f32 v174, v174, s20, v13
	v_med3_f32 v175, v175, s20, v13
	v_med3_f32 v176, v176, s20, v13
	v_med3_f32 v177, v177, s20, v13
	v_med3_f32 v196, v196, s20, v13
	v_med3_f32 v197, v197, s20, v13
	v_med3_f32 v198, v198, s20, v13
	v_med3_f32 v199, v199, s20, v13
	v_med3_f32 v200, v200, s20, v13
	v_med3_f32 v201, v201, s20, v13
	v_med3_f32 v202, v202, s20, v13
	v_med3_f32 v203, v203, s20, v13
	v_mov_b32_e32 v208, 0
	v_mov_b32_e32 v209, 0
	v_mov_b32_e32 v210, 0
	v_mov_b32_e32 v211, 0
	v_cvt_pk_fp8_f32 v208, v170, v171
	v_cvt_pk_fp8_f32 v209, v174, v175
	v_cvt_pk_fp8_f32 v210, v196, v197
	v_cvt_pk_fp8_f32 v211, v200, v201
	v_cvt_pk_fp8_f32 v208, v172, v173 op_sel:[0,0,1]
	v_cvt_pk_fp8_f32 v209, v176, v177 op_sel:[0,0,1]
	v_cvt_pk_fp8_f32 v210, v198, v199 op_sel:[0,0,1]
	v_cvt_pk_fp8_f32 v211, v202, v203 op_sel:[0,0,1]
	s_nop 0
	global_store_dwordx4 v12, v[208:211], s[14:15]
	s_waitcnt vmcnt(32)
	v_mul_f32_e32 v36, 0x43000000, v36
	v_mul_f32_e32 v37, 0x43000000, v37
	v_mul_f32_e32 v38, 0x43000000, v38
	v_mul_f32_e32 v39, 0x43000000, v39
	ds_write_b128 v4, v[36:39]
	v_mul_f32_e32 v40, 0x43000000, v40
	v_mul_f32_e32 v41, 0x43000000, v41
	v_mul_f32_e32 v42, 0x43000000, v42
	v_mul_f32_e32 v43, 0x43000000, v43
	ds_write_b128 v4, v[40:43] offset:1024
	v_mul_f32_e32 v44, 0x43000000, v44
	v_mul_f32_e32 v45, 0x43000000, v45
	v_mul_f32_e32 v46, 0x43000000, v46
	v_mul_f32_e32 v47, 0x43000000, v47
	ds_write_b128 v4, v[44:47] offset:2048
	v_mul_f32_e32 v48, 0x43000000, v48
	v_mul_f32_e32 v49, 0x43000000, v49
	v_mul_f32_e32 v50, 0x43000000, v50
	v_mul_f32_e32 v51, 0x43000000, v51
	ds_write_b128 v4, v[48:51] offset:3072
	v_mul_f32_e32 v52, 0x43000000, v52
	v_mul_f32_e32 v53, 0x43000000, v53
	v_mul_f32_e32 v54, 0x43000000, v54
	v_mul_f32_e32 v55, 0x43000000, v55
	ds_write_b128 v4, v[52:55] offset:4096
	v_mul_f32_e32 v56, 0x43000000, v56
	v_mul_f32_e32 v57, 0x43000000, v57
	v_mul_f32_e32 v58, 0x43000000, v58
	v_mul_f32_e32 v59, 0x43000000, v59
	ds_write_b128 v4, v[56:59] offset:5120
	v_mul_f32_e32 v60, 0x43000000, v60
	v_mul_f32_e32 v61, 0x43000000, v61
	v_mul_f32_e32 v62, 0x43000000, v62
	v_mul_f32_e32 v63, 0x43000000, v63
	ds_write_b128 v4, v[60:63] offset:6144
	v_mul_f32_e32 v64, 0x43000000, v64
	v_mul_f32_e32 v65, 0x43000000, v65
	v_mul_f32_e32 v66, 0x43000000, v66
	v_mul_f32_e32 v67, 0x43000000, v67
	ds_write_b128 v4, v[64:67] offset:7168
	s_waitcnt lgkmcnt(0)
	s_barrier
; #define GAS __attribute__((address_space(1)))
; #define LAS __attribute__((address_space(3)))
; #define LDS_WAIT() asm volatile("s_waitcnt lgkmcnt(0)" ::: "memory")
; __device__ __forceinline__ unsigned pk4_fp8(float a, float b, float c, float d) {
;     a = fminf(fmaxf(a, -448.f), 448.f); b = fminf(fmaxf(b, -448.f), 448.f); c = fminf(fmaxf(c, -448.f), 448.f); d = fminf(fmaxf(d, -448.f), 448.f);
;     int w = __builtin_amdgcn_cvt_pk_fp8_f32(a, b, 0, false); w = __builtin_amdgcn_cvt_pk_fp8_f32(c, d, w, true); return (unsigned)w; }
;     const int pr = item >> 1, kb = 2 * (pr / nblk) + (item & 1), nb = pr % nblk, k0 = 64 * kb, n0 = 32 * nb;
;     const int nr = n0 + (lane & 31); const int sc = MAP == 1 ? src_col_in(nr) : nr;
;     float v[32];
; #pragma unroll
;     for (int i = 0; i < 32; ++i) v[i] = sc >= 0 ? W[(size_t)(k0 + 2 * i + (lane >> 5)) * Nsrc + sc] : 0.f;
; #pragma unroll
;     for (int i = 0; i < 32; ++i) { const int k = k0 + 2 * i + (lane >> 5); float x = v[i] * wscale; if (KS) x *= (k < ksplit ? ksA[k] : ksB[k - ksplit]); scr[(2 * i + (lane >> 5)) * 33 + (lane & 31)] = x; }
;     LDS_WAIT(); asm volatile("" ::: "memory");
;     const int c = lane & 7;
; #pragma unroll
;     for (int j = 0; j < 4; ++j) { const int n = (lane >> 3) + 8 * j; const LAS float* s = scr + (8 * c) * 33 + n;
;         const unsigned long long o = (unsigned long long)pg8::pk4_fp8(s[0 * 33], s[1 * 33], s[2 * 33], s[3 * 33]) | ((unsigned long long)pg8::pk4_fp8(s[4 * 33], s[5 * 33], s[6 * 33], s[7 * 33]) << 32);
;         *(GAS unsigned long long*)(WT + (size_t)(n0 + n) * K + k0 + 8 * c) = o; }
;     LDS_WAIT(); asm volatile("" ::: "memory");
	s_add_i32 s17, s16, 1152
	s_min_u32 s17, s17, 0xfff
	s_lshr_b32 s18, s17, 5
	s_add_i32 s18, s18, 0
	s_and_b32 s19, s17, 31
	s_lshl_b32 s18, s18, 21
	s_lshl_b32 s19, s19, 9
	s_add_u32 s18, s18, s19
	s_add_u32 s12, s2, s18
	s_addc_u32 s13, s3, 0
	global_load_dwordx4 v[36:39], v10, s[12:13]
	s_add_u32 s12, s12, 0x8000
	s_addc_u32 s13, s13, 0
	global_load_dwordx4 v[40:43], v10, s[12:13]
	s_add_u32 s12, s12, 0x8000
	s_addc_u32 s13, s13, 0
	global_load_dwordx4 v[44:47], v10, s[12:13]
	s_add_u32 s12, s12, 0x8000
	s_addc_u32 s13, s13, 0
	global_load_dwordx4 v[48:51], v10, s[12:13]
	s_add_u32 s12, s12, 0x8000
	s_addc_u32 s13, s13, 0
	global_load_dwordx4 v[52:55], v10, s[12:13]
	s_add_u32 s12, s12, 0x8000
	s_addc_u32 s13, s13, 0
	global_load_dwordx4 v[56:59], v10, s[12:13]
	s_add_u32 s12, s12, 0x8000
	s_addc_u32 s13, s13, 0
	global_load_dwordx4 v[60:63], v10, s[12:13]
	s_add_u32 s12, s12, 0x8000
	s_addc_u32 s13, s13, 0
	global_load_dwordx4 v[64:67], v10, s[12:13]
	s_add_i32 s17, s16, 768
	s_min_u32 s17, s17, 0xfff
	s_lshr_b32 s18, s17, 5
	s_add_i32 s18, s18, 0
	s_and_b32 s19, s17, 31
	s_lshl_b32 s19, s19, 21
	s_lshl_b32 s18, s18, 7
	s_add_u32 s18, s18, s19
	s_add_u32 s14, s4, s18
	s_addc_u32 s15, s5, 0
	ds_read_b32 v170, v6
	ds_read_b32 v171, v6 offset:512
	ds_read_b32 v172, v6 offset:1024
	ds_read_b32 v173, v6 offset:1536
	ds_read_b32 v174, v6 offset:2048
	ds_read_b32 v175, v6 offset:2560
	ds_read_b32 v176, v6 offset:3072
	ds_read_b32 v177, v6 offset:3584
	ds_read_b32 v196, v6 offset:4096
	ds_read_b32 v197, v6 offset:4608
	ds_read_b32 v198, v6 offset:5120
	ds_read_b32 v199, v6 offset:5632
	ds_read_b32 v200, v6 offset:6144
	ds_read_b32 v201, v6 offset:6656
	ds_read_b32 v202, v6 offset:7168
	ds_read_b32 v203, v6 offset:7680
	s_waitcnt lgkmcnt(0)
	v_max_f32_e32 v170, v170, v170
	v_max_f32_e32 v171, v171, v171
	v_max_f32_e32 v172, v172, v172
	v_max_f32_e32 v173, v173, v173
	v_max_f32_e32 v174, v174, v174
	v_max_f32_e32 v175, v175, v175
	v_max_f32_e32 v176, v176, v176
	v_max_f32_e32 v177, v177, v177
	v_max_f32_e32 v196, v196, v196
	v_max_f32_e32 v197, v197, v197
	v_max_f32_e32 v198, v198, v198
	v_max_f32_e32 v199, v199, v199
	v_max_f32_e32 v200, v200, v200
	v_max_f32_e32 v201, v201, v201
	v_max_f32_e32 v202, v202, v202
	v_max_f32_e32 v203, v203, v203
	v_med3_f32 v170, v170, s20, v13
	v_med3_f32 v171, v171, s20, v13
	v_med3_f32 v172, v172, s20, v13
	v_med3_f32 v173, v173, s20, v13
	v_med3_f32 v174, v174, s20, v13
	v_med3_f32 v175, v175, s20, v13
	v_med3_f32 v176, v176, s20, v13
	v_med3_f32 v177, v177, s20, v13
	v_med3_f32 v196, v196, s20, v13
	v_med3_f32 v197, v197, s20, v13
	v_med3_f32 v198, v198, s20, v13
	v_med3_f32 v199, v199, s20, v13
	v_med3_f32 v200, v200, s20, v13
	v_med3_f32 v201, v201, s20, v13
	v_med3_f32 v202, v202, s20, v13
	v_med3_f32 v203, v203, s20, v13
	v_mov_b32_e32 v208, 0
	v_mov_b32_e32 v209, 0
	v_mov_b32_e32 v210, 0
	v_mov_b32_e32 v211, 0
	v_cvt_pk_fp8_f32 v208, v170, v171
	v_cvt_pk_fp8_f32 v209, v174, v175
	v_cvt_pk_fp8_f32 v210, v196, v197
	v_cvt_pk_fp8_f32 v211, v200, v201
	v_cvt_pk_fp8_f32 v208, v172, v173 op_sel:[0,0,1]
	v_cvt_pk_fp8_f32 v209, v176, v177 op_sel:[0,0,1]
	v_cvt_pk_fp8_f32 v210, v198, v199 op_sel:[0,0,1]
	v_cvt_pk_fp8_f32 v211, v202, v203 op_sel:[0,0,1]
	s_nop 0
	global_store_dwordx4 v11, v[208:211], s[14:15]
	ds_read_b32 v170, v8
	ds_read_b32 v171, v8 offset:512
	ds_read_b32 v172, v8 offset:1024
	ds_read_b32 v173, v8 offset:1536
	ds_read_b32 v174, v8 offset:2048
	ds_read_b32 v175, v8 offset:2560
	ds_read_b32 v176, v8 offset:3072
	ds_read_b32 v177, v8 offset:3584
	ds_read_b32 v196, v8 offset:4096
	ds_read_b32 v197, v8 offset:4608
	ds_read_b32 v198, v8 offset:5120
	ds_read_b32 v199, v8 offset:5632
	ds_read_b32 v200, v8 offset:6144
	ds_read_b32 v201, v8 offset:6656
	ds_read_b32 v202, v8 offset:7168
	ds_read_b32 v203, v8 offset:7680
	s_waitcnt lgkmcnt(0)
	v_max_f32_e32 v170, v170, v170
	v_max_f32_e32 v171, v171, v171
	v_max_f32_e32 v172, v172, v172
	v_max_f32_e32 v173, v173, v173
	v_max_f32_e32 v174, v174, v174
	v_max_f32_e32 v175, v175, v175
	v_max_f32_e32 v176, v176, v176
	v_max_f32_e32 v177, v177, v177
	v_max_f32_e32 v196, v196, v196
	v_max_f32_e32 v197, v197, v197
	v_max_f32_e32 v198, v198, v198
	v_max_f32_e32 v199, v199, v199
	v_max_f32_e32 v200, v200, v200
	v_max_f32_e32 v201, v201, v201
	v_max_f32_e32 v202, v202, v202
	v_max_f32_e32 v203, v203, v203
	v_med3_f32 v170, v170, s20, v13
	v_med3_f32 v171, v171, s20, v13
	v_med3_f32 v172, v172, s20, v13
	v_med3_f32 v173, v173, s20, v13
	v_med3_f32 v174, v174, s20, v13
	v_med3_f32 v175, v175, s20, v13
	v_med3_f32 v176, v176, s20, v13
	v_med3_f32 v177, v177, s20, v13
	v_med3_f32 v196, v196, s20, v13
	v_med3_f32 v197, v197, s20, v13
	v_med3_f32 v198, v198, s20, v13
	v_med3_f32 v199, v199, s20, v13
	v_med3_f32 v200, v200, s20, v13
	v_med3_f32 v201, v201, s20, v13
	v_med3_f32 v202, v202, s20, v13
	v_med3_f32 v203, v203, s20, v13
	v_mov_b32_e32 v208, 0
	v_mov_b32_e32 v209, 0
	v_mov_b32_e32 v210, 0
	v_mov_b32_e32 v211, 0
	v_cvt_pk_fp8_f32 v208, v170, v171
	v_cvt_pk_fp8_f32 v209, v174, v175
	v_cvt_pk_fp8_f32 v210, v196, v197
	v_cvt_pk_fp8_f32 v211, v200, v201
	v_cvt_pk_fp8_f32 v208, v172, v173 op_sel:[0,0,1]
	v_cvt_pk_fp8_f32 v209, v176, v177 op_sel:[0,0,1]
	v_cvt_pk_fp8_f32 v210, v198, v199 op_sel:[0,0,1]
	v_cvt_pk_fp8_f32 v211, v202, v203 op_sel:[0,0,1]
	s_nop 0
	global_store_dwordx4 v12, v[208:211], s[14:15]
	s_waitcnt vmcnt(32)
	v_mul_f32_e32 v68, 0x43000000, v68
	v_mul_f32_e32 v69, 0x43000000, v69
	v_mul_f32_e32 v70, 0x43000000, v70
	v_mul_f32_e32 v71, 0x43000000, v71
	ds_write_b128 v5, v[68:71]
	v_mul_f32_e32 v72, 0x43000000, v72
	v_mul_f32_e32 v73, 0x43000000, v73
	v_mul_f32_e32 v74, 0x43000000, v74
	v_mul_f32_e32 v75, 0x43000000, v75
	ds_write_b128 v5, v[72:75] offset:1024
	v_mul_f32_e32 v76, 0x43000000, v76
	v_mul_f32_e32 v77, 0x43000000, v77
	v_mul_f32_e32 v78, 0x43000000, v78
	v_mul_f32_e32 v79, 0x43000000, v79
	ds_write_b128 v5, v[76:79] offset:2048
	v_mul_f32_e32 v80, 0x43000000, v80
	v_mul_f32_e32 v81, 0x43000000, v81
	v_mul_f32_e32 v82, 0x43000000, v82
	v_mul_f32_e32 v83, 0x43000000, v83
	ds_write_b128 v5, v[80:83] offset:3072
	v_mul_f32_e32 v84, 0x43000000, v84
	v_mul_f32_e32 v85, 0x43000000, v85
	v_mul_f32_e32 v86, 0x43000000, v86
	v_mul_f32_e32 v87, 0x43000000, v87
	ds_write_b128 v5, v[84:87] offset:4096
	v_mul_f32_e32 v88, 0x43000000, v88
	v_mul_f32_e32 v89, 0x43000000, v89
	v_mul_f32_e32 v90, 0x43000000, v90
	v_mul_f32_e32 v91, 0x43000000, v91
	ds_write_b128 v5, v[88:91] offset:5120
	v_mul_f32_e32 v92, 0x43000000, v92
	v_mul_f32_e32 v93, 0x43000000, v93
	v_mul_f32_e32 v94, 0x43000000, v94
	v_mul_f32_e32 v95, 0x43000000, v95
	ds_write_b128 v5, v[92:95] offset:6144
	v_mul_f32_e32 v96, 0x43000000, v96
	v_mul_f32_e32 v97, 0x43000000, v97
	v_mul_f32_e32 v98, 0x43000000, v98
	v_mul_f32_e32 v99, 0x43000000, v99
	ds_write_b128 v5, v[96:99] offset:7168
	s_waitcnt lgkmcnt(0)
	s_barrier
; #define GAS __attribute__((address_space(1)))
; #define LAS __attribute__((address_space(3)))
; #define LDS_WAIT() asm volatile("s_waitcnt lgkmcnt(0)" ::: "memory")
; __device__ __forceinline__ unsigned pk4_fp8(float a, float b, float c, float d) {
;     a = fminf(fmaxf(a, -448.f), 448.f); b = fminf(fmaxf(b, -448.f), 448.f); c = fminf(fmaxf(c, -448.f), 448.f); d = fminf(fmaxf(d, -448.f), 448.f);
;     int w = __builtin_amdgcn_cvt_pk_fp8_f32(a, b, 0, false); w = __builtin_amdgcn_cvt_pk_fp8_f32(c, d, w, true); return (unsigned)w; }
;     const int pr = item >> 1, kb = 2 * (pr / nblk) + (item & 1), nb = pr % nblk, k0 = 64 * kb, n0 = 32 * nb;
;     const int nr = n0 + (lane & 31); const int sc = MAP == 1 ? src_col_in(nr) : nr;
;     float v[32];
; #pragma unroll
;     for (int i = 0; i < 32; ++i) v[i] = sc >= 0 ? W[(size_t)(k0 + 2 * i + (lane >> 5)) * Nsrc + sc] : 0.f;
; #pragma unroll
;     for (int i = 0; i < 32; ++i) { const int k = k0 + 2 * i + (lane >> 5); float x = v[i] * wscale; if (KS) x *= (k < ksplit ? ksA[k] : ksB[k - ksplit]); scr[(2 * i + (lane >> 5)) * 33 + (lane & 31)] = x; }
;     LDS_WAIT(); asm volatile("" ::: "memory");
;     const int c = lane & 7;
; #pragma unroll
;     for (int j = 0; j < 4; ++j) { const int n = (lane >> 3) + 8 * j; const LAS float* s = scr + (8 * c) * 33 + n;
;         const unsigned long long o = (unsigned long long)pg8::pk4_fp8(s[0 * 33], s[1 * 33], s[2 * 33], s[3 * 33]) | ((unsigned long long)pg8::pk4_fp8(s[4 * 33], s[5 * 33], s[6 * 33], s[7 * 33]) << 32);
;         *(GAS unsigned long long*)(WT + (size_t)(n0 + n) * K + k0 + 8 * c) = o; }
;     LDS_WAIT(); asm volatile("" ::: "memory");
	s_add_i32 s17, s16, 1248
	s_min_u32 s17, s17, 0xfff
	s_lshr_b32 s18, s17, 5
	s_add_i32 s18, s18, 0
	s_and_b32 s19, s17, 31
	s_lshl_b32 s18, s18, 21
	s_lshl_b32 s19, s19, 9
	s_add_u32 s18, s18, s19
	s_add_u32 s12, s2, s18
	s_addc_u32 s13, s3, 0
	global_load_dwordx4 v[68:71], v10, s[12:13]
	s_add_u32 s12, s12, 0x8000
	s_addc_u32 s13, s13, 0
	global_load_dwordx4 v[72:75], v10, s[12:13]
	s_add_u32 s12, s12, 0x8000
	s_addc_u32 s13, s13, 0
	global_load_dwordx4 v[76:79], v10, s[12:13]
	s_add_u32 s12, s12, 0x8000
	s_addc_u32 s13, s13, 0
	global_load_dwordx4 v[80:83], v10, s[12:13]
	s_add_u32 s12, s12, 0x8000
	s_addc_u32 s13, s13, 0
	global_load_dwordx4 v[84:87], v10, s[12:13]
	s_add_u32 s12, s12, 0x8000
	s_addc_u32 s13, s13, 0
	global_load_dwordx4 v[88:91], v10, s[12:13]
	s_add_u32 s12, s12, 0x8000
	s_addc_u32 s13, s13, 0
	global_load_dwordx4 v[92:95], v10, s[12:13]
	s_add_u32 s12, s12, 0x8000
	s_addc_u32 s13, s13, 0
	global_load_dwordx4 v[96:99], v10, s[12:13]
	s_add_i32 s17, s16, 864
	s_min_u32 s17, s17, 0xfff
	s_lshr_b32 s18, s17, 5
	s_add_i32 s18, s18, 0
	s_and_b32 s19, s17, 31
	s_lshl_b32 s19, s19, 21
	s_lshl_b32 s18, s18, 7
	s_add_u32 s18, s18, s19
	s_add_u32 s14, s4, s18
	s_addc_u32 s15, s5, 0
	ds_read_b32 v170, v7
	ds_read_b32 v171, v7 offset:512
	ds_read_b32 v172, v7 offset:1024
	ds_read_b32 v173, v7 offset:1536
	ds_read_b32 v174, v7 offset:2048
	ds_read_b32 v175, v7 offset:2560
	ds_read_b32 v176, v7 offset:3072
	ds_read_b32 v177, v7 offset:3584
	ds_read_b32 v196, v7 offset:4096
	ds_read_b32 v197, v7 offset:4608
	ds_read_b32 v198, v7 offset:5120
	ds_read_b32 v199, v7 offset:5632
	ds_read_b32 v200, v7 offset:6144
	ds_read_b32 v201, v7 offset:6656
	ds_read_b32 v202, v7 offset:7168
	ds_read_b32 v203, v7 offset:7680
	s_waitcnt lgkmcnt(0)
	v_max_f32_e32 v170, v170, v170
	v_max_f32_e32 v171, v171, v171
	v_max_f32_e32 v172, v172, v172
	v_max_f32_e32 v173, v173, v173
	v_max_f32_e32 v174, v174, v174
	v_max_f32_e32 v175, v175, v175
	v_max_f32_e32 v176, v176, v176
	v_max_f32_e32 v177, v177, v177
	v_max_f32_e32 v196, v196, v196
	v_max_f32_e32 v197, v197, v197
	v_max_f32_e32 v198, v198, v198
	v_max_f32_e32 v199, v199, v199
	v_max_f32_e32 v200, v200, v200
	v_max_f32_e32 v201, v201, v201
	v_max_f32_e32 v202, v202, v202
	v_max_f32_e32 v203, v203, v203
	v_med3_f32 v170, v170, s20, v13
	v_med3_f32 v171, v171, s20, v13
	v_med3_f32 v172, v172, s20, v13
	v_med3_f32 v173, v173, s20, v13
	v_med3_f32 v174, v174, s20, v13
	v_med3_f32 v175, v175, s20, v13
	v_med3_f32 v176, v176, s20, v13
	v_med3_f32 v177, v177, s20, v13
	v_med3_f32 v196, v196, s20, v13
	v_med3_f32 v197, v197, s20, v13
	v_med3_f32 v198, v198, s20, v13
	v_med3_f32 v199, v199, s20, v13
	v_med3_f32 v200, v200, s20, v13
	v_med3_f32 v201, v201, s20, v13
	v_med3_f32 v202, v202, s20, v13
	v_med3_f32 v203, v203, s20, v13
	v_mov_b32_e32 v208, 0
	v_mov_b32_e32 v209, 0
	v_mov_b32_e32 v210, 0
	v_mov_b32_e32 v211, 0
	v_cvt_pk_fp8_f32 v208, v170, v171
	v_cvt_pk_fp8_f32 v209, v174, v175
	v_cvt_pk_fp8_f32 v210, v196, v197
	v_cvt_pk_fp8_f32 v211, v200, v201
	v_cvt_pk_fp8_f32 v208, v172, v173 op_sel:[0,0,1]
	v_cvt_pk_fp8_f32 v209, v176, v177 op_sel:[0,0,1]
	v_cvt_pk_fp8_f32 v210, v198, v199 op_sel:[0,0,1]
	v_cvt_pk_fp8_f32 v211, v202, v203 op_sel:[0,0,1]
	s_nop 0
	global_store_dwordx4 v11, v[208:211], s[14:15]
	ds_read_b32 v170, v9
	ds_read_b32 v171, v9 offset:512
	ds_read_b32 v172, v9 offset:1024
	ds_read_b32 v173, v9 offset:1536
	ds_read_b32 v174, v9 offset:2048
	ds_read_b32 v175, v9 offset:2560
	ds_read_b32 v176, v9 offset:3072
	ds_read_b32 v177, v9 offset:3584
	ds_read_b32 v196, v9 offset:4096
	ds_read_b32 v197, v9 offset:4608
	ds_read_b32 v198, v9 offset:5120
	ds_read_b32 v199, v9 offset:5632
	ds_read_b32 v200, v9 offset:6144
	ds_read_b32 v201, v9 offset:6656
	ds_read_b32 v202, v9 offset:7168
	ds_read_b32 v203, v9 offset:7680
	s_waitcnt lgkmcnt(0)
	v_max_f32_e32 v170, v170, v170
	v_max_f32_e32 v171, v171, v171
	v_max_f32_e32 v172, v172, v172
	v_max_f32_e32 v173, v173, v173
	v_max_f32_e32 v174, v174, v174
	v_max_f32_e32 v175, v175, v175
	v_max_f32_e32 v176, v176, v176
	v_max_f32_e32 v177, v177, v177
	v_max_f32_e32 v196, v196, v196
	v_max_f32_e32 v197, v197, v197
	v_max_f32_e32 v198, v198, v198
	v_max_f32_e32 v199, v199, v199
	v_max_f32_e32 v200, v200, v200
	v_max_f32_e32 v201, v201, v201
	v_max_f32_e32 v202, v202, v202
	v_max_f32_e32 v203, v203, v203
	v_med3_f32 v170, v170, s20, v13
	v_med3_f32 v171, v171, s20, v13
	v_med3_f32 v172, v172, s20, v13
	v_med3_f32 v173, v173, s20, v13
	v_med3_f32 v174, v174, s20, v13
	v_med3_f32 v175, v175, s20, v13
	v_med3_f32 v176, v176, s20, v13
	v_med3_f32 v177, v177, s20, v13
	v_med3_f32 v196, v196, s20, v13
	v_med3_f32 v197, v197, s20, v13
	v_med3_f32 v198, v198, s20, v13
	v_med3_f32 v199, v199, s20, v13
	v_med3_f32 v200, v200, s20, v13
	v_med3_f32 v201, v201, s20, v13
	v_med3_f32 v202, v202, s20, v13
	v_med3_f32 v203, v203, s20, v13
	v_mov_b32_e32 v208, 0
	v_mov_b32_e32 v209, 0
	v_mov_b32_e32 v210, 0
	v_mov_b32_e32 v211, 0
	v_cvt_pk_fp8_f32 v208, v170, v171
	v_cvt_pk_fp8_f32 v209, v174, v175
	v_cvt_pk_fp8_f32 v210, v196, v197
	v_cvt_pk_fp8_f32 v211, v200, v201
	v_cvt_pk_fp8_f32 v208, v172, v173 op_sel:[0,0,1]
	v_cvt_pk_fp8_f32 v209, v176, v177 op_sel:[0,0,1]
	v_cvt_pk_fp8_f32 v210, v198, v199 op_sel:[0,0,1]
	v_cvt_pk_fp8_f32 v211, v202, v203 op_sel:[0,0,1]
	s_nop 0
	global_store_dwordx4 v12, v[208:211], s[14:15]
	s_waitcnt vmcnt(32)
	v_mul_f32_e32 v100, 0x43000000, v100
	v_mul_f32_e32 v101, 0x43000000, v101
	v_mul_f32_e32 v102, 0x43000000, v102
	v_mul_f32_e32 v103, 0x43000000, v103
	ds_write_b128 v4, v[100:103]
	v_mul_f32_e32 v104, 0x43000000, v104
	v_mul_f32_e32 v105, 0x43000000, v105
	v_mul_f32_e32 v106, 0x43000000, v106
	v_mul_f32_e32 v107, 0x43000000, v107
	ds_write_b128 v4, v[104:107] offset:1024
	v_mul_f32_e32 v108, 0x43000000, v108
	v_mul_f32_e32 v109, 0x43000000, v109
	v_mul_f32_e32 v110, 0x43000000, v110
	v_mul_f32_e32 v111, 0x43000000, v111
	ds_write_b128 v4, v[108:111] offset:2048
	v_mul_f32_e32 v112, 0x43000000, v112
	v_mul_f32_e32 v113, 0x43000000, v113
	v_mul_f32_e32 v114, 0x43000000, v114
	v_mul_f32_e32 v115, 0x43000000, v115
	ds_write_b128 v4, v[112:115] offset:3072
	v_mul_f32_e32 v116, 0x43000000, v116
	v_mul_f32_e32 v117, 0x43000000, v117
	v_mul_f32_e32 v118, 0x43000000, v118
	v_mul_f32_e32 v119, 0x43000000, v119
	ds_write_b128 v4, v[116:119] offset:4096
	v_mul_f32_e32 v120, 0x43000000, v120
	v_mul_f32_e32 v121, 0x43000000, v121
	v_mul_f32_e32 v122, 0x43000000, v122
	v_mul_f32_e32 v123, 0x43000000, v123
	ds_write_b128 v4, v[120:123] offset:5120
	v_mul_f32_e32 v124, 0x43000000, v124
	v_mul_f32_e32 v125, 0x43000000, v125
	v_mul_f32_e32 v126, 0x43000000, v126
	v_mul_f32_e32 v127, 0x43000000, v127
	ds_write_b128 v4, v[124:127] offset:6144
	v_mul_f32_e32 v128, 0x43000000, v128
	v_mul_f32_e32 v129, 0x43000000, v129
	v_mul_f32_e32 v130, 0x43000000, v130
	v_mul_f32_e32 v131, 0x43000000, v131
	ds_write_b128 v4, v[128:131] offset:7168
	s_waitcnt lgkmcnt(0)
	s_barrier
; #define GAS __attribute__((address_space(1)))
; #define LAS __attribute__((address_space(3)))
; #define LDS_WAIT() asm volatile("s_waitcnt lgkmcnt(0)" ::: "memory")
; __device__ __forceinline__ unsigned pk4_fp8(float a, float b, float c, float d) {
;     a = fminf(fmaxf(a, -448.f), 448.f); b = fminf(fmaxf(b, -448.f), 448.f); c = fminf(fmaxf(c, -448.f), 448.f); d = fminf(fmaxf(d, -448.f), 448.f);
;     int w = __builtin_amdgcn_cvt_pk_fp8_f32(a, b, 0, false); w = __builtin_amdgcn_cvt_pk_fp8_f32(c, d, w, true); return (unsigned)w; }
;     const int pr = item >> 1, kb = 2 * (pr / nblk) + (item & 1), nb = pr % nblk, k0 = 64 * kb, n0 = 32 * nb;
;     const int nr = n0 + (lane & 31); const int sc = MAP == 1 ? src_col_in(nr) : nr;
;     float v[32];
; #pragma unroll
;     for (int i = 0; i < 32; ++i) v[i] = sc >= 0 ? W[(size_t)(k0 + 2 * i + (lane >> 5)) * Nsrc + sc] : 0.f;
; #pragma unroll
;     for (int i = 0; i < 32; ++i) { const int k = k0 + 2 * i + (lane >> 5); float x = v[i] * wscale; if (KS) x *= (k < ksplit ? ksA[k] : ksB[k - ksplit]); scr[(2 * i + (lane >> 5)) * 33 + (lane & 31)] = x; }
;     LDS_WAIT(); asm volatile("" ::: "memory");
;     const int c = lane & 7;
; #pragma unroll
;     for (int j = 0; j < 4; ++j) { const int n = (lane >> 3) + 8 * j; const LAS float* s = scr + (8 * c) * 33 + n;
;         const unsigned long long o = (unsigned long long)pg8::pk4_fp8(s[0 * 33], s[1 * 33], s[2 * 33], s[3 * 33]) | ((unsigned long long)pg8::pk4_fp8(s[4 * 33], s[5 * 33], s[6 * 33], s[7 * 33]) << 32);
;         *(GAS unsigned long long*)(WT + (size_t)(n0 + n) * K + k0 + 8 * c) = o; }
;     LDS_WAIT(); asm volatile("" ::: "memory");
	s_add_i32 s17, s16, 1344
	s_min_u32 s17, s17, 0xfff
	s_lshr_b32 s18, s17, 5
	s_add_i32 s18, s18, 0
	s_and_b32 s19, s17, 31
	s_lshl_b32 s18, s18, 21
	s_lshl_b32 s19, s19, 9
	s_add_u32 s18, s18, s19
	s_add_u32 s12, s2, s18
	s_addc_u32 s13, s3, 0
	global_load_dwordx4 v[100:103], v10, s[12:13]
	s_add_u32 s12, s12, 0x8000
	s_addc_u32 s13, s13, 0
	global_load_dwordx4 v[104:107], v10, s[12:13]
	s_add_u32 s12, s12, 0x8000
	s_addc_u32 s13, s13, 0
	global_load_dwordx4 v[108:111], v10, s[12:13]
	s_add_u32 s12, s12, 0x8000
	s_addc_u32 s13, s13, 0
	global_load_dwordx4 v[112:115], v10, s[12:13]
	s_add_u32 s12, s12, 0x8000
	s_addc_u32 s13, s13, 0
	global_load_dwordx4 v[116:119], v10, s[12:13]
	s_add_u32 s12, s12, 0x8000
	s_addc_u32 s13, s13, 0
	global_load_dwordx4 v[120:123], v10, s[12:13]
	s_add_u32 s12, s12, 0x8000
	s_addc_u32 s13, s13, 0
	global_load_dwordx4 v[124:127], v10, s[12:13]
	s_add_u32 s12, s12, 0x8000
	s_addc_u32 s13, s13, 0
	global_load_dwordx4 v[128:131], v10, s[12:13]
	s_add_i32 s17, s16, 960
	s_min_u32 s17, s17, 0xfff
	s_lshr_b32 s18, s17, 5
	s_add_i32 s18, s18, 0
	s_and_b32 s19, s17, 31
	s_lshl_b32 s19, s19, 21
	s_lshl_b32 s18, s18, 7
	s_add_u32 s18, s18, s19
	s_add_u32 s14, s4, s18
	s_addc_u32 s15, s5, 0
	ds_read_b32 v170, v6
	ds_read_b32 v171, v6 offset:512
	ds_read_b32 v172, v6 offset:1024
	ds_read_b32 v173, v6 offset:1536
	ds_read_b32 v174, v6 offset:2048
	ds_read_b32 v175, v6 offset:2560
	ds_read_b32 v176, v6 offset:3072
	ds_read_b32 v177, v6 offset:3584
	ds_read_b32 v196, v6 offset:4096
	ds_read_b32 v197, v6 offset:4608
	ds_read_b32 v198, v6 offset:5120
	ds_read_b32 v199, v6 offset:5632
	ds_read_b32 v200, v6 offset:6144
	ds_read_b32 v201, v6 offset:6656
	ds_read_b32 v202, v6 offset:7168
	ds_read_b32 v203, v6 offset:7680
	s_waitcnt lgkmcnt(0)
	v_max_f32_e32 v170, v170, v170
	v_max_f32_e32 v171, v171, v171
	v_max_f32_e32 v172, v172, v172
	v_max_f32_e32 v173, v173, v173
	v_max_f32_e32 v174, v174, v174
	v_max_f32_e32 v175, v175, v175
	v_max_f32_e32 v176, v176, v176
	v_max_f32_e32 v177, v177, v177
	v_max_f32_e32 v196, v196, v196
	v_max_f32_e32 v197, v197, v197
	v_max_f32_e32 v198, v198, v198
	v_max_f32_e32 v199, v199, v199
	v_max_f32_e32 v200, v200, v200
	v_max_f32_e32 v201, v201, v201
	v_max_f32_e32 v202, v202, v202
	v_max_f32_e32 v203, v203, v203
	v_med3_f32 v170, v170, s20, v13
	v_med3_f32 v171, v171, s20, v13
	v_med3_f32 v172, v172, s20, v13
	v_med3_f32 v173, v173, s20, v13
	v_med3_f32 v174, v174, s20, v13
	v_med3_f32 v175, v175, s20, v13
	v_med3_f32 v176, v176, s20, v13
	v_med3_f32 v177, v177, s20, v13
	v_med3_f32 v196, v196, s20, v13
	v_med3_f32 v197, v197, s20, v13
	v_med3_f32 v198, v198, s20, v13
	v_med3_f32 v199, v199, s20, v13
	v_med3_f32 v200, v200, s20, v13
	v_med3_f32 v201, v201, s20, v13
	v_med3_f32 v202, v202, s20, v13
	v_med3_f32 v203, v203, s20, v13
	v_mov_b32_e32 v208, 0
	v_mov_b32_e32 v209, 0
	v_mov_b32_e32 v210, 0
	v_mov_b32_e32 v211, 0
	v_cvt_pk_fp8_f32 v208, v170, v171
	v_cvt_pk_fp8_f32 v209, v174, v175
	v_cvt_pk_fp8_f32 v210, v196, v197
	v_cvt_pk_fp8_f32 v211, v200, v201
	v_cvt_pk_fp8_f32 v208, v172, v173 op_sel:[0,0,1]
	v_cvt_pk_fp8_f32 v209, v176, v177 op_sel:[0,0,1]
	v_cvt_pk_fp8_f32 v210, v198, v199 op_sel:[0,0,1]
	v_cvt_pk_fp8_f32 v211, v202, v203 op_sel:[0,0,1]
	s_nop 0
	global_store_dwordx4 v11, v[208:211], s[14:15]
	ds_read_b32 v170, v8
	ds_read_b32 v171, v8 offset:512
	ds_read_b32 v172, v8 offset:1024
	ds_read_b32 v173, v8 offset:1536
	ds_read_b32 v174, v8 offset:2048
	ds_read_b32 v175, v8 offset:2560
	ds_read_b32 v176, v8 offset:3072
	ds_read_b32 v177, v8 offset:3584
	ds_read_b32 v196, v8 offset:4096
	ds_read_b32 v197, v8 offset:4608
	ds_read_b32 v198, v8 offset:5120
	ds_read_b32 v199, v8 offset:5632
	ds_read_b32 v200, v8 offset:6144
	ds_read_b32 v201, v8 offset:6656
	ds_read_b32 v202, v8 offset:7168
	ds_read_b32 v203, v8 offset:7680
	s_waitcnt lgkmcnt(0)
	v_max_f32_e32 v170, v170, v170
	v_max_f32_e32 v171, v171, v171
	v_max_f32_e32 v172, v172, v172
	v_max_f32_e32 v173, v173, v173
	v_max_f32_e32 v174, v174, v174
	v_max_f32_e32 v175, v175, v175
	v_max_f32_e32 v176, v176, v176
	v_max_f32_e32 v177, v177, v177
	v_max_f32_e32 v196, v196, v196
	v_max_f32_e32 v197, v197, v197
	v_max_f32_e32 v198, v198, v198
	v_max_f32_e32 v199, v199, v199
	v_max_f32_e32 v200, v200, v200
	v_max_f32_e32 v201, v201, v201
	v_max_f32_e32 v202, v202, v202
	v_max_f32_e32 v203, v203, v203
	v_med3_f32 v170, v170, s20, v13
	v_med3_f32 v171, v171, s20, v13
	v_med3_f32 v172, v172, s20, v13
	v_med3_f32 v173, v173, s20, v13
	v_med3_f32 v174, v174, s20, v13
	v_med3_f32 v175, v175, s20, v13
	v_med3_f32 v176, v176, s20, v13
	v_med3_f32 v177, v177, s20, v13
	v_med3_f32 v196, v196, s20, v13
	v_med3_f32 v197, v197, s20, v13
	v_med3_f32 v198, v198, s20, v13
	v_med3_f32 v199, v199, s20, v13
	v_med3_f32 v200, v200, s20, v13
	v_med3_f32 v201, v201, s20, v13
	v_med3_f32 v202, v202, s20, v13
	v_med3_f32 v203, v203, s20, v13
	v_mov_b32_e32 v208, 0
	v_mov_b32_e32 v209, 0
	v_mov_b32_e32 v210, 0
	v_mov_b32_e32 v211, 0
	v_cvt_pk_fp8_f32 v208, v170, v171
	v_cvt_pk_fp8_f32 v209, v174, v175
	v_cvt_pk_fp8_f32 v210, v196, v197
	v_cvt_pk_fp8_f32 v211, v200, v201
	v_cvt_pk_fp8_f32 v208, v172, v173 op_sel:[0,0,1]
	v_cvt_pk_fp8_f32 v209, v176, v177 op_sel:[0,0,1]
	v_cvt_pk_fp8_f32 v210, v198, v199 op_sel:[0,0,1]
	v_cvt_pk_fp8_f32 v211, v202, v203 op_sel:[0,0,1]
	s_nop 0
	global_store_dwordx4 v12, v[208:211], s[14:15]
	s_waitcnt vmcnt(32)
	v_mul_f32_e32 v132, 0x43000000, v132
	v_mul_f32_e32 v133, 0x43000000, v133
	v_mul_f32_e32 v134, 0x43000000, v134
	v_mul_f32_e32 v135, 0x43000000, v135
	ds_write_b128 v5, v[132:135]
	v_mul_f32_e32 v136, 0x43000000, v136
	v_mul_f32_e32 v137, 0x43000000, v137
	v_mul_f32_e32 v138, 0x43000000, v138
	v_mul_f32_e32 v139, 0x43000000, v139
	ds_write_b128 v5, v[136:139] offset:1024
	v_mul_f32_e32 v140, 0x43000000, v140
	v_mul_f32_e32 v141, 0x43000000, v141
	v_mul_f32_e32 v142, 0x43000000, v142
	v_mul_f32_e32 v143, 0x43000000, v143
	ds_write_b128 v5, v[140:143] offset:2048
	v_mul_f32_e32 v144, 0x43000000, v144
	v_mul_f32_e32 v145, 0x43000000, v145
	v_mul_f32_e32 v146, 0x43000000, v146
	v_mul_f32_e32 v147, 0x43000000, v147
	ds_write_b128 v5, v[144:147] offset:3072
	v_mul_f32_e32 v148, 0x43000000, v148
	v_mul_f32_e32 v149, 0x43000000, v149
	v_mul_f32_e32 v150, 0x43000000, v150
	v_mul_f32_e32 v151, 0x43000000, v151
	ds_write_b128 v5, v[148:151] offset:4096
	v_mul_f32_e32 v152, 0x43000000, v152
	v_mul_f32_e32 v153, 0x43000000, v153
	v_mul_f32_e32 v154, 0x43000000, v154
	v_mul_f32_e32 v155, 0x43000000, v155
	ds_write_b128 v5, v[152:155] offset:5120
	v_mul_f32_e32 v156, 0x43000000, v156
	v_mul_f32_e32 v157, 0x43000000, v157
	v_mul_f32_e32 v158, 0x43000000, v158
	v_mul_f32_e32 v159, 0x43000000, v159
	ds_write_b128 v5, v[156:159] offset:6144
	v_mul_f32_e32 v160, 0x43000000, v160
	v_mul_f32_e32 v161, 0x43000000, v161
	v_mul_f32_e32 v162, 0x43000000, v162
	v_mul_f32_e32 v163, 0x43000000, v163
	ds_write_b128 v5, v[160:163] offset:7168
	s_waitcnt lgkmcnt(0)
	s_barrier
; #define GAS __attribute__((address_space(1)))
; #define LAS __attribute__((address_space(3)))
; #define LDS_WAIT() asm volatile("s_waitcnt lgkmcnt(0)" ::: "memory")
; __device__ __forceinline__ unsigned pk4_fp8(float a, float b, float c, float d) {
;     a = fminf(fmaxf(a, -448.f), 448.f); b = fminf(fmaxf(b, -448.f), 448.f); c = fminf(fmaxf(c, -448.f), 448.f); d = fminf(fmaxf(d, -448.f), 448.f);
;     int w = __builtin_amdgcn_cvt_pk_fp8_f32(a, b, 0, false); w = __builtin_amdgcn_cvt_pk_fp8_f32(c, d, w, true); return (unsigned)w; }
;     const int pr = item >> 1, kb = 2 * (pr / nblk) + (item & 1), nb = pr % nblk, k0 = 64 * kb, n0 = 32 * nb;
;     const int nr = n0 + (lane & 31); const int sc = MAP == 1 ? src_col_in(nr) : nr;
;     float v[32];
; #pragma unroll
;     for (int i = 0; i < 32; ++i) v[i] = sc >= 0 ? W[(size_t)(k0 + 2 * i + (lane >> 5)) * Nsrc + sc] : 0.f;
; #pragma unroll
;     for (int i = 0; i < 32; ++i) { const int k = k0 + 2 * i + (lane >> 5); float x = v[i] * wscale; if (KS) x *= (k < ksplit ? ksA[k] : ksB[k - ksplit]); scr[(2 * i + (lane >> 5)) * 33 + (lane & 31)] = x; }
;     LDS_WAIT(); asm volatile("" ::: "memory");
;     const int c = lane & 7;
; #pragma unroll
;     for (int j = 0; j < 4; ++j) { const int n = (lane >> 3) + 8 * j; const LAS float* s = scr + (8 * c) * 33 + n;
;         const unsigned long long o = (unsigned long long)pg8::pk4_fp8(s[0 * 33], s[1 * 33], s[2 * 33], s[3 * 33]) | ((unsigned long long)pg8::pk4_fp8(s[4 * 33], s[5 * 33], s[6 * 33], s[7 * 33]) << 32);
;         *(GAS unsigned long long*)(WT + (size_t)(n0 + n) * K + k0 + 8 * c) = o; }
;     LDS_WAIT(); asm volatile("" ::: "memory");
; }
	s_add_i32 s17, s16, 1440
	s_min_u32 s17, s17, 0xfff
	s_lshr_b32 s18, s17, 5
	s_add_i32 s18, s18, 0
	s_and_b32 s19, s17, 31
	s_lshl_b32 s18, s18, 21
	s_lshl_b32 s19, s19, 9
	s_add_u32 s18, s18, s19
	s_add_u32 s12, s2, s18
	s_addc_u32 s13, s3, 0
	global_load_dwordx4 v[132:135], v10, s[12:13]
	s_add_u32 s12, s12, 0x8000
	s_addc_u32 s13, s13, 0
	global_load_dwordx4 v[136:139], v10, s[12:13]
	s_add_u32 s12, s12, 0x8000
	s_addc_u32 s13, s13, 0
	global_load_dwordx4 v[140:143], v10, s[12:13]
	s_add_u32 s12, s12, 0x8000
	s_addc_u32 s13, s13, 0
	global_load_dwordx4 v[144:147], v10, s[12:13]
	s_add_u32 s12, s12, 0x8000
	s_addc_u32 s13, s13, 0
	global_load_dwordx4 v[148:151], v10, s[12:13]
	s_add_u32 s12, s12, 0x8000
	s_addc_u32 s13, s13, 0
	global_load_dwordx4 v[152:155], v10, s[12:13]
	s_add_u32 s12, s12, 0x8000
	s_addc_u32 s13, s13, 0
	global_load_dwordx4 v[156:159], v10, s[12:13]
	s_add_u32 s12, s12, 0x8000
	s_addc_u32 s13, s13, 0
	global_load_dwordx4 v[160:163], v10, s[12:13]
	s_add_i32 s17, s16, 1056
	s_min_u32 s17, s17, 0xfff
	s_lshr_b32 s18, s17, 5
	s_add_i32 s18, s18, 0
	s_and_b32 s19, s17, 31
	s_lshl_b32 s19, s19, 21
	s_lshl_b32 s18, s18, 7
	s_add_u32 s18, s18, s19
	s_add_u32 s14, s4, s18
	s_addc_u32 s15, s5, 0
	ds_read_b32 v170, v7
	ds_read_b32 v171, v7 offset:512
	ds_read_b32 v172, v7 offset:1024
	ds_read_b32 v173, v7 offset:1536
	ds_read_b32 v174, v7 offset:2048
	ds_read_b32 v175, v7 offset:2560
	ds_read_b32 v176, v7 offset:3072
	ds_read_b32 v177, v7 offset:3584
	ds_read_b32 v196, v7 offset:4096
	ds_read_b32 v197, v7 offset:4608
	ds_read_b32 v198, v7 offset:5120
	ds_read_b32 v199, v7 offset:5632
	ds_read_b32 v200, v7 offset:6144
	ds_read_b32 v201, v7 offset:6656
	ds_read_b32 v202, v7 offset:7168
	ds_read_b32 v203, v7 offset:7680
	s_waitcnt lgkmcnt(0)
	v_max_f32_e32 v170, v170, v170
	v_max_f32_e32 v171, v171, v171
	v_max_f32_e32 v172, v172, v172
	v_max_f32_e32 v173, v173, v173
	v_max_f32_e32 v174, v174, v174
	v_max_f32_e32 v175, v175, v175
	v_max_f32_e32 v176, v176, v176
	v_max_f32_e32 v177, v177, v177
	v_max_f32_e32 v196, v196, v196
	v_max_f32_e32 v197, v197, v197
	v_max_f32_e32 v198, v198, v198
	v_max_f32_e32 v199, v199, v199
	v_max_f32_e32 v200, v200, v200
	v_max_f32_e32 v201, v201, v201
	v_max_f32_e32 v202, v202, v202
	v_max_f32_e32 v203, v203, v203
	v_med3_f32 v170, v170, s20, v13
	v_med3_f32 v171, v171, s20, v13
	v_med3_f32 v172, v172, s20, v13
	v_med3_f32 v173, v173, s20, v13
	v_med3_f32 v174, v174, s20, v13
	v_med3_f32 v175, v175, s20, v13
	v_med3_f32 v176, v176, s20, v13
	v_med3_f32 v177, v177, s20, v13
	v_med3_f32 v196, v196, s20, v13
	v_med3_f32 v197, v197, s20, v13
	v_med3_f32 v198, v198, s20, v13
	v_med3_f32 v199, v199, s20, v13
	v_med3_f32 v200, v200, s20, v13
	v_med3_f32 v201, v201, s20, v13
	v_med3_f32 v202, v202, s20, v13
	v_med3_f32 v203, v203, s20, v13
	v_mov_b32_e32 v208, 0
	v_mov_b32_e32 v209, 0
	v_mov_b32_e32 v210, 0
	v_mov_b32_e32 v211, 0
	v_cvt_pk_fp8_f32 v208, v170, v171
	v_cvt_pk_fp8_f32 v209, v174, v175
	v_cvt_pk_fp8_f32 v210, v196, v197
	v_cvt_pk_fp8_f32 v211, v200, v201
	v_cvt_pk_fp8_f32 v208, v172, v173 op_sel:[0,0,1]
	v_cvt_pk_fp8_f32 v209, v176, v177 op_sel:[0,0,1]
	v_cvt_pk_fp8_f32 v210, v198, v199 op_sel:[0,0,1]
	v_cvt_pk_fp8_f32 v211, v202, v203 op_sel:[0,0,1]
	s_nop 0
	global_store_dwordx4 v11, v[208:211], s[14:15]
	ds_read_b32 v170, v9
	ds_read_b32 v171, v9 offset:512
	ds_read_b32 v172, v9 offset:1024
	ds_read_b32 v173, v9 offset:1536
	ds_read_b32 v174, v9 offset:2048
	ds_read_b32 v175, v9 offset:2560
	ds_read_b32 v176, v9 offset:3072
	ds_read_b32 v177, v9 offset:3584
	ds_read_b32 v196, v9 offset:4096
	ds_read_b32 v197, v9 offset:4608
	ds_read_b32 v198, v9 offset:5120
	ds_read_b32 v199, v9 offset:5632
	ds_read_b32 v200, v9 offset:6144
	ds_read_b32 v201, v9 offset:6656
	ds_read_b32 v202, v9 offset:7168
	ds_read_b32 v203, v9 offset:7680
	s_waitcnt lgkmcnt(0)
	v_max_f32_e32 v170, v170, v170
	v_max_f32_e32 v171, v171, v171
	v_max_f32_e32 v172, v172, v172
	v_max_f32_e32 v173, v173, v173
	v_max_f32_e32 v174, v174, v174
	v_max_f32_e32 v175, v175, v175
	v_max_f32_e32 v176, v176, v176
	v_max_f32_e32 v177, v177, v177
	v_max_f32_e32 v196, v196, v196
	v_max_f32_e32 v197, v197, v197
	v_max_f32_e32 v198, v198, v198
	v_max_f32_e32 v199, v199, v199
	v_max_f32_e32 v200, v200, v200
	v_max_f32_e32 v201, v201, v201
	v_max_f32_e32 v202, v202, v202
	v_max_f32_e32 v203, v203, v203
	v_med3_f32 v170, v170, s20, v13
	v_med3_f32 v171, v171, s20, v13
	v_med3_f32 v172, v172, s20, v13
	v_med3_f32 v173, v173, s20, v13
	v_med3_f32 v174, v174, s20, v13
	v_med3_f32 v175, v175, s20, v13
	v_med3_f32 v176, v176, s20, v13
	v_med3_f32 v177, v177, s20, v13
	v_med3_f32 v196, v196, s20, v13
	v_med3_f32 v197, v197, s20, v13
	v_med3_f32 v198, v198, s20, v13
	v_med3_f32 v199, v199, s20, v13
	v_med3_f32 v200, v200, s20, v13
	v_med3_f32 v201, v201, s20, v13
	v_med3_f32 v202, v202, s20, v13
	v_med3_f32 v203, v203, s20, v13
	v_mov_b32_e32 v208, 0
	v_mov_b32_e32 v209, 0
	v_mov_b32_e32 v210, 0
	v_mov_b32_e32 v211, 0
	v_cvt_pk_fp8_f32 v208, v170, v171
	v_cvt_pk_fp8_f32 v209, v174, v175
	v_cvt_pk_fp8_f32 v210, v196, v197
	v_cvt_pk_fp8_f32 v211, v200, v201
	v_cvt_pk_fp8_f32 v208, v172, v173 op_sel:[0,0,1]
	v_cvt_pk_fp8_f32 v209, v176, v177 op_sel:[0,0,1]
	v_cvt_pk_fp8_f32 v210, v198, v199 op_sel:[0,0,1]
	v_cvt_pk_fp8_f32 v211, v202, v203 op_sel:[0,0,1]
	s_nop 0
	global_store_dwordx4 v12, v[208:211], s[14:15]
	s_waitcnt vmcnt(32)
	v_mul_f32_e32 v36, 0x43000000, v36
	v_mul_f32_e32 v37, 0x43000000, v37
	v_mul_f32_e32 v38, 0x43000000, v38
	v_mul_f32_e32 v39, 0x43000000, v39
	ds_write_b128 v4, v[36:39]
	v_mul_f32_e32 v40, 0x43000000, v40
	v_mul_f32_e32 v41, 0x43000000, v41
	v_mul_f32_e32 v42, 0x43000000, v42
	v_mul_f32_e32 v43, 0x43000000, v43
	ds_write_b128 v4, v[40:43] offset:1024
	v_mul_f32_e32 v44, 0x43000000, v44
	v_mul_f32_e32 v45, 0x43000000, v45
	v_mul_f32_e32 v46, 0x43000000, v46
	v_mul_f32_e32 v47, 0x43000000, v47
	ds_write_b128 v4, v[44:47] offset:2048
	v_mul_f32_e32 v48, 0x43000000, v48
	v_mul_f32_e32 v49, 0x43000000, v49
	v_mul_f32_e32 v50, 0x43000000, v50
	v_mul_f32_e32 v51, 0x43000000, v51
	ds_write_b128 v4, v[48:51] offset:3072
	v_mul_f32_e32 v52, 0x43000000, v52
	v_mul_f32_e32 v53, 0x43000000, v53
	v_mul_f32_e32 v54, 0x43000000, v54
	v_mul_f32_e32 v55, 0x43000000, v55
	ds_write_b128 v4, v[52:55] offset:4096
	v_mul_f32_e32 v56, 0x43000000, v56
	v_mul_f32_e32 v57, 0x43000000, v57
	v_mul_f32_e32 v58, 0x43000000, v58
	v_mul_f32_e32 v59, 0x43000000, v59
	ds_write_b128 v4, v[56:59] offset:5120
	v_mul_f32_e32 v60, 0x43000000, v60
	v_mul_f32_e32 v61, 0x43000000, v61
	v_mul_f32_e32 v62, 0x43000000, v62
	v_mul_f32_e32 v63, 0x43000000, v63
	ds_write_b128 v4, v[60:63] offset:6144
	v_mul_f32_e32 v64, 0x43000000, v64
	v_mul_f32_e32 v65, 0x43000000, v65
	v_mul_f32_e32 v66, 0x43000000, v66
	v_mul_f32_e32 v67, 0x43000000, v67
	ds_write_b128 v4, v[64:67] offset:7168
	s_waitcnt lgkmcnt(0)
	s_barrier
; #define GAS __attribute__((address_space(1)))
; #define LAS __attribute__((address_space(3)))
; #define LDS_WAIT() asm volatile("s_waitcnt lgkmcnt(0)" ::: "memory")
; __device__ __forceinline__ unsigned pk4_fp8(float a, float b, float c, float d) {
;     a = fminf(fmaxf(a, -448.f), 448.f); b = fminf(fmaxf(b, -448.f), 448.f); c = fminf(fmaxf(c, -448.f), 448.f); d = fminf(fmaxf(d, -448.f), 448.f);
;     int w = __builtin_amdgcn_cvt_pk_fp8_f32(a, b, 0, false); w = __builtin_amdgcn_cvt_pk_fp8_f32(c, d, w, true); return (unsigned)w; }
;     const int pr = item >> 1, kb = 2 * (pr / nblk) + (item & 1), nb = pr % nblk, k0 = 64 * kb, n0 = 32 * nb;
;     const int nr = n0 + (lane & 31); const int sc = MAP == 1 ? src_col_in(nr) : nr;
;     float v[32];
; #pragma unroll
;     for (int i = 0; i < 32; ++i) v[i] = sc >= 0 ? W[(size_t)(k0 + 2 * i + (lane >> 5)) * Nsrc + sc] : 0.f;
; #pragma unroll
;     for (int i = 0; i < 32; ++i) { const int k = k0 + 2 * i + (lane >> 5); float x = v[i] * wscale; if (KS) x *= (k < ksplit ? ksA[k] : ksB[k - ksplit]); scr[(2 * i + (lane >> 5)) * 33 + (lane & 31)] = x; }
;     LDS_WAIT(); asm volatile("" ::: "memory");
;     const int c = lane & 7;
; #pragma unroll
;     for (int j = 0; j < 4; ++j) { const int n = (lane >> 3) + 8 * j; const LAS float* s = scr + (8 * c) * 33 + n;
;         const unsigned long long o = (unsigned long long)pg8::pk4_fp8(s[0 * 33], s[1 * 33], s[2 * 33], s[3 * 33]) | ((unsigned long long)pg8::pk4_fp8(s[4 * 33], s[5 * 33], s[6 * 33], s[7 * 33]) << 32);
;         *(GAS unsigned long long*)(WT + (size_t)(n0 + n) * K + k0 + 8 * c) = o; }
;     LDS_WAIT(); asm volatile("" ::: "memory");
; }
	s_add_i32 s17, s16, 1536
	s_min_u32 s17, s17, 0xfff
	s_lshr_b32 s18, s17, 5
	s_add_i32 s18, s18, 0
	s_and_b32 s19, s17, 31
	s_lshl_b32 s18, s18, 21
	s_lshl_b32 s19, s19, 9
	s_add_u32 s18, s18, s19
	s_add_u32 s12, s2, s18
	s_addc_u32 s13, s3, 0
	global_load_dwordx4 v[36:39], v10, s[12:13]
	s_add_u32 s12, s12, 0x8000
	s_addc_u32 s13, s13, 0
	global_load_dwordx4 v[40:43], v10, s[12:13]
	s_add_u32 s12, s12, 0x8000
	s_addc_u32 s13, s13, 0
	global_load_dwordx4 v[44:47], v10, s[12:13]
	s_add_u32 s12, s12, 0x8000
	s_addc_u32 s13, s13, 0
	global_load_dwordx4 v[48:51], v10, s[12:13]
	s_add_u32 s12, s12, 0x8000
	s_addc_u32 s13, s13, 0
	global_load_dwordx4 v[52:55], v10, s[12:13]
	s_add_u32 s12, s12, 0x8000
	s_addc_u32 s13, s13, 0
	global_load_dwordx4 v[56:59], v10, s[12:13]
	s_add_u32 s12, s12, 0x8000
	s_addc_u32 s13, s13, 0
	global_load_dwordx4 v[60:63], v10, s[12:13]
	s_add_u32 s12, s12, 0x8000
	s_addc_u32 s13, s13, 0
	global_load_dwordx4 v[64:67], v10, s[12:13]
	s_add_i32 s17, s16, 1152
	s_min_u32 s17, s17, 0xfff
	s_lshr_b32 s18, s17, 5
	s_add_i32 s18, s18, 0
	s_and_b32 s19, s17, 31
	s_lshl_b32 s19, s19, 21
	s_lshl_b32 s18, s18, 7
	s_add_u32 s18, s18, s19
	s_add_u32 s14, s4, s18
	s_addc_u32 s15, s5, 0
	ds_read_b32 v170, v6
	ds_read_b32 v171, v6 offset:512
	ds_read_b32 v172, v6 offset:1024
	ds_read_b32 v173, v6 offset:1536
	ds_read_b32 v174, v6 offset:2048
	ds_read_b32 v175, v6 offset:2560
	ds_read_b32 v176, v6 offset:3072
	ds_read_b32 v177, v6 offset:3584
	ds_read_b32 v196, v6 offset:4096
	ds_read_b32 v197, v6 offset:4608
	ds_read_b32 v198, v6 offset:5120
	ds_read_b32 v199, v6 offset:5632
	ds_read_b32 v200, v6 offset:6144
	ds_read_b32 v201, v6 offset:6656
	ds_read_b32 v202, v6 offset:7168
	ds_read_b32 v203, v6 offset:7680
	s_waitcnt lgkmcnt(0)
	v_max_f32_e32 v170, v170, v170
	v_max_f32_e32 v171, v171, v171
	v_max_f32_e32 v172, v172, v172
	v_max_f32_e32 v173, v173, v173
	v_max_f32_e32 v174, v174, v174
	v_max_f32_e32 v175, v175, v175
	v_max_f32_e32 v176, v176, v176
	v_max_f32_e32 v177, v177, v177
	v_max_f32_e32 v196, v196, v196
	v_max_f32_e32 v197, v197, v197
	v_max_f32_e32 v198, v198, v198
	v_max_f32_e32 v199, v199, v199
	v_max_f32_e32 v200, v200, v200
	v_max_f32_e32 v201, v201, v201
	v_max_f32_e32 v202, v202, v202
	v_max_f32_e32 v203, v203, v203
	v_med3_f32 v170, v170, s20, v13
	v_med3_f32 v171, v171, s20, v13
	v_med3_f32 v172, v172, s20, v13
	v_med3_f32 v173, v173, s20, v13
	v_med3_f32 v174, v174, s20, v13
	v_med3_f32 v175, v175, s20, v13
	v_med3_f32 v176, v176, s20, v13
	v_med3_f32 v177, v177, s20, v13
	v_med3_f32 v196, v196, s20, v13
	v_med3_f32 v197, v197, s20, v13
	v_med3_f32 v198, v198, s20, v13
	v_med3_f32 v199, v199, s20, v13
	v_med3_f32 v200, v200, s20, v13
	v_med3_f32 v201, v201, s20, v13
	v_med3_f32 v202, v202, s20, v13
	v_med3_f32 v203, v203, s20, v13
	v_mov_b32_e32 v208, 0
	v_mov_b32_e32 v209, 0
	v_mov_b32_e32 v210, 0
	v_mov_b32_e32 v211, 0
	v_cvt_pk_fp8_f32 v208, v170, v171
	v_cvt_pk_fp8_f32 v209, v174, v175
	v_cvt_pk_fp8_f32 v210, v196, v197
	v_cvt_pk_fp8_f32 v211, v200, v201
	v_cvt_pk_fp8_f32 v208, v172, v173 op_sel:[0,0,1]
	v_cvt_pk_fp8_f32 v209, v176, v177 op_sel:[0,0,1]
	v_cvt_pk_fp8_f32 v210, v198, v199 op_sel:[0,0,1]
	v_cvt_pk_fp8_f32 v211, v202, v203 op_sel:[0,0,1]
	s_nop 0
	global_store_dwordx4 v11, v[208:211], s[14:15]
	ds_read_b32 v170, v8
	ds_read_b32 v171, v8 offset:512
	ds_read_b32 v172, v8 offset:1024
	ds_read_b32 v173, v8 offset:1536
	ds_read_b32 v174, v8 offset:2048
	ds_read_b32 v175, v8 offset:2560
	ds_read_b32 v176, v8 offset:3072
	ds_read_b32 v177, v8 offset:3584
	ds_read_b32 v196, v8 offset:4096
	ds_read_b32 v197, v8 offset:4608
	ds_read_b32 v198, v8 offset:5120
	ds_read_b32 v199, v8 offset:5632
	ds_read_b32 v200, v8 offset:6144
	ds_read_b32 v201, v8 offset:6656
	ds_read_b32 v202, v8 offset:7168
	ds_read_b32 v203, v8 offset:7680
	s_waitcnt lgkmcnt(0)
	v_max_f32_e32 v170, v170, v170
	v_max_f32_e32 v171, v171, v171
	v_max_f32_e32 v172, v172, v172
	v_max_f32_e32 v173, v173, v173
	v_max_f32_e32 v174, v174, v174
	v_max_f32_e32 v175, v175, v175
	v_max_f32_e32 v176, v176, v176
	v_max_f32_e32 v177, v177, v177
	v_max_f32_e32 v196, v196, v196
	v_max_f32_e32 v197, v197, v197
	v_max_f32_e32 v198, v198, v198
	v_max_f32_e32 v199, v199, v199
	v_max_f32_e32 v200, v200, v200
	v_max_f32_e32 v201, v201, v201
	v_max_f32_e32 v202, v202, v202
	v_max_f32_e32 v203, v203, v203
	v_med3_f32 v170, v170, s20, v13
	v_med3_f32 v171, v171, s20, v13
	v_med3_f32 v172, v172, s20, v13
	v_med3_f32 v173, v173, s20, v13
	v_med3_f32 v174, v174, s20, v13
	v_med3_f32 v175, v175, s20, v13
	v_med3_f32 v176, v176, s20, v13
	v_med3_f32 v177, v177, s20, v13
	v_med3_f32 v196, v196, s20, v13
	v_med3_f32 v197, v197, s20, v13
	v_med3_f32 v198, v198, s20, v13
	v_med3_f32 v199, v199, s20, v13
	v_med3_f32 v200, v200, s20, v13
	v_med3_f32 v201, v201, s20, v13
	v_med3_f32 v202, v202, s20, v13
	v_med3_f32 v203, v203, s20, v13
	v_mov_b32_e32 v208, 0
	v_mov_b32_e32 v209, 0
	v_mov_b32_e32 v210, 0
	v_mov_b32_e32 v211, 0
	v_cvt_pk_fp8_f32 v208, v170, v171
	v_cvt_pk_fp8_f32 v209, v174, v175
	v_cvt_pk_fp8_f32 v210, v196, v197
	v_cvt_pk_fp8_f32 v211, v200, v201
	v_cvt_pk_fp8_f32 v208, v172, v173 op_sel:[0,0,1]
	v_cvt_pk_fp8_f32 v209, v176, v177 op_sel:[0,0,1]
	v_cvt_pk_fp8_f32 v210, v198, v199 op_sel:[0,0,1]
	v_cvt_pk_fp8_f32 v211, v202, v203 op_sel:[0,0,1]
	s_nop 0
	global_store_dwordx4 v12, v[208:211], s[14:15]
	s_waitcnt vmcnt(32)
	v_mul_f32_e32 v68, 0x43000000, v68
	v_mul_f32_e32 v69, 0x43000000, v69
	v_mul_f32_e32 v70, 0x43000000, v70
	v_mul_f32_e32 v71, 0x43000000, v71
	ds_write_b128 v5, v[68:71]
	v_mul_f32_e32 v72, 0x43000000, v72
	v_mul_f32_e32 v73, 0x43000000, v73
	v_mul_f32_e32 v74, 0x43000000, v74
	v_mul_f32_e32 v75, 0x43000000, v75
	ds_write_b128 v5, v[72:75] offset:1024
	v_mul_f32_e32 v76, 0x43000000, v76
	v_mul_f32_e32 v77, 0x43000000, v77
	v_mul_f32_e32 v78, 0x43000000, v78
	v_mul_f32_e32 v79, 0x43000000, v79
	ds_write_b128 v5, v[76:79] offset:2048
	v_mul_f32_e32 v80, 0x43000000, v80
	v_mul_f32_e32 v81, 0x43000000, v81
	v_mul_f32_e32 v82, 0x43000000, v82
	v_mul_f32_e32 v83, 0x43000000, v83
	ds_write_b128 v5, v[80:83] offset:3072
	v_mul_f32_e32 v84, 0x43000000, v84
	v_mul_f32_e32 v85, 0x43000000, v85
	v_mul_f32_e32 v86, 0x43000000, v86
	v_mul_f32_e32 v87, 0x43000000, v87
	ds_write_b128 v5, v[84:87] offset:4096
	v_mul_f32_e32 v88, 0x43000000, v88
	v_mul_f32_e32 v89, 0x43000000, v89
	v_mul_f32_e32 v90, 0x43000000, v90
	v_mul_f32_e32 v91, 0x43000000, v91
	ds_write_b128 v5, v[88:91] offset:5120
	v_mul_f32_e32 v92, 0x43000000, v92
	v_mul_f32_e32 v93, 0x43000000, v93
	v_mul_f32_e32 v94, 0x43000000, v94
	v_mul_f32_e32 v95, 0x43000000, v95
	ds_write_b128 v5, v[92:95] offset:6144
	v_mul_f32_e32 v96, 0x43000000, v96
	v_mul_f32_e32 v97, 0x43000000, v97
	v_mul_f32_e32 v98, 0x43000000, v98
	v_mul_f32_e32 v99, 0x43000000, v99
	ds_write_b128 v5, v[96:99] offset:7168
	s_waitcnt lgkmcnt(0)
	s_barrier
; #define GAS __attribute__((address_space(1)))
; #define LAS __attribute__((address_space(3)))
; #define LDS_WAIT() asm volatile("s_waitcnt lgkmcnt(0)" ::: "memory")
; __device__ __forceinline__ unsigned pk4_fp8(float a, float b, float c, float d) {
;     a = fminf(fmaxf(a, -448.f), 448.f); b = fminf(fmaxf(b, -448.f), 448.f); c = fminf(fmaxf(c, -448.f), 448.f); d = fminf(fmaxf(d, -448.f), 448.f);
;     int w = __builtin_amdgcn_cvt_pk_fp8_f32(a, b, 0, false); w = __builtin_amdgcn_cvt_pk_fp8_f32(c, d, w, true); return (unsigned)w; }
;     const int pr = item >> 1, kb = 2 * (pr / nblk) + (item & 1), nb = pr % nblk, k0 = 64 * kb, n0 = 32 * nb;
;     const int nr = n0 + (lane & 31); const int sc = MAP == 1 ? src_col_in(nr) : nr;
;     float v[32];
; #pragma unroll
;     for (int i = 0; i < 32; ++i) v[i] = sc >= 0 ? W[(size_t)(k0 + 2 * i + (lane >> 5)) * Nsrc + sc] : 0.f;
; #pragma unroll
;     for (int i = 0; i < 32; ++i) { const int k = k0 + 2 * i + (lane >> 5); float x = v[i] * wscale; if (KS) x *= (k < ksplit ? ksA[k] : ksB[k - ksplit]); scr[(2 * i + (lane >> 5)) * 33 + (lane & 31)] = x; }
;     LDS_WAIT(); asm volatile("" ::: "memory");
;     const int c = lane & 7;
; #pragma unroll
;     for (int j = 0; j < 4; ++j) { const int n = (lane >> 3) + 8 * j; const LAS float* s = scr + (8 * c) * 33 + n;
;         const unsigned long long o = (unsigned long long)pg8::pk4_fp8(s[0 * 33], s[1 * 33], s[2 * 33], s[3 * 33]) | ((unsigned long long)pg8::pk4_fp8(s[4 * 33], s[5 * 33], s[6 * 33], s[7 * 33]) << 32);
;         *(GAS unsigned long long*)(WT + (size_t)(n0 + n) * K + k0 + 8 * c) = o; }
;     LDS_WAIT(); asm volatile("" ::: "memory");
; }
	s_add_i32 s17, s16, 1632
	s_min_u32 s17, s17, 0xfff
	s_lshr_b32 s18, s17, 5
	s_add_i32 s18, s18, 0
	s_and_b32 s19, s17, 31
	s_lshl_b32 s18, s18, 21
	s_lshl_b32 s19, s19, 9
	s_add_u32 s18, s18, s19
	s_add_u32 s12, s2, s18
	s_addc_u32 s13, s3, 0
	global_load_dwordx4 v[68:71], v10, s[12:13]
	s_add_u32 s12, s12, 0x8000
	s_addc_u32 s13, s13, 0
	global_load_dwordx4 v[72:75], v10, s[12:13]
	s_add_u32 s12, s12, 0x8000
	s_addc_u32 s13, s13, 0
	global_load_dwordx4 v[76:79], v10, s[12:13]
	s_add_u32 s12, s12, 0x8000
	s_addc_u32 s13, s13, 0
	global_load_dwordx4 v[80:83], v10, s[12:13]
	s_add_u32 s12, s12, 0x8000
	s_addc_u32 s13, s13, 0
	global_load_dwordx4 v[84:87], v10, s[12:13]
	s_add_u32 s12, s12, 0x8000
	s_addc_u32 s13, s13, 0
	global_load_dwordx4 v[88:91], v10, s[12:13]
	s_add_u32 s12, s12, 0x8000
	s_addc_u32 s13, s13, 0
	global_load_dwordx4 v[92:95], v10, s[12:13]
	s_add_u32 s12, s12, 0x8000
	s_addc_u32 s13, s13, 0
	global_load_dwordx4 v[96:99], v10, s[12:13]
	s_add_i32 s17, s16, 1248
	s_min_u32 s17, s17, 0xfff
	s_lshr_b32 s18, s17, 5
	s_add_i32 s18, s18, 0
	s_and_b32 s19, s17, 31
	s_lshl_b32 s19, s19, 21
	s_lshl_b32 s18, s18, 7
	s_add_u32 s18, s18, s19
	s_add_u32 s14, s4, s18
	s_addc_u32 s15, s5, 0
	ds_read_b32 v170, v7
	ds_read_b32 v171, v7 offset:512
	ds_read_b32 v172, v7 offset:1024
	ds_read_b32 v173, v7 offset:1536
	ds_read_b32 v174, v7 offset:2048
	ds_read_b32 v175, v7 offset:2560
	ds_read_b32 v176, v7 offset:3072
	ds_read_b32 v177, v7 offset:3584
	ds_read_b32 v196, v7 offset:4096
	ds_read_b32 v197, v7 offset:4608
	ds_read_b32 v198, v7 offset:5120
	ds_read_b32 v199, v7 offset:5632
	ds_read_b32 v200, v7 offset:6144
	ds_read_b32 v201, v7 offset:6656
	ds_read_b32 v202, v7 offset:7168
	ds_read_b32 v203, v7 offset:7680
	s_waitcnt lgkmcnt(0)
	v_max_f32_e32 v170, v170, v170
	v_max_f32_e32 v171, v171, v171
	v_max_f32_e32 v172, v172, v172
	v_max_f32_e32 v173, v173, v173
	v_max_f32_e32 v174, v174, v174
	v_max_f32_e32 v175, v175, v175
	v_max_f32_e32 v176, v176, v176
	v_max_f32_e32 v177, v177, v177
	v_max_f32_e32 v196, v196, v196
	v_max_f32_e32 v197, v197, v197
	v_max_f32_e32 v198, v198, v198
	v_max_f32_e32 v199, v199, v199
	v_max_f32_e32 v200, v200, v200
	v_max_f32_e32 v201, v201, v201
	v_max_f32_e32 v202, v202, v202
	v_max_f32_e32 v203, v203, v203
	v_med3_f32 v170, v170, s20, v13
	v_med3_f32 v171, v171, s20, v13
	v_med3_f32 v172, v172, s20, v13
	v_med3_f32 v173, v173, s20, v13
	v_med3_f32 v174, v174, s20, v13
	v_med3_f32 v175, v175, s20, v13
	v_med3_f32 v176, v176, s20, v13
	v_med3_f32 v177, v177, s20, v13
	v_med3_f32 v196, v196, s20, v13
	v_med3_f32 v197, v197, s20, v13
	v_med3_f32 v198, v198, s20, v13
	v_med3_f32 v199, v199, s20, v13
	v_med3_f32 v200, v200, s20, v13
	v_med3_f32 v201, v201, s20, v13
	v_med3_f32 v202, v202, s20, v13
	v_med3_f32 v203, v203, s20, v13
	v_mov_b32_e32 v208, 0
	v_mov_b32_e32 v209, 0
	v_mov_b32_e32 v210, 0
	v_mov_b32_e32 v211, 0
	v_cvt_pk_fp8_f32 v208, v170, v171
	v_cvt_pk_fp8_f32 v209, v174, v175
	v_cvt_pk_fp8_f32 v210, v196, v197
	v_cvt_pk_fp8_f32 v211, v200, v201
	v_cvt_pk_fp8_f32 v208, v172, v173 op_sel:[0,0,1]
	v_cvt_pk_fp8_f32 v209, v176, v177 op_sel:[0,0,1]
	v_cvt_pk_fp8_f32 v210, v198, v199 op_sel:[0,0,1]
	v_cvt_pk_fp8_f32 v211, v202, v203 op_sel:[0,0,1]
	s_nop 0
	global_store_dwordx4 v11, v[208:211], s[14:15]
	ds_read_b32 v170, v9
	ds_read_b32 v171, v9 offset:512
	ds_read_b32 v172, v9 offset:1024
	ds_read_b32 v173, v9 offset:1536
	ds_read_b32 v174, v9 offset:2048
	ds_read_b32 v175, v9 offset:2560
	ds_read_b32 v176, v9 offset:3072
	ds_read_b32 v177, v9 offset:3584
	ds_read_b32 v196, v9 offset:4096
	ds_read_b32 v197, v9 offset:4608
	ds_read_b32 v198, v9 offset:5120
	ds_read_b32 v199, v9 offset:5632
	ds_read_b32 v200, v9 offset:6144
	ds_read_b32 v201, v9 offset:6656
	ds_read_b32 v202, v9 offset:7168
	ds_read_b32 v203, v9 offset:7680
	s_waitcnt lgkmcnt(0)
	v_max_f32_e32 v170, v170, v170
	v_max_f32_e32 v171, v171, v171
	v_max_f32_e32 v172, v172, v172
	v_max_f32_e32 v173, v173, v173
	v_max_f32_e32 v174, v174, v174
	v_max_f32_e32 v175, v175, v175
	v_max_f32_e32 v176, v176, v176
	v_max_f32_e32 v177, v177, v177
	v_max_f32_e32 v196, v196, v196
	v_max_f32_e32 v197, v197, v197
	v_max_f32_e32 v198, v198, v198
	v_max_f32_e32 v199, v199, v199
	v_max_f32_e32 v200, v200, v200
	v_max_f32_e32 v201, v201, v201
	v_max_f32_e32 v202, v202, v202
	v_max_f32_e32 v203, v203, v203
	v_med3_f32 v170, v170, s20, v13
	v_med3_f32 v171, v171, s20, v13
	v_med3_f32 v172, v172, s20, v13
	v_med3_f32 v173, v173, s20, v13
	v_med3_f32 v174, v174, s20, v13
	v_med3_f32 v175, v175, s20, v13
	v_med3_f32 v176, v176, s20, v13
	v_med3_f32 v177, v177, s20, v13
	v_med3_f32 v196, v196, s20, v13
	v_med3_f32 v197, v197, s20, v13
	v_med3_f32 v198, v198, s20, v13
	v_med3_f32 v199, v199, s20, v13
	v_med3_f32 v200, v200, s20, v13
	v_med3_f32 v201, v201, s20, v13
	v_med3_f32 v202, v202, s20, v13
	v_med3_f32 v203, v203, s20, v13
	v_mov_b32_e32 v208, 0
	v_mov_b32_e32 v209, 0
	v_mov_b32_e32 v210, 0
	v_mov_b32_e32 v211, 0
	v_cvt_pk_fp8_f32 v208, v170, v171
	v_cvt_pk_fp8_f32 v209, v174, v175
	v_cvt_pk_fp8_f32 v210, v196, v197
	v_cvt_pk_fp8_f32 v211, v200, v201
	v_cvt_pk_fp8_f32 v208, v172, v173 op_sel:[0,0,1]
	v_cvt_pk_fp8_f32 v209, v176, v177 op_sel:[0,0,1]
	v_cvt_pk_fp8_f32 v210, v198, v199 op_sel:[0,0,1]
	v_cvt_pk_fp8_f32 v211, v202, v203 op_sel:[0,0,1]
	s_nop 0
	global_store_dwordx4 v12, v[208:211], s[14:15]
	s_waitcnt vmcnt(32)
	v_mul_f32_e32 v100, 0x43000000, v100
	v_mul_f32_e32 v101, 0x43000000, v101
	v_mul_f32_e32 v102, 0x43000000, v102
	v_mul_f32_e32 v103, 0x43000000, v103
	ds_write_b128 v4, v[100:103]
	v_mul_f32_e32 v104, 0x43000000, v104
	v_mul_f32_e32 v105, 0x43000000, v105
	v_mul_f32_e32 v106, 0x43000000, v106
	v_mul_f32_e32 v107, 0x43000000, v107
	ds_write_b128 v4, v[104:107] offset:1024
	v_mul_f32_e32 v108, 0x43000000, v108
	v_mul_f32_e32 v109, 0x43000000, v109
	v_mul_f32_e32 v110, 0x43000000, v110
	v_mul_f32_e32 v111, 0x43000000, v111
	ds_write_b128 v4, v[108:111] offset:2048
	v_mul_f32_e32 v112, 0x43000000, v112
	v_mul_f32_e32 v113, 0x43000000, v113
	v_mul_f32_e32 v114, 0x43000000, v114
	v_mul_f32_e32 v115, 0x43000000, v115
	ds_write_b128 v4, v[112:115] offset:3072
	v_mul_f32_e32 v116, 0x43000000, v116
	v_mul_f32_e32 v117, 0x43000000, v117
	v_mul_f32_e32 v118, 0x43000000, v118
	v_mul_f32_e32 v119, 0x43000000, v119
	ds_write_b128 v4, v[116:119] offset:4096
	v_mul_f32_e32 v120, 0x43000000, v120
	v_mul_f32_e32 v121, 0x43000000, v121
	v_mul_f32_e32 v122, 0x43000000, v122
	v_mul_f32_e32 v123, 0x43000000, v123
	ds_write_b128 v4, v[120:123] offset:5120
	v_mul_f32_e32 v124, 0x43000000, v124
	v_mul_f32_e32 v125, 0x43000000, v125
	v_mul_f32_e32 v126, 0x43000000, v126
	v_mul_f32_e32 v127, 0x43000000, v127
	ds_write_b128 v4, v[124:127] offset:6144
	v_mul_f32_e32 v128, 0x43000000, v128
	v_mul_f32_e32 v129, 0x43000000, v129
	v_mul_f32_e32 v130, 0x43000000, v130
	v_mul_f32_e32 v131, 0x43000000, v131
	ds_write_b128 v4, v[128:131] offset:7168
	s_waitcnt lgkmcnt(0)
	s_barrier
; #define GAS __attribute__((address_space(1)))
; #define LAS __attribute__((address_space(3)))
; #define LDS_WAIT() asm volatile("s_waitcnt lgkmcnt(0)" ::: "memory")
; __device__ __forceinline__ unsigned pk4_fp8(float a, float b, float c, float d) {
;     a = fminf(fmaxf(a, -448.f), 448.f); b = fminf(fmaxf(b, -448.f), 448.f); c = fminf(fmaxf(c, -448.f), 448.f); d = fminf(fmaxf(d, -448.f), 448.f);
;     int w = __builtin_amdgcn_cvt_pk_fp8_f32(a, b, 0, false); w = __builtin_amdgcn_cvt_pk_fp8_f32(c, d, w, true); return (unsigned)w; }
;     const int pr = item >> 1, kb = 2 * (pr / nblk) + (item & 1), nb = pr % nblk, k0 = 64 * kb, n0 = 32 * nb;
;     const int nr = n0 + (lane & 31); const int sc = MAP == 1 ? src_col_in(nr) : nr;
;     float v[32];
; #pragma unroll
;     for (int i = 0; i < 32; ++i) v[i] = sc >= 0 ? W[(size_t)(k0 + 2 * i + (lane >> 5)) * Nsrc + sc] : 0.f;
; #pragma unroll
;     for (int i = 0; i < 32; ++i) { const int k = k0 + 2 * i + (lane >> 5); float x = v[i] * wscale; if (KS) x *= (k < ksplit ? ksA[k] : ksB[k - ksplit]); scr[(2 * i + (lane >> 5)) * 33 + (lane & 31)] = x; }
;     LDS_WAIT(); asm volatile("" ::: "memory");
;     const int c = lane & 7;
; #pragma unroll
;     for (int j = 0; j < 4; ++j) { const int n = (lane >> 3) + 8 * j; const LAS float* s = scr + (8 * c) * 33 + n;
;         const unsigned long long o = (unsigned long long)pg8::pk4_fp8(s[0 * 33], s[1 * 33], s[2 * 33], s[3 * 33]) | ((unsigned long long)pg8::pk4_fp8(s[4 * 33], s[5 * 33], s[6 * 33], s[7 * 33]) << 32);
;         *(GAS unsigned long long*)(WT + (size_t)(n0 + n) * K + k0 + 8 * c) = o; }
;     LDS_WAIT(); asm volatile("" ::: "memory");
; }
	s_add_i32 s17, s16, 1728
	s_min_u32 s17, s17, 0xfff
	s_lshr_b32 s18, s17, 5
	s_add_i32 s18, s18, 0
	s_and_b32 s19, s17, 31
	s_lshl_b32 s18, s18, 21
	s_lshl_b32 s19, s19, 9
	s_add_u32 s18, s18, s19
	s_add_u32 s12, s2, s18
	s_addc_u32 s13, s3, 0
	global_load_dwordx4 v[100:103], v10, s[12:13]
	s_add_u32 s12, s12, 0x8000
	s_addc_u32 s13, s13, 0
	global_load_dwordx4 v[104:107], v10, s[12:13]
	s_add_u32 s12, s12, 0x8000
	s_addc_u32 s13, s13, 0
	global_load_dwordx4 v[108:111], v10, s[12:13]
	s_add_u32 s12, s12, 0x8000
	s_addc_u32 s13, s13, 0
	global_load_dwordx4 v[112:115], v10, s[12:13]
	s_add_u32 s12, s12, 0x8000
	s_addc_u32 s13, s13, 0
	global_load_dwordx4 v[116:119], v10, s[12:13]
	s_add_u32 s12, s12, 0x8000
	s_addc_u32 s13, s13, 0
	global_load_dwordx4 v[120:123], v10, s[12:13]
	s_add_u32 s12, s12, 0x8000
	s_addc_u32 s13, s13, 0
	global_load_dwordx4 v[124:127], v10, s[12:13]
	s_add_u32 s12, s12, 0x8000
	s_addc_u32 s13, s13, 0
	global_load_dwordx4 v[128:131], v10, s[12:13]
	s_add_i32 s17, s16, 1344
	s_min_u32 s17, s17, 0xfff
	s_lshr_b32 s18, s17, 5
	s_add_i32 s18, s18, 0
	s_and_b32 s19, s17, 31
	s_lshl_b32 s19, s19, 21
	s_lshl_b32 s18, s18, 7
	s_add_u32 s18, s18, s19
	s_add_u32 s14, s4, s18
	s_addc_u32 s15, s5, 0
	ds_read_b32 v170, v6
	ds_read_b32 v171, v6 offset:512
	ds_read_b32 v172, v6 offset:1024
	ds_read_b32 v173, v6 offset:1536
	ds_read_b32 v174, v6 offset:2048
	ds_read_b32 v175, v6 offset:2560
	ds_read_b32 v176, v6 offset:3072
	ds_read_b32 v177, v6 offset:3584
	ds_read_b32 v196, v6 offset:4096
	ds_read_b32 v197, v6 offset:4608
	ds_read_b32 v198, v6 offset:5120
	ds_read_b32 v199, v6 offset:5632
	ds_read_b32 v200, v6 offset:6144
	ds_read_b32 v201, v6 offset:6656
	ds_read_b32 v202, v6 offset:7168
	ds_read_b32 v203, v6 offset:7680
	s_waitcnt lgkmcnt(0)
	v_max_f32_e32 v170, v170, v170
	v_max_f32_e32 v171, v171, v171
	v_max_f32_e32 v172, v172, v172
	v_max_f32_e32 v173, v173, v173
	v_max_f32_e32 v174, v174, v174
	v_max_f32_e32 v175, v175, v175
	v_max_f32_e32 v176, v176, v176
	v_max_f32_e32 v177, v177, v177
	v_max_f32_e32 v196, v196, v196
	v_max_f32_e32 v197, v197, v197
	v_max_f32_e32 v198, v198, v198
	v_max_f32_e32 v199, v199, v199
	v_max_f32_e32 v200, v200, v200
	v_max_f32_e32 v201, v201, v201
	v_max_f32_e32 v202, v202, v202
	v_max_f32_e32 v203, v203, v203
	v_med3_f32 v170, v170, s20, v13
	v_med3_f32 v171, v171, s20, v13
	v_med3_f32 v172, v172, s20, v13
	v_med3_f32 v173, v173, s20, v13
	v_med3_f32 v174, v174, s20, v13
	v_med3_f32 v175, v175, s20, v13
	v_med3_f32 v176, v176, s20, v13
	v_med3_f32 v177, v177, s20, v13
	v_med3_f32 v196, v196, s20, v13
	v_med3_f32 v197, v197, s20, v13
	v_med3_f32 v198, v198, s20, v13
	v_med3_f32 v199, v199, s20, v13
	v_med3_f32 v200, v200, s20, v13
	v_med3_f32 v201, v201, s20, v13
	v_med3_f32 v202, v202, s20, v13
	v_med3_f32 v203, v203, s20, v13
	v_mov_b32_e32 v208, 0
	v_mov_b32_e32 v209, 0
	v_mov_b32_e32 v210, 0
	v_mov_b32_e32 v211, 0
	v_cvt_pk_fp8_f32 v208, v170, v171
	v_cvt_pk_fp8_f32 v209, v174, v175
	v_cvt_pk_fp8_f32 v210, v196, v197
	v_cvt_pk_fp8_f32 v211, v200, v201
	v_cvt_pk_fp8_f32 v208, v172, v173 op_sel:[0,0,1]
	v_cvt_pk_fp8_f32 v209, v176, v177 op_sel:[0,0,1]
	v_cvt_pk_fp8_f32 v210, v198, v199 op_sel:[0,0,1]
	v_cvt_pk_fp8_f32 v211, v202, v203 op_sel:[0,0,1]
	s_nop 0
	global_store_dwordx4 v11, v[208:211], s[14:15]
	ds_read_b32 v170, v8
	ds_read_b32 v171, v8 offset:512
	ds_read_b32 v172, v8 offset:1024
	ds_read_b32 v173, v8 offset:1536
	ds_read_b32 v174, v8 offset:2048
	ds_read_b32 v175, v8 offset:2560
	ds_read_b32 v176, v8 offset:3072
	ds_read_b32 v177, v8 offset:3584
	ds_read_b32 v196, v8 offset:4096
	ds_read_b32 v197, v8 offset:4608
	ds_read_b32 v198, v8 offset:5120
	ds_read_b32 v199, v8 offset:5632
	ds_read_b32 v200, v8 offset:6144
	ds_read_b32 v201, v8 offset:6656
	ds_read_b32 v202, v8 offset:7168
	ds_read_b32 v203, v8 offset:7680
	s_waitcnt lgkmcnt(0)
	v_max_f32_e32 v170, v170, v170
	v_max_f32_e32 v171, v171, v171
	v_max_f32_e32 v172, v172, v172
	v_max_f32_e32 v173, v173, v173
	v_max_f32_e32 v174, v174, v174
	v_max_f32_e32 v175, v175, v175
	v_max_f32_e32 v176, v176, v176
	v_max_f32_e32 v177, v177, v177
	v_max_f32_e32 v196, v196, v196
	v_max_f32_e32 v197, v197, v197
	v_max_f32_e32 v198, v198, v198
	v_max_f32_e32 v199, v199, v199
	v_max_f32_e32 v200, v200, v200
	v_max_f32_e32 v201, v201, v201
	v_max_f32_e32 v202, v202, v202
	v_max_f32_e32 v203, v203, v203
	v_med3_f32 v170, v170, s20, v13
	v_med3_f32 v171, v171, s20, v13
	v_med3_f32 v172, v172, s20, v13
	v_med3_f32 v173, v173, s20, v13
	v_med3_f32 v174, v174, s20, v13
	v_med3_f32 v175, v175, s20, v13
	v_med3_f32 v176, v176, s20, v13
	v_med3_f32 v177, v177, s20, v13
	v_med3_f32 v196, v196, s20, v13
	v_med3_f32 v197, v197, s20, v13
	v_med3_f32 v198, v198, s20, v13
	v_med3_f32 v199, v199, s20, v13
	v_med3_f32 v200, v200, s20, v13
	v_med3_f32 v201, v201, s20, v13
	v_med3_f32 v202, v202, s20, v13
	v_med3_f32 v203, v203, s20, v13
	v_mov_b32_e32 v208, 0
	v_mov_b32_e32 v209, 0
	v_mov_b32_e32 v210, 0
	v_mov_b32_e32 v211, 0
	v_cvt_pk_fp8_f32 v208, v170, v171
	v_cvt_pk_fp8_f32 v209, v174, v175
	v_cvt_pk_fp8_f32 v210, v196, v197
	v_cvt_pk_fp8_f32 v211, v200, v201
	v_cvt_pk_fp8_f32 v208, v172, v173 op_sel:[0,0,1]
	v_cvt_pk_fp8_f32 v209, v176, v177 op_sel:[0,0,1]
	v_cvt_pk_fp8_f32 v210, v198, v199 op_sel:[0,0,1]
	v_cvt_pk_fp8_f32 v211, v202, v203 op_sel:[0,0,1]
	s_nop 0
	global_store_dwordx4 v12, v[208:211], s[14:15]
	s_waitcnt vmcnt(32)
	v_mul_f32_e32 v132, 0x43000000, v132
	v_mul_f32_e32 v133, 0x43000000, v133
	v_mul_f32_e32 v134, 0x43000000, v134
	v_mul_f32_e32 v135, 0x43000000, v135
	ds_write_b128 v5, v[132:135]
	v_mul_f32_e32 v136, 0x43000000, v136
	v_mul_f32_e32 v137, 0x43000000, v137
	v_mul_f32_e32 v138, 0x43000000, v138
	v_mul_f32_e32 v139, 0x43000000, v139
	ds_write_b128 v5, v[136:139] offset:1024
	v_mul_f32_e32 v140, 0x43000000, v140
	v_mul_f32_e32 v141, 0x43000000, v141
	v_mul_f32_e32 v142, 0x43000000, v142
	v_mul_f32_e32 v143, 0x43000000, v143
	ds_write_b128 v5, v[140:143] offset:2048
	v_mul_f32_e32 v144, 0x43000000, v144
	v_mul_f32_e32 v145, 0x43000000, v145
	v_mul_f32_e32 v146, 0x43000000, v146
	v_mul_f32_e32 v147, 0x43000000, v147
	ds_write_b128 v5, v[144:147] offset:3072
	v_mul_f32_e32 v148, 0x43000000, v148
	v_mul_f32_e32 v149, 0x43000000, v149
	v_mul_f32_e32 v150, 0x43000000, v150
	v_mul_f32_e32 v151, 0x43000000, v151
	ds_write_b128 v5, v[148:151] offset:4096
	v_mul_f32_e32 v152, 0x43000000, v152
	v_mul_f32_e32 v153, 0x43000000, v153
	v_mul_f32_e32 v154, 0x43000000, v154
	v_mul_f32_e32 v155, 0x43000000, v155
	ds_write_b128 v5, v[152:155] offset:5120
	v_mul_f32_e32 v156, 0x43000000, v156
	v_mul_f32_e32 v157, 0x43000000, v157
	v_mul_f32_e32 v158, 0x43000000, v158
	v_mul_f32_e32 v159, 0x43000000, v159
	ds_write_b128 v5, v[156:159] offset:6144
	v_mul_f32_e32 v160, 0x43000000, v160
	v_mul_f32_e32 v161, 0x43000000, v161
	v_mul_f32_e32 v162, 0x43000000, v162
	v_mul_f32_e32 v163, 0x43000000, v163
	ds_write_b128 v5, v[160:163] offset:7168
	s_waitcnt lgkmcnt(0)
	s_barrier
; #define GAS __attribute__((address_space(1)))
; #define LAS __attribute__((address_space(3)))
; #define LDS_WAIT() asm volatile("s_waitcnt lgkmcnt(0)" ::: "memory")
; __device__ __forceinline__ unsigned pk4_fp8(float a, float b, float c, float d) {
;     a = fminf(fmaxf(a, -448.f), 448.f); b = fminf(fmaxf(b, -448.f), 448.f); c = fminf(fmaxf(c, -448.f), 448.f); d = fminf(fmaxf(d, -448.f), 448.f);
;     int w = __builtin_amdgcn_cvt_pk_fp8_f32(a, b, 0, false); w = __builtin_amdgcn_cvt_pk_fp8_f32(c, d, w, true); return (unsigned)w; }
;     const int pr = item >> 1, kb = 2 * (pr / nblk) + (item & 1), nb = pr % nblk, k0 = 64 * kb, n0 = 32 * nb;
;     const int nr = n0 + (lane & 31); const int sc = MAP == 1 ? src_col_in(nr) : nr;
;     float v[32];
; #pragma unroll
;     for (int i = 0; i < 32; ++i) v[i] = sc >= 0 ? W[(size_t)(k0 + 2 * i + (lane >> 5)) * Nsrc + sc] : 0.f;
; #pragma unroll
;     for (int i = 0; i < 32; ++i) { const int k = k0 + 2 * i + (lane >> 5); float x = v[i] * wscale; if (KS) x *= (k < ksplit ? ksA[k] : ksB[k - ksplit]); scr[(2 * i + (lane >> 5)) * 33 + (lane & 31)] = x; }
;     LDS_WAIT(); asm volatile("" ::: "memory");
;     const int c = lane & 7;
; #pragma unroll
;     for (int j = 0; j < 4; ++j) { const int n = (lane >> 3) + 8 * j; const LAS float* s = scr + (8 * c) * 33 + n;
;         const unsigned long long o = (unsigned long long)pg8::pk4_fp8(s[0 * 33], s[1 * 33], s[2 * 33], s[3 * 33]) | ((unsigned long long)pg8::pk4_fp8(s[4 * 33], s[5 * 33], s[6 * 33], s[7 * 33]) << 32);
;         *(GAS unsigned long long*)(WT + (size_t)(n0 + n) * K + k0 + 8 * c) = o; }
;     LDS_WAIT(); asm volatile("" ::: "memory");
; }
	s_add_i32 s17, s16, 1824
	s_min_u32 s17, s17, 0xfff
	s_lshr_b32 s18, s17, 5
	s_add_i32 s18, s18, 0
	s_and_b32 s19, s17, 31
	s_lshl_b32 s18, s18, 21
	s_lshl_b32 s19, s19, 9
	s_add_u32 s18, s18, s19
	s_add_u32 s12, s2, s18
	s_addc_u32 s13, s3, 0
	global_load_dwordx4 v[132:135], v10, s[12:13]
	s_add_u32 s12, s12, 0x8000
	s_addc_u32 s13, s13, 0
	global_load_dwordx4 v[136:139], v10, s[12:13]
	s_add_u32 s12, s12, 0x8000
	s_addc_u32 s13, s13, 0
	global_load_dwordx4 v[140:143], v10, s[12:13]
	s_add_u32 s12, s12, 0x8000
	s_addc_u32 s13, s13, 0
	global_load_dwordx4 v[144:147], v10, s[12:13]
	s_add_u32 s12, s12, 0x8000
	s_addc_u32 s13, s13, 0
	global_load_dwordx4 v[148:151], v10, s[12:13]
	s_add_u32 s12, s12, 0x8000
	s_addc_u32 s13, s13, 0
	global_load_dwordx4 v[152:155], v10, s[12:13]
	s_add_u32 s12, s12, 0x8000
	s_addc_u32 s13, s13, 0
	global_load_dwordx4 v[156:159], v10, s[12:13]
	s_add_u32 s12, s12, 0x8000
	s_addc_u32 s13, s13, 0
	global_load_dwordx4 v[160:163], v10, s[12:13]
	s_add_i32 s17, s16, 1440
	s_min_u32 s17, s17, 0xfff
	s_lshr_b32 s18, s17, 5
	s_add_i32 s18, s18, 0
	s_and_b32 s19, s17, 31
	s_lshl_b32 s19, s19, 21
	s_lshl_b32 s18, s18, 7
	s_add_u32 s18, s18, s19
	s_add_u32 s14, s4, s18
	s_addc_u32 s15, s5, 0
	ds_read_b32 v170, v7
	ds_read_b32 v171, v7 offset:512
	ds_read_b32 v172, v7 offset:1024
	ds_read_b32 v173, v7 offset:1536
	ds_read_b32 v174, v7 offset:2048
	ds_read_b32 v175, v7 offset:2560
	ds_read_b32 v176, v7 offset:3072
	ds_read_b32 v177, v7 offset:3584
	ds_read_b32 v196, v7 offset:4096
	ds_read_b32 v197, v7 offset:4608
	ds_read_b32 v198, v7 offset:5120
	ds_read_b32 v199, v7 offset:5632
	ds_read_b32 v200, v7 offset:6144
	ds_read_b32 v201, v7 offset:6656
	ds_read_b32 v202, v7 offset:7168
	ds_read_b32 v203, v7 offset:7680
	s_waitcnt lgkmcnt(0)
	v_max_f32_e32 v170, v170, v170
	v_max_f32_e32 v171, v171, v171
	v_max_f32_e32 v172, v172, v172
	v_max_f32_e32 v173, v173, v173
	v_max_f32_e32 v174, v174, v174
	v_max_f32_e32 v175, v175, v175
	v_max_f32_e32 v176, v176, v176
	v_max_f32_e32 v177, v177, v177
	v_max_f32_e32 v196, v196, v196
	v_max_f32_e32 v197, v197, v197
	v_max_f32_e32 v198, v198, v198
	v_max_f32_e32 v199, v199, v199
	v_max_f32_e32 v200, v200, v200
	v_max_f32_e32 v201, v201, v201
	v_max_f32_e32 v202, v202, v202
	v_max_f32_e32 v203, v203, v203
	v_med3_f32 v170, v170, s20, v13
	v_med3_f32 v171, v171, s20, v13
	v_med3_f32 v172, v172, s20, v13
	v_med3_f32 v173, v173, s20, v13
	v_med3_f32 v174, v174, s20, v13
	v_med3_f32 v175, v175, s20, v13
	v_med3_f32 v176, v176, s20, v13
	v_med3_f32 v177, v177, s20, v13
	v_med3_f32 v196, v196, s20, v13
	v_med3_f32 v197, v197, s20, v13
	v_med3_f32 v198, v198, s20, v13
	v_med3_f32 v199, v199, s20, v13
	v_med3_f32 v200, v200, s20, v13
	v_med3_f32 v201, v201, s20, v13
	v_med3_f32 v202, v202, s20, v13
	v_med3_f32 v203, v203, s20, v13
	v_mov_b32_e32 v208, 0
	v_mov_b32_e32 v209, 0
	v_mov_b32_e32 v210, 0
	v_mov_b32_e32 v211, 0
	v_cvt_pk_fp8_f32 v208, v170, v171
	v_cvt_pk_fp8_f32 v209, v174, v175
	v_cvt_pk_fp8_f32 v210, v196, v197
	v_cvt_pk_fp8_f32 v211, v200, v201
	v_cvt_pk_fp8_f32 v208, v172, v173 op_sel:[0,0,1]
	v_cvt_pk_fp8_f32 v209, v176, v177 op_sel:[0,0,1]
	v_cvt_pk_fp8_f32 v210, v198, v199 op_sel:[0,0,1]
	v_cvt_pk_fp8_f32 v211, v202, v203 op_sel:[0,0,1]
	s_nop 0
	global_store_dwordx4 v11, v[208:211], s[14:15]
	ds_read_b32 v170, v9
	ds_read_b32 v171, v9 offset:512
	ds_read_b32 v172, v9 offset:1024
	ds_read_b32 v173, v9 offset:1536
	ds_read_b32 v174, v9 offset:2048
	ds_read_b32 v175, v9 offset:2560
	ds_read_b32 v176, v9 offset:3072
	ds_read_b32 v177, v9 offset:3584
	ds_read_b32 v196, v9 offset:4096
	ds_read_b32 v197, v9 offset:4608
	ds_read_b32 v198, v9 offset:5120
	ds_read_b32 v199, v9 offset:5632
	ds_read_b32 v200, v9 offset:6144
	ds_read_b32 v201, v9 offset:6656
	ds_read_b32 v202, v9 offset:7168
	ds_read_b32 v203, v9 offset:7680
	s_waitcnt lgkmcnt(0)
	v_max_f32_e32 v170, v170, v170
	v_max_f32_e32 v171, v171, v171
	v_max_f32_e32 v172, v172, v172
	v_max_f32_e32 v173, v173, v173
	v_max_f32_e32 v174, v174, v174
	v_max_f32_e32 v175, v175, v175
	v_max_f32_e32 v176, v176, v176
	v_max_f32_e32 v177, v177, v177
	v_max_f32_e32 v196, v196, v196
	v_max_f32_e32 v197, v197, v197
	v_max_f32_e32 v198, v198, v198
	v_max_f32_e32 v199, v199, v199
	v_max_f32_e32 v200, v200, v200
	v_max_f32_e32 v201, v201, v201
	v_max_f32_e32 v202, v202, v202
	v_max_f32_e32 v203, v203, v203
	v_med3_f32 v170, v170, s20, v13
	v_med3_f32 v171, v171, s20, v13
	v_med3_f32 v172, v172, s20, v13
	v_med3_f32 v173, v173, s20, v13
	v_med3_f32 v174, v174, s20, v13
	v_med3_f32 v175, v175, s20, v13
	v_med3_f32 v176, v176, s20, v13
	v_med3_f32 v177, v177, s20, v13
	v_med3_f32 v196, v196, s20, v13
	v_med3_f32 v197, v197, s20, v13
	v_med3_f32 v198, v198, s20, v13
	v_med3_f32 v199, v199, s20, v13
	v_med3_f32 v200, v200, s20, v13
	v_med3_f32 v201, v201, s20, v13
	v_med3_f32 v202, v202, s20, v13
	v_med3_f32 v203, v203, s20, v13
	v_mov_b32_e32 v208, 0
	v_mov_b32_e32 v209, 0
	v_mov_b32_e32 v210, 0
	v_mov_b32_e32 v211, 0
	v_cvt_pk_fp8_f32 v208, v170, v171
	v_cvt_pk_fp8_f32 v209, v174, v175
	v_cvt_pk_fp8_f32 v210, v196, v197
	v_cvt_pk_fp8_f32 v211, v200, v201
	v_cvt_pk_fp8_f32 v208, v172, v173 op_sel:[0,0,1]
	v_cvt_pk_fp8_f32 v209, v176, v177 op_sel:[0,0,1]
	v_cvt_pk_fp8_f32 v210, v198, v199 op_sel:[0,0,1]
	v_cvt_pk_fp8_f32 v211, v202, v203 op_sel:[0,0,1]
	s_nop 0
	global_store_dwordx4 v12, v[208:211], s[14:15]
	s_waitcnt vmcnt(32)
	v_mul_f32_e32 v36, 0x43000000, v36
	v_mul_f32_e32 v37, 0x43000000, v37
	v_mul_f32_e32 v38, 0x43000000, v38
	v_mul_f32_e32 v39, 0x43000000, v39
	ds_write_b128 v4, v[36:39]
	v_mul_f32_e32 v40, 0x43000000, v40
	v_mul_f32_e32 v41, 0x43000000, v41
	v_mul_f32_e32 v42, 0x43000000, v42
	v_mul_f32_e32 v43, 0x43000000, v43
	ds_write_b128 v4, v[40:43] offset:1024
	v_mul_f32_e32 v44, 0x43000000, v44
	v_mul_f32_e32 v45, 0x43000000, v45
	v_mul_f32_e32 v46, 0x43000000, v46
	v_mul_f32_e32 v47, 0x43000000, v47
	ds_write_b128 v4, v[44:47] offset:2048
	v_mul_f32_e32 v48, 0x43000000, v48
	v_mul_f32_e32 v49, 0x43000000, v49
	v_mul_f32_e32 v50, 0x43000000, v50
	v_mul_f32_e32 v51, 0x43000000, v51
	ds_write_b128 v4, v[48:51] offset:3072
	v_mul_f32_e32 v52, 0x43000000, v52
	v_mul_f32_e32 v53, 0x43000000, v53
	v_mul_f32_e32 v54, 0x43000000, v54
	v_mul_f32_e32 v55, 0x43000000, v55
	ds_write_b128 v4, v[52:55] offset:4096
	v_mul_f32_e32 v56, 0x43000000, v56
	v_mul_f32_e32 v57, 0x43000000, v57
	v_mul_f32_e32 v58, 0x43000000, v58
	v_mul_f32_e32 v59, 0x43000000, v59
	ds_write_b128 v4, v[56:59] offset:5120
	v_mul_f32_e32 v60, 0x43000000, v60
	v_mul_f32_e32 v61, 0x43000000, v61
	v_mul_f32_e32 v62, 0x43000000, v62
	v_mul_f32_e32 v63, 0x43000000, v63
	ds_write_b128 v4, v[60:63] offset:6144
	v_mul_f32_e32 v64, 0x43000000, v64
	v_mul_f32_e32 v65, 0x43000000, v65
	v_mul_f32_e32 v66, 0x43000000, v66
	v_mul_f32_e32 v67, 0x43000000, v67
	ds_write_b128 v4, v[64:67] offset:7168
	s_waitcnt lgkmcnt(0)
	s_barrier
; #define GAS __attribute__((address_space(1)))
; #define LAS __attribute__((address_space(3)))
; #define LDS_WAIT() asm volatile("s_waitcnt lgkmcnt(0)" ::: "memory")
; __device__ __forceinline__ unsigned pk4_fp8(float a, float b, float c, float d) {
;     a = fminf(fmaxf(a, -448.f), 448.f); b = fminf(fmaxf(b, -448.f), 448.f); c = fminf(fmaxf(c, -448.f), 448.f); d = fminf(fmaxf(d, -448.f), 448.f);
;     int w = __builtin_amdgcn_cvt_pk_fp8_f32(a, b, 0, false); w = __builtin_amdgcn_cvt_pk_fp8_f32(c, d, w, true); return (unsigned)w; }
;     const int pr = item >> 1, kb = 2 * (pr / nblk) + (item & 1), nb = pr % nblk, k0 = 64 * kb, n0 = 32 * nb;
;     const int nr = n0 + (lane & 31); const int sc = MAP == 1 ? src_col_in(nr) : nr;
;     float v[32];
; #pragma unroll
;     for (int i = 0; i < 32; ++i) v[i] = sc >= 0 ? W[(size_t)(k0 + 2 * i + (lane >> 5)) * Nsrc + sc] : 0.f;
; #pragma unroll
;     for (int i = 0; i < 32; ++i) { const int k = k0 + 2 * i + (lane >> 5); float x = v[i] * wscale; if (KS) x *= (k < ksplit ? ksA[k] : ksB[k - ksplit]); scr[(2 * i + (lane >> 5)) * 33 + (lane & 31)] = x; }
;     LDS_WAIT(); asm volatile("" ::: "memory");
;     const int c = lane & 7;
; #pragma unroll
;     for (int j = 0; j < 4; ++j) { const int n = (lane >> 3) + 8 * j; const LAS float* s = scr + (8 * c) * 33 + n;
;         const unsigned long long o = (unsigned long long)pg8::pk4_fp8(s[0 * 33], s[1 * 33], s[2 * 33], s[3 * 33]) | ((unsigned long long)pg8::pk4_fp8(s[4 * 33], s[5 * 33], s[6 * 33], s[7 * 33]) << 32);
;         *(GAS unsigned long long*)(WT + (size_t)(n0 + n) * K + k0 + 8 * c) = o; }
;     LDS_WAIT(); asm volatile("" ::: "memory");
; }
	s_add_i32 s17, s16, 1920
	s_min_u32 s17, s17, 0xfff
	s_lshr_b32 s18, s17, 5
	s_add_i32 s18, s18, 0
	s_and_b32 s19, s17, 31
	s_lshl_b32 s18, s18, 21
	s_lshl_b32 s19, s19, 9
	s_add_u32 s18, s18, s19
	s_add_u32 s12, s2, s18
	s_addc_u32 s13, s3, 0
	global_load_dwordx4 v[36:39], v10, s[12:13]
	s_add_u32 s12, s12, 0x8000
	s_addc_u32 s13, s13, 0
	global_load_dwordx4 v[40:43], v10, s[12:13]
	s_add_u32 s12, s12, 0x8000
	s_addc_u32 s13, s13, 0
	global_load_dwordx4 v[44:47], v10, s[12:13]
	s_add_u32 s12, s12, 0x8000
	s_addc_u32 s13, s13, 0
	global_load_dwordx4 v[48:51], v10, s[12:13]
	s_add_u32 s12, s12, 0x8000
	s_addc_u32 s13, s13, 0
	global_load_dwordx4 v[52:55], v10, s[12:13]
	s_add_u32 s12, s12, 0x8000
	s_addc_u32 s13, s13, 0
	global_load_dwordx4 v[56:59], v10, s[12:13]
	s_add_u32 s12, s12, 0x8000
	s_addc_u32 s13, s13, 0
	global_load_dwordx4 v[60:63], v10, s[12:13]
	s_add_u32 s12, s12, 0x8000
	s_addc_u32 s13, s13, 0
	global_load_dwordx4 v[64:67], v10, s[12:13]
	s_add_i32 s17, s16, 1536
	s_min_u32 s17, s17, 0xfff
	s_lshr_b32 s18, s17, 5
	s_add_i32 s18, s18, 0
	s_and_b32 s19, s17, 31
	s_lshl_b32 s19, s19, 21
	s_lshl_b32 s18, s18, 7
	s_add_u32 s18, s18, s19
	s_add_u32 s14, s4, s18
	s_addc_u32 s15, s5, 0
	ds_read_b32 v170, v6
	ds_read_b32 v171, v6 offset:512
	ds_read_b32 v172, v6 offset:1024
	ds_read_b32 v173, v6 offset:1536
	ds_read_b32 v174, v6 offset:2048
	ds_read_b32 v175, v6 offset:2560
	ds_read_b32 v176, v6 offset:3072
	ds_read_b32 v177, v6 offset:3584
	ds_read_b32 v196, v6 offset:4096
	ds_read_b32 v197, v6 offset:4608
	ds_read_b32 v198, v6 offset:5120
	ds_read_b32 v199, v6 offset:5632
	ds_read_b32 v200, v6 offset:6144
	ds_read_b32 v201, v6 offset:6656
	ds_read_b32 v202, v6 offset:7168
	ds_read_b32 v203, v6 offset:7680
	s_waitcnt lgkmcnt(0)
	v_max_f32_e32 v170, v170, v170
	v_max_f32_e32 v171, v171, v171
	v_max_f32_e32 v172, v172, v172
	v_max_f32_e32 v173, v173, v173
	v_max_f32_e32 v174, v174, v174
	v_max_f32_e32 v175, v175, v175
	v_max_f32_e32 v176, v176, v176
	v_max_f32_e32 v177, v177, v177
	v_max_f32_e32 v196, v196, v196
	v_max_f32_e32 v197, v197, v197
	v_max_f32_e32 v198, v198, v198
	v_max_f32_e32 v199, v199, v199
	v_max_f32_e32 v200, v200, v200
	v_max_f32_e32 v201, v201, v201
	v_max_f32_e32 v202, v202, v202
	v_max_f32_e32 v203, v203, v203
	v_med3_f32 v170, v170, s20, v13
	v_med3_f32 v171, v171, s20, v13
	v_med3_f32 v172, v172, s20, v13
	v_med3_f32 v173, v173, s20, v13
	v_med3_f32 v174, v174, s20, v13
	v_med3_f32 v175, v175, s20, v13
	v_med3_f32 v176, v176, s20, v13
	v_med3_f32 v177, v177, s20, v13
	v_med3_f32 v196, v196, s20, v13
	v_med3_f32 v197, v197, s20, v13
	v_med3_f32 v198, v198, s20, v13
	v_med3_f32 v199, v199, s20, v13
	v_med3_f32 v200, v200, s20, v13
	v_med3_f32 v201, v201, s20, v13
	v_med3_f32 v202, v202, s20, v13
	v_med3_f32 v203, v203, s20, v13
	v_mov_b32_e32 v208, 0
	v_mov_b32_e32 v209, 0
	v_mov_b32_e32 v210, 0
	v_mov_b32_e32 v211, 0
	v_cvt_pk_fp8_f32 v208, v170, v171
	v_cvt_pk_fp8_f32 v209, v174, v175
	v_cvt_pk_fp8_f32 v210, v196, v197
	v_cvt_pk_fp8_f32 v211, v200, v201
	v_cvt_pk_fp8_f32 v208, v172, v173 op_sel:[0,0,1]
	v_cvt_pk_fp8_f32 v209, v176, v177 op_sel:[0,0,1]
	v_cvt_pk_fp8_f32 v210, v198, v199 op_sel:[0,0,1]
	v_cvt_pk_fp8_f32 v211, v202, v203 op_sel:[0,0,1]
	s_nop 0
	global_store_dwordx4 v11, v[208:211], s[14:15]
	ds_read_b32 v170, v8
	ds_read_b32 v171, v8 offset:512
	ds_read_b32 v172, v8 offset:1024
	ds_read_b32 v173, v8 offset:1536
	ds_read_b32 v174, v8 offset:2048
	ds_read_b32 v175, v8 offset:2560
	ds_read_b32 v176, v8 offset:3072
	ds_read_b32 v177, v8 offset:3584
	ds_read_b32 v196, v8 offset:4096
	ds_read_b32 v197, v8 offset:4608
	ds_read_b32 v198, v8 offset:5120
	ds_read_b32 v199, v8 offset:5632
	ds_read_b32 v200, v8 offset:6144
	ds_read_b32 v201, v8 offset:6656
	ds_read_b32 v202, v8 offset:7168
	ds_read_b32 v203, v8 offset:7680
	s_waitcnt lgkmcnt(0)
	v_max_f32_e32 v170, v170, v170
	v_max_f32_e32 v171, v171, v171
	v_max_f32_e32 v172, v172, v172
	v_max_f32_e32 v173, v173, v173
	v_max_f32_e32 v174, v174, v174
	v_max_f32_e32 v175, v175, v175
	v_max_f32_e32 v176, v176, v176
	v_max_f32_e32 v177, v177, v177
	v_max_f32_e32 v196, v196, v196
	v_max_f32_e32 v197, v197, v197
	v_max_f32_e32 v198, v198, v198
	v_max_f32_e32 v199, v199, v199
	v_max_f32_e32 v200, v200, v200
	v_max_f32_e32 v201, v201, v201
	v_max_f32_e32 v202, v202, v202
	v_max_f32_e32 v203, v203, v203
	v_med3_f32 v170, v170, s20, v13
	v_med3_f32 v171, v171, s20, v13
	v_med3_f32 v172, v172, s20, v13
	v_med3_f32 v173, v173, s20, v13
	v_med3_f32 v174, v174, s20, v13
	v_med3_f32 v175, v175, s20, v13
	v_med3_f32 v176, v176, s20, v13
	v_med3_f32 v177, v177, s20, v13
	v_med3_f32 v196, v196, s20, v13
	v_med3_f32 v197, v197, s20, v13
	v_med3_f32 v198, v198, s20, v13
	v_med3_f32 v199, v199, s20, v13
	v_med3_f32 v200, v200, s20, v13
	v_med3_f32 v201, v201, s20, v13
	v_med3_f32 v202, v202, s20, v13
	v_med3_f32 v203, v203, s20, v13
	v_mov_b32_e32 v208, 0
	v_mov_b32_e32 v209, 0
	v_mov_b32_e32 v210, 0
	v_mov_b32_e32 v211, 0
	v_cvt_pk_fp8_f32 v208, v170, v171
	v_cvt_pk_fp8_f32 v209, v174, v175
	v_cvt_pk_fp8_f32 v210, v196, v197
	v_cvt_pk_fp8_f32 v211, v200, v201
	v_cvt_pk_fp8_f32 v208, v172, v173 op_sel:[0,0,1]
	v_cvt_pk_fp8_f32 v209, v176, v177 op_sel:[0,0,1]
	v_cvt_pk_fp8_f32 v210, v198, v199 op_sel:[0,0,1]
	v_cvt_pk_fp8_f32 v211, v202, v203 op_sel:[0,0,1]
	s_nop 0
	global_store_dwordx4 v12, v[208:211], s[14:15]
	s_waitcnt vmcnt(32)
	v_mul_f32_e32 v68, 0x43000000, v68
	v_mul_f32_e32 v69, 0x43000000, v69
	v_mul_f32_e32 v70, 0x43000000, v70
	v_mul_f32_e32 v71, 0x43000000, v71
	ds_write_b128 v5, v[68:71]
	v_mul_f32_e32 v72, 0x43000000, v72
	v_mul_f32_e32 v73, 0x43000000, v73
	v_mul_f32_e32 v74, 0x43000000, v74
	v_mul_f32_e32 v75, 0x43000000, v75
	ds_write_b128 v5, v[72:75] offset:1024
	v_mul_f32_e32 v76, 0x43000000, v76
	v_mul_f32_e32 v77, 0x43000000, v77
	v_mul_f32_e32 v78, 0x43000000, v78
	v_mul_f32_e32 v79, 0x43000000, v79
	ds_write_b128 v5, v[76:79] offset:2048
	v_mul_f32_e32 v80, 0x43000000, v80
	v_mul_f32_e32 v81, 0x43000000, v81
	v_mul_f32_e32 v82, 0x43000000, v82
	v_mul_f32_e32 v83, 0x43000000, v83
	ds_write_b128 v5, v[80:83] offset:3072
	v_mul_f32_e32 v84, 0x43000000, v84
	v_mul_f32_e32 v85, 0x43000000, v85
	v_mul_f32_e32 v86, 0x43000000, v86
	v_mul_f32_e32 v87, 0x43000000, v87
	ds_write_b128 v5, v[84:87] offset:4096
	v_mul_f32_e32 v88, 0x43000000, v88
	v_mul_f32_e32 v89, 0x43000000, v89
	v_mul_f32_e32 v90, 0x43000000, v90
	v_mul_f32_e32 v91, 0x43000000, v91
	ds_write_b128 v5, v[88:91] offset:5120
	v_mul_f32_e32 v92, 0x43000000, v92
	v_mul_f32_e32 v93, 0x43000000, v93
	v_mul_f32_e32 v94, 0x43000000, v94
	v_mul_f32_e32 v95, 0x43000000, v95
	ds_write_b128 v5, v[92:95] offset:6144
	v_mul_f32_e32 v96, 0x43000000, v96
	v_mul_f32_e32 v97, 0x43000000, v97
	v_mul_f32_e32 v98, 0x43000000, v98
	v_mul_f32_e32 v99, 0x43000000, v99
	ds_write_b128 v5, v[96:99] offset:7168
	s_waitcnt lgkmcnt(0)
	s_barrier
; #define GAS __attribute__((address_space(1)))
; #define LAS __attribute__((address_space(3)))
; #define LDS_WAIT() asm volatile("s_waitcnt lgkmcnt(0)" ::: "memory")
; __device__ __forceinline__ unsigned pk4_fp8(float a, float b, float c, float d) {
;     a = fminf(fmaxf(a, -448.f), 448.f); b = fminf(fmaxf(b, -448.f), 448.f); c = fminf(fmaxf(c, -448.f), 448.f); d = fminf(fmaxf(d, -448.f), 448.f);
;     int w = __builtin_amdgcn_cvt_pk_fp8_f32(a, b, 0, false); w = __builtin_amdgcn_cvt_pk_fp8_f32(c, d, w, true); return (unsigned)w; }
;     const int pr = item >> 1, kb = 2 * (pr / nblk) + (item & 1), nb = pr % nblk, k0 = 64 * kb, n0 = 32 * nb;
;     const int nr = n0 + (lane & 31); const int sc = MAP == 1 ? src_col_in(nr) : nr;
;     float v[32];
; #pragma unroll
;     for (int i = 0; i < 32; ++i) v[i] = sc >= 0 ? W[(size_t)(k0 + 2 * i + (lane >> 5)) * Nsrc + sc] : 0.f;
; #pragma unroll
;     for (int i = 0; i < 32; ++i) { const int k = k0 + 2 * i + (lane >> 5); float x = v[i] * wscale; if (KS) x *= (k < ksplit ? ksA[k] : ksB[k - ksplit]); scr[(2 * i + (lane >> 5)) * 33 + (lane & 31)] = x; }
;     LDS_WAIT(); asm volatile("" ::: "memory");
;     const int c = lane & 7;
; #pragma unroll
;     for (int j = 0; j < 4; ++j) { const int n = (lane >> 3) + 8 * j; const LAS float* s = scr + (8 * c) * 33 + n;
;         const unsigned long long o = (unsigned long long)pg8::pk4_fp8(s[0 * 33], s[1 * 33], s[2 * 33], s[3 * 33]) | ((unsigned long long)pg8::pk4_fp8(s[4 * 33], s[5 * 33], s[6 * 33], s[7 * 33]) << 32);
;         *(GAS unsigned long long*)(WT + (size_t)(n0 + n) * K + k0 + 8 * c) = o; }
;     LDS_WAIT(); asm volatile("" ::: "memory");
; }
	s_add_i32 s17, s16, 2016
	s_min_u32 s17, s17, 0xfff
	s_lshr_b32 s18, s17, 5
	s_add_i32 s18, s18, 0
	s_and_b32 s19, s17, 31
	s_lshl_b32 s18, s18, 21
	s_lshl_b32 s19, s19, 9
	s_add_u32 s18, s18, s19
	s_add_u32 s12, s2, s18
	s_addc_u32 s13, s3, 0
	global_load_dwordx4 v[68:71], v10, s[12:13]
	s_add_u32 s12, s12, 0x8000
	s_addc_u32 s13, s13, 0
	global_load_dwordx4 v[72:75], v10, s[12:13]
	s_add_u32 s12, s12, 0x8000
	s_addc_u32 s13, s13, 0
	global_load_dwordx4 v[76:79], v10, s[12:13]
	s_add_u32 s12, s12, 0x8000
	s_addc_u32 s13, s13, 0
	global_load_dwordx4 v[80:83], v10, s[12:13]
	s_add_u32 s12, s12, 0x8000
	s_addc_u32 s13, s13, 0
	global_load_dwordx4 v[84:87], v10, s[12:13]
	s_add_u32 s12, s12, 0x8000
	s_addc_u32 s13, s13, 0
	global_load_dwordx4 v[88:91], v10, s[12:13]
	s_add_u32 s12, s12, 0x8000
	s_addc_u32 s13, s13, 0
	global_load_dwordx4 v[92:95], v10, s[12:13]
	s_add_u32 s12, s12, 0x8000
	s_addc_u32 s13, s13, 0
	global_load_dwordx4 v[96:99], v10, s[12:13]
	s_add_i32 s17, s16, 1632
	s_min_u32 s17, s17, 0xfff
	s_lshr_b32 s18, s17, 5
	s_add_i32 s18, s18, 0
	s_and_b32 s19, s17, 31
	s_lshl_b32 s19, s19, 21
	s_lshl_b32 s18, s18, 7
	s_add_u32 s18, s18, s19
	s_add_u32 s14, s4, s18
	s_addc_u32 s15, s5, 0
	ds_read_b32 v170, v7
	ds_read_b32 v171, v7 offset:512
	ds_read_b32 v172, v7 offset:1024
	ds_read_b32 v173, v7 offset:1536
	ds_read_b32 v174, v7 offset:2048
	ds_read_b32 v175, v7 offset:2560
	ds_read_b32 v176, v7 offset:3072
	ds_read_b32 v177, v7 offset:3584
	ds_read_b32 v196, v7 offset:4096
	ds_read_b32 v197, v7 offset:4608
	ds_read_b32 v198, v7 offset:5120
	ds_read_b32 v199, v7 offset:5632
	ds_read_b32 v200, v7 offset:6144
	ds_read_b32 v201, v7 offset:6656
	ds_read_b32 v202, v7 offset:7168
	ds_read_b32 v203, v7 offset:7680
	s_waitcnt lgkmcnt(0)
	v_max_f32_e32 v170, v170, v170
	v_max_f32_e32 v171, v171, v171
	v_max_f32_e32 v172, v172, v172
	v_max_f32_e32 v173, v173, v173
	v_max_f32_e32 v174, v174, v174
	v_max_f32_e32 v175, v175, v175
	v_max_f32_e32 v176, v176, v176
	v_max_f32_e32 v177, v177, v177
	v_max_f32_e32 v196, v196, v196
	v_max_f32_e32 v197, v197, v197
	v_max_f32_e32 v198, v198, v198
	v_max_f32_e32 v199, v199, v199
	v_max_f32_e32 v200, v200, v200
	v_max_f32_e32 v201, v201, v201
	v_max_f32_e32 v202, v202, v202
	v_max_f32_e32 v203, v203, v203
	v_med3_f32 v170, v170, s20, v13
	v_med3_f32 v171, v171, s20, v13
	v_med3_f32 v172, v172, s20, v13
	v_med3_f32 v173, v173, s20, v13
	v_med3_f32 v174, v174, s20, v13
	v_med3_f32 v175, v175, s20, v13
	v_med3_f32 v176, v176, s20, v13
	v_med3_f32 v177, v177, s20, v13
	v_med3_f32 v196, v196, s20, v13
	v_med3_f32 v197, v197, s20, v13
	v_med3_f32 v198, v198, s20, v13
	v_med3_f32 v199, v199, s20, v13
	v_med3_f32 v200, v200, s20, v13
	v_med3_f32 v201, v201, s20, v13
	v_med3_f32 v202, v202, s20, v13
	v_med3_f32 v203, v203, s20, v13
	v_mov_b32_e32 v208, 0
	v_mov_b32_e32 v209, 0
	v_mov_b32_e32 v210, 0
	v_mov_b32_e32 v211, 0
	v_cvt_pk_fp8_f32 v208, v170, v171
	v_cvt_pk_fp8_f32 v209, v174, v175
	v_cvt_pk_fp8_f32 v210, v196, v197
	v_cvt_pk_fp8_f32 v211, v200, v201
	v_cvt_pk_fp8_f32 v208, v172, v173 op_sel:[0,0,1]
	v_cvt_pk_fp8_f32 v209, v176, v177 op_sel:[0,0,1]
	v_cvt_pk_fp8_f32 v210, v198, v199 op_sel:[0,0,1]
	v_cvt_pk_fp8_f32 v211, v202, v203 op_sel:[0,0,1]
	s_nop 0
	global_store_dwordx4 v11, v[208:211], s[14:15]
	ds_read_b32 v170, v9
	ds_read_b32 v171, v9 offset:512
	ds_read_b32 v172, v9 offset:1024
	ds_read_b32 v173, v9 offset:1536
	ds_read_b32 v174, v9 offset:2048
	ds_read_b32 v175, v9 offset:2560
	ds_read_b32 v176, v9 offset:3072
	ds_read_b32 v177, v9 offset:3584
	ds_read_b32 v196, v9 offset:4096
	ds_read_b32 v197, v9 offset:4608
	ds_read_b32 v198, v9 offset:5120
	ds_read_b32 v199, v9 offset:5632
	ds_read_b32 v200, v9 offset:6144
	ds_read_b32 v201, v9 offset:6656
	ds_read_b32 v202, v9 offset:7168
	ds_read_b32 v203, v9 offset:7680
	s_waitcnt lgkmcnt(0)
	v_max_f32_e32 v170, v170, v170
	v_max_f32_e32 v171, v171, v171
	v_max_f32_e32 v172, v172, v172
	v_max_f32_e32 v173, v173, v173
	v_max_f32_e32 v174, v174, v174
	v_max_f32_e32 v175, v175, v175
	v_max_f32_e32 v176, v176, v176
	v_max_f32_e32 v177, v177, v177
	v_max_f32_e32 v196, v196, v196
	v_max_f32_e32 v197, v197, v197
	v_max_f32_e32 v198, v198, v198
	v_max_f32_e32 v199, v199, v199
	v_max_f32_e32 v200, v200, v200
	v_max_f32_e32 v201, v201, v201
	v_max_f32_e32 v202, v202, v202
	v_max_f32_e32 v203, v203, v203
	v_med3_f32 v170, v170, s20, v13
	v_med3_f32 v171, v171, s20, v13
	v_med3_f32 v172, v172, s20, v13
	v_med3_f32 v173, v173, s20, v13
	v_med3_f32 v174, v174, s20, v13
	v_med3_f32 v175, v175, s20, v13
	v_med3_f32 v176, v176, s20, v13
	v_med3_f32 v177, v177, s20, v13
	v_med3_f32 v196, v196, s20, v13
	v_med3_f32 v197, v197, s20, v13
	v_med3_f32 v198, v198, s20, v13
	v_med3_f32 v199, v199, s20, v13
	v_med3_f32 v200, v200, s20, v13
	v_med3_f32 v201, v201, s20, v13
	v_med3_f32 v202, v202, s20, v13
	v_med3_f32 v203, v203, s20, v13
	v_mov_b32_e32 v208, 0
	v_mov_b32_e32 v209, 0
	v_mov_b32_e32 v210, 0
	v_mov_b32_e32 v211, 0
	v_cvt_pk_fp8_f32 v208, v170, v171
	v_cvt_pk_fp8_f32 v209, v174, v175
	v_cvt_pk_fp8_f32 v210, v196, v197
	v_cvt_pk_fp8_f32 v211, v200, v201
	v_cvt_pk_fp8_f32 v208, v172, v173 op_sel:[0,0,1]
	v_cvt_pk_fp8_f32 v209, v176, v177 op_sel:[0,0,1]
	v_cvt_pk_fp8_f32 v210, v198, v199 op_sel:[0,0,1]
	v_cvt_pk_fp8_f32 v211, v202, v203 op_sel:[0,0,1]
	s_nop 0
	global_store_dwordx4 v12, v[208:211], s[14:15]
	s_waitcnt vmcnt(32)
	v_mul_f32_e32 v100, 0x43000000, v100
	v_mul_f32_e32 v101, 0x43000000, v101
	v_mul_f32_e32 v102, 0x43000000, v102
	v_mul_f32_e32 v103, 0x43000000, v103
	ds_write_b128 v4, v[100:103]
	v_mul_f32_e32 v104, 0x43000000, v104
	v_mul_f32_e32 v105, 0x43000000, v105
	v_mul_f32_e32 v106, 0x43000000, v106
	v_mul_f32_e32 v107, 0x43000000, v107
	ds_write_b128 v4, v[104:107] offset:1024
	v_mul_f32_e32 v108, 0x43000000, v108
	v_mul_f32_e32 v109, 0x43000000, v109
	v_mul_f32_e32 v110, 0x43000000, v110
	v_mul_f32_e32 v111, 0x43000000, v111
	ds_write_b128 v4, v[108:111] offset:2048
	v_mul_f32_e32 v112, 0x43000000, v112
	v_mul_f32_e32 v113, 0x43000000, v113
	v_mul_f32_e32 v114, 0x43000000, v114
	v_mul_f32_e32 v115, 0x43000000, v115
	ds_write_b128 v4, v[112:115] offset:3072
	v_mul_f32_e32 v116, 0x43000000, v116
	v_mul_f32_e32 v117, 0x43000000, v117
	v_mul_f32_e32 v118, 0x43000000, v118
	v_mul_f32_e32 v119, 0x43000000, v119
	ds_write_b128 v4, v[116:119] offset:4096
	v_mul_f32_e32 v120, 0x43000000, v120
	v_mul_f32_e32 v121, 0x43000000, v121
	v_mul_f32_e32 v122, 0x43000000, v122
	v_mul_f32_e32 v123, 0x43000000, v123
	ds_write_b128 v4, v[120:123] offset:5120
	v_mul_f32_e32 v124, 0x43000000, v124
	v_mul_f32_e32 v125, 0x43000000, v125
	v_mul_f32_e32 v126, 0x43000000, v126
	v_mul_f32_e32 v127, 0x43000000, v127
	ds_write_b128 v4, v[124:127] offset:6144
	v_mul_f32_e32 v128, 0x43000000, v128
	v_mul_f32_e32 v129, 0x43000000, v129
	v_mul_f32_e32 v130, 0x43000000, v130
	v_mul_f32_e32 v131, 0x43000000, v131
	ds_write_b128 v4, v[128:131] offset:7168
	s_waitcnt lgkmcnt(0)
	s_barrier
; #define GAS __attribute__((address_space(1)))
; #define LAS __attribute__((address_space(3)))
; #define LDS_WAIT() asm volatile("s_waitcnt lgkmcnt(0)" ::: "memory")
; __device__ __forceinline__ unsigned pk4_fp8(float a, float b, float c, float d) {
;     a = fminf(fmaxf(a, -448.f), 448.f); b = fminf(fmaxf(b, -448.f), 448.f); c = fminf(fmaxf(c, -448.f), 448.f); d = fminf(fmaxf(d, -448.f), 448.f);
;     int w = __builtin_amdgcn_cvt_pk_fp8_f32(a, b, 0, false); w = __builtin_amdgcn_cvt_pk_fp8_f32(c, d, w, true); return (unsigned)w; }
;     const int pr = item >> 1, kb = 2 * (pr / nblk) + (item & 1), nb = pr % nblk, k0 = 64 * kb, n0 = 32 * nb;
;     const int nr = n0 + (lane & 31); const int sc = MAP == 1 ? src_col_in(nr) : nr;
;     float v[32];
; #pragma unroll
;     for (int i = 0; i < 32; ++i) v[i] = sc >= 0 ? W[(size_t)(k0 + 2 * i + (lane >> 5)) * Nsrc + sc] : 0.f;
; #pragma unroll
;     for (int i = 0; i < 32; ++i) { const int k = k0 + 2 * i + (lane >> 5); float x = v[i] * wscale; if (KS) x *= (k < ksplit ? ksA[k] : ksB[k - ksplit]); scr[(2 * i + (lane >> 5)) * 33 + (lane & 31)] = x; }
;     LDS_WAIT(); asm volatile("" ::: "memory");
;     const int c = lane & 7;
; #pragma unroll
;     for (int j = 0; j < 4; ++j) { const int n = (lane >> 3) + 8 * j; const LAS float* s = scr + (8 * c) * 33 + n;
;         const unsigned long long o = (unsigned long long)pg8::pk4_fp8(s[0 * 33], s[1 * 33], s[2 * 33], s[3 * 33]) | ((unsigned long long)pg8::pk4_fp8(s[4 * 33], s[5 * 33], s[6 * 33], s[7 * 33]) << 32);
;         *(GAS unsigned long long*)(WT + (size_t)(n0 + n) * K + k0 + 8 * c) = o; }
;     LDS_WAIT(); asm volatile("" ::: "memory");
; }
	s_add_i32 s17, s16, 2112
	s_min_u32 s17, s17, 0xfff
	s_lshr_b32 s18, s17, 5
	s_add_i32 s18, s18, 0
	s_and_b32 s19, s17, 31
	s_lshl_b32 s18, s18, 21
	s_lshl_b32 s19, s19, 9
	s_add_u32 s18, s18, s19
	s_add_u32 s12, s2, s18
	s_addc_u32 s13, s3, 0
	global_load_dwordx4 v[100:103], v10, s[12:13]
	s_add_u32 s12, s12, 0x8000
	s_addc_u32 s13, s13, 0
	global_load_dwordx4 v[104:107], v10, s[12:13]
	s_add_u32 s12, s12, 0x8000
	s_addc_u32 s13, s13, 0
	global_load_dwordx4 v[108:111], v10, s[12:13]
	s_add_u32 s12, s12, 0x8000
	s_addc_u32 s13, s13, 0
	global_load_dwordx4 v[112:115], v10, s[12:13]
	s_add_u32 s12, s12, 0x8000
	s_addc_u32 s13, s13, 0
	global_load_dwordx4 v[116:119], v10, s[12:13]
	s_add_u32 s12, s12, 0x8000
	s_addc_u32 s13, s13, 0
	global_load_dwordx4 v[120:123], v10, s[12:13]
	s_add_u32 s12, s12, 0x8000
	s_addc_u32 s13, s13, 0
	global_load_dwordx4 v[124:127], v10, s[12:13]
	s_add_u32 s12, s12, 0x8000
	s_addc_u32 s13, s13, 0
	global_load_dwordx4 v[128:131], v10, s[12:13]
	s_add_i32 s17, s16, 1728
	s_min_u32 s17, s17, 0xfff
	s_lshr_b32 s18, s17, 5
	s_add_i32 s18, s18, 0
	s_and_b32 s19, s17, 31
	s_lshl_b32 s19, s19, 21
	s_lshl_b32 s18, s18, 7
	s_add_u32 s18, s18, s19
	s_add_u32 s14, s4, s18
	s_addc_u32 s15, s5, 0
	ds_read_b32 v170, v6
	ds_read_b32 v171, v6 offset:512
	ds_read_b32 v172, v6 offset:1024
	ds_read_b32 v173, v6 offset:1536
	ds_read_b32 v174, v6 offset:2048
	ds_read_b32 v175, v6 offset:2560
	ds_read_b32 v176, v6 offset:3072
	ds_read_b32 v177, v6 offset:3584
	ds_read_b32 v196, v6 offset:4096
	ds_read_b32 v197, v6 offset:4608
	ds_read_b32 v198, v6 offset:5120
	ds_read_b32 v199, v6 offset:5632
	ds_read_b32 v200, v6 offset:6144
	ds_read_b32 v201, v6 offset:6656
	ds_read_b32 v202, v6 offset:7168
	ds_read_b32 v203, v6 offset:7680
	s_waitcnt lgkmcnt(0)
	v_max_f32_e32 v170, v170, v170
	v_max_f32_e32 v171, v171, v171
	v_max_f32_e32 v172, v172, v172
	v_max_f32_e32 v173, v173, v173
	v_max_f32_e32 v174, v174, v174
	v_max_f32_e32 v175, v175, v175
	v_max_f32_e32 v176, v176, v176
	v_max_f32_e32 v177, v177, v177
	v_max_f32_e32 v196, v196, v196
	v_max_f32_e32 v197, v197, v197
	v_max_f32_e32 v198, v198, v198
	v_max_f32_e32 v199, v199, v199
	v_max_f32_e32 v200, v200, v200
	v_max_f32_e32 v201, v201, v201
	v_max_f32_e32 v202, v202, v202
	v_max_f32_e32 v203, v203, v203
	v_med3_f32 v170, v170, s20, v13
	v_med3_f32 v171, v171, s20, v13
	v_med3_f32 v172, v172, s20, v13
	v_med3_f32 v173, v173, s20, v13
	v_med3_f32 v174, v174, s20, v13
	v_med3_f32 v175, v175, s20, v13
	v_med3_f32 v176, v176, s20, v13
	v_med3_f32 v177, v177, s20, v13
	v_med3_f32 v196, v196, s20, v13
	v_med3_f32 v197, v197, s20, v13
	v_med3_f32 v198, v198, s20, v13
	v_med3_f32 v199, v199, s20, v13
	v_med3_f32 v200, v200, s20, v13
	v_med3_f32 v201, v201, s20, v13
	v_med3_f32 v202, v202, s20, v13
	v_med3_f32 v203, v203, s20, v13
	v_mov_b32_e32 v208, 0
	v_mov_b32_e32 v209, 0
	v_mov_b32_e32 v210, 0
	v_mov_b32_e32 v211, 0
	v_cvt_pk_fp8_f32 v208, v170, v171
	v_cvt_pk_fp8_f32 v209, v174, v175
	v_cvt_pk_fp8_f32 v210, v196, v197
	v_cvt_pk_fp8_f32 v211, v200, v201
	v_cvt_pk_fp8_f32 v208, v172, v173 op_sel:[0,0,1]
	v_cvt_pk_fp8_f32 v209, v176, v177 op_sel:[0,0,1]
	v_cvt_pk_fp8_f32 v210, v198, v199 op_sel:[0,0,1]
	v_cvt_pk_fp8_f32 v211, v202, v203 op_sel:[0,0,1]
	s_nop 0
	global_store_dwordx4 v11, v[208:211], s[14:15]
	ds_read_b32 v170, v8
	ds_read_b32 v171, v8 offset:512
	ds_read_b32 v172, v8 offset:1024
	ds_read_b32 v173, v8 offset:1536
	ds_read_b32 v174, v8 offset:2048
	ds_read_b32 v175, v8 offset:2560
	ds_read_b32 v176, v8 offset:3072
	ds_read_b32 v177, v8 offset:3584
	ds_read_b32 v196, v8 offset:4096
	ds_read_b32 v197, v8 offset:4608
	ds_read_b32 v198, v8 offset:5120
	ds_read_b32 v199, v8 offset:5632
	ds_read_b32 v200, v8 offset:6144
	ds_read_b32 v201, v8 offset:6656
	ds_read_b32 v202, v8 offset:7168
	ds_read_b32 v203, v8 offset:7680
	s_waitcnt lgkmcnt(0)
	v_max_f32_e32 v170, v170, v170
	v_max_f32_e32 v171, v171, v171
	v_max_f32_e32 v172, v172, v172
	v_max_f32_e32 v173, v173, v173
	v_max_f32_e32 v174, v174, v174
	v_max_f32_e32 v175, v175, v175
	v_max_f32_e32 v176, v176, v176
	v_max_f32_e32 v177, v177, v177
	v_max_f32_e32 v196, v196, v196
	v_max_f32_e32 v197, v197, v197
	v_max_f32_e32 v198, v198, v198
	v_max_f32_e32 v199, v199, v199
	v_max_f32_e32 v200, v200, v200
	v_max_f32_e32 v201, v201, v201
	v_max_f32_e32 v202, v202, v202
	v_max_f32_e32 v203, v203, v203
	v_med3_f32 v170, v170, s20, v13
	v_med3_f32 v171, v171, s20, v13
	v_med3_f32 v172, v172, s20, v13
	v_med3_f32 v173, v173, s20, v13
	v_med3_f32 v174, v174, s20, v13
	v_med3_f32 v175, v175, s20, v13
	v_med3_f32 v176, v176, s20, v13
	v_med3_f32 v177, v177, s20, v13
	v_med3_f32 v196, v196, s20, v13
	v_med3_f32 v197, v197, s20, v13
	v_med3_f32 v198, v198, s20, v13
	v_med3_f32 v199, v199, s20, v13
	v_med3_f32 v200, v200, s20, v13
	v_med3_f32 v201, v201, s20, v13
	v_med3_f32 v202, v202, s20, v13
	v_med3_f32 v203, v203, s20, v13
	v_mov_b32_e32 v208, 0
	v_mov_b32_e32 v209, 0
	v_mov_b32_e32 v210, 0
	v_mov_b32_e32 v211, 0
	v_cvt_pk_fp8_f32 v208, v170, v171
	v_cvt_pk_fp8_f32 v209, v174, v175
	v_cvt_pk_fp8_f32 v210, v196, v197
	v_cvt_pk_fp8_f32 v211, v200, v201
	v_cvt_pk_fp8_f32 v208, v172, v173 op_sel:[0,0,1]
	v_cvt_pk_fp8_f32 v209, v176, v177 op_sel:[0,0,1]
	v_cvt_pk_fp8_f32 v210, v198, v199 op_sel:[0,0,1]
	v_cvt_pk_fp8_f32 v211, v202, v203 op_sel:[0,0,1]
	s_nop 0
	global_store_dwordx4 v12, v[208:211], s[14:15]
	s_waitcnt vmcnt(32)
	v_mul_f32_e32 v132, 0x43000000, v132
	v_mul_f32_e32 v133, 0x43000000, v133
	v_mul_f32_e32 v134, 0x43000000, v134
	v_mul_f32_e32 v135, 0x43000000, v135
	ds_write_b128 v5, v[132:135]
	v_mul_f32_e32 v136, 0x43000000, v136
	v_mul_f32_e32 v137, 0x43000000, v137
	v_mul_f32_e32 v138, 0x43000000, v138
	v_mul_f32_e32 v139, 0x43000000, v139
	ds_write_b128 v5, v[136:139] offset:1024
	v_mul_f32_e32 v140, 0x43000000, v140
	v_mul_f32_e32 v141, 0x43000000, v141
	v_mul_f32_e32 v142, 0x43000000, v142
	v_mul_f32_e32 v143, 0x43000000, v143
	ds_write_b128 v5, v[140:143] offset:2048
	v_mul_f32_e32 v144, 0x43000000, v144
	v_mul_f32_e32 v145, 0x43000000, v145
	v_mul_f32_e32 v146, 0x43000000, v146
	v_mul_f32_e32 v147, 0x43000000, v147
	ds_write_b128 v5, v[144:147] offset:3072
	v_mul_f32_e32 v148, 0x43000000, v148
	v_mul_f32_e32 v149, 0x43000000, v149
	v_mul_f32_e32 v150, 0x43000000, v150
	v_mul_f32_e32 v151, 0x43000000, v151
	ds_write_b128 v5, v[148:151] offset:4096
	v_mul_f32_e32 v152, 0x43000000, v152
	v_mul_f32_e32 v153, 0x43000000, v153
	v_mul_f32_e32 v154, 0x43000000, v154
	v_mul_f32_e32 v155, 0x43000000, v155
	ds_write_b128 v5, v[152:155] offset:5120
	v_mul_f32_e32 v156, 0x43000000, v156
	v_mul_f32_e32 v157, 0x43000000, v157
	v_mul_f32_e32 v158, 0x43000000, v158
	v_mul_f32_e32 v159, 0x43000000, v159
	ds_write_b128 v5, v[156:159] offset:6144
	v_mul_f32_e32 v160, 0x43000000, v160
	v_mul_f32_e32 v161, 0x43000000, v161
	v_mul_f32_e32 v162, 0x43000000, v162
	v_mul_f32_e32 v163, 0x43000000, v163
	ds_write_b128 v5, v[160:163] offset:7168
	s_waitcnt lgkmcnt(0)
	s_barrier
; #define GAS __attribute__((address_space(1)))
; #define LAS __attribute__((address_space(3)))
; #define LDS_WAIT() asm volatile("s_waitcnt lgkmcnt(0)" ::: "memory")
; __device__ __forceinline__ unsigned pk4_fp8(float a, float b, float c, float d) {
;     a = fminf(fmaxf(a, -448.f), 448.f); b = fminf(fmaxf(b, -448.f), 448.f); c = fminf(fmaxf(c, -448.f), 448.f); d = fminf(fmaxf(d, -448.f), 448.f);
;     int w = __builtin_amdgcn_cvt_pk_fp8_f32(a, b, 0, false); w = __builtin_amdgcn_cvt_pk_fp8_f32(c, d, w, true); return (unsigned)w; }
;     const int pr = item >> 1, kb = 2 * (pr / nblk) + (item & 1), nb = pr % nblk, k0 = 64 * kb, n0 = 32 * nb;
;     const int nr = n0 + (lane & 31); const int sc = MAP == 1 ? src_col_in(nr) : nr;
;     float v[32];
; #pragma unroll
;     for (int i = 0; i < 32; ++i) v[i] = sc >= 0 ? W[(size_t)(k0 + 2 * i + (lane >> 5)) * Nsrc + sc] : 0.f;
; #pragma unroll
;     for (int i = 0; i < 32; ++i) { const int k = k0 + 2 * i + (lane >> 5); float x = v[i] * wscale; if (KS) x *= (k < ksplit ? ksA[k] : ksB[k - ksplit]); scr[(2 * i + (lane >> 5)) * 33 + (lane & 31)] = x; }
;     LDS_WAIT(); asm volatile("" ::: "memory");
;     const int c = lane & 7;
; #pragma unroll
;     for (int j = 0; j < 4; ++j) { const int n = (lane >> 3) + 8 * j; const LAS float* s = scr + (8 * c) * 33 + n;
;         const unsigned long long o = (unsigned long long)pg8::pk4_fp8(s[0 * 33], s[1 * 33], s[2 * 33], s[3 * 33]) | ((unsigned long long)pg8::pk4_fp8(s[4 * 33], s[5 * 33], s[6 * 33], s[7 * 33]) << 32);
;         *(GAS unsigned long long*)(WT + (size_t)(n0 + n) * K + k0 + 8 * c) = o; }
;     LDS_WAIT(); asm volatile("" ::: "memory");
; }
	s_add_i32 s17, s16, 2208
	s_min_u32 s17, s17, 0xfff
	s_lshr_b32 s18, s17, 5
	s_add_i32 s18, s18, 0
	s_and_b32 s19, s17, 31
	s_lshl_b32 s18, s18, 21
	s_lshl_b32 s19, s19, 9
	s_add_u32 s18, s18, s19
	s_add_u32 s12, s2, s18
	s_addc_u32 s13, s3, 0
	global_load_dwordx4 v[132:135], v10, s[12:13]
	s_add_u32 s12, s12, 0x8000
	s_addc_u32 s13, s13, 0
	global_load_dwordx4 v[136:139], v10, s[12:13]
	s_add_u32 s12, s12, 0x8000
	s_addc_u32 s13, s13, 0
	global_load_dwordx4 v[140:143], v10, s[12:13]
	s_add_u32 s12, s12, 0x8000
	s_addc_u32 s13, s13, 0
	global_load_dwordx4 v[144:147], v10, s[12:13]
	s_add_u32 s12, s12, 0x8000
	s_addc_u32 s13, s13, 0
	global_load_dwordx4 v[148:151], v10, s[12:13]
	s_add_u32 s12, s12, 0x8000
	s_addc_u32 s13, s13, 0
	global_load_dwordx4 v[152:155], v10, s[12:13]
	s_add_u32 s12, s12, 0x8000
	s_addc_u32 s13, s13, 0
	global_load_dwordx4 v[156:159], v10, s[12:13]
	s_add_u32 s12, s12, 0x8000
	s_addc_u32 s13, s13, 0
	global_load_dwordx4 v[160:163], v10, s[12:13]
	s_add_i32 s17, s16, 1824
	s_min_u32 s17, s17, 0xfff
	s_lshr_b32 s18, s17, 5
	s_add_i32 s18, s18, 0
	s_and_b32 s19, s17, 31
	s_lshl_b32 s19, s19, 21
	s_lshl_b32 s18, s18, 7
	s_add_u32 s18, s18, s19
	s_add_u32 s14, s4, s18
	s_addc_u32 s15, s5, 0
	ds_read_b32 v170, v7
	ds_read_b32 v171, v7 offset:512
	ds_read_b32 v172, v7 offset:1024
	ds_read_b32 v173, v7 offset:1536
	ds_read_b32 v174, v7 offset:2048
	ds_read_b32 v175, v7 offset:2560
	ds_read_b32 v176, v7 offset:3072
	ds_read_b32 v177, v7 offset:3584
	ds_read_b32 v196, v7 offset:4096
	ds_read_b32 v197, v7 offset:4608
	ds_read_b32 v198, v7 offset:5120
	ds_read_b32 v199, v7 offset:5632
	ds_read_b32 v200, v7 offset:6144
	ds_read_b32 v201, v7 offset:6656
	ds_read_b32 v202, v7 offset:7168
	ds_read_b32 v203, v7 offset:7680
	s_waitcnt lgkmcnt(0)
	v_max_f32_e32 v170, v170, v170
	v_max_f32_e32 v171, v171, v171
	v_max_f32_e32 v172, v172, v172
	v_max_f32_e32 v173, v173, v173
	v_max_f32_e32 v174, v174, v174
	v_max_f32_e32 v175, v175, v175
	v_max_f32_e32 v176, v176, v176
	v_max_f32_e32 v177, v177, v177
	v_max_f32_e32 v196, v196, v196
	v_max_f32_e32 v197, v197, v197
	v_max_f32_e32 v198, v198, v198
	v_max_f32_e32 v199, v199, v199
	v_max_f32_e32 v200, v200, v200
	v_max_f32_e32 v201, v201, v201
	v_max_f32_e32 v202, v202, v202
	v_max_f32_e32 v203, v203, v203
	v_med3_f32 v170, v170, s20, v13
	v_med3_f32 v171, v171, s20, v13
	v_med3_f32 v172, v172, s20, v13
	v_med3_f32 v173, v173, s20, v13
	v_med3_f32 v174, v174, s20, v13
	v_med3_f32 v175, v175, s20, v13
	v_med3_f32 v176, v176, s20, v13
	v_med3_f32 v177, v177, s20, v13
	v_med3_f32 v196, v196, s20, v13
	v_med3_f32 v197, v197, s20, v13
	v_med3_f32 v198, v198, s20, v13
	v_med3_f32 v199, v199, s20, v13
	v_med3_f32 v200, v200, s20, v13
	v_med3_f32 v201, v201, s20, v13
	v_med3_f32 v202, v202, s20, v13
	v_med3_f32 v203, v203, s20, v13
	v_mov_b32_e32 v208, 0
	v_mov_b32_e32 v209, 0
	v_mov_b32_e32 v210, 0
	v_mov_b32_e32 v211, 0
	v_cvt_pk_fp8_f32 v208, v170, v171
	v_cvt_pk_fp8_f32 v209, v174, v175
	v_cvt_pk_fp8_f32 v210, v196, v197
	v_cvt_pk_fp8_f32 v211, v200, v201
	v_cvt_pk_fp8_f32 v208, v172, v173 op_sel:[0,0,1]
	v_cvt_pk_fp8_f32 v209, v176, v177 op_sel:[0,0,1]
	v_cvt_pk_fp8_f32 v210, v198, v199 op_sel:[0,0,1]
	v_cvt_pk_fp8_f32 v211, v202, v203 op_sel:[0,0,1]
	s_nop 0
	global_store_dwordx4 v11, v[208:211], s[14:15]
	ds_read_b32 v170, v9
	ds_read_b32 v171, v9 offset:512
	ds_read_b32 v172, v9 offset:1024
	ds_read_b32 v173, v9 offset:1536
	ds_read_b32 v174, v9 offset:2048
	ds_read_b32 v175, v9 offset:2560
	ds_read_b32 v176, v9 offset:3072
	ds_read_b32 v177, v9 offset:3584
	ds_read_b32 v196, v9 offset:4096
	ds_read_b32 v197, v9 offset:4608
	ds_read_b32 v198, v9 offset:5120
	ds_read_b32 v199, v9 offset:5632
	ds_read_b32 v200, v9 offset:6144
	ds_read_b32 v201, v9 offset:6656
	ds_read_b32 v202, v9 offset:7168
	ds_read_b32 v203, v9 offset:7680
	s_waitcnt lgkmcnt(0)
	v_max_f32_e32 v170, v170, v170
	v_max_f32_e32 v171, v171, v171
	v_max_f32_e32 v172, v172, v172
	v_max_f32_e32 v173, v173, v173
	v_max_f32_e32 v174, v174, v174
	v_max_f32_e32 v175, v175, v175
	v_max_f32_e32 v176, v176, v176
	v_max_f32_e32 v177, v177, v177
	v_max_f32_e32 v196, v196, v196
	v_max_f32_e32 v197, v197, v197
	v_max_f32_e32 v198, v198, v198
	v_max_f32_e32 v199, v199, v199
	v_max_f32_e32 v200, v200, v200
	v_max_f32_e32 v201, v201, v201
	v_max_f32_e32 v202, v202, v202
	v_max_f32_e32 v203, v203, v203
	v_med3_f32 v170, v170, s20, v13
	v_med3_f32 v171, v171, s20, v13
	v_med3_f32 v172, v172, s20, v13
	v_med3_f32 v173, v173, s20, v13
	v_med3_f32 v174, v174, s20, v13
	v_med3_f32 v175, v175, s20, v13
	v_med3_f32 v176, v176, s20, v13
	v_med3_f32 v177, v177, s20, v13
	v_med3_f32 v196, v196, s20, v13
	v_med3_f32 v197, v197, s20, v13
	v_med3_f32 v198, v198, s20, v13
	v_med3_f32 v199, v199, s20, v13
	v_med3_f32 v200, v200, s20, v13
	v_med3_f32 v201, v201, s20, v13
	v_med3_f32 v202, v202, s20, v13
	v_med3_f32 v203, v203, s20, v13
	v_mov_b32_e32 v208, 0
	v_mov_b32_e32 v209, 0
	v_mov_b32_e32 v210, 0
	v_mov_b32_e32 v211, 0
	v_cvt_pk_fp8_f32 v208, v170, v171
	v_cvt_pk_fp8_f32 v209, v174, v175
	v_cvt_pk_fp8_f32 v210, v196, v197
	v_cvt_pk_fp8_f32 v211, v200, v201
	v_cvt_pk_fp8_f32 v208, v172, v173 op_sel:[0,0,1]
	v_cvt_pk_fp8_f32 v209, v176, v177 op_sel:[0,0,1]
	v_cvt_pk_fp8_f32 v210, v198, v199 op_sel:[0,0,1]
	v_cvt_pk_fp8_f32 v211, v202, v203 op_sel:[0,0,1]
	s_nop 0
	global_store_dwordx4 v12, v[208:211], s[14:15]
	s_waitcnt vmcnt(32)
	v_mul_f32_e32 v36, 0x43000000, v36
	v_mul_f32_e32 v37, 0x43000000, v37
	v_mul_f32_e32 v38, 0x43000000, v38
	v_mul_f32_e32 v39, 0x43000000, v39
	ds_write_b128 v4, v[36:39]
	v_mul_f32_e32 v40, 0x43000000, v40
	v_mul_f32_e32 v41, 0x43000000, v41
	v_mul_f32_e32 v42, 0x43000000, v42
	v_mul_f32_e32 v43, 0x43000000, v43
	ds_write_b128 v4, v[40:43] offset:1024
	v_mul_f32_e32 v44, 0x43000000, v44
	v_mul_f32_e32 v45, 0x43000000, v45
	v_mul_f32_e32 v46, 0x43000000, v46
	v_mul_f32_e32 v47, 0x43000000, v47
	ds_write_b128 v4, v[44:47] offset:2048
	v_mul_f32_e32 v48, 0x43000000, v48
	v_mul_f32_e32 v49, 0x43000000, v49
	v_mul_f32_e32 v50, 0x43000000, v50
	v_mul_f32_e32 v51, 0x43000000, v51
	ds_write_b128 v4, v[48:51] offset:3072
	v_mul_f32_e32 v52, 0x43000000, v52
	v_mul_f32_e32 v53, 0x43000000, v53
	v_mul_f32_e32 v54, 0x43000000, v54
	v_mul_f32_e32 v55, 0x43000000, v55
	ds_write_b128 v4, v[52:55] offset:4096
	v_mul_f32_e32 v56, 0x43000000, v56
	v_mul_f32_e32 v57, 0x43000000, v57
	v_mul_f32_e32 v58, 0x43000000, v58
	v_mul_f32_e32 v59, 0x43000000, v59
	ds_write_b128 v4, v[56:59] offset:5120
	v_mul_f32_e32 v60, 0x43000000, v60
	v_mul_f32_e32 v61, 0x43000000, v61
	v_mul_f32_e32 v62, 0x43000000, v62
	v_mul_f32_e32 v63, 0x43000000, v63
	ds_write_b128 v4, v[60:63] offset:6144
	v_mul_f32_e32 v64, 0x43000000, v64
	v_mul_f32_e32 v65, 0x43000000, v65
	v_mul_f32_e32 v66, 0x43000000, v66
	v_mul_f32_e32 v67, 0x43000000, v67
	ds_write_b128 v4, v[64:67] offset:7168
	s_waitcnt lgkmcnt(0)
	s_barrier
; #define GAS __attribute__((address_space(1)))
; #define LAS __attribute__((address_space(3)))
; #define LDS_WAIT() asm volatile("s_waitcnt lgkmcnt(0)" ::: "memory")
; __device__ __forceinline__ unsigned pk4_fp8(float a, float b, float c, float d) {
;     a = fminf(fmaxf(a, -448.f), 448.f); b = fminf(fmaxf(b, -448.f), 448.f); c = fminf(fmaxf(c, -448.f), 448.f); d = fminf(fmaxf(d, -448.f), 448.f);
;     int w = __builtin_amdgcn_cvt_pk_fp8_f32(a, b, 0, false); w = __builtin_amdgcn_cvt_pk_fp8_f32(c, d, w, true); return (unsigned)w; }
;     const int pr = item >> 1, kb = 2 * (pr / nblk) + (item & 1), nb = pr % nblk, k0 = 64 * kb, n0 = 32 * nb;
;     const int nr = n0 + (lane & 31); const int sc = MAP == 1 ? src_col_in(nr) : nr;
;     float v[32];
; #pragma unroll
;     for (int i = 0; i < 32; ++i) v[i] = sc >= 0 ? W[(size_t)(k0 + 2 * i + (lane >> 5)) * Nsrc + sc] : 0.f;
; #pragma unroll
;     for (int i = 0; i < 32; ++i) { const int k = k0 + 2 * i + (lane >> 5); float x = v[i] * wscale; if (KS) x *= (k < ksplit ? ksA[k] : ksB[k - ksplit]); scr[(2 * i + (lane >> 5)) * 33 + (lane & 31)] = x; }
;     LDS_WAIT(); asm volatile("" ::: "memory");
;     const int c = lane & 7;
; #pragma unroll
;     for (int j = 0; j < 4; ++j) { const int n = (lane >> 3) + 8 * j; const LAS float* s = scr + (8 * c) * 33 + n;
;         const unsigned long long o = (unsigned long long)pg8::pk4_fp8(s[0 * 33], s[1 * 33], s[2 * 33], s[3 * 33]) | ((unsigned long long)pg8::pk4_fp8(s[4 * 33], s[5 * 33], s[6 * 33], s[7 * 33]) << 32);
;         *(GAS unsigned long long*)(WT + (size_t)(n0 + n) * K + k0 + 8 * c) = o; }
;     LDS_WAIT(); asm volatile("" ::: "memory");
; }
	s_add_i32 s17, s16, 2304
	s_min_u32 s17, s17, 0xfff
	s_lshr_b32 s18, s17, 5
	s_add_i32 s18, s18, 0
	s_and_b32 s19, s17, 31
	s_lshl_b32 s18, s18, 21
	s_lshl_b32 s19, s19, 9
	s_add_u32 s18, s18, s19
	s_add_u32 s12, s2, s18
	s_addc_u32 s13, s3, 0
	global_load_dwordx4 v[36:39], v10, s[12:13]
	s_add_u32 s12, s12, 0x8000
	s_addc_u32 s13, s13, 0
	global_load_dwordx4 v[40:43], v10, s[12:13]
	s_add_u32 s12, s12, 0x8000
	s_addc_u32 s13, s13, 0
	global_load_dwordx4 v[44:47], v10, s[12:13]
	s_add_u32 s12, s12, 0x8000
	s_addc_u32 s13, s13, 0
	global_load_dwordx4 v[48:51], v10, s[12:13]
	s_add_u32 s12, s12, 0x8000
	s_addc_u32 s13, s13, 0
	global_load_dwordx4 v[52:55], v10, s[12:13]
	s_add_u32 s12, s12, 0x8000
	s_addc_u32 s13, s13, 0
	global_load_dwordx4 v[56:59], v10, s[12:13]
	s_add_u32 s12, s12, 0x8000
	s_addc_u32 s13, s13, 0
	global_load_dwordx4 v[60:63], v10, s[12:13]
	s_add_u32 s12, s12, 0x8000
	s_addc_u32 s13, s13, 0
	global_load_dwordx4 v[64:67], v10, s[12:13]
	s_add_i32 s17, s16, 1920
	s_min_u32 s17, s17, 0xfff
	s_lshr_b32 s18, s17, 5
	s_add_i32 s18, s18, 0
	s_and_b32 s19, s17, 31
	s_lshl_b32 s19, s19, 21
	s_lshl_b32 s18, s18, 7
	s_add_u32 s18, s18, s19
	s_add_u32 s14, s4, s18
	s_addc_u32 s15, s5, 0
	ds_read_b32 v170, v6
	ds_read_b32 v171, v6 offset:512
	ds_read_b32 v172, v6 offset:1024
	ds_read_b32 v173, v6 offset:1536
	ds_read_b32 v174, v6 offset:2048
	ds_read_b32 v175, v6 offset:2560
	ds_read_b32 v176, v6 offset:3072
	ds_read_b32 v177, v6 offset:3584
	ds_read_b32 v196, v6 offset:4096
	ds_read_b32 v197, v6 offset:4608
	ds_read_b32 v198, v6 offset:5120
	ds_read_b32 v199, v6 offset:5632
	ds_read_b32 v200, v6 offset:6144
	ds_read_b32 v201, v6 offset:6656
	ds_read_b32 v202, v6 offset:7168
	ds_read_b32 v203, v6 offset:7680
	s_waitcnt lgkmcnt(0)
	v_max_f32_e32 v170, v170, v170
	v_max_f32_e32 v171, v171, v171
	v_max_f32_e32 v172, v172, v172
	v_max_f32_e32 v173, v173, v173
	v_max_f32_e32 v174, v174, v174
	v_max_f32_e32 v175, v175, v175
	v_max_f32_e32 v176, v176, v176
	v_max_f32_e32 v177, v177, v177
	v_max_f32_e32 v196, v196, v196
	v_max_f32_e32 v197, v197, v197
	v_max_f32_e32 v198, v198, v198
	v_max_f32_e32 v199, v199, v199
	v_max_f32_e32 v200, v200, v200
	v_max_f32_e32 v201, v201, v201
	v_max_f32_e32 v202, v202, v202
	v_max_f32_e32 v203, v203, v203
	v_med3_f32 v170, v170, s20, v13
	v_med3_f32 v171, v171, s20, v13
	v_med3_f32 v172, v172, s20, v13
	v_med3_f32 v173, v173, s20, v13
	v_med3_f32 v174, v174, s20, v13
	v_med3_f32 v175, v175, s20, v13
	v_med3_f32 v176, v176, s20, v13
	v_med3_f32 v177, v177, s20, v13
	v_med3_f32 v196, v196, s20, v13
	v_med3_f32 v197, v197, s20, v13
	v_med3_f32 v198, v198, s20, v13
	v_med3_f32 v199, v199, s20, v13
	v_med3_f32 v200, v200, s20, v13
	v_med3_f32 v201, v201, s20, v13
	v_med3_f32 v202, v202, s20, v13
	v_med3_f32 v203, v203, s20, v13
	v_mov_b32_e32 v208, 0
	v_mov_b32_e32 v209, 0
	v_mov_b32_e32 v210, 0
	v_mov_b32_e32 v211, 0
	v_cvt_pk_fp8_f32 v208, v170, v171
	v_cvt_pk_fp8_f32 v209, v174, v175
	v_cvt_pk_fp8_f32 v210, v196, v197
	v_cvt_pk_fp8_f32 v211, v200, v201
	v_cvt_pk_fp8_f32 v208, v172, v173 op_sel:[0,0,1]
	v_cvt_pk_fp8_f32 v209, v176, v177 op_sel:[0,0,1]
	v_cvt_pk_fp8_f32 v210, v198, v199 op_sel:[0,0,1]
	v_cvt_pk_fp8_f32 v211, v202, v203 op_sel:[0,0,1]
	s_nop 0
	global_store_dwordx4 v11, v[208:211], s[14:15]
	ds_read_b32 v170, v8
	ds_read_b32 v171, v8 offset:512
	ds_read_b32 v172, v8 offset:1024
	ds_read_b32 v173, v8 offset:1536
	ds_read_b32 v174, v8 offset:2048
	ds_read_b32 v175, v8 offset:2560
	ds_read_b32 v176, v8 offset:3072
	ds_read_b32 v177, v8 offset:3584
	ds_read_b32 v196, v8 offset:4096
	ds_read_b32 v197, v8 offset:4608
	ds_read_b32 v198, v8 offset:5120
	ds_read_b32 v199, v8 offset:5632
	ds_read_b32 v200, v8 offset:6144
	ds_read_b32 v201, v8 offset:6656
	ds_read_b32 v202, v8 offset:7168
	ds_read_b32 v203, v8 offset:7680
	s_waitcnt lgkmcnt(0)
	v_max_f32_e32 v170, v170, v170
	v_max_f32_e32 v171, v171, v171
	v_max_f32_e32 v172, v172, v172
	v_max_f32_e32 v173, v173, v173
	v_max_f32_e32 v174, v174, v174
	v_max_f32_e32 v175, v175, v175
	v_max_f32_e32 v176, v176, v176
	v_max_f32_e32 v177, v177, v177
	v_max_f32_e32 v196, v196, v196
	v_max_f32_e32 v197, v197, v197
	v_max_f32_e32 v198, v198, v198
	v_max_f32_e32 v199, v199, v199
	v_max_f32_e32 v200, v200, v200
	v_max_f32_e32 v201, v201, v201
	v_max_f32_e32 v202, v202, v202
	v_max_f32_e32 v203, v203, v203
	v_med3_f32 v170, v170, s20, v13
	v_med3_f32 v171, v171, s20, v13
	v_med3_f32 v172, v172, s20, v13
	v_med3_f32 v173, v173, s20, v13
	v_med3_f32 v174, v174, s20, v13
	v_med3_f32 v175, v175, s20, v13
	v_med3_f32 v176, v176, s20, v13
	v_med3_f32 v177, v177, s20, v13
	v_med3_f32 v196, v196, s20, v13
	v_med3_f32 v197, v197, s20, v13
	v_med3_f32 v198, v198, s20, v13
	v_med3_f32 v199, v199, s20, v13
	v_med3_f32 v200, v200, s20, v13
	v_med3_f32 v201, v201, s20, v13
	v_med3_f32 v202, v202, s20, v13
	v_med3_f32 v203, v203, s20, v13
	v_mov_b32_e32 v208, 0
	v_mov_b32_e32 v209, 0
	v_mov_b32_e32 v210, 0
	v_mov_b32_e32 v211, 0
	v_cvt_pk_fp8_f32 v208, v170, v171
	v_cvt_pk_fp8_f32 v209, v174, v175
	v_cvt_pk_fp8_f32 v210, v196, v197
	v_cvt_pk_fp8_f32 v211, v200, v201
	v_cvt_pk_fp8_f32 v208, v172, v173 op_sel:[0,0,1]
	v_cvt_pk_fp8_f32 v209, v176, v177 op_sel:[0,0,1]
	v_cvt_pk_fp8_f32 v210, v198, v199 op_sel:[0,0,1]
	v_cvt_pk_fp8_f32 v211, v202, v203 op_sel:[0,0,1]
	s_nop 0
	global_store_dwordx4 v12, v[208:211], s[14:15]
	s_waitcnt vmcnt(32)
	v_mul_f32_e32 v68, 0x43000000, v68
	v_mul_f32_e32 v69, 0x43000000, v69
	v_mul_f32_e32 v70, 0x43000000, v70
	v_mul_f32_e32 v71, 0x43000000, v71
	ds_write_b128 v5, v[68:71]
	v_mul_f32_e32 v72, 0x43000000, v72
	v_mul_f32_e32 v73, 0x43000000, v73
	v_mul_f32_e32 v74, 0x43000000, v74
	v_mul_f32_e32 v75, 0x43000000, v75
	ds_write_b128 v5, v[72:75] offset:1024
	v_mul_f32_e32 v76, 0x43000000, v76
	v_mul_f32_e32 v77, 0x43000000, v77
	v_mul_f32_e32 v78, 0x43000000, v78
	v_mul_f32_e32 v79, 0x43000000, v79
	ds_write_b128 v5, v[76:79] offset:2048
	v_mul_f32_e32 v80, 0x43000000, v80
	v_mul_f32_e32 v81, 0x43000000, v81
	v_mul_f32_e32 v82, 0x43000000, v82
	v_mul_f32_e32 v83, 0x43000000, v83
	ds_write_b128 v5, v[80:83] offset:3072
	v_mul_f32_e32 v84, 0x43000000, v84
	v_mul_f32_e32 v85, 0x43000000, v85
	v_mul_f32_e32 v86, 0x43000000, v86
	v_mul_f32_e32 v87, 0x43000000, v87
	ds_write_b128 v5, v[84:87] offset:4096
	v_mul_f32_e32 v88, 0x43000000, v88
	v_mul_f32_e32 v89, 0x43000000, v89
	v_mul_f32_e32 v90, 0x43000000, v90
	v_mul_f32_e32 v91, 0x43000000, v91
	ds_write_b128 v5, v[88:91] offset:5120
	v_mul_f32_e32 v92, 0x43000000, v92
	v_mul_f32_e32 v93, 0x43000000, v93
	v_mul_f32_e32 v94, 0x43000000, v94
	v_mul_f32_e32 v95, 0x43000000, v95
	ds_write_b128 v5, v[92:95] offset:6144
	v_mul_f32_e32 v96, 0x43000000, v96
	v_mul_f32_e32 v97, 0x43000000, v97
	v_mul_f32_e32 v98, 0x43000000, v98
	v_mul_f32_e32 v99, 0x43000000, v99
	ds_write_b128 v5, v[96:99] offset:7168
	s_waitcnt lgkmcnt(0)
	s_barrier
; #define GAS __attribute__((address_space(1)))
; #define LAS __attribute__((address_space(3)))
; #define LDS_WAIT() asm volatile("s_waitcnt lgkmcnt(0)" ::: "memory")
; __device__ __forceinline__ unsigned pk4_fp8(float a, float b, float c, float d) {
;     a = fminf(fmaxf(a, -448.f), 448.f); b = fminf(fmaxf(b, -448.f), 448.f); c = fminf(fmaxf(c, -448.f), 448.f); d = fminf(fmaxf(d, -448.f), 448.f);
;     int w = __builtin_amdgcn_cvt_pk_fp8_f32(a, b, 0, false); w = __builtin_amdgcn_cvt_pk_fp8_f32(c, d, w, true); return (unsigned)w; }
;     const int pr = item >> 1, kb = 2 * (pr / nblk) + (item & 1), nb = pr % nblk, k0 = 64 * kb, n0 = 32 * nb;
;     const int nr = n0 + (lane & 31); const int sc = MAP == 1 ? src_col_in(nr) : nr;
;     float v[32];
; #pragma unroll
;     for (int i = 0; i < 32; ++i) v[i] = sc >= 0 ? W[(size_t)(k0 + 2 * i + (lane >> 5)) * Nsrc + sc] : 0.f;
; #pragma unroll
;     for (int i = 0; i < 32; ++i) { const int k = k0 + 2 * i + (lane >> 5); float x = v[i] * wscale; if (KS) x *= (k < ksplit ? ksA[k] : ksB[k - ksplit]); scr[(2 * i + (lane >> 5)) * 33 + (lane & 31)] = x; }
;     LDS_WAIT(); asm volatile("" ::: "memory");
;     const int c = lane & 7;
; #pragma unroll
;     for (int j = 0; j < 4; ++j) { const int n = (lane >> 3) + 8 * j; const LAS float* s = scr + (8 * c) * 33 + n;
;         const unsigned long long o = (unsigned long long)pg8::pk4_fp8(s[0 * 33], s[1 * 33], s[2 * 33], s[3 * 33]) | ((unsigned long long)pg8::pk4_fp8(s[4 * 33], s[5 * 33], s[6 * 33], s[7 * 33]) << 32);
;         *(GAS unsigned long long*)(WT + (size_t)(n0 + n) * K + k0 + 8 * c) = o; }
;     LDS_WAIT(); asm volatile("" ::: "memory");
; }
	s_add_i32 s17, s16, 2400
	s_min_u32 s17, s17, 0xfff
	s_lshr_b32 s18, s17, 5
	s_add_i32 s18, s18, 0
	s_and_b32 s19, s17, 31
	s_lshl_b32 s18, s18, 21
	s_lshl_b32 s19, s19, 9
	s_add_u32 s18, s18, s19
	s_add_u32 s12, s2, s18
	s_addc_u32 s13, s3, 0
	global_load_dwordx4 v[68:71], v10, s[12:13]
	s_add_u32 s12, s12, 0x8000
	s_addc_u32 s13, s13, 0
	global_load_dwordx4 v[72:75], v10, s[12:13]
	s_add_u32 s12, s12, 0x8000
	s_addc_u32 s13, s13, 0
	global_load_dwordx4 v[76:79], v10, s[12:13]
	s_add_u32 s12, s12, 0x8000
	s_addc_u32 s13, s13, 0
	global_load_dwordx4 v[80:83], v10, s[12:13]
	s_add_u32 s12, s12, 0x8000
	s_addc_u32 s13, s13, 0
	global_load_dwordx4 v[84:87], v10, s[12:13]
	s_add_u32 s12, s12, 0x8000
	s_addc_u32 s13, s13, 0
	global_load_dwordx4 v[88:91], v10, s[12:13]
	s_add_u32 s12, s12, 0x8000
	s_addc_u32 s13, s13, 0
	global_load_dwordx4 v[92:95], v10, s[12:13]
	s_add_u32 s12, s12, 0x8000
	s_addc_u32 s13, s13, 0
	global_load_dwordx4 v[96:99], v10, s[12:13]
	s_add_i32 s17, s16, 2016
	s_min_u32 s17, s17, 0xfff
	s_lshr_b32 s18, s17, 5
	s_add_i32 s18, s18, 0
	s_and_b32 s19, s17, 31
	s_lshl_b32 s19, s19, 21
	s_lshl_b32 s18, s18, 7
	s_add_u32 s18, s18, s19
	s_add_u32 s14, s4, s18
	s_addc_u32 s15, s5, 0
	ds_read_b32 v170, v7
	ds_read_b32 v171, v7 offset:512
	ds_read_b32 v172, v7 offset:1024
	ds_read_b32 v173, v7 offset:1536
	ds_read_b32 v174, v7 offset:2048
	ds_read_b32 v175, v7 offset:2560
	ds_read_b32 v176, v7 offset:3072
	ds_read_b32 v177, v7 offset:3584
	ds_read_b32 v196, v7 offset:4096
	ds_read_b32 v197, v7 offset:4608
	ds_read_b32 v198, v7 offset:5120
	ds_read_b32 v199, v7 offset:5632
	ds_read_b32 v200, v7 offset:6144
	ds_read_b32 v201, v7 offset:6656
	ds_read_b32 v202, v7 offset:7168
	ds_read_b32 v203, v7 offset:7680
	s_waitcnt lgkmcnt(0)
	v_max_f32_e32 v170, v170, v170
	v_max_f32_e32 v171, v171, v171
	v_max_f32_e32 v172, v172, v172
	v_max_f32_e32 v173, v173, v173
	v_max_f32_e32 v174, v174, v174
	v_max_f32_e32 v175, v175, v175
	v_max_f32_e32 v176, v176, v176
	v_max_f32_e32 v177, v177, v177
	v_max_f32_e32 v196, v196, v196
	v_max_f32_e32 v197, v197, v197
	v_max_f32_e32 v198, v198, v198
	v_max_f32_e32 v199, v199, v199
	v_max_f32_e32 v200, v200, v200
	v_max_f32_e32 v201, v201, v201
	v_max_f32_e32 v202, v202, v202
	v_max_f32_e32 v203, v203, v203
	v_med3_f32 v170, v170, s20, v13
	v_med3_f32 v171, v171, s20, v13
	v_med3_f32 v172, v172, s20, v13
	v_med3_f32 v173, v173, s20, v13
	v_med3_f32 v174, v174, s20, v13
	v_med3_f32 v175, v175, s20, v13
	v_med3_f32 v176, v176, s20, v13
	v_med3_f32 v177, v177, s20, v13
	v_med3_f32 v196, v196, s20, v13
	v_med3_f32 v197, v197, s20, v13
	v_med3_f32 v198, v198, s20, v13
	v_med3_f32 v199, v199, s20, v13
	v_med3_f32 v200, v200, s20, v13
	v_med3_f32 v201, v201, s20, v13
	v_med3_f32 v202, v202, s20, v13
	v_med3_f32 v203, v203, s20, v13
	v_mov_b32_e32 v208, 0
	v_mov_b32_e32 v209, 0
	v_mov_b32_e32 v210, 0
	v_mov_b32_e32 v211, 0
	v_cvt_pk_fp8_f32 v208, v170, v171
	v_cvt_pk_fp8_f32 v209, v174, v175
	v_cvt_pk_fp8_f32 v210, v196, v197
	v_cvt_pk_fp8_f32 v211, v200, v201
	v_cvt_pk_fp8_f32 v208, v172, v173 op_sel:[0,0,1]
	v_cvt_pk_fp8_f32 v209, v176, v177 op_sel:[0,0,1]
	v_cvt_pk_fp8_f32 v210, v198, v199 op_sel:[0,0,1]
	v_cvt_pk_fp8_f32 v211, v202, v203 op_sel:[0,0,1]
	s_nop 0
	global_store_dwordx4 v11, v[208:211], s[14:15]
	ds_read_b32 v170, v9
	ds_read_b32 v171, v9 offset:512
	ds_read_b32 v172, v9 offset:1024
	ds_read_b32 v173, v9 offset:1536
	ds_read_b32 v174, v9 offset:2048
	ds_read_b32 v175, v9 offset:2560
	ds_read_b32 v176, v9 offset:3072
	ds_read_b32 v177, v9 offset:3584
	ds_read_b32 v196, v9 offset:4096
	ds_read_b32 v197, v9 offset:4608
	ds_read_b32 v198, v9 offset:5120
	ds_read_b32 v199, v9 offset:5632
	ds_read_b32 v200, v9 offset:6144
	ds_read_b32 v201, v9 offset:6656
	ds_read_b32 v202, v9 offset:7168
	ds_read_b32 v203, v9 offset:7680
	s_waitcnt lgkmcnt(0)
	v_max_f32_e32 v170, v170, v170
	v_max_f32_e32 v171, v171, v171
	v_max_f32_e32 v172, v172, v172
	v_max_f32_e32 v173, v173, v173
	v_max_f32_e32 v174, v174, v174
	v_max_f32_e32 v175, v175, v175
	v_max_f32_e32 v176, v176, v176
	v_max_f32_e32 v177, v177, v177
	v_max_f32_e32 v196, v196, v196
	v_max_f32_e32 v197, v197, v197
	v_max_f32_e32 v198, v198, v198
	v_max_f32_e32 v199, v199, v199
	v_max_f32_e32 v200, v200, v200
	v_max_f32_e32 v201, v201, v201
	v_max_f32_e32 v202, v202, v202
	v_max_f32_e32 v203, v203, v203
	v_med3_f32 v170, v170, s20, v13
	v_med3_f32 v171, v171, s20, v13
	v_med3_f32 v172, v172, s20, v13
	v_med3_f32 v173, v173, s20, v13
	v_med3_f32 v174, v174, s20, v13
	v_med3_f32 v175, v175, s20, v13
	v_med3_f32 v176, v176, s20, v13
	v_med3_f32 v177, v177, s20, v13
	v_med3_f32 v196, v196, s20, v13
	v_med3_f32 v197, v197, s20, v13
	v_med3_f32 v198, v198, s20, v13
	v_med3_f32 v199, v199, s20, v13
	v_med3_f32 v200, v200, s20, v13
	v_med3_f32 v201, v201, s20, v13
	v_med3_f32 v202, v202, s20, v13
	v_med3_f32 v203, v203, s20, v13
	v_mov_b32_e32 v208, 0
	v_mov_b32_e32 v209, 0
	v_mov_b32_e32 v210, 0
	v_mov_b32_e32 v211, 0
	v_cvt_pk_fp8_f32 v208, v170, v171
	v_cvt_pk_fp8_f32 v209, v174, v175
	v_cvt_pk_fp8_f32 v210, v196, v197
	v_cvt_pk_fp8_f32 v211, v200, v201
	v_cvt_pk_fp8_f32 v208, v172, v173 op_sel:[0,0,1]
	v_cvt_pk_fp8_f32 v209, v176, v177 op_sel:[0,0,1]
	v_cvt_pk_fp8_f32 v210, v198, v199 op_sel:[0,0,1]
	v_cvt_pk_fp8_f32 v211, v202, v203 op_sel:[0,0,1]
	s_nop 0
	global_store_dwordx4 v12, v[208:211], s[14:15]
	s_waitcnt vmcnt(32)
	v_mul_f32_e32 v100, 0x43000000, v100
	v_mul_f32_e32 v101, 0x43000000, v101
	v_mul_f32_e32 v102, 0x43000000, v102
	v_mul_f32_e32 v103, 0x43000000, v103
	ds_write_b128 v4, v[100:103]
	v_mul_f32_e32 v104, 0x43000000, v104
	v_mul_f32_e32 v105, 0x43000000, v105
	v_mul_f32_e32 v106, 0x43000000, v106
	v_mul_f32_e32 v107, 0x43000000, v107
	ds_write_b128 v4, v[104:107] offset:1024
	v_mul_f32_e32 v108, 0x43000000, v108
	v_mul_f32_e32 v109, 0x43000000, v109
	v_mul_f32_e32 v110, 0x43000000, v110
	v_mul_f32_e32 v111, 0x43000000, v111
	ds_write_b128 v4, v[108:111] offset:2048
	v_mul_f32_e32 v112, 0x43000000, v112
	v_mul_f32_e32 v113, 0x43000000, v113
	v_mul_f32_e32 v114, 0x43000000, v114
	v_mul_f32_e32 v115, 0x43000000, v115
	ds_write_b128 v4, v[112:115] offset:3072
	v_mul_f32_e32 v116, 0x43000000, v116
	v_mul_f32_e32 v117, 0x43000000, v117
	v_mul_f32_e32 v118, 0x43000000, v118
	v_mul_f32_e32 v119, 0x43000000, v119
	ds_write_b128 v4, v[116:119] offset:4096
	v_mul_f32_e32 v120, 0x43000000, v120
	v_mul_f32_e32 v121, 0x43000000, v121
	v_mul_f32_e32 v122, 0x43000000, v122
	v_mul_f32_e32 v123, 0x43000000, v123
	ds_write_b128 v4, v[120:123] offset:5120
	v_mul_f32_e32 v124, 0x43000000, v124
	v_mul_f32_e32 v125, 0x43000000, v125
	v_mul_f32_e32 v126, 0x43000000, v126
	v_mul_f32_e32 v127, 0x43000000, v127
	ds_write_b128 v4, v[124:127] offset:6144
	v_mul_f32_e32 v128, 0x43000000, v128
	v_mul_f32_e32 v129, 0x43000000, v129
	v_mul_f32_e32 v130, 0x43000000, v130
	v_mul_f32_e32 v131, 0x43000000, v131
	ds_write_b128 v4, v[128:131] offset:7168
	s_waitcnt lgkmcnt(0)
	s_barrier
; #define GAS __attribute__((address_space(1)))
; #define LAS __attribute__((address_space(3)))
; #define LDS_WAIT() asm volatile("s_waitcnt lgkmcnt(0)" ::: "memory")
;     ...
;     for (int i = 0; i < 32; ++i) v[i] = sc >= 0 ? W[(size_t)(k0 + 2 * i + (lane >> 5)) * Nsrc + sc] : 0.f;
; #pragma unroll
;     for (int i = 0; i < 32; ++i) { const int k = k0 + 2 * i + (lane >> 5); float x = v[i] * wscale; if (KS) x *= (k < ksplit ? ksA[k] : ksB[k - ksplit]); scr[(2 * i + (lane >> 5)) * 33 + (lane & 31)] = x; }
;     LDS_WAIT(); asm volatile("" ::: "memory");
;     const int c = lane & 7;
; #pragma unroll
;     for (int j = 0; j < 4; ++j) { const int n = (lane >> 3) + 8 * j; const LAS float* s = scr + (8 * c) * 33 + n;
;         const unsigned long long o = (unsigned long long)pg8::pk4_fp8(s[0 * 33], s[1 * 33], s[2 * 33], s[3 * 33]) | ((unsigned long long)pg8::pk4_fp8(s[4 * 33], s[5 * 33], s[6 * 33], s[7 * 33]) << 32);
;         *(GAS unsigned long long*)(WT + (size_t)(n0 + n) * K + k0 + 8 * c) = o; }
; __global__ void __launch_bounds__(NWAVES * 64, 2) hybrid_fwd(Args args) {
;     ...
;             p0_transpose_item_f8<false>(args.in[16] + (size_t)l * FF * DM, FF, DM, DM / 32, (unsigned char*)(ws + WS_WDN + l * SZ_WDN), 128.f, args.in[16], args.in[16], 0, scr, r, lane);
	s_add_i32 s17, s16, 2496
	s_min_u32 s17, s17, 0xfff
	s_lshr_b32 s18, s17, 5
	s_add_i32 s18, s18, 0
	s_and_b32 s19, s17, 31
	s_lshl_b32 s18, s18, 21
	s_lshl_b32 s19, s19, 9
	s_add_u32 s18, s18, s19
	s_add_u32 s12, s2, s18
	s_addc_u32 s13, s3, 0
	global_load_dwordx4 v[100:103], v10, s[12:13]
	s_add_u32 s12, s12, 0x8000
	s_addc_u32 s13, s13, 0
	global_load_dwordx4 v[104:107], v10, s[12:13]
	s_add_u32 s12, s12, 0x8000
	s_addc_u32 s13, s13, 0
	global_load_dwordx4 v[108:111], v10, s[12:13]
	s_add_u32 s12, s12, 0x8000
	s_addc_u32 s13, s13, 0
	global_load_dwordx4 v[112:115], v10, s[12:13]
	s_add_u32 s12, s12, 0x8000
	s_addc_u32 s13, s13, 0
	global_load_dwordx4 v[116:119], v10, s[12:13]
	s_add_u32 s12, s12, 0x8000
	s_addc_u32 s13, s13, 0
	global_load_dwordx4 v[120:123], v10, s[12:13]
	s_add_u32 s12, s12, 0x8000
	s_addc_u32 s13, s13, 0
	global_load_dwordx4 v[124:127], v10, s[12:13]
	s_add_u32 s12, s12, 0x8000
	s_addc_u32 s13, s13, 0
	global_load_dwordx4 v[128:131], v10, s[12:13]
	s_add_i32 s17, s16, 2112
	s_min_u32 s17, s17, 0xfff
	s_lshr_b32 s18, s17, 5
	s_add_i32 s18, s18, 0
	s_and_b32 s19, s17, 31
	s_lshl_b32 s19, s19, 21
	s_lshl_b32 s18, s18, 7
	s_add_u32 s18, s18, s19
	s_add_u32 s14, s4, s18
	s_addc_u32 s15, s5, 0
	ds_read_b32 v170, v6
	ds_read_b32 v171, v6 offset:512
	ds_read_b32 v172, v6 offset:1024
	ds_read_b32 v173, v6 offset:1536
	ds_read_b32 v174, v6 offset:2048
	ds_read_b32 v175, v6 offset:2560
	ds_read_b32 v176, v6 offset:3072
	ds_read_b32 v177, v6 offset:3584
	ds_read_b32 v196, v6 offset:4096
	ds_read_b32 v197, v6 offset:4608
	ds_read_b32 v198, v6 offset:5120
	ds_read_b32 v199, v6 offset:5632
	ds_read_b32 v200, v6 offset:6144
	ds_read_b32 v201, v6 offset:6656
	ds_read_b32 v202, v6 offset:7168
	ds_read_b32 v203, v6 offset:7680
	s_waitcnt lgkmcnt(0)
	v_max_f32_e32 v170, v170, v170
	v_max_f32_e32 v171, v171, v171
	v_max_f32_e32 v172, v172, v172
	v_max_f32_e32 v173, v173, v173
	v_max_f32_e32 v174, v174, v174
	v_max_f32_e32 v175, v175, v175
	v_max_f32_e32 v176, v176, v176
	v_max_f32_e32 v177, v177, v177
	v_max_f32_e32 v196, v196, v196
	v_max_f32_e32 v197, v197, v197
	v_max_f32_e32 v198, v198, v198
	v_max_f32_e32 v199, v199, v199
	v_max_f32_e32 v200, v200, v200
	v_max_f32_e32 v201, v201, v201
	v_max_f32_e32 v202, v202, v202
	v_max_f32_e32 v203, v203, v203
	v_med3_f32 v170, v170, s20, v13
	v_med3_f32 v171, v171, s20, v13
	v_med3_f32 v172, v172, s20, v13
	v_med3_f32 v173, v173, s20, v13
	v_med3_f32 v174, v174, s20, v13
	v_med3_f32 v175, v175, s20, v13
	v_med3_f32 v176, v176, s20, v13
	v_med3_f32 v177, v177, s20, v13
	v_med3_f32 v196, v196, s20, v13
	v_med3_f32 v197, v197, s20, v13
	v_med3_f32 v198, v198, s20, v13
	v_med3_f32 v199, v199, s20, v13
	v_med3_f32 v200, v200, s20, v13
	v_med3_f32 v201, v201, s20, v13
	v_med3_f32 v202, v202, s20, v13
	v_med3_f32 v203, v203, s20, v13
	v_mov_b32_e32 v208, 0
	v_mov_b32_e32 v209, 0
	v_mov_b32_e32 v210, 0
	v_mov_b32_e32 v211, 0
	v_cvt_pk_fp8_f32 v208, v170, v171
	v_cvt_pk_fp8_f32 v209, v174, v175
	v_cvt_pk_fp8_f32 v210, v196, v197
	v_cvt_pk_fp8_f32 v211, v200, v201
	v_cvt_pk_fp8_f32 v208, v172, v173 op_sel:[0,0,1]
	v_cvt_pk_fp8_f32 v209, v176, v177 op_sel:[0,0,1]
	v_cvt_pk_fp8_f32 v210, v198, v199 op_sel:[0,0,1]
	v_cvt_pk_fp8_f32 v211, v202, v203 op_sel:[0,0,1]
	s_nop 0
	global_store_dwordx4 v11, v[208:211], s[14:15]
	ds_read_b32 v170, v8
	ds_read_b32 v171, v8 offset:512
	ds_read_b32 v172, v8 offset:1024
	ds_read_b32 v173, v8 offset:1536
	ds_read_b32 v174, v8 offset:2048
	ds_read_b32 v175, v8 offset:2560
	ds_read_b32 v176, v8 offset:3072
	ds_read_b32 v177, v8 offset:3584
	ds_read_b32 v196, v8 offset:4096
	ds_read_b32 v197, v8 offset:4608
	ds_read_b32 v198, v8 offset:5120
	ds_read_b32 v199, v8 offset:5632
	ds_read_b32 v200, v8 offset:6144
	ds_read_b32 v201, v8 offset:6656
	ds_read_b32 v202, v8 offset:7168
	ds_read_b32 v203, v8 offset:7680
	s_waitcnt lgkmcnt(0)
	v_max_f32_e32 v170, v170, v170
	v_max_f32_e32 v171, v171, v171
	v_max_f32_e32 v172, v172, v172
	v_max_f32_e32 v173, v173, v173
	v_max_f32_e32 v174, v174, v174
	v_max_f32_e32 v175, v175, v175
	v_max_f32_e32 v176, v176, v176
	v_max_f32_e32 v177, v177, v177
	v_max_f32_e32 v196, v196, v196
	v_max_f32_e32 v197, v197, v197
	v_max_f32_e32 v198, v198, v198
	v_max_f32_e32 v199, v199, v199
	v_max_f32_e32 v200, v200, v200
	v_max_f32_e32 v201, v201, v201
	v_max_f32_e32 v202, v202, v202
	v_max_f32_e32 v203, v203, v203
	v_med3_f32 v170, v170, s20, v13
	v_med3_f32 v171, v171, s20, v13
	v_med3_f32 v172, v172, s20, v13
	v_med3_f32 v173, v173, s20, v13
	v_med3_f32 v174, v174, s20, v13
	v_med3_f32 v175, v175, s20, v13
	v_med3_f32 v176, v176, s20, v13
	v_med3_f32 v177, v177, s20, v13
	v_med3_f32 v196, v196, s20, v13
	v_med3_f32 v197, v197, s20, v13
	v_med3_f32 v198, v198, s20, v13
	v_med3_f32 v199, v199, s20, v13
	v_med3_f32 v200, v200, s20, v13
	v_med3_f32 v201, v201, s20, v13
	v_med3_f32 v202, v202, s20, v13
	v_med3_f32 v203, v203, s20, v13
	v_mov_b32_e32 v208, 0
	v_mov_b32_e32 v209, 0
	v_mov_b32_e32 v210, 0
	v_mov_b32_e32 v211, 0
	v_cvt_pk_fp8_f32 v208, v170, v171
	v_cvt_pk_fp8_f32 v209, v174, v175
	v_cvt_pk_fp8_f32 v210, v196, v197
	v_cvt_pk_fp8_f32 v211, v200, v201
	v_cvt_pk_fp8_f32 v208, v172, v173 op_sel:[0,0,1]
	v_cvt_pk_fp8_f32 v209, v176, v177 op_sel:[0,0,1]
	v_cvt_pk_fp8_f32 v210, v198, v199 op_sel:[0,0,1]
	v_cvt_pk_fp8_f32 v211, v202, v203 op_sel:[0,0,1]
	s_nop 0
	global_store_dwordx4 v12, v[208:211], s[14:15]
	s_waitcnt vmcnt(32)
	v_mul_f32_e32 v132, 0x43000000, v132
	v_mul_f32_e32 v133, 0x43000000, v133
	v_mul_f32_e32 v134, 0x43000000, v134
	v_mul_f32_e32 v135, 0x43000000, v135
	ds_write_b128 v5, v[132:135]
	v_mul_f32_e32 v136, 0x43000000, v136
	v_mul_f32_e32 v137, 0x43000000, v137
	v_mul_f32_e32 v138, 0x43000000, v138
	v_mul_f32_e32 v139, 0x43000000, v139
	ds_write_b128 v5, v[136:139] offset:1024
	v_mul_f32_e32 v140, 0x43000000, v140
	v_mul_f32_e32 v141, 0x43000000, v141
	v_mul_f32_e32 v142, 0x43000000, v142
	v_mul_f32_e32 v143, 0x43000000, v143
	ds_write_b128 v5, v[140:143] offset:2048
	v_mul_f32_e32 v144, 0x43000000, v144
	v_mul_f32_e32 v145, 0x43000000, v145
	v_mul_f32_e32 v146, 0x43000000, v146
	v_mul_f32_e32 v147, 0x43000000, v147
	ds_write_b128 v5, v[144:147] offset:3072
	v_mul_f32_e32 v148, 0x43000000, v148
	v_mul_f32_e32 v149, 0x43000000, v149
	v_mul_f32_e32 v150, 0x43000000, v150
	v_mul_f32_e32 v151, 0x43000000, v151
	ds_write_b128 v5, v[148:151] offset:4096
	v_mul_f32_e32 v152, 0x43000000, v152
	v_mul_f32_e32 v153, 0x43000000, v153
	v_mul_f32_e32 v154, 0x43000000, v154
	v_mul_f32_e32 v155, 0x43000000, v155
	ds_write_b128 v5, v[152:155] offset:5120
	v_mul_f32_e32 v156, 0x43000000, v156
	v_mul_f32_e32 v157, 0x43000000, v157
	v_mul_f32_e32 v158, 0x43000000, v158
	v_mul_f32_e32 v159, 0x43000000, v159
	ds_write_b128 v5, v[156:159] offset:6144
	v_mul_f32_e32 v160, 0x43000000, v160
	v_mul_f32_e32 v161, 0x43000000, v161
	v_mul_f32_e32 v162, 0x43000000, v162
	v_mul_f32_e32 v163, 0x43000000, v163
	ds_write_b128 v5, v[160:163] offset:7168
	s_waitcnt lgkmcnt(0)
	s_barrier
; #define GAS __attribute__((address_space(1)))
; #define LAS __attribute__((address_space(3)))
; #define LDS_WAIT() asm volatile("s_waitcnt lgkmcnt(0)" ::: "memory")
;     ...
;     for (int i = 0; i < 32; ++i) v[i] = sc >= 0 ? W[(size_t)(k0 + 2 * i + (lane >> 5)) * Nsrc + sc] : 0.f;
; #pragma unroll
;     for (int i = 0; i < 32; ++i) { const int k = k0 + 2 * i + (lane >> 5); float x = v[i] * wscale; if (KS) x *= (k < ksplit ? ksA[k] : ksB[k - ksplit]); scr[(2 * i + (lane >> 5)) * 33 + (lane & 31)] = x; }
;     LDS_WAIT(); asm volatile("" ::: "memory");
;     const int c = lane & 7;
; #pragma unroll
;     for (int j = 0; j < 4; ++j) { const int n = (lane >> 3) + 8 * j; const LAS float* s = scr + (8 * c) * 33 + n;
;         const unsigned long long o = (unsigned long long)pg8::pk4_fp8(s[0 * 33], s[1 * 33], s[2 * 33], s[3 * 33]) | ((unsigned long long)pg8::pk4_fp8(s[4 * 33], s[5 * 33], s[6 * 33], s[7 * 33]) << 32);
;         *(GAS unsigned long long*)(WT + (size_t)(n0 + n) * K + k0 + 8 * c) = o; }
; __global__ void __launch_bounds__(NWAVES * 64, 2) hybrid_fwd(Args args) {
;     ...
;             p0_transpose_item_f8<false>(args.in[16] + (size_t)l * FF * DM, FF, DM, DM / 32, (unsigned char*)(ws + WS_WDN + l * SZ_WDN), 128.f, args.in[16], args.in[16], 0, scr, r, lane);
	s_add_i32 s17, s16, 2592
	s_min_u32 s17, s17, 0xfff
	s_lshr_b32 s18, s17, 5
	s_add_i32 s18, s18, 0
	s_and_b32 s19, s17, 31
	s_lshl_b32 s18, s18, 21
	s_lshl_b32 s19, s19, 9
	s_add_u32 s18, s18, s19
	s_add_u32 s12, s2, s18
	s_addc_u32 s13, s3, 0
	global_load_dwordx4 v[132:135], v10, s[12:13]
	s_add_u32 s12, s12, 0x8000
	s_addc_u32 s13, s13, 0
	global_load_dwordx4 v[136:139], v10, s[12:13]
	s_add_u32 s12, s12, 0x8000
	s_addc_u32 s13, s13, 0
	global_load_dwordx4 v[140:143], v10, s[12:13]
	s_add_u32 s12, s12, 0x8000
	s_addc_u32 s13, s13, 0
	global_load_dwordx4 v[144:147], v10, s[12:13]
	s_add_u32 s12, s12, 0x8000
	s_addc_u32 s13, s13, 0
	global_load_dwordx4 v[148:151], v10, s[12:13]
	s_add_u32 s12, s12, 0x8000
	s_addc_u32 s13, s13, 0
	global_load_dwordx4 v[152:155], v10, s[12:13]
	s_add_u32 s12, s12, 0x8000
	s_addc_u32 s13, s13, 0
	global_load_dwordx4 v[156:159], v10, s[12:13]
	s_add_u32 s12, s12, 0x8000
	s_addc_u32 s13, s13, 0
	global_load_dwordx4 v[160:163], v10, s[12:13]
	s_add_i32 s17, s16, 2208
	s_min_u32 s17, s17, 0xfff
	s_lshr_b32 s18, s17, 5
	s_add_i32 s18, s18, 0
	s_and_b32 s19, s17, 31
	s_lshl_b32 s19, s19, 21
	s_lshl_b32 s18, s18, 7
	s_add_u32 s18, s18, s19
	s_add_u32 s14, s4, s18
	s_addc_u32 s15, s5, 0
	ds_read_b32 v170, v7
	ds_read_b32 v171, v7 offset:512
	ds_read_b32 v172, v7 offset:1024
	ds_read_b32 v173, v7 offset:1536
	ds_read_b32 v174, v7 offset:2048
	ds_read_b32 v175, v7 offset:2560
	ds_read_b32 v176, v7 offset:3072
	ds_read_b32 v177, v7 offset:3584
	ds_read_b32 v196, v7 offset:4096
	ds_read_b32 v197, v7 offset:4608
	ds_read_b32 v198, v7 offset:5120
	ds_read_b32 v199, v7 offset:5632
	ds_read_b32 v200, v7 offset:6144
	ds_read_b32 v201, v7 offset:6656
	ds_read_b32 v202, v7 offset:7168
	ds_read_b32 v203, v7 offset:7680
	s_waitcnt lgkmcnt(0)
	v_max_f32_e32 v170, v170, v170
	v_max_f32_e32 v171, v171, v171
	v_max_f32_e32 v172, v172, v172
	v_max_f32_e32 v173, v173, v173
	v_max_f32_e32 v174, v174, v174
	v_max_f32_e32 v175, v175, v175
	v_max_f32_e32 v176, v176, v176
	v_max_f32_e32 v177, v177, v177
	v_max_f32_e32 v196, v196, v196
	v_max_f32_e32 v197, v197, v197
	v_max_f32_e32 v198, v198, v198
	v_max_f32_e32 v199, v199, v199
	v_max_f32_e32 v200, v200, v200
	v_max_f32_e32 v201, v201, v201
	v_max_f32_e32 v202, v202, v202
	v_max_f32_e32 v203, v203, v203
	v_med3_f32 v170, v170, s20, v13
	v_med3_f32 v171, v171, s20, v13
	v_med3_f32 v172, v172, s20, v13
	v_med3_f32 v173, v173, s20, v13
	v_med3_f32 v174, v174, s20, v13
	v_med3_f32 v175, v175, s20, v13
	v_med3_f32 v176, v176, s20, v13
	v_med3_f32 v177, v177, s20, v13
	v_med3_f32 v196, v196, s20, v13
	v_med3_f32 v197, v197, s20, v13
	v_med3_f32 v198, v198, s20, v13
	v_med3_f32 v199, v199, s20, v13
	v_med3_f32 v200, v200, s20, v13
	v_med3_f32 v201, v201, s20, v13
	v_med3_f32 v202, v202, s20, v13
	v_med3_f32 v203, v203, s20, v13
	v_mov_b32_e32 v208, 0
	v_mov_b32_e32 v209, 0
	v_mov_b32_e32 v210, 0
	v_mov_b32_e32 v211, 0
	v_cvt_pk_fp8_f32 v208, v170, v171
	v_cvt_pk_fp8_f32 v209, v174, v175
	v_cvt_pk_fp8_f32 v210, v196, v197
	v_cvt_pk_fp8_f32 v211, v200, v201
	v_cvt_pk_fp8_f32 v208, v172, v173 op_sel:[0,0,1]
	v_cvt_pk_fp8_f32 v209, v176, v177 op_sel:[0,0,1]
	v_cvt_pk_fp8_f32 v210, v198, v199 op_sel:[0,0,1]
	v_cvt_pk_fp8_f32 v211, v202, v203 op_sel:[0,0,1]
	s_nop 0
	global_store_dwordx4 v11, v[208:211], s[14:15]
	ds_read_b32 v170, v9
	ds_read_b32 v171, v9 offset:512
	ds_read_b32 v172, v9 offset:1024
	ds_read_b32 v173, v9 offset:1536
	ds_read_b32 v174, v9 offset:2048
	ds_read_b32 v175, v9 offset:2560
	ds_read_b32 v176, v9 offset:3072
	ds_read_b32 v177, v9 offset:3584
	ds_read_b32 v196, v9 offset:4096
	ds_read_b32 v197, v9 offset:4608
	ds_read_b32 v198, v9 offset:5120
	ds_read_b32 v199, v9 offset:5632
	ds_read_b32 v200, v9 offset:6144
	ds_read_b32 v201, v9 offset:6656
	ds_read_b32 v202, v9 offset:7168
	ds_read_b32 v203, v9 offset:7680
	s_waitcnt lgkmcnt(0)
	v_max_f32_e32 v170, v170, v170
	v_max_f32_e32 v171, v171, v171
	v_max_f32_e32 v172, v172, v172
	v_max_f32_e32 v173, v173, v173
	v_max_f32_e32 v174, v174, v174
	v_max_f32_e32 v175, v175, v175
	v_max_f32_e32 v176, v176, v176
	v_max_f32_e32 v177, v177, v177
	v_max_f32_e32 v196, v196, v196
	v_max_f32_e32 v197, v197, v197
	v_max_f32_e32 v198, v198, v198
	v_max_f32_e32 v199, v199, v199
	v_max_f32_e32 v200, v200, v200
	v_max_f32_e32 v201, v201, v201
	v_max_f32_e32 v202, v202, v202
	v_max_f32_e32 v203, v203, v203
	v_med3_f32 v170, v170, s20, v13
	v_med3_f32 v171, v171, s20, v13
	v_med3_f32 v172, v172, s20, v13
	v_med3_f32 v173, v173, s20, v13
	v_med3_f32 v174, v174, s20, v13
	v_med3_f32 v175, v175, s20, v13
	v_med3_f32 v176, v176, s20, v13
	v_med3_f32 v177, v177, s20, v13
	v_med3_f32 v196, v196, s20, v13
	v_med3_f32 v197, v197, s20, v13
	v_med3_f32 v198, v198, s20, v13
	v_med3_f32 v199, v199, s20, v13
	v_med3_f32 v200, v200, s20, v13
	v_med3_f32 v201, v201, s20, v13
	v_med3_f32 v202, v202, s20, v13
	v_med3_f32 v203, v203, s20, v13
	v_mov_b32_e32 v208, 0
	v_mov_b32_e32 v209, 0
	v_mov_b32_e32 v210, 0
	v_mov_b32_e32 v211, 0
	v_cvt_pk_fp8_f32 v208, v170, v171
	v_cvt_pk_fp8_f32 v209, v174, v175
	v_cvt_pk_fp8_f32 v210, v196, v197
	v_cvt_pk_fp8_f32 v211, v200, v201
	v_cvt_pk_fp8_f32 v208, v172, v173 op_sel:[0,0,1]
	v_cvt_pk_fp8_f32 v209, v176, v177 op_sel:[0,0,1]
	v_cvt_pk_fp8_f32 v210, v198, v199 op_sel:[0,0,1]
	v_cvt_pk_fp8_f32 v211, v202, v203 op_sel:[0,0,1]
	s_nop 0
	global_store_dwordx4 v12, v[208:211], s[14:15]
	s_waitcnt vmcnt(32)
	v_mul_f32_e32 v36, 0x43000000, v36
	v_mul_f32_e32 v37, 0x43000000, v37
	v_mul_f32_e32 v38, 0x43000000, v38
	v_mul_f32_e32 v39, 0x43000000, v39
	ds_write_b128 v4, v[36:39]
	v_mul_f32_e32 v40, 0x43000000, v40
	v_mul_f32_e32 v41, 0x43000000, v41
	v_mul_f32_e32 v42, 0x43000000, v42
	v_mul_f32_e32 v43, 0x43000000, v43
	ds_write_b128 v4, v[40:43] offset:1024
	v_mul_f32_e32 v44, 0x43000000, v44
	v_mul_f32_e32 v45, 0x43000000, v45
	v_mul_f32_e32 v46, 0x43000000, v46
	v_mul_f32_e32 v47, 0x43000000, v47
	ds_write_b128 v4, v[44:47] offset:2048
	v_mul_f32_e32 v48, 0x43000000, v48
	v_mul_f32_e32 v49, 0x43000000, v49
	v_mul_f32_e32 v50, 0x43000000, v50
	v_mul_f32_e32 v51, 0x43000000, v51
	ds_write_b128 v4, v[48:51] offset:3072
	v_mul_f32_e32 v52, 0x43000000, v52
	v_mul_f32_e32 v53, 0x43000000, v53
	v_mul_f32_e32 v54, 0x43000000, v54
	v_mul_f32_e32 v55, 0x43000000, v55
	ds_write_b128 v4, v[52:55] offset:4096
	v_mul_f32_e32 v56, 0x43000000, v56
	v_mul_f32_e32 v57, 0x43000000, v57
	v_mul_f32_e32 v58, 0x43000000, v58
	v_mul_f32_e32 v59, 0x43000000, v59
	ds_write_b128 v4, v[56:59] offset:5120
	v_mul_f32_e32 v60, 0x43000000, v60
	v_mul_f32_e32 v61, 0x43000000, v61
	v_mul_f32_e32 v62, 0x43000000, v62
	v_mul_f32_e32 v63, 0x43000000, v63
	ds_write_b128 v4, v[60:63] offset:6144
	v_mul_f32_e32 v64, 0x43000000, v64
	v_mul_f32_e32 v65, 0x43000000, v65
	v_mul_f32_e32 v66, 0x43000000, v66
	v_mul_f32_e32 v67, 0x43000000, v67
	ds_write_b128 v4, v[64:67] offset:7168
	s_waitcnt lgkmcnt(0)
	s_barrier
; #define GAS __attribute__((address_space(1)))
; #define LAS __attribute__((address_space(3)))
; #define LDS_WAIT() asm volatile("s_waitcnt lgkmcnt(0)" ::: "memory")
;     ...
;     for (int i = 0; i < 32; ++i) v[i] = sc >= 0 ? W[(size_t)(k0 + 2 * i + (lane >> 5)) * Nsrc + sc] : 0.f;
; #pragma unroll
;     for (int i = 0; i < 32; ++i) { const int k = k0 + 2 * i + (lane >> 5); float x = v[i] * wscale; if (KS) x *= (k < ksplit ? ksA[k] : ksB[k - ksplit]); scr[(2 * i + (lane >> 5)) * 33 + (lane & 31)] = x; }
;     LDS_WAIT(); asm volatile("" ::: "memory");
;     const int c = lane & 7;
; #pragma unroll
;     for (int j = 0; j < 4; ++j) { const int n = (lane >> 3) + 8 * j; const LAS float* s = scr + (8 * c) * 33 + n;
;         const unsigned long long o = (unsigned long long)pg8::pk4_fp8(s[0 * 33], s[1 * 33], s[2 * 33], s[3 * 33]) | ((unsigned long long)pg8::pk4_fp8(s[4 * 33], s[5 * 33], s[6 * 33], s[7 * 33]) << 32);
;         *(GAS unsigned long long*)(WT + (size_t)(n0 + n) * K + k0 + 8 * c) = o; }
; __global__ void __launch_bounds__(NWAVES * 64, 2) hybrid_fwd(Args args) {
;     ...
;             p0_transpose_item_f8<false>(args.in[16] + (size_t)l * FF * DM, FF, DM, DM / 32, (unsigned char*)(ws + WS_WDN + l * SZ_WDN), 128.f, args.in[16], args.in[16], 0, scr, r, lane);
	s_add_i32 s17, s16, 2688
	s_min_u32 s17, s17, 0xfff
	s_lshr_b32 s18, s17, 5
	s_add_i32 s18, s18, 0
	s_and_b32 s19, s17, 31
	s_lshl_b32 s18, s18, 21
	s_lshl_b32 s19, s19, 9
	s_add_u32 s18, s18, s19
	s_add_u32 s12, s2, s18
	s_addc_u32 s13, s3, 0
	global_load_dwordx4 v[36:39], v10, s[12:13]
	s_add_u32 s12, s12, 0x8000
	s_addc_u32 s13, s13, 0
	global_load_dwordx4 v[40:43], v10, s[12:13]
	s_add_u32 s12, s12, 0x8000
	s_addc_u32 s13, s13, 0
	global_load_dwordx4 v[44:47], v10, s[12:13]
	s_add_u32 s12, s12, 0x8000
	s_addc_u32 s13, s13, 0
	global_load_dwordx4 v[48:51], v10, s[12:13]
	s_add_u32 s12, s12, 0x8000
	s_addc_u32 s13, s13, 0
	global_load_dwordx4 v[52:55], v10, s[12:13]
	s_add_u32 s12, s12, 0x8000
	s_addc_u32 s13, s13, 0
	global_load_dwordx4 v[56:59], v10, s[12:13]
	s_add_u32 s12, s12, 0x8000
	s_addc_u32 s13, s13, 0
	global_load_dwordx4 v[60:63], v10, s[12:13]
	s_add_u32 s12, s12, 0x8000
	s_addc_u32 s13, s13, 0
	global_load_dwordx4 v[64:67], v10, s[12:13]
	s_add_i32 s17, s16, 2304
	s_min_u32 s17, s17, 0xfff
	s_lshr_b32 s18, s17, 5
	s_add_i32 s18, s18, 0
	s_and_b32 s19, s17, 31
	s_lshl_b32 s19, s19, 21
	s_lshl_b32 s18, s18, 7
	s_add_u32 s18, s18, s19
	s_add_u32 s14, s4, s18
	s_addc_u32 s15, s5, 0
	ds_read_b32 v170, v6
	ds_read_b32 v171, v6 offset:512
	ds_read_b32 v172, v6 offset:1024
	ds_read_b32 v173, v6 offset:1536
	ds_read_b32 v174, v6 offset:2048
	ds_read_b32 v175, v6 offset:2560
	ds_read_b32 v176, v6 offset:3072
	ds_read_b32 v177, v6 offset:3584
	ds_read_b32 v196, v6 offset:4096
	ds_read_b32 v197, v6 offset:4608
	ds_read_b32 v198, v6 offset:5120
	ds_read_b32 v199, v6 offset:5632
	ds_read_b32 v200, v6 offset:6144
	ds_read_b32 v201, v6 offset:6656
	ds_read_b32 v202, v6 offset:7168
	ds_read_b32 v203, v6 offset:7680
	s_waitcnt lgkmcnt(0)
	v_max_f32_e32 v170, v170, v170
	v_max_f32_e32 v171, v171, v171
	v_max_f32_e32 v172, v172, v172
	v_max_f32_e32 v173, v173, v173
	v_max_f32_e32 v174, v174, v174
	v_max_f32_e32 v175, v175, v175
	v_max_f32_e32 v176, v176, v176
	v_max_f32_e32 v177, v177, v177
	v_max_f32_e32 v196, v196, v196
	v_max_f32_e32 v197, v197, v197
	v_max_f32_e32 v198, v198, v198
	v_max_f32_e32 v199, v199, v199
	v_max_f32_e32 v200, v200, v200
	v_max_f32_e32 v201, v201, v201
	v_max_f32_e32 v202, v202, v202
	v_max_f32_e32 v203, v203, v203
	v_med3_f32 v170, v170, s20, v13
	v_med3_f32 v171, v171, s20, v13
	v_med3_f32 v172, v172, s20, v13
	v_med3_f32 v173, v173, s20, v13
	v_med3_f32 v174, v174, s20, v13
	v_med3_f32 v175, v175, s20, v13
	v_med3_f32 v176, v176, s20, v13
	v_med3_f32 v177, v177, s20, v13
	v_med3_f32 v196, v196, s20, v13
	v_med3_f32 v197, v197, s20, v13
	v_med3_f32 v198, v198, s20, v13
	v_med3_f32 v199, v199, s20, v13
	v_med3_f32 v200, v200, s20, v13
	v_med3_f32 v201, v201, s20, v13
	v_med3_f32 v202, v202, s20, v13
	v_med3_f32 v203, v203, s20, v13
	v_mov_b32_e32 v208, 0
	v_mov_b32_e32 v209, 0
	v_mov_b32_e32 v210, 0
	v_mov_b32_e32 v211, 0
	v_cvt_pk_fp8_f32 v208, v170, v171
	v_cvt_pk_fp8_f32 v209, v174, v175
	v_cvt_pk_fp8_f32 v210, v196, v197
	v_cvt_pk_fp8_f32 v211, v200, v201
	v_cvt_pk_fp8_f32 v208, v172, v173 op_sel:[0,0,1]
	v_cvt_pk_fp8_f32 v209, v176, v177 op_sel:[0,0,1]
	v_cvt_pk_fp8_f32 v210, v198, v199 op_sel:[0,0,1]
	v_cvt_pk_fp8_f32 v211, v202, v203 op_sel:[0,0,1]
	s_nop 0
	global_store_dwordx4 v11, v[208:211], s[14:15]
	ds_read_b32 v170, v8
	ds_read_b32 v171, v8 offset:512
	ds_read_b32 v172, v8 offset:1024
	ds_read_b32 v173, v8 offset:1536
	ds_read_b32 v174, v8 offset:2048
	ds_read_b32 v175, v8 offset:2560
	ds_read_b32 v176, v8 offset:3072
	ds_read_b32 v177, v8 offset:3584
	ds_read_b32 v196, v8 offset:4096
	ds_read_b32 v197, v8 offset:4608
	ds_read_b32 v198, v8 offset:5120
	ds_read_b32 v199, v8 offset:5632
	ds_read_b32 v200, v8 offset:6144
	ds_read_b32 v201, v8 offset:6656
	ds_read_b32 v202, v8 offset:7168
	ds_read_b32 v203, v8 offset:7680
	s_waitcnt lgkmcnt(0)
	v_max_f32_e32 v170, v170, v170
	v_max_f32_e32 v171, v171, v171
	v_max_f32_e32 v172, v172, v172
	v_max_f32_e32 v173, v173, v173
	v_max_f32_e32 v174, v174, v174
	v_max_f32_e32 v175, v175, v175
	v_max_f32_e32 v176, v176, v176
	v_max_f32_e32 v177, v177, v177
	v_max_f32_e32 v196, v196, v196
	v_max_f32_e32 v197, v197, v197
	v_max_f32_e32 v198, v198, v198
	v_max_f32_e32 v199, v199, v199
	v_max_f32_e32 v200, v200, v200
	v_max_f32_e32 v201, v201, v201
	v_max_f32_e32 v202, v202, v202
	v_max_f32_e32 v203, v203, v203
	v_med3_f32 v170, v170, s20, v13
	v_med3_f32 v171, v171, s20, v13
	v_med3_f32 v172, v172, s20, v13
	v_med3_f32 v173, v173, s20, v13
	v_med3_f32 v174, v174, s20, v13
	v_med3_f32 v175, v175, s20, v13
	v_med3_f32 v176, v176, s20, v13
	v_med3_f32 v177, v177, s20, v13
	v_med3_f32 v196, v196, s20, v13
	v_med3_f32 v197, v197, s20, v13
	v_med3_f32 v198, v198, s20, v13
	v_med3_f32 v199, v199, s20, v13
	v_med3_f32 v200, v200, s20, v13
	v_med3_f32 v201, v201, s20, v13
	v_med3_f32 v202, v202, s20, v13
	v_med3_f32 v203, v203, s20, v13
	v_mov_b32_e32 v208, 0
	v_mov_b32_e32 v209, 0
	v_mov_b32_e32 v210, 0
	v_mov_b32_e32 v211, 0
	v_cvt_pk_fp8_f32 v208, v170, v171
	v_cvt_pk_fp8_f32 v209, v174, v175
	v_cvt_pk_fp8_f32 v210, v196, v197
	v_cvt_pk_fp8_f32 v211, v200, v201
	v_cvt_pk_fp8_f32 v208, v172, v173 op_sel:[0,0,1]
	v_cvt_pk_fp8_f32 v209, v176, v177 op_sel:[0,0,1]
	v_cvt_pk_fp8_f32 v210, v198, v199 op_sel:[0,0,1]
	v_cvt_pk_fp8_f32 v211, v202, v203 op_sel:[0,0,1]
	s_nop 0
	global_store_dwordx4 v12, v[208:211], s[14:15]
	s_waitcnt vmcnt(32)
	v_mul_f32_e32 v68, 0x43000000, v68
	v_mul_f32_e32 v69, 0x43000000, v69
	v_mul_f32_e32 v70, 0x43000000, v70
	v_mul_f32_e32 v71, 0x43000000, v71
	ds_write_b128 v5, v[68:71]
	v_mul_f32_e32 v72, 0x43000000, v72
	v_mul_f32_e32 v73, 0x43000000, v73
	v_mul_f32_e32 v74, 0x43000000, v74
	v_mul_f32_e32 v75, 0x43000000, v75
	ds_write_b128 v5, v[72:75] offset:1024
	v_mul_f32_e32 v76, 0x43000000, v76
	v_mul_f32_e32 v77, 0x43000000, v77
	v_mul_f32_e32 v78, 0x43000000, v78
	v_mul_f32_e32 v79, 0x43000000, v79
	ds_write_b128 v5, v[76:79] offset:2048
	v_mul_f32_e32 v80, 0x43000000, v80
	v_mul_f32_e32 v81, 0x43000000, v81
	v_mul_f32_e32 v82, 0x43000000, v82
	v_mul_f32_e32 v83, 0x43000000, v83
	ds_write_b128 v5, v[80:83] offset:3072
	v_mul_f32_e32 v84, 0x43000000, v84
	v_mul_f32_e32 v85, 0x43000000, v85
	v_mul_f32_e32 v86, 0x43000000, v86
	v_mul_f32_e32 v87, 0x43000000, v87
	ds_write_b128 v5, v[84:87] offset:4096
	v_mul_f32_e32 v88, 0x43000000, v88
	v_mul_f32_e32 v89, 0x43000000, v89
	v_mul_f32_e32 v90, 0x43000000, v90
	v_mul_f32_e32 v91, 0x43000000, v91
	ds_write_b128 v5, v[88:91] offset:5120
	v_mul_f32_e32 v92, 0x43000000, v92
	v_mul_f32_e32 v93, 0x43000000, v93
	v_mul_f32_e32 v94, 0x43000000, v94
	v_mul_f32_e32 v95, 0x43000000, v95
	ds_write_b128 v5, v[92:95] offset:6144
	v_mul_f32_e32 v96, 0x43000000, v96
	v_mul_f32_e32 v97, 0x43000000, v97
	v_mul_f32_e32 v98, 0x43000000, v98
	v_mul_f32_e32 v99, 0x43000000, v99
	ds_write_b128 v5, v[96:99] offset:7168
	s_waitcnt lgkmcnt(0)
	s_barrier
; #define GAS __attribute__((address_space(1)))
; #define LAS __attribute__((address_space(3)))
; #define LDS_WAIT() asm volatile("s_waitcnt lgkmcnt(0)" ::: "memory")
;     ...
;     for (int i = 0; i < 32; ++i) v[i] = sc >= 0 ? W[(size_t)(k0 + 2 * i + (lane >> 5)) * Nsrc + sc] : 0.f;
; #pragma unroll
;     for (int i = 0; i < 32; ++i) { const int k = k0 + 2 * i + (lane >> 5); float x = v[i] * wscale; if (KS) x *= (k < ksplit ? ksA[k] : ksB[k - ksplit]); scr[(2 * i + (lane >> 5)) * 33 + (lane & 31)] = x; }
;     LDS_WAIT(); asm volatile("" ::: "memory");
;     const int c = lane & 7;
; #pragma unroll
;     for (int j = 0; j < 4; ++j) { const int n = (lane >> 3) + 8 * j; const LAS float* s = scr + (8 * c) * 33 + n;
;         const unsigned long long o = (unsigned long long)pg8::pk4_fp8(s[0 * 33], s[1 * 33], s[2 * 33], s[3 * 33]) | ((unsigned long long)pg8::pk4_fp8(s[4 * 33], s[5 * 33], s[6 * 33], s[7 * 33]) << 32);
;         *(GAS unsigned long long*)(WT + (size_t)(n0 + n) * K + k0 + 8 * c) = o; }
; __global__ void __launch_bounds__(NWAVES * 64, 2) hybrid_fwd(Args args) {
;     ...
;             p0_transpose_item_f8<false>(args.in[16] + (size_t)l * FF * DM, FF, DM, DM / 32, (unsigned char*)(ws + WS_WDN + l * SZ_WDN), 128.f, args.in[16], args.in[16], 0, scr, r, lane);
	s_add_i32 s17, s16, 2784
	s_min_u32 s17, s17, 0xfff
	s_lshr_b32 s18, s17, 5
	s_add_i32 s18, s18, 0
	s_and_b32 s19, s17, 31
	s_lshl_b32 s18, s18, 21
	s_lshl_b32 s19, s19, 9
	s_add_u32 s18, s18, s19
	s_add_u32 s12, s2, s18
	s_addc_u32 s13, s3, 0
	global_load_dwordx4 v[68:71], v10, s[12:13]
	s_add_u32 s12, s12, 0x8000
	s_addc_u32 s13, s13, 0
	global_load_dwordx4 v[72:75], v10, s[12:13]
	s_add_u32 s12, s12, 0x8000
	s_addc_u32 s13, s13, 0
	global_load_dwordx4 v[76:79], v10, s[12:13]
	s_add_u32 s12, s12, 0x8000
	s_addc_u32 s13, s13, 0
	global_load_dwordx4 v[80:83], v10, s[12:13]
	s_add_u32 s12, s12, 0x8000
	s_addc_u32 s13, s13, 0
	global_load_dwordx4 v[84:87], v10, s[12:13]
	s_add_u32 s12, s12, 0x8000
	s_addc_u32 s13, s13, 0
	global_load_dwordx4 v[88:91], v10, s[12:13]
	s_add_u32 s12, s12, 0x8000
	s_addc_u32 s13, s13, 0
	global_load_dwordx4 v[92:95], v10, s[12:13]
	s_add_u32 s12, s12, 0x8000
	s_addc_u32 s13, s13, 0
	global_load_dwordx4 v[96:99], v10, s[12:13]
	s_add_i32 s17, s16, 2400
	s_min_u32 s17, s17, 0xfff
	s_lshr_b32 s18, s17, 5
	s_add_i32 s18, s18, 0
	s_and_b32 s19, s17, 31
	s_lshl_b32 s19, s19, 21
	s_lshl_b32 s18, s18, 7
	s_add_u32 s18, s18, s19
	s_add_u32 s14, s4, s18
	s_addc_u32 s15, s5, 0
	ds_read_b32 v170, v7
	ds_read_b32 v171, v7 offset:512
	ds_read_b32 v172, v7 offset:1024
	ds_read_b32 v173, v7 offset:1536
	ds_read_b32 v174, v7 offset:2048
	ds_read_b32 v175, v7 offset:2560
	ds_read_b32 v176, v7 offset:3072
	ds_read_b32 v177, v7 offset:3584
	ds_read_b32 v196, v7 offset:4096
	ds_read_b32 v197, v7 offset:4608
	ds_read_b32 v198, v7 offset:5120
	ds_read_b32 v199, v7 offset:5632
	ds_read_b32 v200, v7 offset:6144
	ds_read_b32 v201, v7 offset:6656
	ds_read_b32 v202, v7 offset:7168
	ds_read_b32 v203, v7 offset:7680
	s_waitcnt lgkmcnt(0)
	v_max_f32_e32 v170, v170, v170
	v_max_f32_e32 v171, v171, v171
	v_max_f32_e32 v172, v172, v172
	v_max_f32_e32 v173, v173, v173
	v_max_f32_e32 v174, v174, v174
	v_max_f32_e32 v175, v175, v175
	v_max_f32_e32 v176, v176, v176
	v_max_f32_e32 v177, v177, v177
	v_max_f32_e32 v196, v196, v196
	v_max_f32_e32 v197, v197, v197
	v_max_f32_e32 v198, v198, v198
	v_max_f32_e32 v199, v199, v199
	v_max_f32_e32 v200, v200, v200
	v_max_f32_e32 v201, v201, v201
	v_max_f32_e32 v202, v202, v202
	v_max_f32_e32 v203, v203, v203
	v_med3_f32 v170, v170, s20, v13
	v_med3_f32 v171, v171, s20, v13
	v_med3_f32 v172, v172, s20, v13
	v_med3_f32 v173, v173, s20, v13
	v_med3_f32 v174, v174, s20, v13
	v_med3_f32 v175, v175, s20, v13
	v_med3_f32 v176, v176, s20, v13
	v_med3_f32 v177, v177, s20, v13
	v_med3_f32 v196, v196, s20, v13
	v_med3_f32 v197, v197, s20, v13
	v_med3_f32 v198, v198, s20, v13
	v_med3_f32 v199, v199, s20, v13
	v_med3_f32 v200, v200, s20, v13
	v_med3_f32 v201, v201, s20, v13
	v_med3_f32 v202, v202, s20, v13
	v_med3_f32 v203, v203, s20, v13
	v_mov_b32_e32 v208, 0
	v_mov_b32_e32 v209, 0
	v_mov_b32_e32 v210, 0
	v_mov_b32_e32 v211, 0
	v_cvt_pk_fp8_f32 v208, v170, v171
	v_cvt_pk_fp8_f32 v209, v174, v175
	v_cvt_pk_fp8_f32 v210, v196, v197
	v_cvt_pk_fp8_f32 v211, v200, v201
	v_cvt_pk_fp8_f32 v208, v172, v173 op_sel:[0,0,1]
	v_cvt_pk_fp8_f32 v209, v176, v177 op_sel:[0,0,1]
	v_cvt_pk_fp8_f32 v210, v198, v199 op_sel:[0,0,1]
	v_cvt_pk_fp8_f32 v211, v202, v203 op_sel:[0,0,1]
	s_nop 0
	global_store_dwordx4 v11, v[208:211], s[14:15]
	ds_read_b32 v170, v9
	ds_read_b32 v171, v9 offset:512
	ds_read_b32 v172, v9 offset:1024
	ds_read_b32 v173, v9 offset:1536
	ds_read_b32 v174, v9 offset:2048
	ds_read_b32 v175, v9 offset:2560
	ds_read_b32 v176, v9 offset:3072
	ds_read_b32 v177, v9 offset:3584
	ds_read_b32 v196, v9 offset:4096
	ds_read_b32 v197, v9 offset:4608
	ds_read_b32 v198, v9 offset:5120
	ds_read_b32 v199, v9 offset:5632
	ds_read_b32 v200, v9 offset:6144
	ds_read_b32 v201, v9 offset:6656
	ds_read_b32 v202, v9 offset:7168
	ds_read_b32 v203, v9 offset:7680
	s_waitcnt lgkmcnt(0)
	v_max_f32_e32 v170, v170, v170
	v_max_f32_e32 v171, v171, v171
	v_max_f32_e32 v172, v172, v172
	v_max_f32_e32 v173, v173, v173
	v_max_f32_e32 v174, v174, v174
	v_max_f32_e32 v175, v175, v175
	v_max_f32_e32 v176, v176, v176
	v_max_f32_e32 v177, v177, v177
	v_max_f32_e32 v196, v196, v196
	v_max_f32_e32 v197, v197, v197
	v_max_f32_e32 v198, v198, v198
	v_max_f32_e32 v199, v199, v199
	v_max_f32_e32 v200, v200, v200
	v_max_f32_e32 v201, v201, v201
	v_max_f32_e32 v202, v202, v202
	v_max_f32_e32 v203, v203, v203
	v_med3_f32 v170, v170, s20, v13
	v_med3_f32 v171, v171, s20, v13
	v_med3_f32 v172, v172, s20, v13
	v_med3_f32 v173, v173, s20, v13
	v_med3_f32 v174, v174, s20, v13
	v_med3_f32 v175, v175, s20, v13
	v_med3_f32 v176, v176, s20, v13
	v_med3_f32 v177, v177, s20, v13
	v_med3_f32 v196, v196, s20, v13
	v_med3_f32 v197, v197, s20, v13
	v_med3_f32 v198, v198, s20, v13
	v_med3_f32 v199, v199, s20, v13
	v_med3_f32 v200, v200, s20, v13
	v_med3_f32 v201, v201, s20, v13
	v_med3_f32 v202, v202, s20, v13
	v_med3_f32 v203, v203, s20, v13
	v_mov_b32_e32 v208, 0
	v_mov_b32_e32 v209, 0
	v_mov_b32_e32 v210, 0
	v_mov_b32_e32 v211, 0
	v_cvt_pk_fp8_f32 v208, v170, v171
	v_cvt_pk_fp8_f32 v209, v174, v175
	v_cvt_pk_fp8_f32 v210, v196, v197
	v_cvt_pk_fp8_f32 v211, v200, v201
	v_cvt_pk_fp8_f32 v208, v172, v173 op_sel:[0,0,1]
	v_cvt_pk_fp8_f32 v209, v176, v177 op_sel:[0,0,1]
	v_cvt_pk_fp8_f32 v210, v198, v199 op_sel:[0,0,1]
	v_cvt_pk_fp8_f32 v211, v202, v203 op_sel:[0,0,1]
	s_nop 0
	global_store_dwordx4 v12, v[208:211], s[14:15]
	s_waitcnt vmcnt(32)
	v_mul_f32_e32 v100, 0x43000000, v100
	v_mul_f32_e32 v101, 0x43000000, v101
	v_mul_f32_e32 v102, 0x43000000, v102
	v_mul_f32_e32 v103, 0x43000000, v103
	ds_write_b128 v4, v[100:103]
	v_mul_f32_e32 v104, 0x43000000, v104
	v_mul_f32_e32 v105, 0x43000000, v105
	v_mul_f32_e32 v106, 0x43000000, v106
	v_mul_f32_e32 v107, 0x43000000, v107
	ds_write_b128 v4, v[104:107] offset:1024
	v_mul_f32_e32 v108, 0x43000000, v108
	v_mul_f32_e32 v109, 0x43000000, v109
	v_mul_f32_e32 v110, 0x43000000, v110
	v_mul_f32_e32 v111, 0x43000000, v111
	ds_write_b128 v4, v[108:111] offset:2048
	v_mul_f32_e32 v112, 0x43000000, v112
	v_mul_f32_e32 v113, 0x43000000, v113
	v_mul_f32_e32 v114, 0x43000000, v114
	v_mul_f32_e32 v115, 0x43000000, v115
	ds_write_b128 v4, v[112:115] offset:3072
	v_mul_f32_e32 v116, 0x43000000, v116
	v_mul_f32_e32 v117, 0x43000000, v117
	v_mul_f32_e32 v118, 0x43000000, v118
	v_mul_f32_e32 v119, 0x43000000, v119
	ds_write_b128 v4, v[116:119] offset:4096
	v_mul_f32_e32 v120, 0x43000000, v120
	v_mul_f32_e32 v121, 0x43000000, v121
	v_mul_f32_e32 v122, 0x43000000, v122
	v_mul_f32_e32 v123, 0x43000000, v123
	ds_write_b128 v4, v[120:123] offset:5120
	v_mul_f32_e32 v124, 0x43000000, v124
	v_mul_f32_e32 v125, 0x43000000, v125
	v_mul_f32_e32 v126, 0x43000000, v126
	v_mul_f32_e32 v127, 0x43000000, v127
	ds_write_b128 v4, v[124:127] offset:6144
	v_mul_f32_e32 v128, 0x43000000, v128
	v_mul_f32_e32 v129, 0x43000000, v129
	v_mul_f32_e32 v130, 0x43000000, v130
	v_mul_f32_e32 v131, 0x43000000, v131
	ds_write_b128 v4, v[128:131] offset:7168
	s_waitcnt lgkmcnt(0)
	s_barrier
; #define GAS __attribute__((address_space(1)))
; #define LAS __attribute__((address_space(3)))
; #define LDS_WAIT() asm volatile("s_waitcnt lgkmcnt(0)" ::: "memory")
;     ...
;     for (int i = 0; i < 32; ++i) v[i] = sc >= 0 ? W[(size_t)(k0 + 2 * i + (lane >> 5)) * Nsrc + sc] : 0.f;
; #pragma unroll
;     for (int i = 0; i < 32; ++i) { const int k = k0 + 2 * i + (lane >> 5); float x = v[i] * wscale; if (KS) x *= (k < ksplit ? ksA[k] : ksB[k - ksplit]); scr[(2 * i + (lane >> 5)) * 33 + (lane & 31)] = x; }
;     LDS_WAIT(); asm volatile("" ::: "memory");
;     const int c = lane & 7;
; #pragma unroll
;     for (int j = 0; j < 4; ++j) { const int n = (lane >> 3) + 8 * j; const LAS float* s = scr + (8 * c) * 33 + n;
;         const unsigned long long o = (unsigned long long)pg8::pk4_fp8(s[0 * 33], s[1 * 33], s[2 * 33], s[3 * 33]) | ((unsigned long long)pg8::pk4_fp8(s[4 * 33], s[5 * 33], s[6 * 33], s[7 * 33]) << 32);
;         *(GAS unsigned long long*)(WT + (size_t)(n0 + n) * K + k0 + 8 * c) = o; }
; __global__ void __launch_bounds__(NWAVES * 64, 2) hybrid_fwd(Args args) {
;     ...
;             p0_transpose_item_f8<false>(args.in[16] + (size_t)l * FF * DM, FF, DM, DM / 32, (unsigned char*)(ws + WS_WDN + l * SZ_WDN), 128.f, args.in[16], args.in[16], 0, scr, r, lane);
	s_add_i32 s17, s16, 2880
	s_min_u32 s17, s17, 0xfff
	s_lshr_b32 s18, s17, 5
	s_add_i32 s18, s18, 0
	s_and_b32 s19, s17, 31
	s_lshl_b32 s18, s18, 21
	s_lshl_b32 s19, s19, 9
	s_add_u32 s18, s18, s19
	s_add_u32 s12, s2, s18
	s_addc_u32 s13, s3, 0
	global_load_dwordx4 v[100:103], v10, s[12:13]
	s_add_u32 s12, s12, 0x8000
	s_addc_u32 s13, s13, 0
	global_load_dwordx4 v[104:107], v10, s[12:13]
	s_add_u32 s12, s12, 0x8000
	s_addc_u32 s13, s13, 0
	global_load_dwordx4 v[108:111], v10, s[12:13]
	s_add_u32 s12, s12, 0x8000
	s_addc_u32 s13, s13, 0
	global_load_dwordx4 v[112:115], v10, s[12:13]
	s_add_u32 s12, s12, 0x8000
	s_addc_u32 s13, s13, 0
	global_load_dwordx4 v[116:119], v10, s[12:13]
	s_add_u32 s12, s12, 0x8000
	s_addc_u32 s13, s13, 0
	global_load_dwordx4 v[120:123], v10, s[12:13]
	s_add_u32 s12, s12, 0x8000
	s_addc_u32 s13, s13, 0
	global_load_dwordx4 v[124:127], v10, s[12:13]
	s_add_u32 s12, s12, 0x8000
	s_addc_u32 s13, s13, 0
	global_load_dwordx4 v[128:131], v10, s[12:13]
	s_add_i32 s17, s16, 2496
	s_min_u32 s17, s17, 0xfff
	s_lshr_b32 s18, s17, 5
	s_add_i32 s18, s18, 0
	s_and_b32 s19, s17, 31
	s_lshl_b32 s19, s19, 21
	s_lshl_b32 s18, s18, 7
	s_add_u32 s18, s18, s19
	s_add_u32 s14, s4, s18
	s_addc_u32 s15, s5, 0
	ds_read_b32 v170, v6
	ds_read_b32 v171, v6 offset:512
	ds_read_b32 v172, v6 offset:1024
	ds_read_b32 v173, v6 offset:1536
	ds_read_b32 v174, v6 offset:2048
	ds_read_b32 v175, v6 offset:2560
	ds_read_b32 v176, v6 offset:3072
	ds_read_b32 v177, v6 offset:3584
	ds_read_b32 v196, v6 offset:4096
	ds_read_b32 v197, v6 offset:4608
	ds_read_b32 v198, v6 offset:5120
	ds_read_b32 v199, v6 offset:5632
	ds_read_b32 v200, v6 offset:6144
	ds_read_b32 v201, v6 offset:6656
	ds_read_b32 v202, v6 offset:7168
	ds_read_b32 v203, v6 offset:7680
	s_waitcnt lgkmcnt(0)
	v_max_f32_e32 v170, v170, v170
	v_max_f32_e32 v171, v171, v171
	v_max_f32_e32 v172, v172, v172
	v_max_f32_e32 v173, v173, v173
	v_max_f32_e32 v174, v174, v174
	v_max_f32_e32 v175, v175, v175
	v_max_f32_e32 v176, v176, v176
	v_max_f32_e32 v177, v177, v177
	v_max_f32_e32 v196, v196, v196
	v_max_f32_e32 v197, v197, v197
	v_max_f32_e32 v198, v198, v198
	v_max_f32_e32 v199, v199, v199
	v_max_f32_e32 v200, v200, v200
	v_max_f32_e32 v201, v201, v201
	v_max_f32_e32 v202, v202, v202
	v_max_f32_e32 v203, v203, v203
	v_med3_f32 v170, v170, s20, v13
	v_med3_f32 v171, v171, s20, v13
	v_med3_f32 v172, v172, s20, v13
	v_med3_f32 v173, v173, s20, v13
	v_med3_f32 v174, v174, s20, v13
	v_med3_f32 v175, v175, s20, v13
	v_med3_f32 v176, v176, s20, v13
	v_med3_f32 v177, v177, s20, v13
	v_med3_f32 v196, v196, s20, v13
	v_med3_f32 v197, v197, s20, v13
	v_med3_f32 v198, v198, s20, v13
	v_med3_f32 v199, v199, s20, v13
	v_med3_f32 v200, v200, s20, v13
	v_med3_f32 v201, v201, s20, v13
	v_med3_f32 v202, v202, s20, v13
	v_med3_f32 v203, v203, s20, v13
	v_mov_b32_e32 v208, 0
	v_mov_b32_e32 v209, 0
	v_mov_b32_e32 v210, 0
	v_mov_b32_e32 v211, 0
	v_cvt_pk_fp8_f32 v208, v170, v171
	v_cvt_pk_fp8_f32 v209, v174, v175
	v_cvt_pk_fp8_f32 v210, v196, v197
	v_cvt_pk_fp8_f32 v211, v200, v201
	v_cvt_pk_fp8_f32 v208, v172, v173 op_sel:[0,0,1]
	v_cvt_pk_fp8_f32 v209, v176, v177 op_sel:[0,0,1]
	v_cvt_pk_fp8_f32 v210, v198, v199 op_sel:[0,0,1]
	v_cvt_pk_fp8_f32 v211, v202, v203 op_sel:[0,0,1]
	s_nop 0
	global_store_dwordx4 v11, v[208:211], s[14:15]
	ds_read_b32 v170, v8
	ds_read_b32 v171, v8 offset:512
	ds_read_b32 v172, v8 offset:1024
	ds_read_b32 v173, v8 offset:1536
	ds_read_b32 v174, v8 offset:2048
	ds_read_b32 v175, v8 offset:2560
	ds_read_b32 v176, v8 offset:3072
	ds_read_b32 v177, v8 offset:3584
	ds_read_b32 v196, v8 offset:4096
	ds_read_b32 v197, v8 offset:4608
	ds_read_b32 v198, v8 offset:5120
	ds_read_b32 v199, v8 offset:5632
	ds_read_b32 v200, v8 offset:6144
	ds_read_b32 v201, v8 offset:6656
	ds_read_b32 v202, v8 offset:7168
	ds_read_b32 v203, v8 offset:7680
	s_waitcnt lgkmcnt(0)
	v_max_f32_e32 v170, v170, v170
	v_max_f32_e32 v171, v171, v171
	v_max_f32_e32 v172, v172, v172
	v_max_f32_e32 v173, v173, v173
	v_max_f32_e32 v174, v174, v174
	v_max_f32_e32 v175, v175, v175
	v_max_f32_e32 v176, v176, v176
	v_max_f32_e32 v177, v177, v177
	v_max_f32_e32 v196, v196, v196
	v_max_f32_e32 v197, v197, v197
	v_max_f32_e32 v198, v198, v198
	v_max_f32_e32 v199, v199, v199
	v_max_f32_e32 v200, v200, v200
	v_max_f32_e32 v201, v201, v201
	v_max_f32_e32 v202, v202, v202
	v_max_f32_e32 v203, v203, v203
	v_med3_f32 v170, v170, s20, v13
	v_med3_f32 v171, v171, s20, v13
	v_med3_f32 v172, v172, s20, v13
	v_med3_f32 v173, v173, s20, v13
	v_med3_f32 v174, v174, s20, v13
	v_med3_f32 v175, v175, s20, v13
	v_med3_f32 v176, v176, s20, v13
	v_med3_f32 v177, v177, s20, v13
	v_med3_f32 v196, v196, s20, v13
	v_med3_f32 v197, v197, s20, v13
	v_med3_f32 v198, v198, s20, v13
	v_med3_f32 v199, v199, s20, v13
	v_med3_f32 v200, v200, s20, v13
	v_med3_f32 v201, v201, s20, v13
	v_med3_f32 v202, v202, s20, v13
	v_med3_f32 v203, v203, s20, v13
	v_mov_b32_e32 v208, 0
	v_mov_b32_e32 v209, 0
	v_mov_b32_e32 v210, 0
	v_mov_b32_e32 v211, 0
	v_cvt_pk_fp8_f32 v208, v170, v171
	v_cvt_pk_fp8_f32 v209, v174, v175
	v_cvt_pk_fp8_f32 v210, v196, v197
	v_cvt_pk_fp8_f32 v211, v200, v201
	v_cvt_pk_fp8_f32 v208, v172, v173 op_sel:[0,0,1]
	v_cvt_pk_fp8_f32 v209, v176, v177 op_sel:[0,0,1]
	v_cvt_pk_fp8_f32 v210, v198, v199 op_sel:[0,0,1]
	v_cvt_pk_fp8_f32 v211, v202, v203 op_sel:[0,0,1]
	s_nop 0
	global_store_dwordx4 v12, v[208:211], s[14:15]
	s_waitcnt vmcnt(32)
	v_mul_f32_e32 v132, 0x43000000, v132
	v_mul_f32_e32 v133, 0x43000000, v133
	v_mul_f32_e32 v134, 0x43000000, v134
	v_mul_f32_e32 v135, 0x43000000, v135
	ds_write_b128 v5, v[132:135]
	v_mul_f32_e32 v136, 0x43000000, v136
	v_mul_f32_e32 v137, 0x43000000, v137
	v_mul_f32_e32 v138, 0x43000000, v138
	v_mul_f32_e32 v139, 0x43000000, v139
	ds_write_b128 v5, v[136:139] offset:1024
	v_mul_f32_e32 v140, 0x43000000, v140
	v_mul_f32_e32 v141, 0x43000000, v141
	v_mul_f32_e32 v142, 0x43000000, v142
	v_mul_f32_e32 v143, 0x43000000, v143
	ds_write_b128 v5, v[140:143] offset:2048
	v_mul_f32_e32 v144, 0x43000000, v144
	v_mul_f32_e32 v145, 0x43000000, v145
	v_mul_f32_e32 v146, 0x43000000, v146
	v_mul_f32_e32 v147, 0x43000000, v147
	ds_write_b128 v5, v[144:147] offset:3072
	v_mul_f32_e32 v148, 0x43000000, v148
	v_mul_f32_e32 v149, 0x43000000, v149
	v_mul_f32_e32 v150, 0x43000000, v150
	v_mul_f32_e32 v151, 0x43000000, v151
	ds_write_b128 v5, v[148:151] offset:4096
	v_mul_f32_e32 v152, 0x43000000, v152
	v_mul_f32_e32 v153, 0x43000000, v153
	v_mul_f32_e32 v154, 0x43000000, v154
	v_mul_f32_e32 v155, 0x43000000, v155
	ds_write_b128 v5, v[152:155] offset:5120
	v_mul_f32_e32 v156, 0x43000000, v156
	v_mul_f32_e32 v157, 0x43000000, v157
	v_mul_f32_e32 v158, 0x43000000, v158
	v_mul_f32_e32 v159, 0x43000000, v159
	ds_write_b128 v5, v[156:159] offset:6144
	v_mul_f32_e32 v160, 0x43000000, v160
	v_mul_f32_e32 v161, 0x43000000, v161
	v_mul_f32_e32 v162, 0x43000000, v162
	v_mul_f32_e32 v163, 0x43000000, v163
	ds_write_b128 v5, v[160:163] offset:7168
	s_waitcnt lgkmcnt(0)
	s_barrier
; #define GAS __attribute__((address_space(1)))
; #define LAS __attribute__((address_space(3)))
; #define LDS_WAIT() asm volatile("s_waitcnt lgkmcnt(0)" ::: "memory")
;     ...
;     for (int i = 0; i < 32; ++i) v[i] = sc >= 0 ? W[(size_t)(k0 + 2 * i + (lane >> 5)) * Nsrc + sc] : 0.f;
; #pragma unroll
;     for (int i = 0; i < 32; ++i) { const int k = k0 + 2 * i + (lane >> 5); float x = v[i] * wscale; if (KS) x *= (k < ksplit ? ksA[k] : ksB[k - ksplit]); scr[(2 * i + (lane >> 5)) * 33 + (lane & 31)] = x; }
;     LDS_WAIT(); asm volatile("" ::: "memory");
;     const int c = lane & 7;
; #pragma unroll
;     for (int j = 0; j < 4; ++j) { const int n = (lane >> 3) + 8 * j; const LAS float* s = scr + (8 * c) * 33 + n;
;         const unsigned long long o = (unsigned long long)pg8::pk4_fp8(s[0 * 33], s[1 * 33], s[2 * 33], s[3 * 33]) | ((unsigned long long)pg8::pk4_fp8(s[4 * 33], s[5 * 33], s[6 * 33], s[7 * 33]) << 32);
;         *(GAS unsigned long long*)(WT + (size_t)(n0 + n) * K + k0 + 8 * c) = o; }
; __global__ void __launch_bounds__(NWAVES * 64, 2) hybrid_fwd(Args args) {
;     ...
;             p0_transpose_item_f8<false>(args.in[16] + (size_t)l * FF * DM, FF, DM, DM / 32, (unsigned char*)(ws + WS_WDN + l * SZ_WDN), 128.f, args.in[16], args.in[16], 0, scr, r, lane);
	s_add_i32 s17, s16, 2976
	s_min_u32 s17, s17, 0xfff
	s_lshr_b32 s18, s17, 5
	s_add_i32 s18, s18, 0
	s_and_b32 s19, s17, 31
	s_lshl_b32 s18, s18, 21
	s_lshl_b32 s19, s19, 9
	s_add_u32 s18, s18, s19
	s_add_u32 s12, s2, s18
	s_addc_u32 s13, s3, 0
	global_load_dwordx4 v[132:135], v10, s[12:13]
	s_add_u32 s12, s12, 0x8000
	s_addc_u32 s13, s13, 0
	global_load_dwordx4 v[136:139], v10, s[12:13]
	s_add_u32 s12, s12, 0x8000
	s_addc_u32 s13, s13, 0
	global_load_dwordx4 v[140:143], v10, s[12:13]
	s_add_u32 s12, s12, 0x8000
	s_addc_u32 s13, s13, 0
	global_load_dwordx4 v[144:147], v10, s[12:13]
	s_add_u32 s12, s12, 0x8000
	s_addc_u32 s13, s13, 0
	global_load_dwordx4 v[148:151], v10, s[12:13]
	s_add_u32 s12, s12, 0x8000
	s_addc_u32 s13, s13, 0
	global_load_dwordx4 v[152:155], v10, s[12:13]
	s_add_u32 s12, s12, 0x8000
	s_addc_u32 s13, s13, 0
	global_load_dwordx4 v[156:159], v10, s[12:13]
	s_add_u32 s12, s12, 0x8000
	s_addc_u32 s13, s13, 0
	global_load_dwordx4 v[160:163], v10, s[12:13]
	s_add_i32 s17, s16, 2592
	s_min_u32 s17, s17, 0xfff
	s_lshr_b32 s18, s17, 5
	s_add_i32 s18, s18, 0
	s_and_b32 s19, s17, 31
	s_lshl_b32 s19, s19, 21
	s_lshl_b32 s18, s18, 7
	s_add_u32 s18, s18, s19
	s_add_u32 s14, s4, s18
	s_addc_u32 s15, s5, 0
	ds_read_b32 v170, v7
	ds_read_b32 v171, v7 offset:512
	ds_read_b32 v172, v7 offset:1024
	ds_read_b32 v173, v7 offset:1536
	ds_read_b32 v174, v7 offset:2048
	ds_read_b32 v175, v7 offset:2560
	ds_read_b32 v176, v7 offset:3072
	ds_read_b32 v177, v7 offset:3584
	ds_read_b32 v196, v7 offset:4096
	ds_read_b32 v197, v7 offset:4608
	ds_read_b32 v198, v7 offset:5120
	ds_read_b32 v199, v7 offset:5632
	ds_read_b32 v200, v7 offset:6144
	ds_read_b32 v201, v7 offset:6656
	ds_read_b32 v202, v7 offset:7168
	ds_read_b32 v203, v7 offset:7680
	s_waitcnt lgkmcnt(0)
	v_max_f32_e32 v170, v170, v170
	v_max_f32_e32 v171, v171, v171
	v_max_f32_e32 v172, v172, v172
	v_max_f32_e32 v173, v173, v173
	v_max_f32_e32 v174, v174, v174
	v_max_f32_e32 v175, v175, v175
	v_max_f32_e32 v176, v176, v176
	v_max_f32_e32 v177, v177, v177
	v_max_f32_e32 v196, v196, v196
	v_max_f32_e32 v197, v197, v197
	v_max_f32_e32 v198, v198, v198
	v_max_f32_e32 v199, v199, v199
	v_max_f32_e32 v200, v200, v200
	v_max_f32_e32 v201, v201, v201
	v_max_f32_e32 v202, v202, v202
	v_max_f32_e32 v203, v203, v203
	v_med3_f32 v170, v170, s20, v13
	v_med3_f32 v171, v171, s20, v13
	v_med3_f32 v172, v172, s20, v13
	v_med3_f32 v173, v173, s20, v13
	v_med3_f32 v174, v174, s20, v13
	v_med3_f32 v175, v175, s20, v13
	v_med3_f32 v176, v176, s20, v13
	v_med3_f32 v177, v177, s20, v13
	v_med3_f32 v196, v196, s20, v13
	v_med3_f32 v197, v197, s20, v13
	v_med3_f32 v198, v198, s20, v13
	v_med3_f32 v199, v199, s20, v13
	v_med3_f32 v200, v200, s20, v13
	v_med3_f32 v201, v201, s20, v13
	v_med3_f32 v202, v202, s20, v13
	v_med3_f32 v203, v203, s20, v13
	v_mov_b32_e32 v208, 0
	v_mov_b32_e32 v209, 0
	v_mov_b32_e32 v210, 0
	v_mov_b32_e32 v211, 0
	v_cvt_pk_fp8_f32 v208, v170, v171
	v_cvt_pk_fp8_f32 v209, v174, v175
	v_cvt_pk_fp8_f32 v210, v196, v197
	v_cvt_pk_fp8_f32 v211, v200, v201
	v_cvt_pk_fp8_f32 v208, v172, v173 op_sel:[0,0,1]
	v_cvt_pk_fp8_f32 v209, v176, v177 op_sel:[0,0,1]
	v_cvt_pk_fp8_f32 v210, v198, v199 op_sel:[0,0,1]
	v_cvt_pk_fp8_f32 v211, v202, v203 op_sel:[0,0,1]
	s_nop 0
	global_store_dwordx4 v11, v[208:211], s[14:15]
	ds_read_b32 v170, v9
	ds_read_b32 v171, v9 offset:512
	ds_read_b32 v172, v9 offset:1024
	ds_read_b32 v173, v9 offset:1536
	ds_read_b32 v174, v9 offset:2048
	ds_read_b32 v175, v9 offset:2560
	ds_read_b32 v176, v9 offset:3072
	ds_read_b32 v177, v9 offset:3584
	ds_read_b32 v196, v9 offset:4096
	ds_read_b32 v197, v9 offset:4608
	ds_read_b32 v198, v9 offset:5120
	ds_read_b32 v199, v9 offset:5632
	ds_read_b32 v200, v9 offset:6144
	ds_read_b32 v201, v9 offset:6656
	ds_read_b32 v202, v9 offset:7168
	ds_read_b32 v203, v9 offset:7680
	s_waitcnt lgkmcnt(0)
	v_max_f32_e32 v170, v170, v170
	v_max_f32_e32 v171, v171, v171
	v_max_f32_e32 v172, v172, v172
	v_max_f32_e32 v173, v173, v173
	v_max_f32_e32 v174, v174, v174
	v_max_f32_e32 v175, v175, v175
	v_max_f32_e32 v176, v176, v176
	v_max_f32_e32 v177, v177, v177
	v_max_f32_e32 v196, v196, v196
	v_max_f32_e32 v197, v197, v197
	v_max_f32_e32 v198, v198, v198
	v_max_f32_e32 v199, v199, v199
	v_max_f32_e32 v200, v200, v200
	v_max_f32_e32 v201, v201, v201
	v_max_f32_e32 v202, v202, v202
	v_max_f32_e32 v203, v203, v203
	v_med3_f32 v170, v170, s20, v13
	v_med3_f32 v171, v171, s20, v13
	v_med3_f32 v172, v172, s20, v13
	v_med3_f32 v173, v173, s20, v13
	v_med3_f32 v174, v174, s20, v13
	v_med3_f32 v175, v175, s20, v13
	v_med3_f32 v176, v176, s20, v13
	v_med3_f32 v177, v177, s20, v13
	v_med3_f32 v196, v196, s20, v13
	v_med3_f32 v197, v197, s20, v13
	v_med3_f32 v198, v198, s20, v13
	v_med3_f32 v199, v199, s20, v13
	v_med3_f32 v200, v200, s20, v13
	v_med3_f32 v201, v201, s20, v13
	v_med3_f32 v202, v202, s20, v13
	v_med3_f32 v203, v203, s20, v13
	v_mov_b32_e32 v208, 0
	v_mov_b32_e32 v209, 0
	v_mov_b32_e32 v210, 0
	v_mov_b32_e32 v211, 0
	v_cvt_pk_fp8_f32 v208, v170, v171
	v_cvt_pk_fp8_f32 v209, v174, v175
	v_cvt_pk_fp8_f32 v210, v196, v197
	v_cvt_pk_fp8_f32 v211, v200, v201
	v_cvt_pk_fp8_f32 v208, v172, v173 op_sel:[0,0,1]
	v_cvt_pk_fp8_f32 v209, v176, v177 op_sel:[0,0,1]
	v_cvt_pk_fp8_f32 v210, v198, v199 op_sel:[0,0,1]
	v_cvt_pk_fp8_f32 v211, v202, v203 op_sel:[0,0,1]
	s_nop 0
	global_store_dwordx4 v12, v[208:211], s[14:15]
	s_waitcnt vmcnt(32)
	v_mul_f32_e32 v36, 0x43000000, v36
	v_mul_f32_e32 v37, 0x43000000, v37
	v_mul_f32_e32 v38, 0x43000000, v38
	v_mul_f32_e32 v39, 0x43000000, v39
	ds_write_b128 v4, v[36:39]
	v_mul_f32_e32 v40, 0x43000000, v40
	v_mul_f32_e32 v41, 0x43000000, v41
	v_mul_f32_e32 v42, 0x43000000, v42
	v_mul_f32_e32 v43, 0x43000000, v43
	ds_write_b128 v4, v[40:43] offset:1024
	v_mul_f32_e32 v44, 0x43000000, v44
	v_mul_f32_e32 v45, 0x43000000, v45
	v_mul_f32_e32 v46, 0x43000000, v46
	v_mul_f32_e32 v47, 0x43000000, v47
	ds_write_b128 v4, v[44:47] offset:2048
	v_mul_f32_e32 v48, 0x43000000, v48
	v_mul_f32_e32 v49, 0x43000000, v49
	v_mul_f32_e32 v50, 0x43000000, v50
	v_mul_f32_e32 v51, 0x43000000, v51
	ds_write_b128 v4, v[48:51] offset:3072
	v_mul_f32_e32 v52, 0x43000000, v52
	v_mul_f32_e32 v53, 0x43000000, v53
	v_mul_f32_e32 v54, 0x43000000, v54
	v_mul_f32_e32 v55, 0x43000000, v55
	ds_write_b128 v4, v[52:55] offset:4096
	v_mul_f32_e32 v56, 0x43000000, v56
	v_mul_f32_e32 v57, 0x43000000, v57
	v_mul_f32_e32 v58, 0x43000000, v58
	v_mul_f32_e32 v59, 0x43000000, v59
	ds_write_b128 v4, v[56:59] offset:5120
	v_mul_f32_e32 v60, 0x43000000, v60
	v_mul_f32_e32 v61, 0x43000000, v61
	v_mul_f32_e32 v62, 0x43000000, v62
	v_mul_f32_e32 v63, 0x43000000, v63
	ds_write_b128 v4, v[60:63] offset:6144
	v_mul_f32_e32 v64, 0x43000000, v64
	v_mul_f32_e32 v65, 0x43000000, v65
	v_mul_f32_e32 v66, 0x43000000, v66
	v_mul_f32_e32 v67, 0x43000000, v67
	ds_write_b128 v4, v[64:67] offset:7168
	s_waitcnt lgkmcnt(0)
	s_barrier
; #define GAS __attribute__((address_space(1)))
; #define LAS __attribute__((address_space(3)))
; #define LDS_WAIT() asm volatile("s_waitcnt lgkmcnt(0)" ::: "memory")
;     ...
;     for (int i = 0; i < 32; ++i) v[i] = sc >= 0 ? W[(size_t)(k0 + 2 * i + (lane >> 5)) * Nsrc + sc] : 0.f;
; #pragma unroll
;     for (int i = 0; i < 32; ++i) { const int k = k0 + 2 * i + (lane >> 5); float x = v[i] * wscale; if (KS) x *= (k < ksplit ? ksA[k] : ksB[k - ksplit]); scr[(2 * i + (lane >> 5)) * 33 + (lane & 31)] = x; }
;     LDS_WAIT(); asm volatile("" ::: "memory");
;     const int c = lane & 7;
; #pragma unroll
;     for (int j = 0; j < 4; ++j) { const int n = (lane >> 3) + 8 * j; const LAS float* s = scr + (8 * c) * 33 + n;
;         const unsigned long long o = (unsigned long long)pg8::pk4_fp8(s[0 * 33], s[1 * 33], s[2 * 33], s[3 * 33]) | ((unsigned long long)pg8::pk4_fp8(s[4 * 33], s[5 * 33], s[6 * 33], s[7 * 33]) << 32);
;         *(GAS unsigned long long*)(WT + (size_t)(n0 + n) * K + k0 + 8 * c) = o; }
; __global__ void __launch_bounds__(NWAVES * 64, 2) hybrid_fwd(Args args) {
;     ...
;             p0_transpose_item_f8<false>(args.in[16] + (size_t)l * FF * DM, FF, DM, DM / 32, (unsigned char*)(ws + WS_WDN + l * SZ_WDN), 128.f, args.in[16], args.in[16], 0, scr, r, lane);
	s_add_i32 s17, s16, 3072
	s_min_u32 s17, s17, 0xfff
	s_lshr_b32 s18, s17, 5
	s_add_i32 s18, s18, 0
	s_and_b32 s19, s17, 31
	s_lshl_b32 s18, s18, 21
	s_lshl_b32 s19, s19, 9
	s_add_u32 s18, s18, s19
	s_add_u32 s12, s2, s18
	s_addc_u32 s13, s3, 0
	global_load_dwordx4 v[36:39], v10, s[12:13]
	s_add_u32 s12, s12, 0x8000
	s_addc_u32 s13, s13, 0
	global_load_dwordx4 v[40:43], v10, s[12:13]
	s_add_u32 s12, s12, 0x8000
	s_addc_u32 s13, s13, 0
	global_load_dwordx4 v[44:47], v10, s[12:13]
	s_add_u32 s12, s12, 0x8000
	s_addc_u32 s13, s13, 0
	global_load_dwordx4 v[48:51], v10, s[12:13]
	s_add_u32 s12, s12, 0x8000
	s_addc_u32 s13, s13, 0
	global_load_dwordx4 v[52:55], v10, s[12:13]
	s_add_u32 s12, s12, 0x8000
	s_addc_u32 s13, s13, 0
	global_load_dwordx4 v[56:59], v10, s[12:13]
	s_add_u32 s12, s12, 0x8000
	s_addc_u32 s13, s13, 0
	global_load_dwordx4 v[60:63], v10, s[12:13]
	s_add_u32 s12, s12, 0x8000
	s_addc_u32 s13, s13, 0
	global_load_dwordx4 v[64:67], v10, s[12:13]
	s_add_i32 s17, s16, 2688
	s_min_u32 s17, s17, 0xfff
	s_lshr_b32 s18, s17, 5
	s_add_i32 s18, s18, 0
	s_and_b32 s19, s17, 31
	s_lshl_b32 s19, s19, 21
	s_lshl_b32 s18, s18, 7
	s_add_u32 s18, s18, s19
	s_add_u32 s14, s4, s18
	s_addc_u32 s15, s5, 0
	ds_read_b32 v170, v6
	ds_read_b32 v171, v6 offset:512
	ds_read_b32 v172, v6 offset:1024
	ds_read_b32 v173, v6 offset:1536
	ds_read_b32 v174, v6 offset:2048
	ds_read_b32 v175, v6 offset:2560
	ds_read_b32 v176, v6 offset:3072
	ds_read_b32 v177, v6 offset:3584
	ds_read_b32 v196, v6 offset:4096
	ds_read_b32 v197, v6 offset:4608
	ds_read_b32 v198, v6 offset:5120
	ds_read_b32 v199, v6 offset:5632
	ds_read_b32 v200, v6 offset:6144
	ds_read_b32 v201, v6 offset:6656
	ds_read_b32 v202, v6 offset:7168
	ds_read_b32 v203, v6 offset:7680
	s_waitcnt lgkmcnt(0)
	v_max_f32_e32 v170, v170, v170
	v_max_f32_e32 v171, v171, v171
	v_max_f32_e32 v172, v172, v172
	v_max_f32_e32 v173, v173, v173
	v_max_f32_e32 v174, v174, v174
	v_max_f32_e32 v175, v175, v175
	v_max_f32_e32 v176, v176, v176
	v_max_f32_e32 v177, v177, v177
	v_max_f32_e32 v196, v196, v196
	v_max_f32_e32 v197, v197, v197
	v_max_f32_e32 v198, v198, v198
	v_max_f32_e32 v199, v199, v199
	v_max_f32_e32 v200, v200, v200
	v_max_f32_e32 v201, v201, v201
	v_max_f32_e32 v202, v202, v202
	v_max_f32_e32 v203, v203, v203
	v_med3_f32 v170, v170, s20, v13
	v_med3_f32 v171, v171, s20, v13
	v_med3_f32 v172, v172, s20, v13
	v_med3_f32 v173, v173, s20, v13
	v_med3_f32 v174, v174, s20, v13
	v_med3_f32 v175, v175, s20, v13
	v_med3_f32 v176, v176, s20, v13
	v_med3_f32 v177, v177, s20, v13
	v_med3_f32 v196, v196, s20, v13
	v_med3_f32 v197, v197, s20, v13
	v_med3_f32 v198, v198, s20, v13
	v_med3_f32 v199, v199, s20, v13
	v_med3_f32 v200, v200, s20, v13
	v_med3_f32 v201, v201, s20, v13
	v_med3_f32 v202, v202, s20, v13
	v_med3_f32 v203, v203, s20, v13
	v_mov_b32_e32 v208, 0
	v_mov_b32_e32 v209, 0
	v_mov_b32_e32 v210, 0
	v_mov_b32_e32 v211, 0
	v_cvt_pk_fp8_f32 v208, v170, v171
	v_cvt_pk_fp8_f32 v209, v174, v175
	v_cvt_pk_fp8_f32 v210, v196, v197
	v_cvt_pk_fp8_f32 v211, v200, v201
	v_cvt_pk_fp8_f32 v208, v172, v173 op_sel:[0,0,1]
	v_cvt_pk_fp8_f32 v209, v176, v177 op_sel:[0,0,1]
	v_cvt_pk_fp8_f32 v210, v198, v199 op_sel:[0,0,1]
	v_cvt_pk_fp8_f32 v211, v202, v203 op_sel:[0,0,1]
	s_nop 0
	global_store_dwordx4 v11, v[208:211], s[14:15]
	ds_read_b32 v170, v8
	ds_read_b32 v171, v8 offset:512
	ds_read_b32 v172, v8 offset:1024
	ds_read_b32 v173, v8 offset:1536
	ds_read_b32 v174, v8 offset:2048
	ds_read_b32 v175, v8 offset:2560
	ds_read_b32 v176, v8 offset:3072
	ds_read_b32 v177, v8 offset:3584
	ds_read_b32 v196, v8 offset:4096
	ds_read_b32 v197, v8 offset:4608
	ds_read_b32 v198, v8 offset:5120
	ds_read_b32 v199, v8 offset:5632
	ds_read_b32 v200, v8 offset:6144
	ds_read_b32 v201, v8 offset:6656
	ds_read_b32 v202, v8 offset:7168
	ds_read_b32 v203, v8 offset:7680
	s_waitcnt lgkmcnt(0)
	v_max_f32_e32 v170, v170, v170
	v_max_f32_e32 v171, v171, v171
	v_max_f32_e32 v172, v172, v172
	v_max_f32_e32 v173, v173, v173
	v_max_f32_e32 v174, v174, v174
	v_max_f32_e32 v175, v175, v175
	v_max_f32_e32 v176, v176, v176
	v_max_f32_e32 v177, v177, v177
	v_max_f32_e32 v196, v196, v196
	v_max_f32_e32 v197, v197, v197
	v_max_f32_e32 v198, v198, v198
	v_max_f32_e32 v199, v199, v199
	v_max_f32_e32 v200, v200, v200
	v_max_f32_e32 v201, v201, v201
	v_max_f32_e32 v202, v202, v202
	v_max_f32_e32 v203, v203, v203
	v_med3_f32 v170, v170, s20, v13
	v_med3_f32 v171, v171, s20, v13
	v_med3_f32 v172, v172, s20, v13
	v_med3_f32 v173, v173, s20, v13
	v_med3_f32 v174, v174, s20, v13
	v_med3_f32 v175, v175, s20, v13
	v_med3_f32 v176, v176, s20, v13
	v_med3_f32 v177, v177, s20, v13
	v_med3_f32 v196, v196, s20, v13
	v_med3_f32 v197, v197, s20, v13
	v_med3_f32 v198, v198, s20, v13
	v_med3_f32 v199, v199, s20, v13
	v_med3_f32 v200, v200, s20, v13
	v_med3_f32 v201, v201, s20, v13
	v_med3_f32 v202, v202, s20, v13
	v_med3_f32 v203, v203, s20, v13
	v_mov_b32_e32 v208, 0
	v_mov_b32_e32 v209, 0
	v_mov_b32_e32 v210, 0
	v_mov_b32_e32 v211, 0
	v_cvt_pk_fp8_f32 v208, v170, v171
	v_cvt_pk_fp8_f32 v209, v174, v175
	v_cvt_pk_fp8_f32 v210, v196, v197
	v_cvt_pk_fp8_f32 v211, v200, v201
	v_cvt_pk_fp8_f32 v208, v172, v173 op_sel:[0,0,1]
	v_cvt_pk_fp8_f32 v209, v176, v177 op_sel:[0,0,1]
	v_cvt_pk_fp8_f32 v210, v198, v199 op_sel:[0,0,1]
	v_cvt_pk_fp8_f32 v211, v202, v203 op_sel:[0,0,1]
	s_nop 0
	global_store_dwordx4 v12, v[208:211], s[14:15]
	s_waitcnt vmcnt(32)
	v_mul_f32_e32 v68, 0x43000000, v68
	v_mul_f32_e32 v69, 0x43000000, v69
	v_mul_f32_e32 v70, 0x43000000, v70
	v_mul_f32_e32 v71, 0x43000000, v71
	ds_write_b128 v5, v[68:71]
	v_mul_f32_e32 v72, 0x43000000, v72
	v_mul_f32_e32 v73, 0x43000000, v73
	v_mul_f32_e32 v74, 0x43000000, v74
	v_mul_f32_e32 v75, 0x43000000, v75
	ds_write_b128 v5, v[72:75] offset:1024
	v_mul_f32_e32 v76, 0x43000000, v76
	v_mul_f32_e32 v77, 0x43000000, v77
	v_mul_f32_e32 v78, 0x43000000, v78
	v_mul_f32_e32 v79, 0x43000000, v79
	ds_write_b128 v5, v[76:79] offset:2048
	v_mul_f32_e32 v80, 0x43000000, v80
	v_mul_f32_e32 v81, 0x43000000, v81
	v_mul_f32_e32 v82, 0x43000000, v82
	v_mul_f32_e32 v83, 0x43000000, v83
	ds_write_b128 v5, v[80:83] offset:3072
	v_mul_f32_e32 v84, 0x43000000, v84
	v_mul_f32_e32 v85, 0x43000000, v85
	v_mul_f32_e32 v86, 0x43000000, v86
	v_mul_f32_e32 v87, 0x43000000, v87
	ds_write_b128 v5, v[84:87] offset:4096
	v_mul_f32_e32 v88, 0x43000000, v88
	v_mul_f32_e32 v89, 0x43000000, v89
	v_mul_f32_e32 v90, 0x43000000, v90
	v_mul_f32_e32 v91, 0x43000000, v91
	ds_write_b128 v5, v[88:91] offset:5120
	v_mul_f32_e32 v92, 0x43000000, v92
	v_mul_f32_e32 v93, 0x43000000, v93
	v_mul_f32_e32 v94, 0x43000000, v94
	v_mul_f32_e32 v95, 0x43000000, v95
	ds_write_b128 v5, v[92:95] offset:6144
	v_mul_f32_e32 v96, 0x43000000, v96
	v_mul_f32_e32 v97, 0x43000000, v97
	v_mul_f32_e32 v98, 0x43000000, v98
	v_mul_f32_e32 v99, 0x43000000, v99
	ds_write_b128 v5, v[96:99] offset:7168
	s_waitcnt lgkmcnt(0)
	s_barrier
; #define GAS __attribute__((address_space(1)))
; #define LAS __attribute__((address_space(3)))
; #define LDS_WAIT() asm volatile("s_waitcnt lgkmcnt(0)" ::: "memory")
;     ...
;     for (int i = 0; i < 32; ++i) v[i] = sc >= 0 ? W[(size_t)(k0 + 2 * i + (lane >> 5)) * Nsrc + sc] : 0.f;
; #pragma unroll
;     for (int i = 0; i < 32; ++i) { const int k = k0 + 2 * i + (lane >> 5); float x = v[i] * wscale; if (KS) x *= (k < ksplit ? ksA[k] : ksB[k - ksplit]); scr[(2 * i + (lane >> 5)) * 33 + (lane & 31)] = x; }
;     LDS_WAIT(); asm volatile("" ::: "memory");
;     const int c = lane & 7;
; #pragma unroll
;     for (int j = 0; j < 4; ++j) { const int n = (lane >> 3) + 8 * j; const LAS float* s = scr + (8 * c) * 33 + n;
;         const unsigned long long o = (unsigned long long)pg8::pk4_fp8(s[0 * 33], s[1 * 33], s[2 * 33], s[3 * 33]) | ((unsigned long long)pg8::pk4_fp8(s[4 * 33], s[5 * 33], s[6 * 33], s[7 * 33]) << 32);
;         *(GAS unsigned long long*)(WT + (size_t)(n0 + n) * K + k0 + 8 * c) = o; }
; __global__ void __launch_bounds__(NWAVES * 64, 2) hybrid_fwd(Args args) {
;     ...
;             p0_transpose_item_f8<false>(args.in[16] + (size_t)l * FF * DM, FF, DM, DM / 32, (unsigned char*)(ws + WS_WDN + l * SZ_WDN), 128.f, args.in[16], args.in[16], 0, scr, r, lane);
	s_add_i32 s17, s16, 3168
	s_min_u32 s17, s17, 0xfff
	s_lshr_b32 s18, s17, 5
	s_add_i32 s18, s18, 0
	s_and_b32 s19, s17, 31
	s_lshl_b32 s18, s18, 21
	s_lshl_b32 s19, s19, 9
	s_add_u32 s18, s18, s19
	s_add_u32 s12, s2, s18
	s_addc_u32 s13, s3, 0
	global_load_dwordx4 v[68:71], v10, s[12:13]
	s_add_u32 s12, s12, 0x8000
	s_addc_u32 s13, s13, 0
	global_load_dwordx4 v[72:75], v10, s[12:13]
	s_add_u32 s12, s12, 0x8000
	s_addc_u32 s13, s13, 0
	global_load_dwordx4 v[76:79], v10, s[12:13]
	s_add_u32 s12, s12, 0x8000
	s_addc_u32 s13, s13, 0
	global_load_dwordx4 v[80:83], v10, s[12:13]
	s_add_u32 s12, s12, 0x8000
	s_addc_u32 s13, s13, 0
	global_load_dwordx4 v[84:87], v10, s[12:13]
	s_add_u32 s12, s12, 0x8000
	s_addc_u32 s13, s13, 0
	global_load_dwordx4 v[88:91], v10, s[12:13]
	s_add_u32 s12, s12, 0x8000
	s_addc_u32 s13, s13, 0
	global_load_dwordx4 v[92:95], v10, s[12:13]
	s_add_u32 s12, s12, 0x8000
	s_addc_u32 s13, s13, 0
	global_load_dwordx4 v[96:99], v10, s[12:13]
	s_add_i32 s17, s16, 2784
	s_min_u32 s17, s17, 0xfff
	s_lshr_b32 s18, s17, 5
	s_add_i32 s18, s18, 0
	s_and_b32 s19, s17, 31
	s_lshl_b32 s19, s19, 21
	s_lshl_b32 s18, s18, 7
	s_add_u32 s18, s18, s19
	s_add_u32 s14, s4, s18
	s_addc_u32 s15, s5, 0
	ds_read_b32 v170, v7
	ds_read_b32 v171, v7 offset:512
	ds_read_b32 v172, v7 offset:1024
	ds_read_b32 v173, v7 offset:1536
	ds_read_b32 v174, v7 offset:2048
	ds_read_b32 v175, v7 offset:2560
	ds_read_b32 v176, v7 offset:3072
	ds_read_b32 v177, v7 offset:3584
	ds_read_b32 v196, v7 offset:4096
	ds_read_b32 v197, v7 offset:4608
	ds_read_b32 v198, v7 offset:5120
	ds_read_b32 v199, v7 offset:5632
	ds_read_b32 v200, v7 offset:6144
	ds_read_b32 v201, v7 offset:6656
	ds_read_b32 v202, v7 offset:7168
	ds_read_b32 v203, v7 offset:7680
	s_waitcnt lgkmcnt(0)
	v_max_f32_e32 v170, v170, v170
	v_max_f32_e32 v171, v171, v171
	v_max_f32_e32 v172, v172, v172
	v_max_f32_e32 v173, v173, v173
	v_max_f32_e32 v174, v174, v174
	v_max_f32_e32 v175, v175, v175
	v_max_f32_e32 v176, v176, v176
	v_max_f32_e32 v177, v177, v177
	v_max_f32_e32 v196, v196, v196
	v_max_f32_e32 v197, v197, v197
	v_max_f32_e32 v198, v198, v198
	v_max_f32_e32 v199, v199, v199
	v_max_f32_e32 v200, v200, v200
	v_max_f32_e32 v201, v201, v201
	v_max_f32_e32 v202, v202, v202
	v_max_f32_e32 v203, v203, v203
	v_med3_f32 v170, v170, s20, v13
	v_med3_f32 v171, v171, s20, v13
	v_med3_f32 v172, v172, s20, v13
	v_med3_f32 v173, v173, s20, v13
	v_med3_f32 v174, v174, s20, v13
	v_med3_f32 v175, v175, s20, v13
	v_med3_f32 v176, v176, s20, v13
	v_med3_f32 v177, v177, s20, v13
	v_med3_f32 v196, v196, s20, v13
	v_med3_f32 v197, v197, s20, v13
	v_med3_f32 v198, v198, s20, v13
	v_med3_f32 v199, v199, s20, v13
	v_med3_f32 v200, v200, s20, v13
	v_med3_f32 v201, v201, s20, v13
	v_med3_f32 v202, v202, s20, v13
	v_med3_f32 v203, v203, s20, v13
	v_mov_b32_e32 v208, 0
	v_mov_b32_e32 v209, 0
	v_mov_b32_e32 v210, 0
	v_mov_b32_e32 v211, 0
	v_cvt_pk_fp8_f32 v208, v170, v171
	v_cvt_pk_fp8_f32 v209, v174, v175
	v_cvt_pk_fp8_f32 v210, v196, v197
	v_cvt_pk_fp8_f32 v211, v200, v201
	v_cvt_pk_fp8_f32 v208, v172, v173 op_sel:[0,0,1]
	v_cvt_pk_fp8_f32 v209, v176, v177 op_sel:[0,0,1]
	v_cvt_pk_fp8_f32 v210, v198, v199 op_sel:[0,0,1]
	v_cvt_pk_fp8_f32 v211, v202, v203 op_sel:[0,0,1]
	s_nop 0
	global_store_dwordx4 v11, v[208:211], s[14:15]
	ds_read_b32 v170, v9
	ds_read_b32 v171, v9 offset:512
	ds_read_b32 v172, v9 offset:1024
	ds_read_b32 v173, v9 offset:1536
	ds_read_b32 v174, v9 offset:2048
	ds_read_b32 v175, v9 offset:2560
	ds_read_b32 v176, v9 offset:3072
	ds_read_b32 v177, v9 offset:3584
	ds_read_b32 v196, v9 offset:4096
	ds_read_b32 v197, v9 offset:4608
	ds_read_b32 v198, v9 offset:5120
	ds_read_b32 v199, v9 offset:5632
	ds_read_b32 v200, v9 offset:6144
	ds_read_b32 v201, v9 offset:6656
	ds_read_b32 v202, v9 offset:7168
	ds_read_b32 v203, v9 offset:7680
	s_waitcnt lgkmcnt(0)
	v_max_f32_e32 v170, v170, v170
	v_max_f32_e32 v171, v171, v171
	v_max_f32_e32 v172, v172, v172
	v_max_f32_e32 v173, v173, v173
	v_max_f32_e32 v174, v174, v174
	v_max_f32_e32 v175, v175, v175
	v_max_f32_e32 v176, v176, v176
	v_max_f32_e32 v177, v177, v177
	v_max_f32_e32 v196, v196, v196
	v_max_f32_e32 v197, v197, v197
	v_max_f32_e32 v198, v198, v198
	v_max_f32_e32 v199, v199, v199
	v_max_f32_e32 v200, v200, v200
	v_max_f32_e32 v201, v201, v201
	v_max_f32_e32 v202, v202, v202
	v_max_f32_e32 v203, v203, v203
	v_med3_f32 v170, v170, s20, v13
	v_med3_f32 v171, v171, s20, v13
	v_med3_f32 v172, v172, s20, v13
	v_med3_f32 v173, v173, s20, v13
	v_med3_f32 v174, v174, s20, v13
	v_med3_f32 v175, v175, s20, v13
	v_med3_f32 v176, v176, s20, v13
	v_med3_f32 v177, v177, s20, v13
	v_med3_f32 v196, v196, s20, v13
	v_med3_f32 v197, v197, s20, v13
	v_med3_f32 v198, v198, s20, v13
	v_med3_f32 v199, v199, s20, v13
	v_med3_f32 v200, v200, s20, v13
	v_med3_f32 v201, v201, s20, v13
	v_med3_f32 v202, v202, s20, v13
	v_med3_f32 v203, v203, s20, v13
	v_mov_b32_e32 v208, 0
	v_mov_b32_e32 v209, 0
	v_mov_b32_e32 v210, 0
	v_mov_b32_e32 v211, 0
	v_cvt_pk_fp8_f32 v208, v170, v171
	v_cvt_pk_fp8_f32 v209, v174, v175
	v_cvt_pk_fp8_f32 v210, v196, v197
	v_cvt_pk_fp8_f32 v211, v200, v201
	v_cvt_pk_fp8_f32 v208, v172, v173 op_sel:[0,0,1]
	v_cvt_pk_fp8_f32 v209, v176, v177 op_sel:[0,0,1]
	v_cvt_pk_fp8_f32 v210, v198, v199 op_sel:[0,0,1]
	v_cvt_pk_fp8_f32 v211, v202, v203 op_sel:[0,0,1]
	s_nop 0
	global_store_dwordx4 v12, v[208:211], s[14:15]
	s_waitcnt vmcnt(32)
	v_mul_f32_e32 v100, 0x43000000, v100
	v_mul_f32_e32 v101, 0x43000000, v101
	v_mul_f32_e32 v102, 0x43000000, v102
	v_mul_f32_e32 v103, 0x43000000, v103
	ds_write_b128 v4, v[100:103]
	v_mul_f32_e32 v104, 0x43000000, v104
	v_mul_f32_e32 v105, 0x43000000, v105
	v_mul_f32_e32 v106, 0x43000000, v106
	v_mul_f32_e32 v107, 0x43000000, v107
	ds_write_b128 v4, v[104:107] offset:1024
	v_mul_f32_e32 v108, 0x43000000, v108
	v_mul_f32_e32 v109, 0x43000000, v109
	v_mul_f32_e32 v110, 0x43000000, v110
	v_mul_f32_e32 v111, 0x43000000, v111
	ds_write_b128 v4, v[108:111] offset:2048
	v_mul_f32_e32 v112, 0x43000000, v112
	v_mul_f32_e32 v113, 0x43000000, v113
	v_mul_f32_e32 v114, 0x43000000, v114
	v_mul_f32_e32 v115, 0x43000000, v115
	ds_write_b128 v4, v[112:115] offset:3072
	v_mul_f32_e32 v116, 0x43000000, v116
	v_mul_f32_e32 v117, 0x43000000, v117
	v_mul_f32_e32 v118, 0x43000000, v118
	v_mul_f32_e32 v119, 0x43000000, v119
	ds_write_b128 v4, v[116:119] offset:4096
	v_mul_f32_e32 v120, 0x43000000, v120
	v_mul_f32_e32 v121, 0x43000000, v121
	v_mul_f32_e32 v122, 0x43000000, v122
	v_mul_f32_e32 v123, 0x43000000, v123
	ds_write_b128 v4, v[120:123] offset:5120
	v_mul_f32_e32 v124, 0x43000000, v124
	v_mul_f32_e32 v125, 0x43000000, v125
	v_mul_f32_e32 v126, 0x43000000, v126
	v_mul_f32_e32 v127, 0x43000000, v127
	ds_write_b128 v4, v[124:127] offset:6144
	v_mul_f32_e32 v128, 0x43000000, v128
	v_mul_f32_e32 v129, 0x43000000, v129
	v_mul_f32_e32 v130, 0x43000000, v130
	v_mul_f32_e32 v131, 0x43000000, v131
	ds_write_b128 v4, v[128:131] offset:7168
	s_waitcnt lgkmcnt(0)
	s_barrier
; #define GAS __attribute__((address_space(1)))
; #define LAS __attribute__((address_space(3)))
; #define LDS_WAIT() asm volatile("s_waitcnt lgkmcnt(0)" ::: "memory")
;     ...
;     for (int i = 0; i < 32; ++i) v[i] = sc >= 0 ? W[(size_t)(k0 + 2 * i + (lane >> 5)) * Nsrc + sc] : 0.f;
; #pragma unroll
;     for (int i = 0; i < 32; ++i) { const int k = k0 + 2 * i + (lane >> 5); float x = v[i] * wscale; if (KS) x *= (k < ksplit ? ksA[k] : ksB[k - ksplit]); scr[(2 * i + (lane >> 5)) * 33 + (lane & 31)] = x; }
;     LDS_WAIT(); asm volatile("" ::: "memory");
;     const int c = lane & 7;
; #pragma unroll
;     for (int j = 0; j < 4; ++j) { const int n = (lane >> 3) + 8 * j; const LAS float* s = scr + (8 * c) * 33 + n;
;         const unsigned long long o = (unsigned long long)pg8::pk4_fp8(s[0 * 33], s[1 * 33], s[2 * 33], s[3 * 33]) | ((unsigned long long)pg8::pk4_fp8(s[4 * 33], s[5 * 33], s[6 * 33], s[7 * 33]) << 32);
;         *(GAS unsigned long long*)(WT + (size_t)(n0 + n) * K + k0 + 8 * c) = o; }
; __global__ void __launch_bounds__(NWAVES * 64, 2) hybrid_fwd(Args args) {
;     ...
;             p0_transpose_item_f8<false>(args.in[16] + (size_t)l * FF * DM, FF, DM, DM / 32, (unsigned char*)(ws + WS_WDN + l * SZ_WDN), 128.f, args.in[16], args.in[16], 0, scr, r, lane);
	s_add_i32 s17, s16, 3264
	s_min_u32 s17, s17, 0xfff
	s_lshr_b32 s18, s17, 5
	s_add_i32 s18, s18, 0
	s_and_b32 s19, s17, 31
	s_lshl_b32 s18, s18, 21
	s_lshl_b32 s19, s19, 9
	s_add_u32 s18, s18, s19
	s_add_u32 s12, s2, s18
	s_addc_u32 s13, s3, 0
	global_load_dwordx4 v[100:103], v10, s[12:13]
	s_add_u32 s12, s12, 0x8000
	s_addc_u32 s13, s13, 0
	global_load_dwordx4 v[104:107], v10, s[12:13]
	s_add_u32 s12, s12, 0x8000
	s_addc_u32 s13, s13, 0
	global_load_dwordx4 v[108:111], v10, s[12:13]
	s_add_u32 s12, s12, 0x8000
	s_addc_u32 s13, s13, 0
	global_load_dwordx4 v[112:115], v10, s[12:13]
	s_add_u32 s12, s12, 0x8000
	s_addc_u32 s13, s13, 0
	global_load_dwordx4 v[116:119], v10, s[12:13]
	s_add_u32 s12, s12, 0x8000
	s_addc_u32 s13, s13, 0
	global_load_dwordx4 v[120:123], v10, s[12:13]
	s_add_u32 s12, s12, 0x8000
	s_addc_u32 s13, s13, 0
	global_load_dwordx4 v[124:127], v10, s[12:13]
	s_add_u32 s12, s12, 0x8000
	s_addc_u32 s13, s13, 0
	global_load_dwordx4 v[128:131], v10, s[12:13]
	s_add_i32 s17, s16, 2880
	s_min_u32 s17, s17, 0xfff
	s_lshr_b32 s18, s17, 5
	s_add_i32 s18, s18, 0
	s_and_b32 s19, s17, 31
	s_lshl_b32 s19, s19, 21
	s_lshl_b32 s18, s18, 7
	s_add_u32 s18, s18, s19
	s_add_u32 s14, s4, s18
	s_addc_u32 s15, s5, 0
	ds_read_b32 v170, v6
	ds_read_b32 v171, v6 offset:512
	ds_read_b32 v172, v6 offset:1024
	ds_read_b32 v173, v6 offset:1536
	ds_read_b32 v174, v6 offset:2048
	ds_read_b32 v175, v6 offset:2560
	ds_read_b32 v176, v6 offset:3072
	ds_read_b32 v177, v6 offset:3584
	ds_read_b32 v196, v6 offset:4096
	ds_read_b32 v197, v6 offset:4608
	ds_read_b32 v198, v6 offset:5120
	ds_read_b32 v199, v6 offset:5632
	ds_read_b32 v200, v6 offset:6144
	ds_read_b32 v201, v6 offset:6656
	ds_read_b32 v202, v6 offset:7168
	ds_read_b32 v203, v6 offset:7680
	s_waitcnt lgkmcnt(0)
	v_max_f32_e32 v170, v170, v170
	v_max_f32_e32 v171, v171, v171
	v_max_f32_e32 v172, v172, v172
	v_max_f32_e32 v173, v173, v173
	v_max_f32_e32 v174, v174, v174
	v_max_f32_e32 v175, v175, v175
	v_max_f32_e32 v176, v176, v176
	v_max_f32_e32 v177, v177, v177
	v_max_f32_e32 v196, v196, v196
	v_max_f32_e32 v197, v197, v197
	v_max_f32_e32 v198, v198, v198
	v_max_f32_e32 v199, v199, v199
	v_max_f32_e32 v200, v200, v200
	v_max_f32_e32 v201, v201, v201
	v_max_f32_e32 v202, v202, v202
	v_max_f32_e32 v203, v203, v203
	v_med3_f32 v170, v170, s20, v13
	v_med3_f32 v171, v171, s20, v13
	v_med3_f32 v172, v172, s20, v13
	v_med3_f32 v173, v173, s20, v13
	v_med3_f32 v174, v174, s20, v13
	v_med3_f32 v175, v175, s20, v13
	v_med3_f32 v176, v176, s20, v13
	v_med3_f32 v177, v177, s20, v13
	v_med3_f32 v196, v196, s20, v13
	v_med3_f32 v197, v197, s20, v13
	v_med3_f32 v198, v198, s20, v13
	v_med3_f32 v199, v199, s20, v13
	v_med3_f32 v200, v200, s20, v13
	v_med3_f32 v201, v201, s20, v13
	v_med3_f32 v202, v202, s20, v13
	v_med3_f32 v203, v203, s20, v13
	v_mov_b32_e32 v208, 0
	v_mov_b32_e32 v209, 0
	v_mov_b32_e32 v210, 0
	v_mov_b32_e32 v211, 0
	v_cvt_pk_fp8_f32 v208, v170, v171
	v_cvt_pk_fp8_f32 v209, v174, v175
	v_cvt_pk_fp8_f32 v210, v196, v197
	v_cvt_pk_fp8_f32 v211, v200, v201
	v_cvt_pk_fp8_f32 v208, v172, v173 op_sel:[0,0,1]
	v_cvt_pk_fp8_f32 v209, v176, v177 op_sel:[0,0,1]
	v_cvt_pk_fp8_f32 v210, v198, v199 op_sel:[0,0,1]
	v_cvt_pk_fp8_f32 v211, v202, v203 op_sel:[0,0,1]
	s_nop 0
	global_store_dwordx4 v11, v[208:211], s[14:15]
	ds_read_b32 v170, v8
	ds_read_b32 v171, v8 offset:512
	ds_read_b32 v172, v8 offset:1024
	ds_read_b32 v173, v8 offset:1536
	ds_read_b32 v174, v8 offset:2048
	ds_read_b32 v175, v8 offset:2560
	ds_read_b32 v176, v8 offset:3072
	ds_read_b32 v177, v8 offset:3584
	ds_read_b32 v196, v8 offset:4096
	ds_read_b32 v197, v8 offset:4608
	ds_read_b32 v198, v8 offset:5120
	ds_read_b32 v199, v8 offset:5632
	ds_read_b32 v200, v8 offset:6144
	ds_read_b32 v201, v8 offset:6656
	ds_read_b32 v202, v8 offset:7168
	ds_read_b32 v203, v8 offset:7680
	s_waitcnt lgkmcnt(0)
	v_max_f32_e32 v170, v170, v170
	v_max_f32_e32 v171, v171, v171
	v_max_f32_e32 v172, v172, v172
	v_max_f32_e32 v173, v173, v173
	v_max_f32_e32 v174, v174, v174
	v_max_f32_e32 v175, v175, v175
	v_max_f32_e32 v176, v176, v176
	v_max_f32_e32 v177, v177, v177
	v_max_f32_e32 v196, v196, v196
	v_max_f32_e32 v197, v197, v197
	v_max_f32_e32 v198, v198, v198
	v_max_f32_e32 v199, v199, v199
	v_max_f32_e32 v200, v200, v200
	v_max_f32_e32 v201, v201, v201
	v_max_f32_e32 v202, v202, v202
	v_max_f32_e32 v203, v203, v203
	v_med3_f32 v170, v170, s20, v13
	v_med3_f32 v171, v171, s20, v13
	v_med3_f32 v172, v172, s20, v13
	v_med3_f32 v173, v173, s20, v13
	v_med3_f32 v174, v174, s20, v13
	v_med3_f32 v175, v175, s20, v13
	v_med3_f32 v176, v176, s20, v13
	v_med3_f32 v177, v177, s20, v13
	v_med3_f32 v196, v196, s20, v13
	v_med3_f32 v197, v197, s20, v13
	v_med3_f32 v198, v198, s20, v13
	v_med3_f32 v199, v199, s20, v13
	v_med3_f32 v200, v200, s20, v13
	v_med3_f32 v201, v201, s20, v13
	v_med3_f32 v202, v202, s20, v13
	v_med3_f32 v203, v203, s20, v13
	v_mov_b32_e32 v208, 0
	v_mov_b32_e32 v209, 0
	v_mov_b32_e32 v210, 0
	v_mov_b32_e32 v211, 0
	v_cvt_pk_fp8_f32 v208, v170, v171
	v_cvt_pk_fp8_f32 v209, v174, v175
	v_cvt_pk_fp8_f32 v210, v196, v197
	v_cvt_pk_fp8_f32 v211, v200, v201
	v_cvt_pk_fp8_f32 v208, v172, v173 op_sel:[0,0,1]
	v_cvt_pk_fp8_f32 v209, v176, v177 op_sel:[0,0,1]
	v_cvt_pk_fp8_f32 v210, v198, v199 op_sel:[0,0,1]
	v_cvt_pk_fp8_f32 v211, v202, v203 op_sel:[0,0,1]
	s_nop 0
	global_store_dwordx4 v12, v[208:211], s[14:15]
	s_waitcnt vmcnt(32)
	v_mul_f32_e32 v132, 0x43000000, v132
	v_mul_f32_e32 v133, 0x43000000, v133
	v_mul_f32_e32 v134, 0x43000000, v134
	v_mul_f32_e32 v135, 0x43000000, v135
	ds_write_b128 v5, v[132:135]
	v_mul_f32_e32 v136, 0x43000000, v136
	v_mul_f32_e32 v137, 0x43000000, v137
	v_mul_f32_e32 v138, 0x43000000, v138
	v_mul_f32_e32 v139, 0x43000000, v139
	ds_write_b128 v5, v[136:139] offset:1024
	v_mul_f32_e32 v140, 0x43000000, v140
	v_mul_f32_e32 v141, 0x43000000, v141
	v_mul_f32_e32 v142, 0x43000000, v142
	v_mul_f32_e32 v143, 0x43000000, v143
	ds_write_b128 v5, v[140:143] offset:2048
	v_mul_f32_e32 v144, 0x43000000, v144
	v_mul_f32_e32 v145, 0x43000000, v145
	v_mul_f32_e32 v146, 0x43000000, v146
	v_mul_f32_e32 v147, 0x43000000, v147
	ds_write_b128 v5, v[144:147] offset:3072
	v_mul_f32_e32 v148, 0x43000000, v148
	v_mul_f32_e32 v149, 0x43000000, v149
	v_mul_f32_e32 v150, 0x43000000, v150
	v_mul_f32_e32 v151, 0x43000000, v151
	ds_write_b128 v5, v[148:151] offset:4096
	v_mul_f32_e32 v152, 0x43000000, v152
	v_mul_f32_e32 v153, 0x43000000, v153
	v_mul_f32_e32 v154, 0x43000000, v154
	v_mul_f32_e32 v155, 0x43000000, v155
	ds_write_b128 v5, v[152:155] offset:5120
	v_mul_f32_e32 v156, 0x43000000, v156
	v_mul_f32_e32 v157, 0x43000000, v157
	v_mul_f32_e32 v158, 0x43000000, v158
	v_mul_f32_e32 v159, 0x43000000, v159
	ds_write_b128 v5, v[156:159] offset:6144
	v_mul_f32_e32 v160, 0x43000000, v160
	v_mul_f32_e32 v161, 0x43000000, v161
	v_mul_f32_e32 v162, 0x43000000, v162
	v_mul_f32_e32 v163, 0x43000000, v163
	ds_write_b128 v5, v[160:163] offset:7168
	s_waitcnt lgkmcnt(0)
	s_barrier
; #define GAS __attribute__((address_space(1)))
; #define LAS __attribute__((address_space(3)))
; #define LDS_WAIT() asm volatile("s_waitcnt lgkmcnt(0)" ::: "memory")
;     ...
;     for (int i = 0; i < 32; ++i) v[i] = sc >= 0 ? W[(size_t)(k0 + 2 * i + (lane >> 5)) * Nsrc + sc] : 0.f;
; #pragma unroll
;     for (int i = 0; i < 32; ++i) { const int k = k0 + 2 * i + (lane >> 5); float x = v[i] * wscale; if (KS) x *= (k < ksplit ? ksA[k] : ksB[k - ksplit]); scr[(2 * i + (lane >> 5)) * 33 + (lane & 31)] = x; }
;     LDS_WAIT(); asm volatile("" ::: "memory");
;     const int c = lane & 7;
; #pragma unroll
;     for (int j = 0; j < 4; ++j) { const int n = (lane >> 3) + 8 * j; const LAS float* s = scr + (8 * c) * 33 + n;
;         const unsigned long long o = (unsigned long long)pg8::pk4_fp8(s[0 * 33], s[1 * 33], s[2 * 33], s[3 * 33]) | ((unsigned long long)pg8::pk4_fp8(s[4 * 33], s[5 * 33], s[6 * 33], s[7 * 33]) << 32);
;         *(GAS unsigned long long*)(WT + (size_t)(n0 + n) * K + k0 + 8 * c) = o; }
; __global__ void __launch_bounds__(NWAVES * 64, 2) hybrid_fwd(Args args) {
;     ...
;             p0_transpose_item_f8<false>(args.in[16] + (size_t)l * FF * DM, FF, DM, DM / 32, (unsigned char*)(ws + WS_WDN + l * SZ_WDN), 128.f, args.in[16], args.in[16], 0, scr, r, lane);
	s_add_i32 s17, s16, 3360
	s_min_u32 s17, s17, 0xfff
	s_lshr_b32 s18, s17, 5
	s_add_i32 s18, s18, 0
	s_and_b32 s19, s17, 31
	s_lshl_b32 s18, s18, 21
	s_lshl_b32 s19, s19, 9
	s_add_u32 s18, s18, s19
	s_add_u32 s12, s2, s18
	s_addc_u32 s13, s3, 0
	global_load_dwordx4 v[132:135], v10, s[12:13]
	s_add_u32 s12, s12, 0x8000
	s_addc_u32 s13, s13, 0
	global_load_dwordx4 v[136:139], v10, s[12:13]
	s_add_u32 s12, s12, 0x8000
	s_addc_u32 s13, s13, 0
	global_load_dwordx4 v[140:143], v10, s[12:13]
	s_add_u32 s12, s12, 0x8000
	s_addc_u32 s13, s13, 0
	global_load_dwordx4 v[144:147], v10, s[12:13]
	s_add_u32 s12, s12, 0x8000
	s_addc_u32 s13, s13, 0
	global_load_dwordx4 v[148:151], v10, s[12:13]
	s_add_u32 s12, s12, 0x8000
	s_addc_u32 s13, s13, 0
	global_load_dwordx4 v[152:155], v10, s[12:13]
	s_add_u32 s12, s12, 0x8000
	s_addc_u32 s13, s13, 0
	global_load_dwordx4 v[156:159], v10, s[12:13]
	s_add_u32 s12, s12, 0x8000
	s_addc_u32 s13, s13, 0
	global_load_dwordx4 v[160:163], v10, s[12:13]
	s_add_i32 s17, s16, 2976
	s_min_u32 s17, s17, 0xfff
	s_lshr_b32 s18, s17, 5
	s_add_i32 s18, s18, 0
	s_and_b32 s19, s17, 31
	s_lshl_b32 s19, s19, 21
	s_lshl_b32 s18, s18, 7
	s_add_u32 s18, s18, s19
	s_add_u32 s14, s4, s18
	s_addc_u32 s15, s5, 0
	ds_read_b32 v170, v7
	ds_read_b32 v171, v7 offset:512
	ds_read_b32 v172, v7 offset:1024
	ds_read_b32 v173, v7 offset:1536
	ds_read_b32 v174, v7 offset:2048
	ds_read_b32 v175, v7 offset:2560
	ds_read_b32 v176, v7 offset:3072
	ds_read_b32 v177, v7 offset:3584
	ds_read_b32 v196, v7 offset:4096
	ds_read_b32 v197, v7 offset:4608
	ds_read_b32 v198, v7 offset:5120
	ds_read_b32 v199, v7 offset:5632
	ds_read_b32 v200, v7 offset:6144
	ds_read_b32 v201, v7 offset:6656
	ds_read_b32 v202, v7 offset:7168
	ds_read_b32 v203, v7 offset:7680
	s_waitcnt lgkmcnt(0)
	v_max_f32_e32 v170, v170, v170
	v_max_f32_e32 v171, v171, v171
	v_max_f32_e32 v172, v172, v172
	v_max_f32_e32 v173, v173, v173
	v_max_f32_e32 v174, v174, v174
	v_max_f32_e32 v175, v175, v175
	v_max_f32_e32 v176, v176, v176
	v_max_f32_e32 v177, v177, v177
	v_max_f32_e32 v196, v196, v196
	v_max_f32_e32 v197, v197, v197
	v_max_f32_e32 v198, v198, v198
	v_max_f32_e32 v199, v199, v199
	v_max_f32_e32 v200, v200, v200
	v_max_f32_e32 v201, v201, v201
	v_max_f32_e32 v202, v202, v202
	v_max_f32_e32 v203, v203, v203
	v_med3_f32 v170, v170, s20, v13
	v_med3_f32 v171, v171, s20, v13
	v_med3_f32 v172, v172, s20, v13
	v_med3_f32 v173, v173, s20, v13
	v_med3_f32 v174, v174, s20, v13
	v_med3_f32 v175, v175, s20, v13
	v_med3_f32 v176, v176, s20, v13
	v_med3_f32 v177, v177, s20, v13
	v_med3_f32 v196, v196, s20, v13
	v_med3_f32 v197, v197, s20, v13
	v_med3_f32 v198, v198, s20, v13
	v_med3_f32 v199, v199, s20, v13
	v_med3_f32 v200, v200, s20, v13
	v_med3_f32 v201, v201, s20, v13
	v_med3_f32 v202, v202, s20, v13
	v_med3_f32 v203, v203, s20, v13
	v_mov_b32_e32 v208, 0
	v_mov_b32_e32 v209, 0
	v_mov_b32_e32 v210, 0
	v_mov_b32_e32 v211, 0
	v_cvt_pk_fp8_f32 v208, v170, v171
	v_cvt_pk_fp8_f32 v209, v174, v175
	v_cvt_pk_fp8_f32 v210, v196, v197
	v_cvt_pk_fp8_f32 v211, v200, v201
	v_cvt_pk_fp8_f32 v208, v172, v173 op_sel:[0,0,1]
	v_cvt_pk_fp8_f32 v209, v176, v177 op_sel:[0,0,1]
	v_cvt_pk_fp8_f32 v210, v198, v199 op_sel:[0,0,1]
	v_cvt_pk_fp8_f32 v211, v202, v203 op_sel:[0,0,1]
	s_nop 0
	global_store_dwordx4 v11, v[208:211], s[14:15]
	ds_read_b32 v170, v9
	ds_read_b32 v171, v9 offset:512
	ds_read_b32 v172, v9 offset:1024
	ds_read_b32 v173, v9 offset:1536
	ds_read_b32 v174, v9 offset:2048
	ds_read_b32 v175, v9 offset:2560
	ds_read_b32 v176, v9 offset:3072
	ds_read_b32 v177, v9 offset:3584
	ds_read_b32 v196, v9 offset:4096
	ds_read_b32 v197, v9 offset:4608
	ds_read_b32 v198, v9 offset:5120
	ds_read_b32 v199, v9 offset:5632
	ds_read_b32 v200, v9 offset:6144
	ds_read_b32 v201, v9 offset:6656
	ds_read_b32 v202, v9 offset:7168
	ds_read_b32 v203, v9 offset:7680
	s_waitcnt lgkmcnt(0)
	v_max_f32_e32 v170, v170, v170
	v_max_f32_e32 v171, v171, v171
	v_max_f32_e32 v172, v172, v172
	v_max_f32_e32 v173, v173, v173
	v_max_f32_e32 v174, v174, v174
	v_max_f32_e32 v175, v175, v175
	v_max_f32_e32 v176, v176, v176
	v_max_f32_e32 v177, v177, v177
	v_max_f32_e32 v196, v196, v196
	v_max_f32_e32 v197, v197, v197
	v_max_f32_e32 v198, v198, v198
	v_max_f32_e32 v199, v199, v199
	v_max_f32_e32 v200, v200, v200
	v_max_f32_e32 v201, v201, v201
	v_max_f32_e32 v202, v202, v202
	v_max_f32_e32 v203, v203, v203
	v_med3_f32 v170, v170, s20, v13
	v_med3_f32 v171, v171, s20, v13
	v_med3_f32 v172, v172, s20, v13
	v_med3_f32 v173, v173, s20, v13
	v_med3_f32 v174, v174, s20, v13
	v_med3_f32 v175, v175, s20, v13
	v_med3_f32 v176, v176, s20, v13
	v_med3_f32 v177, v177, s20, v13
	v_med3_f32 v196, v196, s20, v13
	v_med3_f32 v197, v197, s20, v13
	v_med3_f32 v198, v198, s20, v13
	v_med3_f32 v199, v199, s20, v13
	v_med3_f32 v200, v200, s20, v13
	v_med3_f32 v201, v201, s20, v13
	v_med3_f32 v202, v202, s20, v13
	v_med3_f32 v203, v203, s20, v13
	v_mov_b32_e32 v208, 0
	v_mov_b32_e32 v209, 0
	v_mov_b32_e32 v210, 0
	v_mov_b32_e32 v211, 0
	v_cvt_pk_fp8_f32 v208, v170, v171
	v_cvt_pk_fp8_f32 v209, v174, v175
	v_cvt_pk_fp8_f32 v210, v196, v197
	v_cvt_pk_fp8_f32 v211, v200, v201
	v_cvt_pk_fp8_f32 v208, v172, v173 op_sel:[0,0,1]
	v_cvt_pk_fp8_f32 v209, v176, v177 op_sel:[0,0,1]
	v_cvt_pk_fp8_f32 v210, v198, v199 op_sel:[0,0,1]
	v_cvt_pk_fp8_f32 v211, v202, v203 op_sel:[0,0,1]
	s_nop 0
	global_store_dwordx4 v12, v[208:211], s[14:15]
	s_waitcnt vmcnt(32)
	v_mul_f32_e32 v36, 0x43000000, v36
	v_mul_f32_e32 v37, 0x43000000, v37
	v_mul_f32_e32 v38, 0x43000000, v38
	v_mul_f32_e32 v39, 0x43000000, v39
	ds_write_b128 v4, v[36:39]
	v_mul_f32_e32 v40, 0x43000000, v40
	v_mul_f32_e32 v41, 0x43000000, v41
	v_mul_f32_e32 v42, 0x43000000, v42
	v_mul_f32_e32 v43, 0x43000000, v43
	ds_write_b128 v4, v[40:43] offset:1024
	v_mul_f32_e32 v44, 0x43000000, v44
	v_mul_f32_e32 v45, 0x43000000, v45
	v_mul_f32_e32 v46, 0x43000000, v46
	v_mul_f32_e32 v47, 0x43000000, v47
	ds_write_b128 v4, v[44:47] offset:2048
	v_mul_f32_e32 v48, 0x43000000, v48
	v_mul_f32_e32 v49, 0x43000000, v49
	v_mul_f32_e32 v50, 0x43000000, v50
	v_mul_f32_e32 v51, 0x43000000, v51
	ds_write_b128 v4, v[48:51] offset:3072
	v_mul_f32_e32 v52, 0x43000000, v52
	v_mul_f32_e32 v53, 0x43000000, v53
	v_mul_f32_e32 v54, 0x43000000, v54
	v_mul_f32_e32 v55, 0x43000000, v55
	ds_write_b128 v4, v[52:55] offset:4096
	v_mul_f32_e32 v56, 0x43000000, v56
	v_mul_f32_e32 v57, 0x43000000, v57
	v_mul_f32_e32 v58, 0x43000000, v58
	v_mul_f32_e32 v59, 0x43000000, v59
	ds_write_b128 v4, v[56:59] offset:5120
	v_mul_f32_e32 v60, 0x43000000, v60
	v_mul_f32_e32 v61, 0x43000000, v61
	v_mul_f32_e32 v62, 0x43000000, v62
	v_mul_f32_e32 v63, 0x43000000, v63
	ds_write_b128 v4, v[60:63] offset:6144
	v_mul_f32_e32 v64, 0x43000000, v64
	v_mul_f32_e32 v65, 0x43000000, v65
	v_mul_f32_e32 v66, 0x43000000, v66
	v_mul_f32_e32 v67, 0x43000000, v67
	ds_write_b128 v4, v[64:67] offset:7168
	s_waitcnt lgkmcnt(0)
	s_barrier
; #define GAS __attribute__((address_space(1)))
; #define LAS __attribute__((address_space(3)))
; #define LDS_WAIT() asm volatile("s_waitcnt lgkmcnt(0)" ::: "memory")
;     ...
;     for (int i = 0; i < 32; ++i) v[i] = sc >= 0 ? W[(size_t)(k0 + 2 * i + (lane >> 5)) * Nsrc + sc] : 0.f;
; #pragma unroll
;     for (int i = 0; i < 32; ++i) { const int k = k0 + 2 * i + (lane >> 5); float x = v[i] * wscale; if (KS) x *= (k < ksplit ? ksA[k] : ksB[k - ksplit]); scr[(2 * i + (lane >> 5)) * 33 + (lane & 31)] = x; }
;     LDS_WAIT(); asm volatile("" ::: "memory");
;     const int c = lane & 7;
; #pragma unroll
;     for (int j = 0; j < 4; ++j) { const int n = (lane >> 3) + 8 * j; const LAS float* s = scr + (8 * c) * 33 + n;
;         const unsigned long long o = (unsigned long long)pg8::pk4_fp8(s[0 * 33], s[1 * 33], s[2 * 33], s[3 * 33]) | ((unsigned long long)pg8::pk4_fp8(s[4 * 33], s[5 * 33], s[6 * 33], s[7 * 33]) << 32);
;         *(GAS unsigned long long*)(WT + (size_t)(n0 + n) * K + k0 + 8 * c) = o; }
; __global__ void __launch_bounds__(NWAVES * 64, 2) hybrid_fwd(Args args) {
;     ...
;             p0_transpose_item_f8<false>(args.in[16] + (size_t)l * FF * DM, FF, DM, DM / 32, (unsigned char*)(ws + WS_WDN + l * SZ_WDN), 128.f, args.in[16], args.in[16], 0, scr, r, lane);
	s_add_i32 s17, s16, 3456
	s_min_u32 s17, s17, 0xfff
	s_lshr_b32 s18, s17, 5
	s_add_i32 s18, s18, 0
	s_and_b32 s19, s17, 31
	s_lshl_b32 s18, s18, 21
	s_lshl_b32 s19, s19, 9
	s_add_u32 s18, s18, s19
	s_add_u32 s12, s2, s18
	s_addc_u32 s13, s3, 0
	global_load_dwordx4 v[36:39], v10, s[12:13]
	s_add_u32 s12, s12, 0x8000
	s_addc_u32 s13, s13, 0
	global_load_dwordx4 v[40:43], v10, s[12:13]
	s_add_u32 s12, s12, 0x8000
	s_addc_u32 s13, s13, 0
	global_load_dwordx4 v[44:47], v10, s[12:13]
	s_add_u32 s12, s12, 0x8000
	s_addc_u32 s13, s13, 0
	global_load_dwordx4 v[48:51], v10, s[12:13]
	s_add_u32 s12, s12, 0x8000
	s_addc_u32 s13, s13, 0
	global_load_dwordx4 v[52:55], v10, s[12:13]
	s_add_u32 s12, s12, 0x8000
	s_addc_u32 s13, s13, 0
	global_load_dwordx4 v[56:59], v10, s[12:13]
	s_add_u32 s12, s12, 0x8000
	s_addc_u32 s13, s13, 0
	global_load_dwordx4 v[60:63], v10, s[12:13]
	s_add_u32 s12, s12, 0x8000
	s_addc_u32 s13, s13, 0
	global_load_dwordx4 v[64:67], v10, s[12:13]
	s_add_i32 s17, s16, 3072
	s_min_u32 s17, s17, 0xfff
	s_lshr_b32 s18, s17, 5
	s_add_i32 s18, s18, 0
	s_and_b32 s19, s17, 31
	s_lshl_b32 s19, s19, 21
	s_lshl_b32 s18, s18, 7
	s_add_u32 s18, s18, s19
	s_add_u32 s14, s4, s18
	s_addc_u32 s15, s5, 0
	ds_read_b32 v170, v6
	ds_read_b32 v171, v6 offset:512
	ds_read_b32 v172, v6 offset:1024
	ds_read_b32 v173, v6 offset:1536
	ds_read_b32 v174, v6 offset:2048
	ds_read_b32 v175, v6 offset:2560
	ds_read_b32 v176, v6 offset:3072
	ds_read_b32 v177, v6 offset:3584
	ds_read_b32 v196, v6 offset:4096
	ds_read_b32 v197, v6 offset:4608
	ds_read_b32 v198, v6 offset:5120
	ds_read_b32 v199, v6 offset:5632
	ds_read_b32 v200, v6 offset:6144
	ds_read_b32 v201, v6 offset:6656
	ds_read_b32 v202, v6 offset:7168
	ds_read_b32 v203, v6 offset:7680
	s_waitcnt lgkmcnt(0)
	v_max_f32_e32 v170, v170, v170
	v_max_f32_e32 v171, v171, v171
	v_max_f32_e32 v172, v172, v172
	v_max_f32_e32 v173, v173, v173
	v_max_f32_e32 v174, v174, v174
	v_max_f32_e32 v175, v175, v175
	v_max_f32_e32 v176, v176, v176
	v_max_f32_e32 v177, v177, v177
	v_max_f32_e32 v196, v196, v196
	v_max_f32_e32 v197, v197, v197
	v_max_f32_e32 v198, v198, v198
	v_max_f32_e32 v199, v199, v199
	v_max_f32_e32 v200, v200, v200
	v_max_f32_e32 v201, v201, v201
	v_max_f32_e32 v202, v202, v202
	v_max_f32_e32 v203, v203, v203
	v_med3_f32 v170, v170, s20, v13
	v_med3_f32 v171, v171, s20, v13
	v_med3_f32 v172, v172, s20, v13
	v_med3_f32 v173, v173, s20, v13
	v_med3_f32 v174, v174, s20, v13
	v_med3_f32 v175, v175, s20, v13
	v_med3_f32 v176, v176, s20, v13
	v_med3_f32 v177, v177, s20, v13
	v_med3_f32 v196, v196, s20, v13
	v_med3_f32 v197, v197, s20, v13
	v_med3_f32 v198, v198, s20, v13
	v_med3_f32 v199, v199, s20, v13
	v_med3_f32 v200, v200, s20, v13
	v_med3_f32 v201, v201, s20, v13
	v_med3_f32 v202, v202, s20, v13
	v_med3_f32 v203, v203, s20, v13
	v_mov_b32_e32 v208, 0
	v_mov_b32_e32 v209, 0
	v_mov_b32_e32 v210, 0
	v_mov_b32_e32 v211, 0
	v_cvt_pk_fp8_f32 v208, v170, v171
	v_cvt_pk_fp8_f32 v209, v174, v175
	v_cvt_pk_fp8_f32 v210, v196, v197
	v_cvt_pk_fp8_f32 v211, v200, v201
	v_cvt_pk_fp8_f32 v208, v172, v173 op_sel:[0,0,1]
	v_cvt_pk_fp8_f32 v209, v176, v177 op_sel:[0,0,1]
	v_cvt_pk_fp8_f32 v210, v198, v199 op_sel:[0,0,1]
	v_cvt_pk_fp8_f32 v211, v202, v203 op_sel:[0,0,1]
	s_nop 0
	global_store_dwordx4 v11, v[208:211], s[14:15]
	ds_read_b32 v170, v8
	ds_read_b32 v171, v8 offset:512
	ds_read_b32 v172, v8 offset:1024
	ds_read_b32 v173, v8 offset:1536
	ds_read_b32 v174, v8 offset:2048
	ds_read_b32 v175, v8 offset:2560
	ds_read_b32 v176, v8 offset:3072
	ds_read_b32 v177, v8 offset:3584
	ds_read_b32 v196, v8 offset:4096
	ds_read_b32 v197, v8 offset:4608
	ds_read_b32 v198, v8 offset:5120
	ds_read_b32 v199, v8 offset:5632
	ds_read_b32 v200, v8 offset:6144
	ds_read_b32 v201, v8 offset:6656
	ds_read_b32 v202, v8 offset:7168
	ds_read_b32 v203, v8 offset:7680
	s_waitcnt lgkmcnt(0)
	v_max_f32_e32 v170, v170, v170
	v_max_f32_e32 v171, v171, v171
	v_max_f32_e32 v172, v172, v172
	v_max_f32_e32 v173, v173, v173
	v_max_f32_e32 v174, v174, v174
	v_max_f32_e32 v175, v175, v175
	v_max_f32_e32 v176, v176, v176
	v_max_f32_e32 v177, v177, v177
	v_max_f32_e32 v196, v196, v196
	v_max_f32_e32 v197, v197, v197
	v_max_f32_e32 v198, v198, v198
	v_max_f32_e32 v199, v199, v199
	v_max_f32_e32 v200, v200, v200
	v_max_f32_e32 v201, v201, v201
	v_max_f32_e32 v202, v202, v202
	v_max_f32_e32 v203, v203, v203
	v_med3_f32 v170, v170, s20, v13
	v_med3_f32 v171, v171, s20, v13
	v_med3_f32 v172, v172, s20, v13
	v_med3_f32 v173, v173, s20, v13
	v_med3_f32 v174, v174, s20, v13
	v_med3_f32 v175, v175, s20, v13
	v_med3_f32 v176, v176, s20, v13
	v_med3_f32 v177, v177, s20, v13
	v_med3_f32 v196, v196, s20, v13
	v_med3_f32 v197, v197, s20, v13
	v_med3_f32 v198, v198, s20, v13
	v_med3_f32 v199, v199, s20, v13
	v_med3_f32 v200, v200, s20, v13
	v_med3_f32 v201, v201, s20, v13
	v_med3_f32 v202, v202, s20, v13
	v_med3_f32 v203, v203, s20, v13
	v_mov_b32_e32 v208, 0
	v_mov_b32_e32 v209, 0
	v_mov_b32_e32 v210, 0
	v_mov_b32_e32 v211, 0
	v_cvt_pk_fp8_f32 v208, v170, v171
	v_cvt_pk_fp8_f32 v209, v174, v175
	v_cvt_pk_fp8_f32 v210, v196, v197
	v_cvt_pk_fp8_f32 v211, v200, v201
	v_cvt_pk_fp8_f32 v208, v172, v173 op_sel:[0,0,1]
	v_cvt_pk_fp8_f32 v209, v176, v177 op_sel:[0,0,1]
	v_cvt_pk_fp8_f32 v210, v198, v199 op_sel:[0,0,1]
	v_cvt_pk_fp8_f32 v211, v202, v203 op_sel:[0,0,1]
	s_nop 0
	global_store_dwordx4 v12, v[208:211], s[14:15]
	s_waitcnt vmcnt(32)
	v_mul_f32_e32 v68, 0x43000000, v68
	v_mul_f32_e32 v69, 0x43000000, v69
	v_mul_f32_e32 v70, 0x43000000, v70
	v_mul_f32_e32 v71, 0x43000000, v71
	ds_write_b128 v5, v[68:71]
	v_mul_f32_e32 v72, 0x43000000, v72
	v_mul_f32_e32 v73, 0x43000000, v73
	v_mul_f32_e32 v74, 0x43000000, v74
	v_mul_f32_e32 v75, 0x43000000, v75
	ds_write_b128 v5, v[72:75] offset:1024
	v_mul_f32_e32 v76, 0x43000000, v76
	v_mul_f32_e32 v77, 0x43000000, v77
	v_mul_f32_e32 v78, 0x43000000, v78
	v_mul_f32_e32 v79, 0x43000000, v79
	ds_write_b128 v5, v[76:79] offset:2048
	v_mul_f32_e32 v80, 0x43000000, v80
	v_mul_f32_e32 v81, 0x43000000, v81
	v_mul_f32_e32 v82, 0x43000000, v82
	v_mul_f32_e32 v83, 0x43000000, v83
	ds_write_b128 v5, v[80:83] offset:3072
	v_mul_f32_e32 v84, 0x43000000, v84
	v_mul_f32_e32 v85, 0x43000000, v85
	v_mul_f32_e32 v86, 0x43000000, v86
	v_mul_f32_e32 v87, 0x43000000, v87
	ds_write_b128 v5, v[84:87] offset:4096
	v_mul_f32_e32 v88, 0x43000000, v88
	v_mul_f32_e32 v89, 0x43000000, v89
	v_mul_f32_e32 v90, 0x43000000, v90
	v_mul_f32_e32 v91, 0x43000000, v91
	ds_write_b128 v5, v[88:91] offset:5120
	v_mul_f32_e32 v92, 0x43000000, v92
	v_mul_f32_e32 v93, 0x43000000, v93
	v_mul_f32_e32 v94, 0x43000000, v94
	v_mul_f32_e32 v95, 0x43000000, v95
	ds_write_b128 v5, v[92:95] offset:6144
	v_mul_f32_e32 v96, 0x43000000, v96
	v_mul_f32_e32 v97, 0x43000000, v97
	v_mul_f32_e32 v98, 0x43000000, v98
	v_mul_f32_e32 v99, 0x43000000, v99
	ds_write_b128 v5, v[96:99] offset:7168
	s_waitcnt lgkmcnt(0)
	s_barrier
; #define GAS __attribute__((address_space(1)))
; #define LAS __attribute__((address_space(3)))
; #define LDS_WAIT() asm volatile("s_waitcnt lgkmcnt(0)" ::: "memory")
;     ...
;     for (int i = 0; i < 32; ++i) v[i] = sc >= 0 ? W[(size_t)(k0 + 2 * i + (lane >> 5)) * Nsrc + sc] : 0.f;
; #pragma unroll
;     for (int i = 0; i < 32; ++i) { const int k = k0 + 2 * i + (lane >> 5); float x = v[i] * wscale; if (KS) x *= (k < ksplit ? ksA[k] : ksB[k - ksplit]); scr[(2 * i + (lane >> 5)) * 33 + (lane & 31)] = x; }
;     LDS_WAIT(); asm volatile("" ::: "memory");
;     const int c = lane & 7;
; #pragma unroll
;     for (int j = 0; j < 4; ++j) { const int n = (lane >> 3) + 8 * j; const LAS float* s = scr + (8 * c) * 33 + n;
;         const unsigned long long o = (unsigned long long)pg8::pk4_fp8(s[0 * 33], s[1 * 33], s[2 * 33], s[3 * 33]) | ((unsigned long long)pg8::pk4_fp8(s[4 * 33], s[5 * 33], s[6 * 33], s[7 * 33]) << 32);
;         *(GAS unsigned long long*)(WT + (size_t)(n0 + n) * K + k0 + 8 * c) = o; }
; __global__ void __launch_bounds__(NWAVES * 64, 2) hybrid_fwd(Args args) {
;     ...
;             p0_transpose_item_f8<false>(args.in[16] + (size_t)l * FF * DM, FF, DM, DM / 32, (unsigned char*)(ws + WS_WDN + l * SZ_WDN), 128.f, args.in[16], args.in[16], 0, scr, r, lane);
	s_add_i32 s17, s16, 3552
	s_min_u32 s17, s17, 0xfff
	s_lshr_b32 s18, s17, 5
	s_add_i32 s18, s18, 0
	s_and_b32 s19, s17, 31
	s_lshl_b32 s18, s18, 21
	s_lshl_b32 s19, s19, 9
	s_add_u32 s18, s18, s19
	s_add_u32 s12, s2, s18
	s_addc_u32 s13, s3, 0
	global_load_dwordx4 v[68:71], v10, s[12:13]
	s_add_u32 s12, s12, 0x8000
	s_addc_u32 s13, s13, 0
	global_load_dwordx4 v[72:75], v10, s[12:13]
	s_add_u32 s12, s12, 0x8000
	s_addc_u32 s13, s13, 0
	global_load_dwordx4 v[76:79], v10, s[12:13]
	s_add_u32 s12, s12, 0x8000
	s_addc_u32 s13, s13, 0
	global_load_dwordx4 v[80:83], v10, s[12:13]
	s_add_u32 s12, s12, 0x8000
	s_addc_u32 s13, s13, 0
	global_load_dwordx4 v[84:87], v10, s[12:13]
	s_add_u32 s12, s12, 0x8000
	s_addc_u32 s13, s13, 0
	global_load_dwordx4 v[88:91], v10, s[12:13]
	s_add_u32 s12, s12, 0x8000
	s_addc_u32 s13, s13, 0
	global_load_dwordx4 v[92:95], v10, s[12:13]
	s_add_u32 s12, s12, 0x8000
	s_addc_u32 s13, s13, 0
	global_load_dwordx4 v[96:99], v10, s[12:13]
	s_add_i32 s17, s16, 3168
	s_min_u32 s17, s17, 0xfff
	s_lshr_b32 s18, s17, 5
	s_add_i32 s18, s18, 0
	s_and_b32 s19, s17, 31
	s_lshl_b32 s19, s19, 21
	s_lshl_b32 s18, s18, 7
	s_add_u32 s18, s18, s19
	s_add_u32 s14, s4, s18
	s_addc_u32 s15, s5, 0
	ds_read_b32 v170, v7
	ds_read_b32 v171, v7 offset:512
	ds_read_b32 v172, v7 offset:1024
	ds_read_b32 v173, v7 offset:1536
	ds_read_b32 v174, v7 offset:2048
	ds_read_b32 v175, v7 offset:2560
	ds_read_b32 v176, v7 offset:3072
	ds_read_b32 v177, v7 offset:3584
	ds_read_b32 v196, v7 offset:4096
	ds_read_b32 v197, v7 offset:4608
	ds_read_b32 v198, v7 offset:5120
	ds_read_b32 v199, v7 offset:5632
	ds_read_b32 v200, v7 offset:6144
	ds_read_b32 v201, v7 offset:6656
	ds_read_b32 v202, v7 offset:7168
	ds_read_b32 v203, v7 offset:7680
	s_waitcnt lgkmcnt(0)
	v_max_f32_e32 v170, v170, v170
	v_max_f32_e32 v171, v171, v171
	v_max_f32_e32 v172, v172, v172
	v_max_f32_e32 v173, v173, v173
	v_max_f32_e32 v174, v174, v174
	v_max_f32_e32 v175, v175, v175
	v_max_f32_e32 v176, v176, v176
	v_max_f32_e32 v177, v177, v177
	v_max_f32_e32 v196, v196, v196
	v_max_f32_e32 v197, v197, v197
	v_max_f32_e32 v198, v198, v198
	v_max_f32_e32 v199, v199, v199
	v_max_f32_e32 v200, v200, v200
	v_max_f32_e32 v201, v201, v201
	v_max_f32_e32 v202, v202, v202
	v_max_f32_e32 v203, v203, v203
	v_med3_f32 v170, v170, s20, v13
	v_med3_f32 v171, v171, s20, v13
	v_med3_f32 v172, v172, s20, v13
	v_med3_f32 v173, v173, s20, v13
	v_med3_f32 v174, v174, s20, v13
	v_med3_f32 v175, v175, s20, v13
	v_med3_f32 v176, v176, s20, v13
	v_med3_f32 v177, v177, s20, v13
	v_med3_f32 v196, v196, s20, v13
	v_med3_f32 v197, v197, s20, v13
	v_med3_f32 v198, v198, s20, v13
	v_med3_f32 v199, v199, s20, v13
	v_med3_f32 v200, v200, s20, v13
	v_med3_f32 v201, v201, s20, v13
	v_med3_f32 v202, v202, s20, v13
	v_med3_f32 v203, v203, s20, v13
	v_mov_b32_e32 v208, 0
	v_mov_b32_e32 v209, 0
	v_mov_b32_e32 v210, 0
	v_mov_b32_e32 v211, 0
	v_cvt_pk_fp8_f32 v208, v170, v171
	v_cvt_pk_fp8_f32 v209, v174, v175
	v_cvt_pk_fp8_f32 v210, v196, v197
	v_cvt_pk_fp8_f32 v211, v200, v201
	v_cvt_pk_fp8_f32 v208, v172, v173 op_sel:[0,0,1]
	v_cvt_pk_fp8_f32 v209, v176, v177 op_sel:[0,0,1]
	v_cvt_pk_fp8_f32 v210, v198, v199 op_sel:[0,0,1]
	v_cvt_pk_fp8_f32 v211, v202, v203 op_sel:[0,0,1]
	s_nop 0
	global_store_dwordx4 v11, v[208:211], s[14:15]
	ds_read_b32 v170, v9
	ds_read_b32 v171, v9 offset:512
	ds_read_b32 v172, v9 offset:1024
	ds_read_b32 v173, v9 offset:1536
	ds_read_b32 v174, v9 offset:2048
	ds_read_b32 v175, v9 offset:2560
	ds_read_b32 v176, v9 offset:3072
	ds_read_b32 v177, v9 offset:3584
	ds_read_b32 v196, v9 offset:4096
	ds_read_b32 v197, v9 offset:4608
	ds_read_b32 v198, v9 offset:5120
	ds_read_b32 v199, v9 offset:5632
	ds_read_b32 v200, v9 offset:6144
	ds_read_b32 v201, v9 offset:6656
	ds_read_b32 v202, v9 offset:7168
	ds_read_b32 v203, v9 offset:7680
	s_waitcnt lgkmcnt(0)
	v_max_f32_e32 v170, v170, v170
	v_max_f32_e32 v171, v171, v171
	v_max_f32_e32 v172, v172, v172
	v_max_f32_e32 v173, v173, v173
	v_max_f32_e32 v174, v174, v174
	v_max_f32_e32 v175, v175, v175
	v_max_f32_e32 v176, v176, v176
	v_max_f32_e32 v177, v177, v177
	v_max_f32_e32 v196, v196, v196
	v_max_f32_e32 v197, v197, v197
	v_max_f32_e32 v198, v198, v198
	v_max_f32_e32 v199, v199, v199
	v_max_f32_e32 v200, v200, v200
	v_max_f32_e32 v201, v201, v201
	v_max_f32_e32 v202, v202, v202
	v_max_f32_e32 v203, v203, v203
	v_med3_f32 v170, v170, s20, v13
	v_med3_f32 v171, v171, s20, v13
	v_med3_f32 v172, v172, s20, v13
	v_med3_f32 v173, v173, s20, v13
	v_med3_f32 v174, v174, s20, v13
	v_med3_f32 v175, v175, s20, v13
	v_med3_f32 v176, v176, s20, v13
	v_med3_f32 v177, v177, s20, v13
	v_med3_f32 v196, v196, s20, v13
	v_med3_f32 v197, v197, s20, v13
	v_med3_f32 v198, v198, s20, v13
	v_med3_f32 v199, v199, s20, v13
	v_med3_f32 v200, v200, s20, v13
	v_med3_f32 v201, v201, s20, v13
	v_med3_f32 v202, v202, s20, v13
	v_med3_f32 v203, v203, s20, v13
	v_mov_b32_e32 v208, 0
	v_mov_b32_e32 v209, 0
	v_mov_b32_e32 v210, 0
	v_mov_b32_e32 v211, 0
	v_cvt_pk_fp8_f32 v208, v170, v171
	v_cvt_pk_fp8_f32 v209, v174, v175
	v_cvt_pk_fp8_f32 v210, v196, v197
	v_cvt_pk_fp8_f32 v211, v200, v201
	v_cvt_pk_fp8_f32 v208, v172, v173 op_sel:[0,0,1]
	v_cvt_pk_fp8_f32 v209, v176, v177 op_sel:[0,0,1]
	v_cvt_pk_fp8_f32 v210, v198, v199 op_sel:[0,0,1]
	v_cvt_pk_fp8_f32 v211, v202, v203 op_sel:[0,0,1]
	s_nop 0
	global_store_dwordx4 v12, v[208:211], s[14:15]
	s_waitcnt vmcnt(32)
	v_mul_f32_e32 v100, 0x43000000, v100
	v_mul_f32_e32 v101, 0x43000000, v101
	v_mul_f32_e32 v102, 0x43000000, v102
	v_mul_f32_e32 v103, 0x43000000, v103
	ds_write_b128 v4, v[100:103]
	v_mul_f32_e32 v104, 0x43000000, v104
	v_mul_f32_e32 v105, 0x43000000, v105
	v_mul_f32_e32 v106, 0x43000000, v106
	v_mul_f32_e32 v107, 0x43000000, v107
	ds_write_b128 v4, v[104:107] offset:1024
	v_mul_f32_e32 v108, 0x43000000, v108
	v_mul_f32_e32 v109, 0x43000000, v109
	v_mul_f32_e32 v110, 0x43000000, v110
	v_mul_f32_e32 v111, 0x43000000, v111
	ds_write_b128 v4, v[108:111] offset:2048
	v_mul_f32_e32 v112, 0x43000000, v112
	v_mul_f32_e32 v113, 0x43000000, v113
	v_mul_f32_e32 v114, 0x43000000, v114
	v_mul_f32_e32 v115, 0x43000000, v115
	ds_write_b128 v4, v[112:115] offset:3072
	v_mul_f32_e32 v116, 0x43000000, v116
	v_mul_f32_e32 v117, 0x43000000, v117
	v_mul_f32_e32 v118, 0x43000000, v118
	v_mul_f32_e32 v119, 0x43000000, v119
	ds_write_b128 v4, v[116:119] offset:4096
	v_mul_f32_e32 v120, 0x43000000, v120
	v_mul_f32_e32 v121, 0x43000000, v121
	v_mul_f32_e32 v122, 0x43000000, v122
	v_mul_f32_e32 v123, 0x43000000, v123
	ds_write_b128 v4, v[120:123] offset:5120
	v_mul_f32_e32 v124, 0x43000000, v124
	v_mul_f32_e32 v125, 0x43000000, v125
	v_mul_f32_e32 v126, 0x43000000, v126
	v_mul_f32_e32 v127, 0x43000000, v127
	ds_write_b128 v4, v[124:127] offset:6144
	v_mul_f32_e32 v128, 0x43000000, v128
	v_mul_f32_e32 v129, 0x43000000, v129
	v_mul_f32_e32 v130, 0x43000000, v130
	v_mul_f32_e32 v131, 0x43000000, v131
	ds_write_b128 v4, v[128:131] offset:7168
	s_waitcnt lgkmcnt(0)
	s_barrier
; #define GAS __attribute__((address_space(1)))
; #define LAS __attribute__((address_space(3)))
; #define LDS_WAIT() asm volatile("s_waitcnt lgkmcnt(0)" ::: "memory")
;     ...
;     for (int i = 0; i < 32; ++i) v[i] = sc >= 0 ? W[(size_t)(k0 + 2 * i + (lane >> 5)) * Nsrc + sc] : 0.f;
; #pragma unroll
;     for (int i = 0; i < 32; ++i) { const int k = k0 + 2 * i + (lane >> 5); float x = v[i] * wscale; if (KS) x *= (k < ksplit ? ksA[k] : ksB[k - ksplit]); scr[(2 * i + (lane >> 5)) * 33 + (lane & 31)] = x; }
;     LDS_WAIT(); asm volatile("" ::: "memory");
;     const int c = lane & 7;
; #pragma unroll
;     for (int j = 0; j < 4; ++j) { const int n = (lane >> 3) + 8 * j; const LAS float* s = scr + (8 * c) * 33 + n;
;         const unsigned long long o = (unsigned long long)pg8::pk4_fp8(s[0 * 33], s[1 * 33], s[2 * 33], s[3 * 33]) | ((unsigned long long)pg8::pk4_fp8(s[4 * 33], s[5 * 33], s[6 * 33], s[7 * 33]) << 32);
;         *(GAS unsigned long long*)(WT + (size_t)(n0 + n) * K + k0 + 8 * c) = o; }
; __global__ void __launch_bounds__(NWAVES * 64, 2) hybrid_fwd(Args args) {
;     ...
;             p0_transpose_item_f8<false>(args.in[16] + (size_t)l * FF * DM, FF, DM, DM / 32, (unsigned char*)(ws + WS_WDN + l * SZ_WDN), 128.f, args.in[16], args.in[16], 0, scr, r, lane);
	s_add_i32 s17, s16, 3648
	s_min_u32 s17, s17, 0xfff
	s_lshr_b32 s18, s17, 5
	s_add_i32 s18, s18, 0
	s_and_b32 s19, s17, 31
	s_lshl_b32 s18, s18, 21
	s_lshl_b32 s19, s19, 9
	s_add_u32 s18, s18, s19
	s_add_u32 s12, s2, s18
	s_addc_u32 s13, s3, 0
	global_load_dwordx4 v[100:103], v10, s[12:13]
	s_add_u32 s12, s12, 0x8000
	s_addc_u32 s13, s13, 0
	global_load_dwordx4 v[104:107], v10, s[12:13]
	s_add_u32 s12, s12, 0x8000
	s_addc_u32 s13, s13, 0
	global_load_dwordx4 v[108:111], v10, s[12:13]
	s_add_u32 s12, s12, 0x8000
	s_addc_u32 s13, s13, 0
	global_load_dwordx4 v[112:115], v10, s[12:13]
	s_add_u32 s12, s12, 0x8000
	s_addc_u32 s13, s13, 0
	global_load_dwordx4 v[116:119], v10, s[12:13]
	s_add_u32 s12, s12, 0x8000
	s_addc_u32 s13, s13, 0
	global_load_dwordx4 v[120:123], v10, s[12:13]
	s_add_u32 s12, s12, 0x8000
	s_addc_u32 s13, s13, 0
	global_load_dwordx4 v[124:127], v10, s[12:13]
	s_add_u32 s12, s12, 0x8000
	s_addc_u32 s13, s13, 0
	global_load_dwordx4 v[128:131], v10, s[12:13]
	s_add_i32 s17, s16, 3264
	s_min_u32 s17, s17, 0xfff
	s_lshr_b32 s18, s17, 5
	s_add_i32 s18, s18, 0
	s_and_b32 s19, s17, 31
	s_lshl_b32 s19, s19, 21
	s_lshl_b32 s18, s18, 7
	s_add_u32 s18, s18, s19
	s_add_u32 s14, s4, s18
	s_addc_u32 s15, s5, 0
	ds_read_b32 v170, v6
	ds_read_b32 v171, v6 offset:512
	ds_read_b32 v172, v6 offset:1024
	ds_read_b32 v173, v6 offset:1536
	ds_read_b32 v174, v6 offset:2048
	ds_read_b32 v175, v6 offset:2560
	ds_read_b32 v176, v6 offset:3072
	ds_read_b32 v177, v6 offset:3584
	ds_read_b32 v196, v6 offset:4096
	ds_read_b32 v197, v6 offset:4608
	ds_read_b32 v198, v6 offset:5120
	ds_read_b32 v199, v6 offset:5632
	ds_read_b32 v200, v6 offset:6144
	ds_read_b32 v201, v6 offset:6656
	ds_read_b32 v202, v6 offset:7168
	ds_read_b32 v203, v6 offset:7680
	s_waitcnt lgkmcnt(0)
	v_max_f32_e32 v170, v170, v170
	v_max_f32_e32 v171, v171, v171
	v_max_f32_e32 v172, v172, v172
	v_max_f32_e32 v173, v173, v173
	v_max_f32_e32 v174, v174, v174
	v_max_f32_e32 v175, v175, v175
	v_max_f32_e32 v176, v176, v176
	v_max_f32_e32 v177, v177, v177
	v_max_f32_e32 v196, v196, v196
	v_max_f32_e32 v197, v197, v197
	v_max_f32_e32 v198, v198, v198
	v_max_f32_e32 v199, v199, v199
	v_max_f32_e32 v200, v200, v200
	v_max_f32_e32 v201, v201, v201
	v_max_f32_e32 v202, v202, v202
	v_max_f32_e32 v203, v203, v203
	v_med3_f32 v170, v170, s20, v13
	v_med3_f32 v171, v171, s20, v13
	v_med3_f32 v172, v172, s20, v13
	v_med3_f32 v173, v173, s20, v13
	v_med3_f32 v174, v174, s20, v13
	v_med3_f32 v175, v175, s20, v13
	v_med3_f32 v176, v176, s20, v13
	v_med3_f32 v177, v177, s20, v13
	v_med3_f32 v196, v196, s20, v13
	v_med3_f32 v197, v197, s20, v13
	v_med3_f32 v198, v198, s20, v13
	v_med3_f32 v199, v199, s20, v13
	v_med3_f32 v200, v200, s20, v13
	v_med3_f32 v201, v201, s20, v13
	v_med3_f32 v202, v202, s20, v13
	v_med3_f32 v203, v203, s20, v13
	v_mov_b32_e32 v208, 0
	v_mov_b32_e32 v209, 0
	v_mov_b32_e32 v210, 0
	v_mov_b32_e32 v211, 0
	v_cvt_pk_fp8_f32 v208, v170, v171
	v_cvt_pk_fp8_f32 v209, v174, v175
	v_cvt_pk_fp8_f32 v210, v196, v197
	v_cvt_pk_fp8_f32 v211, v200, v201
	v_cvt_pk_fp8_f32 v208, v172, v173 op_sel:[0,0,1]
	v_cvt_pk_fp8_f32 v209, v176, v177 op_sel:[0,0,1]
	v_cvt_pk_fp8_f32 v210, v198, v199 op_sel:[0,0,1]
	v_cvt_pk_fp8_f32 v211, v202, v203 op_sel:[0,0,1]
	s_nop 0
	global_store_dwordx4 v11, v[208:211], s[14:15]
	ds_read_b32 v170, v8
	ds_read_b32 v171, v8 offset:512
	ds_read_b32 v172, v8 offset:1024
	ds_read_b32 v173, v8 offset:1536
	ds_read_b32 v174, v8 offset:2048
	ds_read_b32 v175, v8 offset:2560
	ds_read_b32 v176, v8 offset:3072
	ds_read_b32 v177, v8 offset:3584
	ds_read_b32 v196, v8 offset:4096
	ds_read_b32 v197, v8 offset:4608
	ds_read_b32 v198, v8 offset:5120
	ds_read_b32 v199, v8 offset:5632
	ds_read_b32 v200, v8 offset:6144
	ds_read_b32 v201, v8 offset:6656
	ds_read_b32 v202, v8 offset:7168
	ds_read_b32 v203, v8 offset:7680
	s_waitcnt lgkmcnt(0)
	v_max_f32_e32 v170, v170, v170
	v_max_f32_e32 v171, v171, v171
	v_max_f32_e32 v172, v172, v172
	v_max_f32_e32 v173, v173, v173
	v_max_f32_e32 v174, v174, v174
	v_max_f32_e32 v175, v175, v175
	v_max_f32_e32 v176, v176, v176
	v_max_f32_e32 v177, v177, v177
	v_max_f32_e32 v196, v196, v196
	v_max_f32_e32 v197, v197, v197
	v_max_f32_e32 v198, v198, v198
	v_max_f32_e32 v199, v199, v199
	v_max_f32_e32 v200, v200, v200
	v_max_f32_e32 v201, v201, v201
	v_max_f32_e32 v202, v202, v202
	v_max_f32_e32 v203, v203, v203
	v_med3_f32 v170, v170, s20, v13
	v_med3_f32 v171, v171, s20, v13
	v_med3_f32 v172, v172, s20, v13
	v_med3_f32 v173, v173, s20, v13
	v_med3_f32 v174, v174, s20, v13
	v_med3_f32 v175, v175, s20, v13
	v_med3_f32 v176, v176, s20, v13
	v_med3_f32 v177, v177, s20, v13
	v_med3_f32 v196, v196, s20, v13
	v_med3_f32 v197, v197, s20, v13
	v_med3_f32 v198, v198, s20, v13
	v_med3_f32 v199, v199, s20, v13
	v_med3_f32 v200, v200, s20, v13
	v_med3_f32 v201, v201, s20, v13
	v_med3_f32 v202, v202, s20, v13
	v_med3_f32 v203, v203, s20, v13
	v_mov_b32_e32 v208, 0
	v_mov_b32_e32 v209, 0
	v_mov_b32_e32 v210, 0
	v_mov_b32_e32 v211, 0
	v_cvt_pk_fp8_f32 v208, v170, v171
	v_cvt_pk_fp8_f32 v209, v174, v175
	v_cvt_pk_fp8_f32 v210, v196, v197
	v_cvt_pk_fp8_f32 v211, v200, v201
	v_cvt_pk_fp8_f32 v208, v172, v173 op_sel:[0,0,1]
	v_cvt_pk_fp8_f32 v209, v176, v177 op_sel:[0,0,1]
	v_cvt_pk_fp8_f32 v210, v198, v199 op_sel:[0,0,1]
	v_cvt_pk_fp8_f32 v211, v202, v203 op_sel:[0,0,1]
	s_nop 0
	global_store_dwordx4 v12, v[208:211], s[14:15]
	s_waitcnt vmcnt(32)
	v_mul_f32_e32 v132, 0x43000000, v132
	v_mul_f32_e32 v133, 0x43000000, v133
	v_mul_f32_e32 v134, 0x43000000, v134
	v_mul_f32_e32 v135, 0x43000000, v135
	ds_write_b128 v5, v[132:135]
	v_mul_f32_e32 v136, 0x43000000, v136
	v_mul_f32_e32 v137, 0x43000000, v137
	v_mul_f32_e32 v138, 0x43000000, v138
	v_mul_f32_e32 v139, 0x43000000, v139
	ds_write_b128 v5, v[136:139] offset:1024
	v_mul_f32_e32 v140, 0x43000000, v140
	v_mul_f32_e32 v141, 0x43000000, v141
	v_mul_f32_e32 v142, 0x43000000, v142
	v_mul_f32_e32 v143, 0x43000000, v143
	ds_write_b128 v5, v[140:143] offset:2048
	v_mul_f32_e32 v144, 0x43000000, v144
	v_mul_f32_e32 v145, 0x43000000, v145
	v_mul_f32_e32 v146, 0x43000000, v146
	v_mul_f32_e32 v147, 0x43000000, v147
	ds_write_b128 v5, v[144:147] offset:3072
	v_mul_f32_e32 v148, 0x43000000, v148
	v_mul_f32_e32 v149, 0x43000000, v149
	v_mul_f32_e32 v150, 0x43000000, v150
	v_mul_f32_e32 v151, 0x43000000, v151
	ds_write_b128 v5, v[148:151] offset:4096
	v_mul_f32_e32 v152, 0x43000000, v152
	v_mul_f32_e32 v153, 0x43000000, v153
	v_mul_f32_e32 v154, 0x43000000, v154
	v_mul_f32_e32 v155, 0x43000000, v155
	ds_write_b128 v5, v[152:155] offset:5120
	v_mul_f32_e32 v156, 0x43000000, v156
	v_mul_f32_e32 v157, 0x43000000, v157
	v_mul_f32_e32 v158, 0x43000000, v158
	v_mul_f32_e32 v159, 0x43000000, v159
	ds_write_b128 v5, v[156:159] offset:6144
	v_mul_f32_e32 v160, 0x43000000, v160
	v_mul_f32_e32 v161, 0x43000000, v161
	v_mul_f32_e32 v162, 0x43000000, v162
	v_mul_f32_e32 v163, 0x43000000, v163
	ds_write_b128 v5, v[160:163] offset:7168
	s_waitcnt lgkmcnt(0)
	s_barrier
; #define GAS __attribute__((address_space(1)))
; #define LAS __attribute__((address_space(3)))
; #define LDS_WAIT() asm volatile("s_waitcnt lgkmcnt(0)" ::: "memory")
;     ...
;     for (int i = 0; i < 32; ++i) v[i] = sc >= 0 ? W[(size_t)(k0 + 2 * i + (lane >> 5)) * Nsrc + sc] : 0.f;
; #pragma unroll
;     for (int i = 0; i < 32; ++i) { const int k = k0 + 2 * i + (lane >> 5); float x = v[i] * wscale; if (KS) x *= (k < ksplit ? ksA[k] : ksB[k - ksplit]); scr[(2 * i + (lane >> 5)) * 33 + (lane & 31)] = x; }
;     LDS_WAIT(); asm volatile("" ::: "memory");
;     const int c = lane & 7;
; #pragma unroll
;     for (int j = 0; j < 4; ++j) { const int n = (lane >> 3) + 8 * j; const LAS float* s = scr + (8 * c) * 33 + n;
;         const unsigned long long o = (unsigned long long)pg8::pk4_fp8(s[0 * 33], s[1 * 33], s[2 * 33], s[3 * 33]) | ((unsigned long long)pg8::pk4_fp8(s[4 * 33], s[5 * 33], s[6 * 33], s[7 * 33]) << 32);
;         *(GAS unsigned long long*)(WT + (size_t)(n0 + n) * K + k0 + 8 * c) = o; }
; __global__ void __launch_bounds__(NWAVES * 64, 2) hybrid_fwd(Args args) {
;     ...
;             p0_transpose_item_f8<false>(args.in[16] + (size_t)l * FF * DM, FF, DM, DM / 32, (unsigned char*)(ws + WS_WDN + l * SZ_WDN), 128.f, args.in[16], args.in[16], 0, scr, r, lane);
	s_add_i32 s17, s16, 3744
	s_min_u32 s17, s17, 0xfff
	s_lshr_b32 s18, s17, 5
	s_add_i32 s18, s18, 0
	s_and_b32 s19, s17, 31
	s_lshl_b32 s18, s18, 21
	s_lshl_b32 s19, s19, 9
	s_add_u32 s18, s18, s19
	s_add_u32 s12, s2, s18
	s_addc_u32 s13, s3, 0
	global_load_dwordx4 v[132:135], v10, s[12:13]
	s_add_u32 s12, s12, 0x8000
	s_addc_u32 s13, s13, 0
	global_load_dwordx4 v[136:139], v10, s[12:13]
	s_add_u32 s12, s12, 0x8000
	s_addc_u32 s13, s13, 0
	global_load_dwordx4 v[140:143], v10, s[12:13]
	s_add_u32 s12, s12, 0x8000
	s_addc_u32 s13, s13, 0
	global_load_dwordx4 v[144:147], v10, s[12:13]
	s_add_u32 s12, s12, 0x8000
	s_addc_u32 s13, s13, 0
	global_load_dwordx4 v[148:151], v10, s[12:13]
	s_add_u32 s12, s12, 0x8000
	s_addc_u32 s13, s13, 0
	global_load_dwordx4 v[152:155], v10, s[12:13]
	s_add_u32 s12, s12, 0x8000
	s_addc_u32 s13, s13, 0
	global_load_dwordx4 v[156:159], v10, s[12:13]
	s_add_u32 s12, s12, 0x8000
	s_addc_u32 s13, s13, 0
	global_load_dwordx4 v[160:163], v10, s[12:13]
	s_add_i32 s17, s16, 3360
	s_min_u32 s17, s17, 0xfff
	s_lshr_b32 s18, s17, 5
	s_add_i32 s18, s18, 0
	s_and_b32 s19, s17, 31
	s_lshl_b32 s19, s19, 21
	s_lshl_b32 s18, s18, 7
	s_add_u32 s18, s18, s19
	s_add_u32 s14, s4, s18
	s_addc_u32 s15, s5, 0
	ds_read_b32 v170, v7
	ds_read_b32 v171, v7 offset:512
	ds_read_b32 v172, v7 offset:1024
	ds_read_b32 v173, v7 offset:1536
	ds_read_b32 v174, v7 offset:2048
	ds_read_b32 v175, v7 offset:2560
	ds_read_b32 v176, v7 offset:3072
	ds_read_b32 v177, v7 offset:3584
	ds_read_b32 v196, v7 offset:4096
	ds_read_b32 v197, v7 offset:4608
	ds_read_b32 v198, v7 offset:5120
	ds_read_b32 v199, v7 offset:5632
	ds_read_b32 v200, v7 offset:6144
	ds_read_b32 v201, v7 offset:6656
	ds_read_b32 v202, v7 offset:7168
	ds_read_b32 v203, v7 offset:7680
	s_waitcnt lgkmcnt(0)
	v_max_f32_e32 v170, v170, v170
	v_max_f32_e32 v171, v171, v171
	v_max_f32_e32 v172, v172, v172
	v_max_f32_e32 v173, v173, v173
	v_max_f32_e32 v174, v174, v174
	v_max_f32_e32 v175, v175, v175
	v_max_f32_e32 v176, v176, v176
	v_max_f32_e32 v177, v177, v177
	v_max_f32_e32 v196, v196, v196
	v_max_f32_e32 v197, v197, v197
	v_max_f32_e32 v198, v198, v198
	v_max_f32_e32 v199, v199, v199
	v_max_f32_e32 v200, v200, v200
	v_max_f32_e32 v201, v201, v201
	v_max_f32_e32 v202, v202, v202
	v_max_f32_e32 v203, v203, v203
	v_med3_f32 v170, v170, s20, v13
	v_med3_f32 v171, v171, s20, v13
	v_med3_f32 v172, v172, s20, v13
	v_med3_f32 v173, v173, s20, v13
	v_med3_f32 v174, v174, s20, v13
	v_med3_f32 v175, v175, s20, v13
	v_med3_f32 v176, v176, s20, v13
	v_med3_f32 v177, v177, s20, v13
	v_med3_f32 v196, v196, s20, v13
	v_med3_f32 v197, v197, s20, v13
	v_med3_f32 v198, v198, s20, v13
	v_med3_f32 v199, v199, s20, v13
	v_med3_f32 v200, v200, s20, v13
	v_med3_f32 v201, v201, s20, v13
	v_med3_f32 v202, v202, s20, v13
	v_med3_f32 v203, v203, s20, v13
	v_mov_b32_e32 v208, 0
	v_mov_b32_e32 v209, 0
	v_mov_b32_e32 v210, 0
	v_mov_b32_e32 v211, 0
	v_cvt_pk_fp8_f32 v208, v170, v171
	v_cvt_pk_fp8_f32 v209, v174, v175
	v_cvt_pk_fp8_f32 v210, v196, v197
	v_cvt_pk_fp8_f32 v211, v200, v201
	v_cvt_pk_fp8_f32 v208, v172, v173 op_sel:[0,0,1]
	v_cvt_pk_fp8_f32 v209, v176, v177 op_sel:[0,0,1]
	v_cvt_pk_fp8_f32 v210, v198, v199 op_sel:[0,0,1]
	v_cvt_pk_fp8_f32 v211, v202, v203 op_sel:[0,0,1]
	s_nop 0
	global_store_dwordx4 v11, v[208:211], s[14:15]
	ds_read_b32 v170, v9
	ds_read_b32 v171, v9 offset:512
	ds_read_b32 v172, v9 offset:1024
	ds_read_b32 v173, v9 offset:1536
	ds_read_b32 v174, v9 offset:2048
	ds_read_b32 v175, v9 offset:2560
	ds_read_b32 v176, v9 offset:3072
	ds_read_b32 v177, v9 offset:3584
	ds_read_b32 v196, v9 offset:4096
	ds_read_b32 v197, v9 offset:4608
	ds_read_b32 v198, v9 offset:5120
	ds_read_b32 v199, v9 offset:5632
	ds_read_b32 v200, v9 offset:6144
	ds_read_b32 v201, v9 offset:6656
	ds_read_b32 v202, v9 offset:7168
	ds_read_b32 v203, v9 offset:7680
	s_waitcnt lgkmcnt(0)
	v_max_f32_e32 v170, v170, v170
	v_max_f32_e32 v171, v171, v171
	v_max_f32_e32 v172, v172, v172
	v_max_f32_e32 v173, v173, v173
	v_max_f32_e32 v174, v174, v174
	v_max_f32_e32 v175, v175, v175
	v_max_f32_e32 v176, v176, v176
	v_max_f32_e32 v177, v177, v177
	v_max_f32_e32 v196, v196, v196
	v_max_f32_e32 v197, v197, v197
	v_max_f32_e32 v198, v198, v198
	v_max_f32_e32 v199, v199, v199
	v_max_f32_e32 v200, v200, v200
	v_max_f32_e32 v201, v201, v201
	v_max_f32_e32 v202, v202, v202
	v_max_f32_e32 v203, v203, v203
	v_med3_f32 v170, v170, s20, v13
	v_med3_f32 v171, v171, s20, v13
	v_med3_f32 v172, v172, s20, v13
	v_med3_f32 v173, v173, s20, v13
	v_med3_f32 v174, v174, s20, v13
	v_med3_f32 v175, v175, s20, v13
	v_med3_f32 v176, v176, s20, v13
	v_med3_f32 v177, v177, s20, v13
	v_med3_f32 v196, v196, s20, v13
	v_med3_f32 v197, v197, s20, v13
	v_med3_f32 v198, v198, s20, v13
	v_med3_f32 v199, v199, s20, v13
	v_med3_f32 v200, v200, s20, v13
	v_med3_f32 v201, v201, s20, v13
	v_med3_f32 v202, v202, s20, v13
	v_med3_f32 v203, v203, s20, v13
	v_mov_b32_e32 v208, 0
	v_mov_b32_e32 v209, 0
	v_mov_b32_e32 v210, 0
	v_mov_b32_e32 v211, 0
	v_cvt_pk_fp8_f32 v208, v170, v171
	v_cvt_pk_fp8_f32 v209, v174, v175
	v_cvt_pk_fp8_f32 v210, v196, v197
	v_cvt_pk_fp8_f32 v211, v200, v201
	v_cvt_pk_fp8_f32 v208, v172, v173 op_sel:[0,0,1]
	v_cvt_pk_fp8_f32 v209, v176, v177 op_sel:[0,0,1]
	v_cvt_pk_fp8_f32 v210, v198, v199 op_sel:[0,0,1]
	v_cvt_pk_fp8_f32 v211, v202, v203 op_sel:[0,0,1]
	s_nop 0
	global_store_dwordx4 v12, v[208:211], s[14:15]
	s_waitcnt vmcnt(32)
	v_mul_f32_e32 v36, 0x43000000, v36
	v_mul_f32_e32 v37, 0x43000000, v37
	v_mul_f32_e32 v38, 0x43000000, v38
	v_mul_f32_e32 v39, 0x43000000, v39
	ds_write_b128 v4, v[36:39]
	v_mul_f32_e32 v40, 0x43000000, v40
	v_mul_f32_e32 v41, 0x43000000, v41
	v_mul_f32_e32 v42, 0x43000000, v42
	v_mul_f32_e32 v43, 0x43000000, v43
	ds_write_b128 v4, v[40:43] offset:1024
	v_mul_f32_e32 v44, 0x43000000, v44
	v_mul_f32_e32 v45, 0x43000000, v45
	v_mul_f32_e32 v46, 0x43000000, v46
	v_mul_f32_e32 v47, 0x43000000, v47
	ds_write_b128 v4, v[44:47] offset:2048
	v_mul_f32_e32 v48, 0x43000000, v48
	v_mul_f32_e32 v49, 0x43000000, v49
	v_mul_f32_e32 v50, 0x43000000, v50
	v_mul_f32_e32 v51, 0x43000000, v51
	ds_write_b128 v4, v[48:51] offset:3072
	v_mul_f32_e32 v52, 0x43000000, v52
	v_mul_f32_e32 v53, 0x43000000, v53
	v_mul_f32_e32 v54, 0x43000000, v54
	v_mul_f32_e32 v55, 0x43000000, v55
	ds_write_b128 v4, v[52:55] offset:4096
	v_mul_f32_e32 v56, 0x43000000, v56
	v_mul_f32_e32 v57, 0x43000000, v57
	v_mul_f32_e32 v58, 0x43000000, v58
	v_mul_f32_e32 v59, 0x43000000, v59
	ds_write_b128 v4, v[56:59] offset:5120
	v_mul_f32_e32 v60, 0x43000000, v60
	v_mul_f32_e32 v61, 0x43000000, v61
	v_mul_f32_e32 v62, 0x43000000, v62
	v_mul_f32_e32 v63, 0x43000000, v63
	ds_write_b128 v4, v[60:63] offset:6144
	v_mul_f32_e32 v64, 0x43000000, v64
	v_mul_f32_e32 v65, 0x43000000, v65
	v_mul_f32_e32 v66, 0x43000000, v66
	v_mul_f32_e32 v67, 0x43000000, v67
	ds_write_b128 v4, v[64:67] offset:7168
	s_waitcnt lgkmcnt(0)
	s_barrier
; #define GAS __attribute__((address_space(1)))
; #define LAS __attribute__((address_space(3)))
; #define LDS_WAIT() asm volatile("s_waitcnt lgkmcnt(0)" ::: "memory")
; __device__ __forceinline__ unsigned pk4_fp8(float a, float b, float c, float d) {
;     a = fminf(fmaxf(a, -448.f), 448.f); b = fminf(fmaxf(b, -448.f), 448.f); c = fminf(fmaxf(c, -448.f), 448.f); d = fminf(fmaxf(d, -448.f), 448.f);
;     int w = __builtin_amdgcn_cvt_pk_fp8_f32(a, b, 0, false); w = __builtin_amdgcn_cvt_pk_fp8_f32(c, d, w, true); return (unsigned)w; }
;     const int pr = item >> 1, kb = 2 * (pr / nblk) + (item & 1), nb = pr % nblk, k0 = 64 * kb, n0 = 32 * nb;
;     const int nr = n0 + (lane & 31); const int sc = MAP == 1 ? src_col_in(nr) : nr;
;     float v[32];
; #pragma unroll
;     for (int i = 0; i < 32; ++i) v[i] = sc >= 0 ? W[(size_t)(k0 + 2 * i + (lane >> 5)) * Nsrc + sc] : 0.f;
; #pragma unroll
;     for (int i = 0; i < 32; ++i) { const int k = k0 + 2 * i + (lane >> 5); float x = v[i] * wscale; if (KS) x *= (k < ksplit ? ksA[k] : ksB[k - ksplit]); scr[(2 * i + (lane >> 5)) * 33 + (lane & 31)] = x; }
;     LDS_WAIT(); asm volatile("" ::: "memory");
;     const int c = lane & 7;
; #pragma unroll
;     for (int j = 0; j < 4; ++j) { const int n = (lane >> 3) + 8 * j; const LAS float* s = scr + (8 * c) * 33 + n;
;         const unsigned long long o = (unsigned long long)pg8::pk4_fp8(s[0 * 33], s[1 * 33], s[2 * 33], s[3 * 33]) | ((unsigned long long)pg8::pk4_fp8(s[4 * 33], s[5 * 33], s[6 * 33], s[7 * 33]) << 32);
;         *(GAS unsigned long long*)(WT + (size_t)(n0 + n) * K + k0 + 8 * c) = o; }
;     LDS_WAIT(); asm volatile("" ::: "memory");
	s_add_i32 s17, s16, 3840
	s_min_u32 s17, s17, 0xfff
	s_lshr_b32 s18, s17, 5
	s_add_i32 s18, s18, 0
	s_and_b32 s19, s17, 31
	s_lshl_b32 s18, s18, 21
	s_lshl_b32 s19, s19, 9
	s_add_u32 s18, s18, s19
	s_add_u32 s12, s2, s18
	s_addc_u32 s13, s3, 0
	global_load_dwordx4 v[36:39], v10, s[12:13]
	s_add_u32 s12, s12, 0x8000
	s_addc_u32 s13, s13, 0
	global_load_dwordx4 v[40:43], v10, s[12:13]
	s_add_u32 s12, s12, 0x8000
	s_addc_u32 s13, s13, 0
	global_load_dwordx4 v[44:47], v10, s[12:13]
	s_add_u32 s12, s12, 0x8000
	s_addc_u32 s13, s13, 0
	global_load_dwordx4 v[48:51], v10, s[12:13]
	s_add_u32 s12, s12, 0x8000
	s_addc_u32 s13, s13, 0
	global_load_dwordx4 v[52:55], v10, s[12:13]
	s_add_u32 s12, s12, 0x8000
	s_addc_u32 s13, s13, 0
	global_load_dwordx4 v[56:59], v10, s[12:13]
	s_add_u32 s12, s12, 0x8000
	s_addc_u32 s13, s13, 0
	global_load_dwordx4 v[60:63], v10, s[12:13]
	s_add_u32 s12, s12, 0x8000
	s_addc_u32 s13, s13, 0
	global_load_dwordx4 v[64:67], v10, s[12:13]
	s_add_i32 s17, s16, 3456
	s_min_u32 s17, s17, 0xfff
	s_lshr_b32 s18, s17, 5
	s_add_i32 s18, s18, 0
	s_and_b32 s19, s17, 31
	s_lshl_b32 s19, s19, 21
	s_lshl_b32 s18, s18, 7
	s_add_u32 s18, s18, s19
	s_add_u32 s14, s4, s18
	s_addc_u32 s15, s5, 0
	ds_read_b32 v170, v6
	ds_read_b32 v171, v6 offset:512
	ds_read_b32 v172, v6 offset:1024
	ds_read_b32 v173, v6 offset:1536
	ds_read_b32 v174, v6 offset:2048
	ds_read_b32 v175, v6 offset:2560
	ds_read_b32 v176, v6 offset:3072
	ds_read_b32 v177, v6 offset:3584
	ds_read_b32 v196, v6 offset:4096
	ds_read_b32 v197, v6 offset:4608
	ds_read_b32 v198, v6 offset:5120
	ds_read_b32 v199, v6 offset:5632
	ds_read_b32 v200, v6 offset:6144
	ds_read_b32 v201, v6 offset:6656
	ds_read_b32 v202, v6 offset:7168
	ds_read_b32 v203, v6 offset:7680
	s_waitcnt lgkmcnt(0)
	v_max_f32_e32 v170, v170, v170
	v_max_f32_e32 v171, v171, v171
	v_max_f32_e32 v172, v172, v172
	v_max_f32_e32 v173, v173, v173
	v_max_f32_e32 v174, v174, v174
	v_max_f32_e32 v175, v175, v175
	v_max_f32_e32 v176, v176, v176
	v_max_f32_e32 v177, v177, v177
	v_max_f32_e32 v196, v196, v196
	v_max_f32_e32 v197, v197, v197
	v_max_f32_e32 v198, v198, v198
	v_max_f32_e32 v199, v199, v199
	v_max_f32_e32 v200, v200, v200
	v_max_f32_e32 v201, v201, v201
	v_max_f32_e32 v202, v202, v202
	v_max_f32_e32 v203, v203, v203
	v_med3_f32 v170, v170, s20, v13
	v_med3_f32 v171, v171, s20, v13
	v_med3_f32 v172, v172, s20, v13
	v_med3_f32 v173, v173, s20, v13
	v_med3_f32 v174, v174, s20, v13
	v_med3_f32 v175, v175, s20, v13
	v_med3_f32 v176, v176, s20, v13
	v_med3_f32 v177, v177, s20, v13
	v_med3_f32 v196, v196, s20, v13
	v_med3_f32 v197, v197, s20, v13
	v_med3_f32 v198, v198, s20, v13
	v_med3_f32 v199, v199, s20, v13
	v_med3_f32 v200, v200, s20, v13
	v_med3_f32 v201, v201, s20, v13
	v_med3_f32 v202, v202, s20, v13
	v_med3_f32 v203, v203, s20, v13
	v_mov_b32_e32 v208, 0
	v_mov_b32_e32 v209, 0
	v_mov_b32_e32 v210, 0
	v_mov_b32_e32 v211, 0
	v_cvt_pk_fp8_f32 v208, v170, v171
	v_cvt_pk_fp8_f32 v209, v174, v175
	v_cvt_pk_fp8_f32 v210, v196, v197
	v_cvt_pk_fp8_f32 v211, v200, v201
	v_cvt_pk_fp8_f32 v208, v172, v173 op_sel:[0,0,1]
	v_cvt_pk_fp8_f32 v209, v176, v177 op_sel:[0,0,1]
	v_cvt_pk_fp8_f32 v210, v198, v199 op_sel:[0,0,1]
	v_cvt_pk_fp8_f32 v211, v202, v203 op_sel:[0,0,1]
	s_nop 0
	global_store_dwordx4 v11, v[208:211], s[14:15]
	ds_read_b32 v170, v8
	ds_read_b32 v171, v8 offset:512
	ds_read_b32 v172, v8 offset:1024
	ds_read_b32 v173, v8 offset:1536
	ds_read_b32 v174, v8 offset:2048
	ds_read_b32 v175, v8 offset:2560
	ds_read_b32 v176, v8 offset:3072
	ds_read_b32 v177, v8 offset:3584
	ds_read_b32 v196, v8 offset:4096
	ds_read_b32 v197, v8 offset:4608
	ds_read_b32 v198, v8 offset:5120
	ds_read_b32 v199, v8 offset:5632
	ds_read_b32 v200, v8 offset:6144
	ds_read_b32 v201, v8 offset:6656
	ds_read_b32 v202, v8 offset:7168
	ds_read_b32 v203, v8 offset:7680
	s_waitcnt lgkmcnt(0)
	v_max_f32_e32 v170, v170, v170
	v_max_f32_e32 v171, v171, v171
	v_max_f32_e32 v172, v172, v172
	v_max_f32_e32 v173, v173, v173
	v_max_f32_e32 v174, v174, v174
	v_max_f32_e32 v175, v175, v175
	v_max_f32_e32 v176, v176, v176
	v_max_f32_e32 v177, v177, v177
	v_max_f32_e32 v196, v196, v196
	v_max_f32_e32 v197, v197, v197
	v_max_f32_e32 v198, v198, v198
	v_max_f32_e32 v199, v199, v199
	v_max_f32_e32 v200, v200, v200
	v_max_f32_e32 v201, v201, v201
	v_max_f32_e32 v202, v202, v202
	v_max_f32_e32 v203, v203, v203
	v_med3_f32 v170, v170, s20, v13
	v_med3_f32 v171, v171, s20, v13
	v_med3_f32 v172, v172, s20, v13
	v_med3_f32 v173, v173, s20, v13
	v_med3_f32 v174, v174, s20, v13
	v_med3_f32 v175, v175, s20, v13
	v_med3_f32 v176, v176, s20, v13
	v_med3_f32 v177, v177, s20, v13
	v_med3_f32 v196, v196, s20, v13
	v_med3_f32 v197, v197, s20, v13
	v_med3_f32 v198, v198, s20, v13
	v_med3_f32 v199, v199, s20, v13
	v_med3_f32 v200, v200, s20, v13
	v_med3_f32 v201, v201, s20, v13
	v_med3_f32 v202, v202, s20, v13
	v_med3_f32 v203, v203, s20, v13
	v_mov_b32_e32 v208, 0
	v_mov_b32_e32 v209, 0
	v_mov_b32_e32 v210, 0
	v_mov_b32_e32 v211, 0
	v_cvt_pk_fp8_f32 v208, v170, v171
	v_cvt_pk_fp8_f32 v209, v174, v175
	v_cvt_pk_fp8_f32 v210, v196, v197
	v_cvt_pk_fp8_f32 v211, v200, v201
	v_cvt_pk_fp8_f32 v208, v172, v173 op_sel:[0,0,1]
	v_cvt_pk_fp8_f32 v209, v176, v177 op_sel:[0,0,1]
	v_cvt_pk_fp8_f32 v210, v198, v199 op_sel:[0,0,1]
	v_cvt_pk_fp8_f32 v211, v202, v203 op_sel:[0,0,1]
	s_nop 0
	global_store_dwordx4 v12, v[208:211], s[14:15]
	s_waitcnt vmcnt(32)
	v_mul_f32_e32 v68, 0x43000000, v68
	v_mul_f32_e32 v69, 0x43000000, v69
	v_mul_f32_e32 v70, 0x43000000, v70
	v_mul_f32_e32 v71, 0x43000000, v71
	ds_write_b128 v5, v[68:71]
	v_mul_f32_e32 v72, 0x43000000, v72
	v_mul_f32_e32 v73, 0x43000000, v73
	v_mul_f32_e32 v74, 0x43000000, v74
	v_mul_f32_e32 v75, 0x43000000, v75
	ds_write_b128 v5, v[72:75] offset:1024
	v_mul_f32_e32 v76, 0x43000000, v76
	v_mul_f32_e32 v77, 0x43000000, v77
	v_mul_f32_e32 v78, 0x43000000, v78
	v_mul_f32_e32 v79, 0x43000000, v79
	ds_write_b128 v5, v[76:79] offset:2048
	v_mul_f32_e32 v80, 0x43000000, v80
	v_mul_f32_e32 v81, 0x43000000, v81
	v_mul_f32_e32 v82, 0x43000000, v82
	v_mul_f32_e32 v83, 0x43000000, v83
	ds_write_b128 v5, v[80:83] offset:3072
	v_mul_f32_e32 v84, 0x43000000, v84
	v_mul_f32_e32 v85, 0x43000000, v85
	v_mul_f32_e32 v86, 0x43000000, v86
	v_mul_f32_e32 v87, 0x43000000, v87
	ds_write_b128 v5, v[84:87] offset:4096
	v_mul_f32_e32 v88, 0x43000000, v88
	v_mul_f32_e32 v89, 0x43000000, v89
	v_mul_f32_e32 v90, 0x43000000, v90
	v_mul_f32_e32 v91, 0x43000000, v91
	ds_write_b128 v5, v[88:91] offset:5120
	v_mul_f32_e32 v92, 0x43000000, v92
	v_mul_f32_e32 v93, 0x43000000, v93
	v_mul_f32_e32 v94, 0x43000000, v94
	v_mul_f32_e32 v95, 0x43000000, v95
	ds_write_b128 v5, v[92:95] offset:6144
	v_mul_f32_e32 v96, 0x43000000, v96
	v_mul_f32_e32 v97, 0x43000000, v97
	v_mul_f32_e32 v98, 0x43000000, v98
	v_mul_f32_e32 v99, 0x43000000, v99
	ds_write_b128 v5, v[96:99] offset:7168
	s_waitcnt lgkmcnt(0)
	s_barrier
; #define GAS __attribute__((address_space(1)))
; #define LAS __attribute__((address_space(3)))
; #define LDS_WAIT() asm volatile("s_waitcnt lgkmcnt(0)" ::: "memory")
; __device__ __forceinline__ unsigned pk4_fp8(float a, float b, float c, float d) {
;     a = fminf(fmaxf(a, -448.f), 448.f); b = fminf(fmaxf(b, -448.f), 448.f); c = fminf(fmaxf(c, -448.f), 448.f); d = fminf(fmaxf(d, -448.f), 448.f);
;     int w = __builtin_amdgcn_cvt_pk_fp8_f32(a, b, 0, false); w = __builtin_amdgcn_cvt_pk_fp8_f32(c, d, w, true); return (unsigned)w; }
;     const int pr = item >> 1, kb = 2 * (pr / nblk) + (item & 1), nb = pr % nblk, k0 = 64 * kb, n0 = 32 * nb;
;     const int nr = n0 + (lane & 31); const int sc = MAP == 1 ? src_col_in(nr) : nr;
;     float v[32];
; #pragma unroll
;     for (int i = 0; i < 32; ++i) v[i] = sc >= 0 ? W[(size_t)(k0 + 2 * i + (lane >> 5)) * Nsrc + sc] : 0.f;
; #pragma unroll
;     for (int i = 0; i < 32; ++i) { const int k = k0 + 2 * i + (lane >> 5); float x = v[i] * wscale; if (KS) x *= (k < ksplit ? ksA[k] : ksB[k - ksplit]); scr[(2 * i + (lane >> 5)) * 33 + (lane & 31)] = x; }
;     LDS_WAIT(); asm volatile("" ::: "memory");
;     const int c = lane & 7;
; #pragma unroll
;     for (int j = 0; j < 4; ++j) { const int n = (lane >> 3) + 8 * j; const LAS float* s = scr + (8 * c) * 33 + n;
;         const unsigned long long o = (unsigned long long)pg8::pk4_fp8(s[0 * 33], s[1 * 33], s[2 * 33], s[3 * 33]) | ((unsigned long long)pg8::pk4_fp8(s[4 * 33], s[5 * 33], s[6 * 33], s[7 * 33]) << 32);
;         *(GAS unsigned long long*)(WT + (size_t)(n0 + n) * K + k0 + 8 * c) = o; }
;     LDS_WAIT(); asm volatile("" ::: "memory");
	s_add_i32 s17, s16, 3936
	s_min_u32 s17, s17, 0xfff
	s_lshr_b32 s18, s17, 5
	s_add_i32 s18, s18, 0
	s_and_b32 s19, s17, 31
	s_lshl_b32 s18, s18, 21
	s_lshl_b32 s19, s19, 9
	s_add_u32 s18, s18, s19
	s_add_u32 s12, s2, s18
	s_addc_u32 s13, s3, 0
	global_load_dwordx4 v[68:71], v10, s[12:13]
	s_add_u32 s12, s12, 0x8000
	s_addc_u32 s13, s13, 0
	global_load_dwordx4 v[72:75], v10, s[12:13]
	s_add_u32 s12, s12, 0x8000
	s_addc_u32 s13, s13, 0
	global_load_dwordx4 v[76:79], v10, s[12:13]
	s_add_u32 s12, s12, 0x8000
	s_addc_u32 s13, s13, 0
	global_load_dwordx4 v[80:83], v10, s[12:13]
	s_add_u32 s12, s12, 0x8000
	s_addc_u32 s13, s13, 0
	global_load_dwordx4 v[84:87], v10, s[12:13]
	s_add_u32 s12, s12, 0x8000
	s_addc_u32 s13, s13, 0
	global_load_dwordx4 v[88:91], v10, s[12:13]
	s_add_u32 s12, s12, 0x8000
	s_addc_u32 s13, s13, 0
	global_load_dwordx4 v[92:95], v10, s[12:13]
	s_add_u32 s12, s12, 0x8000
	s_addc_u32 s13, s13, 0
	global_load_dwordx4 v[96:99], v10, s[12:13]
	s_add_i32 s17, s16, 3552
	s_min_u32 s17, s17, 0xfff
	s_lshr_b32 s18, s17, 5
	s_add_i32 s18, s18, 0
	s_and_b32 s19, s17, 31
	s_lshl_b32 s19, s19, 21
	s_lshl_b32 s18, s18, 7
	s_add_u32 s18, s18, s19
	s_add_u32 s14, s4, s18
	s_addc_u32 s15, s5, 0
	ds_read_b32 v170, v7
	ds_read_b32 v171, v7 offset:512
	ds_read_b32 v172, v7 offset:1024
	ds_read_b32 v173, v7 offset:1536
	ds_read_b32 v174, v7 offset:2048
	ds_read_b32 v175, v7 offset:2560
	ds_read_b32 v176, v7 offset:3072
	ds_read_b32 v177, v7 offset:3584
	ds_read_b32 v196, v7 offset:4096
	ds_read_b32 v197, v7 offset:4608
	ds_read_b32 v198, v7 offset:5120
	ds_read_b32 v199, v7 offset:5632
	ds_read_b32 v200, v7 offset:6144
	ds_read_b32 v201, v7 offset:6656
	ds_read_b32 v202, v7 offset:7168
	ds_read_b32 v203, v7 offset:7680
	s_waitcnt lgkmcnt(0)
	v_max_f32_e32 v170, v170, v170
	v_max_f32_e32 v171, v171, v171
	v_max_f32_e32 v172, v172, v172
	v_max_f32_e32 v173, v173, v173
	v_max_f32_e32 v174, v174, v174
	v_max_f32_e32 v175, v175, v175
	v_max_f32_e32 v176, v176, v176
	v_max_f32_e32 v177, v177, v177
	v_max_f32_e32 v196, v196, v196
	v_max_f32_e32 v197, v197, v197
	v_max_f32_e32 v198, v198, v198
	v_max_f32_e32 v199, v199, v199
	v_max_f32_e32 v200, v200, v200
	v_max_f32_e32 v201, v201, v201
	v_max_f32_e32 v202, v202, v202
	v_max_f32_e32 v203, v203, v203
	v_med3_f32 v170, v170, s20, v13
	v_med3_f32 v171, v171, s20, v13
	v_med3_f32 v172, v172, s20, v13
	v_med3_f32 v173, v173, s20, v13
	v_med3_f32 v174, v174, s20, v13
	v_med3_f32 v175, v175, s20, v13
	v_med3_f32 v176, v176, s20, v13
	v_med3_f32 v177, v177, s20, v13
	v_med3_f32 v196, v196, s20, v13
	v_med3_f32 v197, v197, s20, v13
	v_med3_f32 v198, v198, s20, v13
	v_med3_f32 v199, v199, s20, v13
	v_med3_f32 v200, v200, s20, v13
	v_med3_f32 v201, v201, s20, v13
	v_med3_f32 v202, v202, s20, v13
	v_med3_f32 v203, v203, s20, v13
	v_mov_b32_e32 v208, 0
	v_mov_b32_e32 v209, 0
	v_mov_b32_e32 v210, 0
	v_mov_b32_e32 v211, 0
	v_cvt_pk_fp8_f32 v208, v170, v171
	v_cvt_pk_fp8_f32 v209, v174, v175
	v_cvt_pk_fp8_f32 v210, v196, v197
	v_cvt_pk_fp8_f32 v211, v200, v201
	v_cvt_pk_fp8_f32 v208, v172, v173 op_sel:[0,0,1]
	v_cvt_pk_fp8_f32 v209, v176, v177 op_sel:[0,0,1]
	v_cvt_pk_fp8_f32 v210, v198, v199 op_sel:[0,0,1]
	v_cvt_pk_fp8_f32 v211, v202, v203 op_sel:[0,0,1]
	s_nop 0
	global_store_dwordx4 v11, v[208:211], s[14:15]
	ds_read_b32 v170, v9
	ds_read_b32 v171, v9 offset:512
	ds_read_b32 v172, v9 offset:1024
	ds_read_b32 v173, v9 offset:1536
	ds_read_b32 v174, v9 offset:2048
	ds_read_b32 v175, v9 offset:2560
	ds_read_b32 v176, v9 offset:3072
	ds_read_b32 v177, v9 offset:3584
	ds_read_b32 v196, v9 offset:4096
	ds_read_b32 v197, v9 offset:4608
	ds_read_b32 v198, v9 offset:5120
	ds_read_b32 v199, v9 offset:5632
	ds_read_b32 v200, v9 offset:6144
	ds_read_b32 v201, v9 offset:6656
	ds_read_b32 v202, v9 offset:7168
	ds_read_b32 v203, v9 offset:7680
	s_waitcnt lgkmcnt(0)
	v_max_f32_e32 v170, v170, v170
	v_max_f32_e32 v171, v171, v171
	v_max_f32_e32 v172, v172, v172
	v_max_f32_e32 v173, v173, v173
	v_max_f32_e32 v174, v174, v174
	v_max_f32_e32 v175, v175, v175
	v_max_f32_e32 v176, v176, v176
	v_max_f32_e32 v177, v177, v177
	v_max_f32_e32 v196, v196, v196
	v_max_f32_e32 v197, v197, v197
	v_max_f32_e32 v198, v198, v198
	v_max_f32_e32 v199, v199, v199
	v_max_f32_e32 v200, v200, v200
	v_max_f32_e32 v201, v201, v201
	v_max_f32_e32 v202, v202, v202
	v_max_f32_e32 v203, v203, v203
	v_med3_f32 v170, v170, s20, v13
	v_med3_f32 v171, v171, s20, v13
	v_med3_f32 v172, v172, s20, v13
	v_med3_f32 v173, v173, s20, v13
	v_med3_f32 v174, v174, s20, v13
	v_med3_f32 v175, v175, s20, v13
	v_med3_f32 v176, v176, s20, v13
	v_med3_f32 v177, v177, s20, v13
	v_med3_f32 v196, v196, s20, v13
	v_med3_f32 v197, v197, s20, v13
	v_med3_f32 v198, v198, s20, v13
	v_med3_f32 v199, v199, s20, v13
	v_med3_f32 v200, v200, s20, v13
	v_med3_f32 v201, v201, s20, v13
	v_med3_f32 v202, v202, s20, v13
	v_med3_f32 v203, v203, s20, v13
	v_mov_b32_e32 v208, 0
	v_mov_b32_e32 v209, 0
	v_mov_b32_e32 v210, 0
	v_mov_b32_e32 v211, 0
	v_cvt_pk_fp8_f32 v208, v170, v171
	v_cvt_pk_fp8_f32 v209, v174, v175
	v_cvt_pk_fp8_f32 v210, v196, v197
	v_cvt_pk_fp8_f32 v211, v200, v201
	v_cvt_pk_fp8_f32 v208, v172, v173 op_sel:[0,0,1]
	v_cvt_pk_fp8_f32 v209, v176, v177 op_sel:[0,0,1]
	v_cvt_pk_fp8_f32 v210, v198, v199 op_sel:[0,0,1]
	v_cvt_pk_fp8_f32 v211, v202, v203 op_sel:[0,0,1]
	s_nop 0
	global_store_dwordx4 v12, v[208:211], s[14:15]
	s_waitcnt vmcnt(32)
	v_mul_f32_e32 v100, 0x43000000, v100
	v_mul_f32_e32 v101, 0x43000000, v101
	v_mul_f32_e32 v102, 0x43000000, v102
	v_mul_f32_e32 v103, 0x43000000, v103
	ds_write_b128 v4, v[100:103]
	v_mul_f32_e32 v104, 0x43000000, v104
	v_mul_f32_e32 v105, 0x43000000, v105
	v_mul_f32_e32 v106, 0x43000000, v106
	v_mul_f32_e32 v107, 0x43000000, v107
	ds_write_b128 v4, v[104:107] offset:1024
	v_mul_f32_e32 v108, 0x43000000, v108
	v_mul_f32_e32 v109, 0x43000000, v109
	v_mul_f32_e32 v110, 0x43000000, v110
	v_mul_f32_e32 v111, 0x43000000, v111
	ds_write_b128 v4, v[108:111] offset:2048
	v_mul_f32_e32 v112, 0x43000000, v112
	v_mul_f32_e32 v113, 0x43000000, v113
	v_mul_f32_e32 v114, 0x43000000, v114
	v_mul_f32_e32 v115, 0x43000000, v115
	ds_write_b128 v4, v[112:115] offset:3072
	v_mul_f32_e32 v116, 0x43000000, v116
	v_mul_f32_e32 v117, 0x43000000, v117
	v_mul_f32_e32 v118, 0x43000000, v118
	v_mul_f32_e32 v119, 0x43000000, v119
	ds_write_b128 v4, v[116:119] offset:4096
	v_mul_f32_e32 v120, 0x43000000, v120
	v_mul_f32_e32 v121, 0x43000000, v121
	v_mul_f32_e32 v122, 0x43000000, v122
	v_mul_f32_e32 v123, 0x43000000, v123
	ds_write_b128 v4, v[120:123] offset:5120
	v_mul_f32_e32 v124, 0x43000000, v124
	v_mul_f32_e32 v125, 0x43000000, v125
	v_mul_f32_e32 v126, 0x43000000, v126
	v_mul_f32_e32 v127, 0x43000000, v127
	ds_write_b128 v4, v[124:127] offset:6144
	v_mul_f32_e32 v128, 0x43000000, v128
	v_mul_f32_e32 v129, 0x43000000, v129
	v_mul_f32_e32 v130, 0x43000000, v130
	v_mul_f32_e32 v131, 0x43000000, v131
	ds_write_b128 v4, v[128:131] offset:7168
	s_waitcnt lgkmcnt(0)
	s_barrier
; #define GAS __attribute__((address_space(1)))
; #define LAS __attribute__((address_space(3)))
; #define LDS_WAIT() asm volatile("s_waitcnt lgkmcnt(0)" ::: "memory")
; __device__ __forceinline__ unsigned pk4_fp8(float a, float b, float c, float d) {
;     a = fminf(fmaxf(a, -448.f), 448.f); b = fminf(fmaxf(b, -448.f), 448.f); c = fminf(fmaxf(c, -448.f), 448.f); d = fminf(fmaxf(d, -448.f), 448.f);
;     int w = __builtin_amdgcn_cvt_pk_fp8_f32(a, b, 0, false); w = __builtin_amdgcn_cvt_pk_fp8_f32(c, d, w, true); return (unsigned)w; }
;     const int pr = item >> 1, kb = 2 * (pr / nblk) + (item & 1), nb = pr % nblk, k0 = 64 * kb, n0 = 32 * nb;
;     const int nr = n0 + (lane & 31); const int sc = MAP == 1 ? src_col_in(nr) : nr;
;     float v[32];
; #pragma unroll
;     for (int i = 0; i < 32; ++i) v[i] = sc >= 0 ? W[(size_t)(k0 + 2 * i + (lane >> 5)) * Nsrc + sc] : 0.f;
; #pragma unroll
;     for (int i = 0; i < 32; ++i) { const int k = k0 + 2 * i + (lane >> 5); float x = v[i] * wscale; if (KS) x *= (k < ksplit ? ksA[k] : ksB[k - ksplit]); scr[(2 * i + (lane >> 5)) * 33 + (lane & 31)] = x; }
;     LDS_WAIT(); asm volatile("" ::: "memory");
;     const int c = lane & 7;
; #pragma unroll
;     for (int j = 0; j < 4; ++j) { const int n = (lane >> 3) + 8 * j; const LAS float* s = scr + (8 * c) * 33 + n;
;         const unsigned long long o = (unsigned long long)pg8::pk4_fp8(s[0 * 33], s[1 * 33], s[2 * 33], s[3 * 33]) | ((unsigned long long)pg8::pk4_fp8(s[4 * 33], s[5 * 33], s[6 * 33], s[7 * 33]) << 32);
;         *(GAS unsigned long long*)(WT + (size_t)(n0 + n) * K + k0 + 8 * c) = o; }
;     LDS_WAIT(); asm volatile("" ::: "memory");
	s_add_i32 s17, s16, 4032
	s_min_u32 s17, s17, 0xfff
	s_lshr_b32 s18, s17, 5
	s_add_i32 s18, s18, 0
	s_and_b32 s19, s17, 31
	s_lshl_b32 s18, s18, 21
	s_lshl_b32 s19, s19, 9
	s_add_u32 s18, s18, s19
	s_add_u32 s12, s2, s18
	s_addc_u32 s13, s3, 0
	global_load_dwordx4 v[100:103], v10, s[12:13]
	s_add_u32 s12, s12, 0x8000
	s_addc_u32 s13, s13, 0
	global_load_dwordx4 v[104:107], v10, s[12:13]
	s_add_u32 s12, s12, 0x8000
	s_addc_u32 s13, s13, 0
	global_load_dwordx4 v[108:111], v10, s[12:13]
	s_add_u32 s12, s12, 0x8000
	s_addc_u32 s13, s13, 0
	global_load_dwordx4 v[112:115], v10, s[12:13]
	s_add_u32 s12, s12, 0x8000
	s_addc_u32 s13, s13, 0
	global_load_dwordx4 v[116:119], v10, s[12:13]
	s_add_u32 s12, s12, 0x8000
	s_addc_u32 s13, s13, 0
	global_load_dwordx4 v[120:123], v10, s[12:13]
	s_add_u32 s12, s12, 0x8000
	s_addc_u32 s13, s13, 0
	global_load_dwordx4 v[124:127], v10, s[12:13]
	s_add_u32 s12, s12, 0x8000
	s_addc_u32 s13, s13, 0
	global_load_dwordx4 v[128:131], v10, s[12:13]
	s_add_i32 s17, s16, 3648
	s_min_u32 s17, s17, 0xfff
	s_lshr_b32 s18, s17, 5
	s_add_i32 s18, s18, 0
	s_and_b32 s19, s17, 31
	s_lshl_b32 s19, s19, 21
	s_lshl_b32 s18, s18, 7
	s_add_u32 s18, s18, s19
	s_add_u32 s14, s4, s18
	s_addc_u32 s15, s5, 0
	ds_read_b32 v170, v6
	ds_read_b32 v171, v6 offset:512
	ds_read_b32 v172, v6 offset:1024
	ds_read_b32 v173, v6 offset:1536
	ds_read_b32 v174, v6 offset:2048
	ds_read_b32 v175, v6 offset:2560
	ds_read_b32 v176, v6 offset:3072
	ds_read_b32 v177, v6 offset:3584
	ds_read_b32 v196, v6 offset:4096
	ds_read_b32 v197, v6 offset:4608
	ds_read_b32 v198, v6 offset:5120
	ds_read_b32 v199, v6 offset:5632
	ds_read_b32 v200, v6 offset:6144
	ds_read_b32 v201, v6 offset:6656
	ds_read_b32 v202, v6 offset:7168
	ds_read_b32 v203, v6 offset:7680
	s_waitcnt lgkmcnt(0)
	v_max_f32_e32 v170, v170, v170
	v_max_f32_e32 v171, v171, v171
	v_max_f32_e32 v172, v172, v172
	v_max_f32_e32 v173, v173, v173
	v_max_f32_e32 v174, v174, v174
	v_max_f32_e32 v175, v175, v175
	v_max_f32_e32 v176, v176, v176
	v_max_f32_e32 v177, v177, v177
	v_max_f32_e32 v196, v196, v196
	v_max_f32_e32 v197, v197, v197
	v_max_f32_e32 v198, v198, v198
	v_max_f32_e32 v199, v199, v199
	v_max_f32_e32 v200, v200, v200
	v_max_f32_e32 v201, v201, v201
	v_max_f32_e32 v202, v202, v202
	v_max_f32_e32 v203, v203, v203
	v_med3_f32 v170, v170, s20, v13
	v_med3_f32 v171, v171, s20, v13
	v_med3_f32 v172, v172, s20, v13
	v_med3_f32 v173, v173, s20, v13
	v_med3_f32 v174, v174, s20, v13
	v_med3_f32 v175, v175, s20, v13
	v_med3_f32 v176, v176, s20, v13
	v_med3_f32 v177, v177, s20, v13
	v_med3_f32 v196, v196, s20, v13
	v_med3_f32 v197, v197, s20, v13
	v_med3_f32 v198, v198, s20, v13
	v_med3_f32 v199, v199, s20, v13
	v_med3_f32 v200, v200, s20, v13
	v_med3_f32 v201, v201, s20, v13
	v_med3_f32 v202, v202, s20, v13
	v_med3_f32 v203, v203, s20, v13
	v_mov_b32_e32 v208, 0
	v_mov_b32_e32 v209, 0
	v_mov_b32_e32 v210, 0
	v_mov_b32_e32 v211, 0
	v_cvt_pk_fp8_f32 v208, v170, v171
	v_cvt_pk_fp8_f32 v209, v174, v175
	v_cvt_pk_fp8_f32 v210, v196, v197
	v_cvt_pk_fp8_f32 v211, v200, v201
	v_cvt_pk_fp8_f32 v208, v172, v173 op_sel:[0,0,1]
	v_cvt_pk_fp8_f32 v209, v176, v177 op_sel:[0,0,1]
	v_cvt_pk_fp8_f32 v210, v198, v199 op_sel:[0,0,1]
	v_cvt_pk_fp8_f32 v211, v202, v203 op_sel:[0,0,1]
	s_nop 0
	global_store_dwordx4 v11, v[208:211], s[14:15]
	ds_read_b32 v170, v8
	ds_read_b32 v171, v8 offset:512
	ds_read_b32 v172, v8 offset:1024
	ds_read_b32 v173, v8 offset:1536
	ds_read_b32 v174, v8 offset:2048
	ds_read_b32 v175, v8 offset:2560
	ds_read_b32 v176, v8 offset:3072
	ds_read_b32 v177, v8 offset:3584
	ds_read_b32 v196, v8 offset:4096
	ds_read_b32 v197, v8 offset:4608
	ds_read_b32 v198, v8 offset:5120
	ds_read_b32 v199, v8 offset:5632
	ds_read_b32 v200, v8 offset:6144
	ds_read_b32 v201, v8 offset:6656
	ds_read_b32 v202, v8 offset:7168
	ds_read_b32 v203, v8 offset:7680
	s_waitcnt lgkmcnt(0)
	v_max_f32_e32 v170, v170, v170
	v_max_f32_e32 v171, v171, v171
	v_max_f32_e32 v172, v172, v172
	v_max_f32_e32 v173, v173, v173
	v_max_f32_e32 v174, v174, v174
	v_max_f32_e32 v175, v175, v175
	v_max_f32_e32 v176, v176, v176
	v_max_f32_e32 v177, v177, v177
	v_max_f32_e32 v196, v196, v196
	v_max_f32_e32 v197, v197, v197
	v_max_f32_e32 v198, v198, v198
	v_max_f32_e32 v199, v199, v199
	v_max_f32_e32 v200, v200, v200
	v_max_f32_e32 v201, v201, v201
	v_max_f32_e32 v202, v202, v202
	v_max_f32_e32 v203, v203, v203
	v_med3_f32 v170, v170, s20, v13
	v_med3_f32 v171, v171, s20, v13
	v_med3_f32 v172, v172, s20, v13
	v_med3_f32 v173, v173, s20, v13
	v_med3_f32 v174, v174, s20, v13
	v_med3_f32 v175, v175, s20, v13
	v_med3_f32 v176, v176, s20, v13
	v_med3_f32 v177, v177, s20, v13
	v_med3_f32 v196, v196, s20, v13
	v_med3_f32 v197, v197, s20, v13
	v_med3_f32 v198, v198, s20, v13
	v_med3_f32 v199, v199, s20, v13
	v_med3_f32 v200, v200, s20, v13
	v_med3_f32 v201, v201, s20, v13
	v_med3_f32 v202, v202, s20, v13
	v_med3_f32 v203, v203, s20, v13
	v_mov_b32_e32 v208, 0
	v_mov_b32_e32 v209, 0
	v_mov_b32_e32 v210, 0
	v_mov_b32_e32 v211, 0
	v_cvt_pk_fp8_f32 v208, v170, v171
	v_cvt_pk_fp8_f32 v209, v174, v175
	v_cvt_pk_fp8_f32 v210, v196, v197
	v_cvt_pk_fp8_f32 v211, v200, v201
	v_cvt_pk_fp8_f32 v208, v172, v173 op_sel:[0,0,1]
	v_cvt_pk_fp8_f32 v209, v176, v177 op_sel:[0,0,1]
	v_cvt_pk_fp8_f32 v210, v198, v199 op_sel:[0,0,1]
	v_cvt_pk_fp8_f32 v211, v202, v203 op_sel:[0,0,1]
	s_nop 0
	global_store_dwordx4 v12, v[208:211], s[14:15]
	s_waitcnt vmcnt(32)
	v_mul_f32_e32 v132, 0x43000000, v132
	v_mul_f32_e32 v133, 0x43000000, v133
	v_mul_f32_e32 v134, 0x43000000, v134
	v_mul_f32_e32 v135, 0x43000000, v135
	ds_write_b128 v5, v[132:135]
	v_mul_f32_e32 v136, 0x43000000, v136
	v_mul_f32_e32 v137, 0x43000000, v137
	v_mul_f32_e32 v138, 0x43000000, v138
	v_mul_f32_e32 v139, 0x43000000, v139
	ds_write_b128 v5, v[136:139] offset:1024
	v_mul_f32_e32 v140, 0x43000000, v140
	v_mul_f32_e32 v141, 0x43000000, v141
	v_mul_f32_e32 v142, 0x43000000, v142
	v_mul_f32_e32 v143, 0x43000000, v143
	ds_write_b128 v5, v[140:143] offset:2048
	v_mul_f32_e32 v144, 0x43000000, v144
	v_mul_f32_e32 v145, 0x43000000, v145
	v_mul_f32_e32 v146, 0x43000000, v146
	v_mul_f32_e32 v147, 0x43000000, v147
	ds_write_b128 v5, v[144:147] offset:3072
	v_mul_f32_e32 v148, 0x43000000, v148
	v_mul_f32_e32 v149, 0x43000000, v149
	v_mul_f32_e32 v150, 0x43000000, v150
	v_mul_f32_e32 v151, 0x43000000, v151
	ds_write_b128 v5, v[148:151] offset:4096
	v_mul_f32_e32 v152, 0x43000000, v152
	v_mul_f32_e32 v153, 0x43000000, v153
	v_mul_f32_e32 v154, 0x43000000, v154
	v_mul_f32_e32 v155, 0x43000000, v155
	ds_write_b128 v5, v[152:155] offset:5120
	v_mul_f32_e32 v156, 0x43000000, v156
	v_mul_f32_e32 v157, 0x43000000, v157
	v_mul_f32_e32 v158, 0x43000000, v158
	v_mul_f32_e32 v159, 0x43000000, v159
	ds_write_b128 v5, v[156:159] offset:6144
	v_mul_f32_e32 v160, 0x43000000, v160
	v_mul_f32_e32 v161, 0x43000000, v161
	v_mul_f32_e32 v162, 0x43000000, v162
	v_mul_f32_e32 v163, 0x43000000, v163
	ds_write_b128 v5, v[160:163] offset:7168
	s_waitcnt lgkmcnt(0)
	s_barrier
; #define GAS __attribute__((address_space(1)))
; #define LAS __attribute__((address_space(3)))
; #define LDS_WAIT() asm volatile("s_waitcnt lgkmcnt(0)" ::: "memory")
; __device__ __forceinline__ unsigned pk4_fp8(float a, float b, float c, float d) {
;     a = fminf(fmaxf(a, -448.f), 448.f); b = fminf(fmaxf(b, -448.f), 448.f); c = fminf(fmaxf(c, -448.f), 448.f); d = fminf(fmaxf(d, -448.f), 448.f);
;     int w = __builtin_amdgcn_cvt_pk_fp8_f32(a, b, 0, false); w = __builtin_amdgcn_cvt_pk_fp8_f32(c, d, w, true); return (unsigned)w; }
;     ...
;     LDS_WAIT(); asm volatile("" ::: "memory");
;     const int c = lane & 7;
; #pragma unroll
;     for (int j = 0; j < 4; ++j) { const int n = (lane >> 3) + 8 * j; const LAS float* s = scr + (8 * c) * 33 + n;
;         const unsigned long long o = (unsigned long long)pg8::pk4_fp8(s[0 * 33], s[1 * 33], s[2 * 33], s[3 * 33]) | ((unsigned long long)pg8::pk4_fp8(s[4 * 33], s[5 * 33], s[6 * 33], s[7 * 33]) << 32);
;         *(GAS unsigned long long*)(WT + (size_t)(n0 + n) * K + k0 + 8 * c) = o; }
;     LDS_WAIT(); asm volatile("" ::: "memory");
	s_add_i32 s17, s16, 3744
	s_min_u32 s17, s17, 0xfff
	s_lshr_b32 s18, s17, 5
	s_add_i32 s18, s18, 0
	s_and_b32 s19, s17, 31
	s_lshl_b32 s19, s19, 21
	s_lshl_b32 s18, s18, 7
	s_add_u32 s18, s18, s19
	s_add_u32 s14, s4, s18
	s_addc_u32 s15, s5, 0
	ds_read_b32 v170, v7
	ds_read_b32 v171, v7 offset:512
	ds_read_b32 v172, v7 offset:1024
	ds_read_b32 v173, v7 offset:1536
	ds_read_b32 v174, v7 offset:2048
	ds_read_b32 v175, v7 offset:2560
	ds_read_b32 v176, v7 offset:3072
	ds_read_b32 v177, v7 offset:3584
	ds_read_b32 v196, v7 offset:4096
	ds_read_b32 v197, v7 offset:4608
	ds_read_b32 v198, v7 offset:5120
	ds_read_b32 v199, v7 offset:5632
	ds_read_b32 v200, v7 offset:6144
	ds_read_b32 v201, v7 offset:6656
	ds_read_b32 v202, v7 offset:7168
	ds_read_b32 v203, v7 offset:7680
	s_waitcnt lgkmcnt(0)
	v_max_f32_e32 v170, v170, v170
	v_max_f32_e32 v171, v171, v171
	v_max_f32_e32 v172, v172, v172
	v_max_f32_e32 v173, v173, v173
	v_max_f32_e32 v174, v174, v174
	v_max_f32_e32 v175, v175, v175
	v_max_f32_e32 v176, v176, v176
	v_max_f32_e32 v177, v177, v177
	v_max_f32_e32 v196, v196, v196
	v_max_f32_e32 v197, v197, v197
	v_max_f32_e32 v198, v198, v198
	v_max_f32_e32 v199, v199, v199
	v_max_f32_e32 v200, v200, v200
	v_max_f32_e32 v201, v201, v201
	v_max_f32_e32 v202, v202, v202
	v_max_f32_e32 v203, v203, v203
	v_med3_f32 v170, v170, s20, v13
	v_med3_f32 v171, v171, s20, v13
	v_med3_f32 v172, v172, s20, v13
	v_med3_f32 v173, v173, s20, v13
	v_med3_f32 v174, v174, s20, v13
	v_med3_f32 v175, v175, s20, v13
	v_med3_f32 v176, v176, s20, v13
	v_med3_f32 v177, v177, s20, v13
	v_med3_f32 v196, v196, s20, v13
	v_med3_f32 v197, v197, s20, v13
	v_med3_f32 v198, v198, s20, v13
	v_med3_f32 v199, v199, s20, v13
	v_med3_f32 v200, v200, s20, v13
	v_med3_f32 v201, v201, s20, v13
	v_med3_f32 v202, v202, s20, v13
	v_med3_f32 v203, v203, s20, v13
	v_mov_b32_e32 v208, 0
	v_mov_b32_e32 v209, 0
	v_mov_b32_e32 v210, 0
	v_mov_b32_e32 v211, 0
	v_cvt_pk_fp8_f32 v208, v170, v171
	v_cvt_pk_fp8_f32 v209, v174, v175
	v_cvt_pk_fp8_f32 v210, v196, v197
	v_cvt_pk_fp8_f32 v211, v200, v201
	v_cvt_pk_fp8_f32 v208, v172, v173 op_sel:[0,0,1]
	v_cvt_pk_fp8_f32 v209, v176, v177 op_sel:[0,0,1]
	v_cvt_pk_fp8_f32 v210, v198, v199 op_sel:[0,0,1]
	v_cvt_pk_fp8_f32 v211, v202, v203 op_sel:[0,0,1]
	s_nop 0
	global_store_dwordx4 v11, v[208:211], s[14:15]
	ds_read_b32 v170, v9
	ds_read_b32 v171, v9 offset:512
	ds_read_b32 v172, v9 offset:1024
	ds_read_b32 v173, v9 offset:1536
	ds_read_b32 v174, v9 offset:2048
	ds_read_b32 v175, v9 offset:2560
	ds_read_b32 v176, v9 offset:3072
	ds_read_b32 v177, v9 offset:3584
	ds_read_b32 v196, v9 offset:4096
	ds_read_b32 v197, v9 offset:4608
	ds_read_b32 v198, v9 offset:5120
	ds_read_b32 v199, v9 offset:5632
	ds_read_b32 v200, v9 offset:6144
	ds_read_b32 v201, v9 offset:6656
	ds_read_b32 v202, v9 offset:7168
	ds_read_b32 v203, v9 offset:7680
	s_waitcnt lgkmcnt(0)
	v_max_f32_e32 v170, v170, v170
	v_max_f32_e32 v171, v171, v171
	v_max_f32_e32 v172, v172, v172
	v_max_f32_e32 v173, v173, v173
	v_max_f32_e32 v174, v174, v174
	v_max_f32_e32 v175, v175, v175
	v_max_f32_e32 v176, v176, v176
	v_max_f32_e32 v177, v177, v177
	v_max_f32_e32 v196, v196, v196
	v_max_f32_e32 v197, v197, v197
	v_max_f32_e32 v198, v198, v198
	v_max_f32_e32 v199, v199, v199
	v_max_f32_e32 v200, v200, v200
	v_max_f32_e32 v201, v201, v201
	v_max_f32_e32 v202, v202, v202
	v_max_f32_e32 v203, v203, v203
	v_med3_f32 v170, v170, s20, v13
	v_med3_f32 v171, v171, s20, v13
	v_med3_f32 v172, v172, s20, v13
	v_med3_f32 v173, v173, s20, v13
	v_med3_f32 v174, v174, s20, v13
	v_med3_f32 v175, v175, s20, v13
	v_med3_f32 v176, v176, s20, v13
	v_med3_f32 v177, v177, s20, v13
	v_med3_f32 v196, v196, s20, v13
	v_med3_f32 v197, v197, s20, v13
	v_med3_f32 v198, v198, s20, v13
	v_med3_f32 v199, v199, s20, v13
	v_med3_f32 v200, v200, s20, v13
	v_med3_f32 v201, v201, s20, v13
	v_med3_f32 v202, v202, s20, v13
	v_med3_f32 v203, v203, s20, v13
	v_mov_b32_e32 v208, 0
	v_mov_b32_e32 v209, 0
	v_mov_b32_e32 v210, 0
	v_mov_b32_e32 v211, 0
	v_cvt_pk_fp8_f32 v208, v170, v171
	v_cvt_pk_fp8_f32 v209, v174, v175
	v_cvt_pk_fp8_f32 v210, v196, v197
	v_cvt_pk_fp8_f32 v211, v200, v201
	v_cvt_pk_fp8_f32 v208, v172, v173 op_sel:[0,0,1]
	v_cvt_pk_fp8_f32 v209, v176, v177 op_sel:[0,0,1]
	v_cvt_pk_fp8_f32 v210, v198, v199 op_sel:[0,0,1]
	v_cvt_pk_fp8_f32 v211, v202, v203 op_sel:[0,0,1]
	s_nop 0
	global_store_dwordx4 v12, v[208:211], s[14:15]
	s_waitcnt vmcnt(24)
	v_mul_f32_e32 v36, 0x43000000, v36
	v_mul_f32_e32 v37, 0x43000000, v37
	v_mul_f32_e32 v38, 0x43000000, v38
	v_mul_f32_e32 v39, 0x43000000, v39
	ds_write_b128 v4, v[36:39]
	v_mul_f32_e32 v40, 0x43000000, v40
	v_mul_f32_e32 v41, 0x43000000, v41
	v_mul_f32_e32 v42, 0x43000000, v42
	v_mul_f32_e32 v43, 0x43000000, v43
	ds_write_b128 v4, v[40:43] offset:1024
	v_mul_f32_e32 v44, 0x43000000, v44
	v_mul_f32_e32 v45, 0x43000000, v45
	v_mul_f32_e32 v46, 0x43000000, v46
	v_mul_f32_e32 v47, 0x43000000, v47
	ds_write_b128 v4, v[44:47] offset:2048
	v_mul_f32_e32 v48, 0x43000000, v48
	v_mul_f32_e32 v49, 0x43000000, v49
	v_mul_f32_e32 v50, 0x43000000, v50
	v_mul_f32_e32 v51, 0x43000000, v51
	ds_write_b128 v4, v[48:51] offset:3072
	v_mul_f32_e32 v52, 0x43000000, v52
	v_mul_f32_e32 v53, 0x43000000, v53
	v_mul_f32_e32 v54, 0x43000000, v54
	v_mul_f32_e32 v55, 0x43000000, v55
	ds_write_b128 v4, v[52:55] offset:4096
	v_mul_f32_e32 v56, 0x43000000, v56
	v_mul_f32_e32 v57, 0x43000000, v57
	v_mul_f32_e32 v58, 0x43000000, v58
	v_mul_f32_e32 v59, 0x43000000, v59
	ds_write_b128 v4, v[56:59] offset:5120
	v_mul_f32_e32 v60, 0x43000000, v60
	v_mul_f32_e32 v61, 0x43000000, v61
	v_mul_f32_e32 v62, 0x43000000, v62
	v_mul_f32_e32 v63, 0x43000000, v63
	ds_write_b128 v4, v[60:63] offset:6144
	v_mul_f32_e32 v64, 0x43000000, v64
	v_mul_f32_e32 v65, 0x43000000, v65
	v_mul_f32_e32 v66, 0x43000000, v66
	v_mul_f32_e32 v67, 0x43000000, v67
	ds_write_b128 v4, v[64:67] offset:7168
	s_waitcnt lgkmcnt(0)
	s_barrier
; #define GAS __attribute__((address_space(1)))
; #define LAS __attribute__((address_space(3)))
; #define LDS_WAIT() asm volatile("s_waitcnt lgkmcnt(0)" ::: "memory")
; __device__ __forceinline__ unsigned pk4_fp8(float a, float b, float c, float d) {
;     a = fminf(fmaxf(a, -448.f), 448.f); b = fminf(fmaxf(b, -448.f), 448.f); c = fminf(fmaxf(c, -448.f), 448.f); d = fminf(fmaxf(d, -448.f), 448.f);
;     int w = __builtin_amdgcn_cvt_pk_fp8_f32(a, b, 0, false); w = __builtin_amdgcn_cvt_pk_fp8_f32(c, d, w, true); return (unsigned)w; }
;     ...
;     LDS_WAIT(); asm volatile("" ::: "memory");
;     const int c = lane & 7;
; #pragma unroll
;     for (int j = 0; j < 4; ++j) { const int n = (lane >> 3) + 8 * j; const LAS float* s = scr + (8 * c) * 33 + n;
;         const unsigned long long o = (unsigned long long)pg8::pk4_fp8(s[0 * 33], s[1 * 33], s[2 * 33], s[3 * 33]) | ((unsigned long long)pg8::pk4_fp8(s[4 * 33], s[5 * 33], s[6 * 33], s[7 * 33]) << 32);
;         *(GAS unsigned long long*)(WT + (size_t)(n0 + n) * K + k0 + 8 * c) = o; }
;     LDS_WAIT(); asm volatile("" ::: "memory");
	s_add_i32 s17, s16, 3840
	s_min_u32 s17, s17, 0xfff
	s_lshr_b32 s18, s17, 5
	s_add_i32 s18, s18, 0
	s_and_b32 s19, s17, 31
	s_lshl_b32 s19, s19, 21
	s_lshl_b32 s18, s18, 7
	s_add_u32 s18, s18, s19
	s_add_u32 s14, s4, s18
	s_addc_u32 s15, s5, 0
	ds_read_b32 v170, v6
	ds_read_b32 v171, v6 offset:512
	ds_read_b32 v172, v6 offset:1024
	ds_read_b32 v173, v6 offset:1536
	ds_read_b32 v174, v6 offset:2048
	ds_read_b32 v175, v6 offset:2560
	ds_read_b32 v176, v6 offset:3072
	ds_read_b32 v177, v6 offset:3584
	ds_read_b32 v196, v6 offset:4096
	ds_read_b32 v197, v6 offset:4608
	ds_read_b32 v198, v6 offset:5120
	ds_read_b32 v199, v6 offset:5632
	ds_read_b32 v200, v6 offset:6144
	ds_read_b32 v201, v6 offset:6656
	ds_read_b32 v202, v6 offset:7168
	ds_read_b32 v203, v6 offset:7680
	s_waitcnt lgkmcnt(0)
	v_max_f32_e32 v170, v170, v170
	v_max_f32_e32 v171, v171, v171
	v_max_f32_e32 v172, v172, v172
	v_max_f32_e32 v173, v173, v173
	v_max_f32_e32 v174, v174, v174
	v_max_f32_e32 v175, v175, v175
	v_max_f32_e32 v176, v176, v176
	v_max_f32_e32 v177, v177, v177
	v_max_f32_e32 v196, v196, v196
	v_max_f32_e32 v197, v197, v197
	v_max_f32_e32 v198, v198, v198
	v_max_f32_e32 v199, v199, v199
	v_max_f32_e32 v200, v200, v200
	v_max_f32_e32 v201, v201, v201
	v_max_f32_e32 v202, v202, v202
	v_max_f32_e32 v203, v203, v203
	v_med3_f32 v170, v170, s20, v13
	v_med3_f32 v171, v171, s20, v13
	v_med3_f32 v172, v172, s20, v13
	v_med3_f32 v173, v173, s20, v13
	v_med3_f32 v174, v174, s20, v13
	v_med3_f32 v175, v175, s20, v13
	v_med3_f32 v176, v176, s20, v13
	v_med3_f32 v177, v177, s20, v13
	v_med3_f32 v196, v196, s20, v13
	v_med3_f32 v197, v197, s20, v13
	v_med3_f32 v198, v198, s20, v13
	v_med3_f32 v199, v199, s20, v13
	v_med3_f32 v200, v200, s20, v13
	v_med3_f32 v201, v201, s20, v13
	v_med3_f32 v202, v202, s20, v13
	v_med3_f32 v203, v203, s20, v13
	v_mov_b32_e32 v208, 0
	v_mov_b32_e32 v209, 0
	v_mov_b32_e32 v210, 0
	v_mov_b32_e32 v211, 0
	v_cvt_pk_fp8_f32 v208, v170, v171
	v_cvt_pk_fp8_f32 v209, v174, v175
	v_cvt_pk_fp8_f32 v210, v196, v197
	v_cvt_pk_fp8_f32 v211, v200, v201
	v_cvt_pk_fp8_f32 v208, v172, v173 op_sel:[0,0,1]
	v_cvt_pk_fp8_f32 v209, v176, v177 op_sel:[0,0,1]
	v_cvt_pk_fp8_f32 v210, v198, v199 op_sel:[0,0,1]
	v_cvt_pk_fp8_f32 v211, v202, v203 op_sel:[0,0,1]
	s_nop 0
	global_store_dwordx4 v11, v[208:211], s[14:15]
	ds_read_b32 v170, v8
	ds_read_b32 v171, v8 offset:512
	ds_read_b32 v172, v8 offset:1024
	ds_read_b32 v173, v8 offset:1536
	ds_read_b32 v174, v8 offset:2048
	ds_read_b32 v175, v8 offset:2560
	ds_read_b32 v176, v8 offset:3072
	ds_read_b32 v177, v8 offset:3584
	ds_read_b32 v196, v8 offset:4096
	ds_read_b32 v197, v8 offset:4608
	ds_read_b32 v198, v8 offset:5120
	ds_read_b32 v199, v8 offset:5632
	ds_read_b32 v200, v8 offset:6144
	ds_read_b32 v201, v8 offset:6656
	ds_read_b32 v202, v8 offset:7168
	ds_read_b32 v203, v8 offset:7680
	s_waitcnt lgkmcnt(0)
	v_max_f32_e32 v170, v170, v170
	v_max_f32_e32 v171, v171, v171
	v_max_f32_e32 v172, v172, v172
	v_max_f32_e32 v173, v173, v173
	v_max_f32_e32 v174, v174, v174
	v_max_f32_e32 v175, v175, v175
	v_max_f32_e32 v176, v176, v176
	v_max_f32_e32 v177, v177, v177
	v_max_f32_e32 v196, v196, v196
	v_max_f32_e32 v197, v197, v197
	v_max_f32_e32 v198, v198, v198
	v_max_f32_e32 v199, v199, v199
	v_max_f32_e32 v200, v200, v200
	v_max_f32_e32 v201, v201, v201
	v_max_f32_e32 v202, v202, v202
	v_max_f32_e32 v203, v203, v203
	v_med3_f32 v170, v170, s20, v13
	v_med3_f32 v171, v171, s20, v13
	v_med3_f32 v172, v172, s20, v13
	v_med3_f32 v173, v173, s20, v13
	v_med3_f32 v174, v174, s20, v13
	v_med3_f32 v175, v175, s20, v13
	v_med3_f32 v176, v176, s20, v13
	v_med3_f32 v177, v177, s20, v13
	v_med3_f32 v196, v196, s20, v13
	v_med3_f32 v197, v197, s20, v13
	v_med3_f32 v198, v198, s20, v13
	v_med3_f32 v199, v199, s20, v13
	v_med3_f32 v200, v200, s20, v13
	v_med3_f32 v201, v201, s20, v13
	v_med3_f32 v202, v202, s20, v13
	v_med3_f32 v203, v203, s20, v13
	v_mov_b32_e32 v208, 0
	v_mov_b32_e32 v209, 0
	v_mov_b32_e32 v210, 0
	v_mov_b32_e32 v211, 0
	v_cvt_pk_fp8_f32 v208, v170, v171
	v_cvt_pk_fp8_f32 v209, v174, v175
	v_cvt_pk_fp8_f32 v210, v196, v197
	v_cvt_pk_fp8_f32 v211, v200, v201
	v_cvt_pk_fp8_f32 v208, v172, v173 op_sel:[0,0,1]
	v_cvt_pk_fp8_f32 v209, v176, v177 op_sel:[0,0,1]
	v_cvt_pk_fp8_f32 v210, v198, v199 op_sel:[0,0,1]
	v_cvt_pk_fp8_f32 v211, v202, v203 op_sel:[0,0,1]
	s_nop 0
	global_store_dwordx4 v12, v[208:211], s[14:15]
	s_waitcnt vmcnt(16)
	v_mul_f32_e32 v68, 0x43000000, v68
	v_mul_f32_e32 v69, 0x43000000, v69
	v_mul_f32_e32 v70, 0x43000000, v70
	v_mul_f32_e32 v71, 0x43000000, v71
	ds_write_b128 v5, v[68:71]
	v_mul_f32_e32 v72, 0x43000000, v72
	v_mul_f32_e32 v73, 0x43000000, v73
	v_mul_f32_e32 v74, 0x43000000, v74
	v_mul_f32_e32 v75, 0x43000000, v75
	ds_write_b128 v5, v[72:75] offset:1024
	v_mul_f32_e32 v76, 0x43000000, v76
	v_mul_f32_e32 v77, 0x43000000, v77
	v_mul_f32_e32 v78, 0x43000000, v78
	v_mul_f32_e32 v79, 0x43000000, v79
	ds_write_b128 v5, v[76:79] offset:2048
	v_mul_f32_e32 v80, 0x43000000, v80
	v_mul_f32_e32 v81, 0x43000000, v81
	v_mul_f32_e32 v82, 0x43000000, v82
	v_mul_f32_e32 v83, 0x43000000, v83
	ds_write_b128 v5, v[80:83] offset:3072
	v_mul_f32_e32 v84, 0x43000000, v84
	v_mul_f32_e32 v85, 0x43000000, v85
	v_mul_f32_e32 v86, 0x43000000, v86
	v_mul_f32_e32 v87, 0x43000000, v87
	ds_write_b128 v5, v[84:87] offset:4096
	v_mul_f32_e32 v88, 0x43000000, v88
	v_mul_f32_e32 v89, 0x43000000, v89
	v_mul_f32_e32 v90, 0x43000000, v90
	v_mul_f32_e32 v91, 0x43000000, v91
	ds_write_b128 v5, v[88:91] offset:5120
	v_mul_f32_e32 v92, 0x43000000, v92
	v_mul_f32_e32 v93, 0x43000000, v93
	v_mul_f32_e32 v94, 0x43000000, v94
	v_mul_f32_e32 v95, 0x43000000, v95
	ds_write_b128 v5, v[92:95] offset:6144
	v_mul_f32_e32 v96, 0x43000000, v96
	v_mul_f32_e32 v97, 0x43000000, v97
	v_mul_f32_e32 v98, 0x43000000, v98
	v_mul_f32_e32 v99, 0x43000000, v99
	ds_write_b128 v5, v[96:99] offset:7168
	s_waitcnt lgkmcnt(0)
	s_barrier
; #define GAS __attribute__((address_space(1)))
; #define LAS __attribute__((address_space(3)))
; #define LDS_WAIT() asm volatile("s_waitcnt lgkmcnt(0)" ::: "memory")
; __device__ __forceinline__ unsigned pk4_fp8(float a, float b, float c, float d) {
;     a = fminf(fmaxf(a, -448.f), 448.f); b = fminf(fmaxf(b, -448.f), 448.f); c = fminf(fmaxf(c, -448.f), 448.f); d = fminf(fmaxf(d, -448.f), 448.f);
;     int w = __builtin_amdgcn_cvt_pk_fp8_f32(a, b, 0, false); w = __builtin_amdgcn_cvt_pk_fp8_f32(c, d, w, true); return (unsigned)w; }
;     ...
;     LDS_WAIT(); asm volatile("" ::: "memory");
;     const int c = lane & 7;
; #pragma unroll
;     for (int j = 0; j < 4; ++j) { const int n = (lane >> 3) + 8 * j; const LAS float* s = scr + (8 * c) * 33 + n;
;         const unsigned long long o = (unsigned long long)pg8::pk4_fp8(s[0 * 33], s[1 * 33], s[2 * 33], s[3 * 33]) | ((unsigned long long)pg8::pk4_fp8(s[4 * 33], s[5 * 33], s[6 * 33], s[7 * 33]) << 32);
;         *(GAS unsigned long long*)(WT + (size_t)(n0 + n) * K + k0 + 8 * c) = o; }
;     LDS_WAIT(); asm volatile("" ::: "memory");
	s_add_i32 s17, s16, 3936
	s_min_u32 s17, s17, 0xfff
	s_lshr_b32 s18, s17, 5
	s_add_i32 s18, s18, 0
	s_and_b32 s19, s17, 31
	s_lshl_b32 s19, s19, 21
	s_lshl_b32 s18, s18, 7
	s_add_u32 s18, s18, s19
	s_add_u32 s14, s4, s18
	s_addc_u32 s15, s5, 0
	ds_read_b32 v170, v7
	ds_read_b32 v171, v7 offset:512
	ds_read_b32 v172, v7 offset:1024
	ds_read_b32 v173, v7 offset:1536
	ds_read_b32 v174, v7 offset:2048
	ds_read_b32 v175, v7 offset:2560
	ds_read_b32 v176, v7 offset:3072
	ds_read_b32 v177, v7 offset:3584
	ds_read_b32 v196, v7 offset:4096
	ds_read_b32 v197, v7 offset:4608
	ds_read_b32 v198, v7 offset:5120
	ds_read_b32 v199, v7 offset:5632
	ds_read_b32 v200, v7 offset:6144
	ds_read_b32 v201, v7 offset:6656
	ds_read_b32 v202, v7 offset:7168
	ds_read_b32 v203, v7 offset:7680
	s_waitcnt lgkmcnt(0)
	v_max_f32_e32 v170, v170, v170
	v_max_f32_e32 v171, v171, v171
	v_max_f32_e32 v172, v172, v172
	v_max_f32_e32 v173, v173, v173
	v_max_f32_e32 v174, v174, v174
	v_max_f32_e32 v175, v175, v175
	v_max_f32_e32 v176, v176, v176
	v_max_f32_e32 v177, v177, v177
	v_max_f32_e32 v196, v196, v196
	v_max_f32_e32 v197, v197, v197
	v_max_f32_e32 v198, v198, v198
	v_max_f32_e32 v199, v199, v199
	v_max_f32_e32 v200, v200, v200
	v_max_f32_e32 v201, v201, v201
	v_max_f32_e32 v202, v202, v202
	v_max_f32_e32 v203, v203, v203
	v_med3_f32 v170, v170, s20, v13
	v_med3_f32 v171, v171, s20, v13
	v_med3_f32 v172, v172, s20, v13
	v_med3_f32 v173, v173, s20, v13
	v_med3_f32 v174, v174, s20, v13
	v_med3_f32 v175, v175, s20, v13
	v_med3_f32 v176, v176, s20, v13
	v_med3_f32 v177, v177, s20, v13
	v_med3_f32 v196, v196, s20, v13
	v_med3_f32 v197, v197, s20, v13
	v_med3_f32 v198, v198, s20, v13
	v_med3_f32 v199, v199, s20, v13
	v_med3_f32 v200, v200, s20, v13
	v_med3_f32 v201, v201, s20, v13
	v_med3_f32 v202, v202, s20, v13
	v_med3_f32 v203, v203, s20, v13
	v_mov_b32_e32 v208, 0
	v_mov_b32_e32 v209, 0
	v_mov_b32_e32 v210, 0
	v_mov_b32_e32 v211, 0
	v_cvt_pk_fp8_f32 v208, v170, v171
	v_cvt_pk_fp8_f32 v209, v174, v175
	v_cvt_pk_fp8_f32 v210, v196, v197
	v_cvt_pk_fp8_f32 v211, v200, v201
	v_cvt_pk_fp8_f32 v208, v172, v173 op_sel:[0,0,1]
	v_cvt_pk_fp8_f32 v209, v176, v177 op_sel:[0,0,1]
	v_cvt_pk_fp8_f32 v210, v198, v199 op_sel:[0,0,1]
	v_cvt_pk_fp8_f32 v211, v202, v203 op_sel:[0,0,1]
	s_nop 0
	global_store_dwordx4 v11, v[208:211], s[14:15]
	ds_read_b32 v170, v9
	ds_read_b32 v171, v9 offset:512
	ds_read_b32 v172, v9 offset:1024
	ds_read_b32 v173, v9 offset:1536
	ds_read_b32 v174, v9 offset:2048
	ds_read_b32 v175, v9 offset:2560
	ds_read_b32 v176, v9 offset:3072
	ds_read_b32 v177, v9 offset:3584
	ds_read_b32 v196, v9 offset:4096
	ds_read_b32 v197, v9 offset:4608
	ds_read_b32 v198, v9 offset:5120
	ds_read_b32 v199, v9 offset:5632
	ds_read_b32 v200, v9 offset:6144
	ds_read_b32 v201, v9 offset:6656
	ds_read_b32 v202, v9 offset:7168
	ds_read_b32 v203, v9 offset:7680
	s_waitcnt lgkmcnt(0)
	v_max_f32_e32 v170, v170, v170
	v_max_f32_e32 v171, v171, v171
	v_max_f32_e32 v172, v172, v172
	v_max_f32_e32 v173, v173, v173
	v_max_f32_e32 v174, v174, v174
	v_max_f32_e32 v175, v175, v175
	v_max_f32_e32 v176, v176, v176
	v_max_f32_e32 v177, v177, v177
	v_max_f32_e32 v196, v196, v196
	v_max_f32_e32 v197, v197, v197
	v_max_f32_e32 v198, v198, v198
	v_max_f32_e32 v199, v199, v199
	v_max_f32_e32 v200, v200, v200
	v_max_f32_e32 v201, v201, v201
	v_max_f32_e32 v202, v202, v202
	v_max_f32_e32 v203, v203, v203
	v_med3_f32 v170, v170, s20, v13
	v_med3_f32 v171, v171, s20, v13
	v_med3_f32 v172, v172, s20, v13
	v_med3_f32 v173, v173, s20, v13
	v_med3_f32 v174, v174, s20, v13
	v_med3_f32 v175, v175, s20, v13
	v_med3_f32 v176, v176, s20, v13
	v_med3_f32 v177, v177, s20, v13
	v_med3_f32 v196, v196, s20, v13
	v_med3_f32 v197, v197, s20, v13
	v_med3_f32 v198, v198, s20, v13
	v_med3_f32 v199, v199, s20, v13
	v_med3_f32 v200, v200, s20, v13
	v_med3_f32 v201, v201, s20, v13
	v_med3_f32 v202, v202, s20, v13
	v_med3_f32 v203, v203, s20, v13
	v_mov_b32_e32 v208, 0
	v_mov_b32_e32 v209, 0
	v_mov_b32_e32 v210, 0
	v_mov_b32_e32 v211, 0
	v_cvt_pk_fp8_f32 v208, v170, v171
	v_cvt_pk_fp8_f32 v209, v174, v175
	v_cvt_pk_fp8_f32 v210, v196, v197
	v_cvt_pk_fp8_f32 v211, v200, v201
	v_cvt_pk_fp8_f32 v208, v172, v173 op_sel:[0,0,1]
	v_cvt_pk_fp8_f32 v209, v176, v177 op_sel:[0,0,1]
	v_cvt_pk_fp8_f32 v210, v198, v199 op_sel:[0,0,1]
	v_cvt_pk_fp8_f32 v211, v202, v203 op_sel:[0,0,1]
	s_nop 0
	global_store_dwordx4 v12, v[208:211], s[14:15]
	s_waitcnt vmcnt(8)
	v_mul_f32_e32 v100, 0x43000000, v100
	v_mul_f32_e32 v101, 0x43000000, v101
	v_mul_f32_e32 v102, 0x43000000, v102
	v_mul_f32_e32 v103, 0x43000000, v103
	ds_write_b128 v4, v[100:103]
	v_mul_f32_e32 v104, 0x43000000, v104
	v_mul_f32_e32 v105, 0x43000000, v105
	v_mul_f32_e32 v106, 0x43000000, v106
	v_mul_f32_e32 v107, 0x43000000, v107
	ds_write_b128 v4, v[104:107] offset:1024
	v_mul_f32_e32 v108, 0x43000000, v108
	v_mul_f32_e32 v109, 0x43000000, v109
	v_mul_f32_e32 v110, 0x43000000, v110
	v_mul_f32_e32 v111, 0x43000000, v111
	ds_write_b128 v4, v[108:111] offset:2048
	v_mul_f32_e32 v112, 0x43000000, v112
	v_mul_f32_e32 v113, 0x43000000, v113
	v_mul_f32_e32 v114, 0x43000000, v114
	v_mul_f32_e32 v115, 0x43000000, v115
	ds_write_b128 v4, v[112:115] offset:3072
	v_mul_f32_e32 v116, 0x43000000, v116
	v_mul_f32_e32 v117, 0x43000000, v117
	v_mul_f32_e32 v118, 0x43000000, v118
	v_mul_f32_e32 v119, 0x43000000, v119
	ds_write_b128 v4, v[116:119] offset:4096
	v_mul_f32_e32 v120, 0x43000000, v120
	v_mul_f32_e32 v121, 0x43000000, v121
	v_mul_f32_e32 v122, 0x43000000, v122
	v_mul_f32_e32 v123, 0x43000000, v123
	ds_write_b128 v4, v[120:123] offset:5120
	v_mul_f32_e32 v124, 0x43000000, v124
	v_mul_f32_e32 v125, 0x43000000, v125
	v_mul_f32_e32 v126, 0x43000000, v126
	v_mul_f32_e32 v127, 0x43000000, v127
	ds_write_b128 v4, v[124:127] offset:6144
	v_mul_f32_e32 v128, 0x43000000, v128
	v_mul_f32_e32 v129, 0x43000000, v129
	v_mul_f32_e32 v130, 0x43000000, v130
	v_mul_f32_e32 v131, 0x43000000, v131
	ds_write_b128 v4, v[128:131] offset:7168
	s_waitcnt lgkmcnt(0)
	s_barrier
; #define GAS __attribute__((address_space(1)))
; #define LAS __attribute__((address_space(3)))
; #define LDS_WAIT() asm volatile("s_waitcnt lgkmcnt(0)" ::: "memory")
; __device__ __forceinline__ unsigned pk4_fp8(float a, float b, float c, float d) {
;     a = fminf(fmaxf(a, -448.f), 448.f); b = fminf(fmaxf(b, -448.f), 448.f); c = fminf(fmaxf(c, -448.f), 448.f); d = fminf(fmaxf(d, -448.f), 448.f);
;     int w = __builtin_amdgcn_cvt_pk_fp8_f32(a, b, 0, false); w = __builtin_amdgcn_cvt_pk_fp8_f32(c, d, w, true); return (unsigned)w; }
;     ...
;     LDS_WAIT(); asm volatile("" ::: "memory");
;     const int c = lane & 7;
; #pragma unroll
;     for (int j = 0; j < 4; ++j) { const int n = (lane >> 3) + 8 * j; const LAS float* s = scr + (8 * c) * 33 + n;
;         const unsigned long long o = (unsigned long long)pg8::pk4_fp8(s[0 * 33], s[1 * 33], s[2 * 33], s[3 * 33]) | ((unsigned long long)pg8::pk4_fp8(s[4 * 33], s[5 * 33], s[6 * 33], s[7 * 33]) << 32);
;         *(GAS unsigned long long*)(WT + (size_t)(n0 + n) * K + k0 + 8 * c) = o; }
;     LDS_WAIT(); asm volatile("" ::: "memory");
	s_add_i32 s17, s16, 4032
	s_min_u32 s17, s17, 0xfff
	s_lshr_b32 s18, s17, 5
	s_add_i32 s18, s18, 0
	s_and_b32 s19, s17, 31
	s_lshl_b32 s19, s19, 21
	s_lshl_b32 s18, s18, 7
	s_add_u32 s18, s18, s19
	s_add_u32 s14, s4, s18
	s_addc_u32 s15, s5, 0
	ds_read_b32 v170, v6
	ds_read_b32 v171, v6 offset:512
	ds_read_b32 v172, v6 offset:1024
	ds_read_b32 v173, v6 offset:1536
	ds_read_b32 v174, v6 offset:2048
	ds_read_b32 v175, v6 offset:2560
	ds_read_b32 v176, v6 offset:3072
	ds_read_b32 v177, v6 offset:3584
	ds_read_b32 v196, v6 offset:4096
	ds_read_b32 v197, v6 offset:4608
	ds_read_b32 v198, v6 offset:5120
	ds_read_b32 v199, v6 offset:5632
	ds_read_b32 v200, v6 offset:6144
	ds_read_b32 v201, v6 offset:6656
	ds_read_b32 v202, v6 offset:7168
	ds_read_b32 v203, v6 offset:7680
	s_waitcnt lgkmcnt(0)
	v_max_f32_e32 v170, v170, v170
	v_max_f32_e32 v171, v171, v171
	v_max_f32_e32 v172, v172, v172
	v_max_f32_e32 v173, v173, v173
	v_max_f32_e32 v174, v174, v174
	v_max_f32_e32 v175, v175, v175
	v_max_f32_e32 v176, v176, v176
	v_max_f32_e32 v177, v177, v177
	v_max_f32_e32 v196, v196, v196
	v_max_f32_e32 v197, v197, v197
	v_max_f32_e32 v198, v198, v198
	v_max_f32_e32 v199, v199, v199
	v_max_f32_e32 v200, v200, v200
	v_max_f32_e32 v201, v201, v201
	v_max_f32_e32 v202, v202, v202
	v_max_f32_e32 v203, v203, v203
	v_med3_f32 v170, v170, s20, v13
	v_med3_f32 v171, v171, s20, v13
	v_med3_f32 v172, v172, s20, v13
	v_med3_f32 v173, v173, s20, v13
	v_med3_f32 v174, v174, s20, v13
	v_med3_f32 v175, v175, s20, v13
	v_med3_f32 v176, v176, s20, v13
	v_med3_f32 v177, v177, s20, v13
	v_med3_f32 v196, v196, s20, v13
	v_med3_f32 v197, v197, s20, v13
	v_med3_f32 v198, v198, s20, v13
	v_med3_f32 v199, v199, s20, v13
	v_med3_f32 v200, v200, s20, v13
	v_med3_f32 v201, v201, s20, v13
	v_med3_f32 v202, v202, s20, v13
	v_med3_f32 v203, v203, s20, v13
	v_mov_b32_e32 v208, 0
	v_mov_b32_e32 v209, 0
	v_mov_b32_e32 v210, 0
	v_mov_b32_e32 v211, 0
	v_cvt_pk_fp8_f32 v208, v170, v171
	v_cvt_pk_fp8_f32 v209, v174, v175
	v_cvt_pk_fp8_f32 v210, v196, v197
	v_cvt_pk_fp8_f32 v211, v200, v201
	v_cvt_pk_fp8_f32 v208, v172, v173 op_sel:[0,0,1]
	v_cvt_pk_fp8_f32 v209, v176, v177 op_sel:[0,0,1]
	v_cvt_pk_fp8_f32 v210, v198, v199 op_sel:[0,0,1]
	v_cvt_pk_fp8_f32 v211, v202, v203 op_sel:[0,0,1]
	s_nop 0
	global_store_dwordx4 v11, v[208:211], s[14:15]
	ds_read_b32 v170, v8
	ds_read_b32 v171, v8 offset:512
	ds_read_b32 v172, v8 offset:1024
	ds_read_b32 v173, v8 offset:1536
	ds_read_b32 v174, v8 offset:2048
	ds_read_b32 v175, v8 offset:2560
	ds_read_b32 v176, v8 offset:3072
	ds_read_b32 v177, v8 offset:3584
	ds_read_b32 v196, v8 offset:4096
	ds_read_b32 v197, v8 offset:4608
	ds_read_b32 v198, v8 offset:5120
	ds_read_b32 v199, v8 offset:5632
	ds_read_b32 v200, v8 offset:6144
	ds_read_b32 v201, v8 offset:6656
	ds_read_b32 v202, v8 offset:7168
	ds_read_b32 v203, v8 offset:7680
	s_waitcnt lgkmcnt(0)
	v_max_f32_e32 v170, v170, v170
	v_max_f32_e32 v171, v171, v171
	v_max_f32_e32 v172, v172, v172
	v_max_f32_e32 v173, v173, v173
	v_max_f32_e32 v174, v174, v174
	v_max_f32_e32 v175, v175, v175
	v_max_f32_e32 v176, v176, v176
	v_max_f32_e32 v177, v177, v177
	v_max_f32_e32 v196, v196, v196
	v_max_f32_e32 v197, v197, v197
	v_max_f32_e32 v198, v198, v198
	v_max_f32_e32 v199, v199, v199
	v_max_f32_e32 v200, v200, v200
	v_max_f32_e32 v201, v201, v201
	v_max_f32_e32 v202, v202, v202
	v_max_f32_e32 v203, v203, v203
	v_med3_f32 v170, v170, s20, v13
	v_med3_f32 v171, v171, s20, v13
	v_med3_f32 v172, v172, s20, v13
	v_med3_f32 v173, v173, s20, v13
	v_med3_f32 v174, v174, s20, v13
	v_med3_f32 v175, v175, s20, v13
	v_med3_f32 v176, v176, s20, v13
	v_med3_f32 v177, v177, s20, v13
	v_med3_f32 v196, v196, s20, v13
	v_med3_f32 v197, v197, s20, v13
	v_med3_f32 v198, v198, s20, v13
	v_med3_f32 v199, v199, s20, v13
	v_med3_f32 v200, v200, s20, v13
	v_med3_f32 v201, v201, s20, v13
	v_med3_f32 v202, v202, s20, v13
	v_med3_f32 v203, v203, s20, v13
	v_mov_b32_e32 v208, 0
	v_mov_b32_e32 v209, 0
	v_mov_b32_e32 v210, 0
	v_mov_b32_e32 v211, 0
	v_cvt_pk_fp8_f32 v208, v170, v171
	v_cvt_pk_fp8_f32 v209, v174, v175
	v_cvt_pk_fp8_f32 v210, v196, v197
	v_cvt_pk_fp8_f32 v211, v200, v201
	v_cvt_pk_fp8_f32 v208, v172, v173 op_sel:[0,0,1]
	v_cvt_pk_fp8_f32 v209, v176, v177 op_sel:[0,0,1]
	v_cvt_pk_fp8_f32 v210, v198, v199 op_sel:[0,0,1]
	v_cvt_pk_fp8_f32 v211, v202, v203 op_sel:[0,0,1]
	s_nop 0
	global_store_dwordx4 v12, v[208:211], s[14:15]
	s_waitcnt vmcnt(0) lgkmcnt(0)
	s_barrier
